# non-temporal cache policy on all GEMM tile-epilogue result stores (QKV, in-proj, out-proj, GEMM1, GEMM2), on top of v017
# baseline (speedup 1.0000x reference)
.LBB0_127:
	v_add_f32_e32 v66, v134, v139
	v_fmamk_f32 v66, v66, 0x37800000, v225
	v_mul_f32_e32 v66, 0x3c800000, v66
	v_rsq_f32_e32 v66, v66
	v_mov_b32_e32 v67, 0x3d800000
	v_cndmask_b32_e64 v154, v67, v228, s[46:47]
	s_mul_i32 s1, s1, 3
	v_cndmask_b32_e64 v66, 1.0, v66, s[44:45]
	v_mul_f32_e32 v66, v154, v66
	v_pk_mul_f32 v[68:69], v[126:127], v[66:67] op_sel_hi:[1,0]
	v_pk_mul_f32 v[126:127], v[128:129], v[66:67] op_sel_hi:[1,0]
	v_pk_mul_f32 v[68:69], v[68:69], v[148:149]
	v_pk_mul_f32 v[122:123], v[122:123], v[66:67] op_sel_hi:[1,0]
	v_pk_mul_f32 v[124:125], v[124:125], v[66:67] op_sel_hi:[1,0]
	v_min_f32_e64 v67, |v68|, s33
	v_bfi_b32 v67, s2, v67, v68
	v_min_f32_e64 v68, |v69|, s33
	v_bfi_b32 v68, s2, v68, v69
	v_mov_b32_e32 v128, v207
	v_cvt_pk_fp8_f32 v128, v67, v68
	v_pk_mul_f32 v[126:127], v[126:127], v[152:153]
	v_pk_mul_f32 v[122:123], v[122:123], v[146:147]
	v_min_f32_e64 v69, |v126|, s33
	v_min_f32_e64 v68, |v127|, s33
	v_bfi_b32 v67, s2, v69, v126
	v_bfi_b32 v68, s2, v68, v127
	v_cvt_pk_fp8_f32 v128, v67, v68 op_sel:[0,0,1]
	v_min_f32_e64 v67, |v122|, s33
	v_min_f32_e64 v68, |v123|, s33
	v_bfi_b32 v67, s2, v67, v122
	v_bfi_b32 v68, s2, v68, v123
	v_mov_b32_e32 v126, v207
	v_cvt_pk_fp8_f32 v126, v67, v68
	v_pk_mul_f32 v[124:125], v[124:125], v[150:151]
	s_add_i32 s4, s1, s4
	v_min_f32_e64 v69, |v124|, s33
	v_min_f32_e64 v68, |v125|, s33
	v_bfi_b32 v67, s2, v69, v124
	v_bfi_b32 v68, s2, v68, v125
	v_cvt_pk_fp8_f32 v126, v67, v68 op_sel:[0,0,1]
	v_lshlrev_b32_e32 v67, 2, v135
	v_pk_mul_f32 v[118:119], v[118:119], v[66:67] op_sel_hi:[1,0]
	v_and_b32_e32 v206, 32, v67
	v_pk_mul_f32 v[118:119], v[118:119], v[136:137]
	v_pk_mul_f32 v[120:121], v[120:121], v[66:67] op_sel_hi:[1,0]
	v_pk_mul_f32 v[114:115], v[114:115], v[66:67] op_sel_hi:[1,0]
	v_pk_mul_f32 v[66:67], v[116:117], v[66:67] op_sel_hi:[1,0]
	v_min_f32_e64 v116, |v118|, s33
	v_bfi_b32 v117, s2, v116, v118
	v_min_f32_e64 v116, |v119|, s33
	v_bfi_b32 v118, s2, v116, v119
	v_mov_b32_e32 v116, v207
	v_cvt_pk_fp8_f32 v116, v117, v118
	v_pk_mul_f32 v[120:121], v[120:121], v[144:145]
	s_ashr_i32 s5, s4, 31
	v_min_f32_e64 v119, |v120|, s33
	v_min_f32_e64 v118, |v121|, s33
	s_lshl_b64 s[4:5], s[4:5], 24
	v_pk_mul_f32 v[114:115], v[114:115], v[140:141]
	v_bfi_b32 v117, s2, v119, v120
	v_bfi_b32 v118, s2, v118, v121
	s_add_u32 s1, s31, s4
	v_cvt_pk_fp8_f32 v116, v117, v118 op_sel:[0,0,1]
	v_min_f32_e64 v117, |v114|, s33
	s_addc_u32 s4, s34, s5
	s_lshl_b32 s0, s0, 18
	v_bfi_b32 v114, s2, v117, v114
	v_min_f32_e64 v117, |v115|, s33
	s_and_b32 s0, s0, 0x1c0000
	v_bfi_b32 v115, s2, v117, v115
	v_mov_b32_e32 v117, v207
	s_add_u32 s0, s1, s0
	v_cvt_pk_fp8_f32 v117, v114, v115
	s_addc_u32 s1, s4, 0
	v_pk_mul_f32 v[66:67], v[66:67], v[142:143]
	v_lshl_add_u64 v[68:69], s[0:1], 0, v[206:207]
	s_lshl_b32 s0, s10, 8
	v_min_f32_e64 v118, |v66|, s33
	v_min_f32_e64 v114, |v67|, s33
	s_add_i32 s0, s0, s30
	v_bfi_b32 v66, s2, v118, v66
	v_bfi_b32 v67, s2, v114, v67
	v_and_b32_e32 v146, 15, v135
	s_ashr_i32 s4, s0, 12
	v_cvt_pk_fp8_f32 v117, v66, v67 op_sel:[0,0,1]
	v_mov_b32_e32 v139, v207
	v_or_b32_e32 v124, s0, v146
	s_ashr_i32 s5, s4, 31
	v_lshl_add_u64 v[122:123], v[68:69], 0, v[138:139]
	s_lshl_b64 s[4:5], s[4:5], 21
	v_lshlrev_b32_e32 v114, 6, v124
	v_lshl_add_u64 v[68:69], v[122:123], 0, s[4:5]
	v_mov_b32_e32 v66, v128
	v_mov_b32_e32 v67, v126
	v_and_b32_e32 v206, 0x3f1c0, v114
	v_mov_b32_dpp v66, v116 row_ror:8 row_mask:0xf bank_mask:0xc
	v_mov_b32_dpp v67, v117 row_ror:8 row_mask:0xf bank_mask:0xc
	v_lshl_add_u64 v[114:115], v[68:69], 0, v[206:207]
	v_mov_b32_dpp v116, v128 row_ror:8 row_mask:0xf bank_mask:0x3
	v_mov_b32_dpp v117, v126 row_ror:8 row_mask:0xf bank_mask:0x3
	global_store_dwordx2 v[114:115], v[66:67], off nt
	global_store_dwordx2 v[114:115], v[116:117], off offset:512 nt
	v_mul_f32_e32 v66, v107, v107
	v_mul_f32_e32 v67, v109, v109
	v_fmac_f32_e32 v66, v106, v106
	v_fmac_f32_e32 v67, v108, v108
	v_add_f32_e32 v66, v66, v67
	v_mul_f32_e32 v67, v99, v99
	v_mul_f32_e32 v68, v101, v101
	v_fmac_f32_e32 v67, v98, v98
	v_fmac_f32_e32 v68, v100, v100
	v_add_f32_e32 v67, v67, v68
	v_add_f32_e32 v66, v66, v67
	v_mul_f32_e32 v67, v111, v111
	v_mul_f32_e32 v68, v113, v113
	v_fmac_f32_e32 v67, v110, v110
	v_fmac_f32_e32 v68, v112, v112
	v_add_f32_e32 v67, v67, v68
	v_add_f32_e32 v66, v66, v67
	v_mul_f32_e32 v67, v103, v103
	v_mul_f32_e32 v68, v105, v105
	v_fmac_f32_e32 v67, v102, v102
	v_fmac_f32_e32 v68, v104, v104
	v_add_f32_e32 v67, v67, v68
	v_add_f32_e32 v66, v66, v67
	v_mov_b32_e32 v67, v66
	s_nop 1
	v_permlane16_swap_b32_e32 v66, v67
	v_add_f32_e32 v116, v66, v67
	v_mov_b32_e32 v117, v116
	v_mov_b32_e32 v134, 1.0
	s_nop 0
	v_permlane32_swap_b32_e32 v116, v117
	s_and_b64 vcc, exec, s[42:43]
	v_mov_b32_e32 v124, 1.0
	v_mov_b32_e32 v125, 1.0
	v_mov_b32_e32 v138, 1.0
	v_mov_b32_e32 v139, 1.0
	v_mov_b32_e32 v120, 1.0
	v_mov_b32_e32 v121, 1.0
	v_mov_b32_e32 v128, 1.0
	v_mov_b32_e32 v129, 1.0
	s_cbranch_vccnz .LBB0_129
	global_load_dwordx4 v[66:69], v[132:133], off
	global_load_dwordx4 v[118:121], v[132:133], off offset:16
	v_mov_b32_e32 v126, v130
	v_mov_b32_e32 v127, v130
	s_waitcnt vmcnt(0)
	v_pk_mul_f32 v[138:139], v[126:127], v[68:69]
	v_pk_mul_f32 v[124:125], v[130:131], v[66:67]
	v_pk_mul_f32 v[128:129], v[126:127], v[120:121]
	v_pk_mul_f32 v[120:121], v[130:131], v[118:119]

.LBB0_131:
	v_add_f32_e32 v66, v116, v117
	v_fmamk_f32 v66, v66, 0x37800000, v225
	v_mul_f32_e32 v66, 0x3c800000, v66
	v_rsq_f32_e32 v66, v66
	v_mov_b32_e32 v116, 1.0
	s_and_b64 vcc, exec, s[42:43]
	v_cndmask_b32_e64 v66, 1.0, v66, s[44:45]
	v_mul_f32_e32 v66, v154, v66
	v_pk_mul_f32 v[106:107], v[106:107], v[66:67] op_sel_hi:[1,0]
	v_pk_mul_f32 v[68:69], v[108:109], v[66:67] op_sel_hi:[1,0]
	v_pk_mul_f32 v[106:107], v[106:107], v[124:125]
	v_pk_mul_f32 v[100:101], v[100:101], v[66:67] op_sel_hi:[1,0]
	v_pk_mul_f32 v[98:99], v[98:99], v[66:67] op_sel_hi:[1,0]
	v_min_f32_e64 v67, |v106|, s33
	v_bfi_b32 v67, s2, v67, v106
	v_min_f32_e64 v106, |v107|, s33
	v_bfi_b32 v106, s2, v106, v107
	v_mov_b32_e32 v108, v207
	v_pk_mul_f32 v[68:69], v[68:69], v[138:139]
	v_cvt_pk_fp8_f32 v108, v67, v106
	v_min_f32_e64 v107, |v68|, s33
	v_bfi_b32 v67, s2, v107, v68
	v_min_f32_e64 v68, |v69|, s33
	v_pk_mul_f32 v[98:99], v[98:99], v[120:121]
	v_bfi_b32 v68, s2, v68, v69
	v_cvt_pk_fp8_f32 v108, v67, v68 op_sel:[0,0,1]
	v_min_f32_e64 v67, |v98|, s33
	v_min_f32_e64 v68, |v99|, s33
	v_pk_mul_f32 v[100:101], v[100:101], v[128:129]
	v_bfi_b32 v67, s2, v67, v98
	v_bfi_b32 v68, s2, v68, v99
	v_mov_b32_e32 v106, v207
	v_min_f32_e64 v69, |v100|, s33
	v_cvt_pk_fp8_f32 v106, v67, v68
	v_bfi_b32 v67, s2, v69, v100
	v_min_f32_e64 v68, |v101|, s33
	v_pk_mul_f32 v[98:99], v[110:111], v[66:67] op_sel_hi:[1,0]
	v_bfi_b32 v68, s2, v68, v101
	v_pk_mul_f32 v[98:99], v[98:99], v[134:135]
	v_cvt_pk_fp8_f32 v106, v67, v68 op_sel:[0,0,1]
	v_pk_mul_f32 v[68:69], v[112:113], v[66:67] op_sel_hi:[1,0]
	v_pk_mul_f32 v[100:101], v[104:105], v[66:67] op_sel_hi:[1,0]
	v_pk_mul_f32 v[66:67], v[102:103], v[66:67] op_sel_hi:[1,0]
	v_min_f32_e64 v102, |v98|, s33
	v_bfi_b32 v102, s2, v102, v98
	v_min_f32_e64 v98, |v99|, s33
	v_bfi_b32 v99, s2, v98, v99
	v_mov_b32_e32 v98, v207
	v_cvt_pk_fp8_f32 v98, v102, v99
	v_pk_mul_f32 v[68:69], v[68:69], v[136:137]
	v_pk_mul_f32 v[66:67], v[66:67], v[118:119]
	v_min_f32_e64 v103, |v68|, s33
	v_min_f32_e64 v99, |v69|, s33
	v_bfi_b32 v68, s2, v103, v68
	v_bfi_b32 v69, s2, v99, v69
	v_cvt_pk_fp8_f32 v98, v68, v69 op_sel:[0,0,1]
	v_min_f32_e64 v68, |v66|, s33
	v_bfi_b32 v66, s2, v68, v66
	v_min_f32_e64 v68, |v67|, s33
	v_bfi_b32 v67, s2, v68, v67
	v_mov_b32_e32 v99, v207
	v_cvt_pk_fp8_f32 v99, v66, v67
	v_pk_mul_f32 v[100:101], v[100:101], v[126:127]
	v_mov_b32_e32 v104, 1.0
	v_min_f32_e64 v68, |v100|, s33
	v_min_f32_e64 v67, |v101|, s33
	v_bfi_b32 v66, s2, v68, v100
	v_bfi_b32 v67, s2, v67, v101
	v_cvt_pk_fp8_f32 v99, v66, v67 op_sel:[0,0,1]
	v_mov_b32_e32 v66, v108
	v_mov_b32_e32 v67, v106
	v_mul_f32_e32 v68, v85, v85
	v_mov_b32_dpp v66, v98 row_ror:8 row_mask:0xf bank_mask:0xc
	v_mov_b32_dpp v67, v99 row_ror:8 row_mask:0xf bank_mask:0xc
	v_mov_b32_dpp v98, v108 row_ror:8 row_mask:0xf bank_mask:0x3
	v_mov_b32_dpp v99, v106 row_ror:8 row_mask:0xf bank_mask:0x3
	global_store_dwordx2 v[114:115], v[66:67], off offset:1024 nt
	global_store_dwordx2 v[114:115], v[98:99], off offset:1536 nt
	v_mul_f32_e32 v66, v91, v91
	v_mul_f32_e32 v67, v93, v93
	v_fmac_f32_e32 v66, v90, v90
	v_fmac_f32_e32 v67, v92, v92
	v_add_f32_e32 v66, v66, v67
	v_mul_f32_e32 v67, v83, v83
	v_fmac_f32_e32 v67, v82, v82
	v_fmac_f32_e32 v68, v84, v84
	v_add_f32_e32 v67, v67, v68
	v_add_f32_e32 v66, v66, v67
	v_mul_f32_e32 v67, v95, v95
	v_mul_f32_e32 v68, v97, v97
	v_fmac_f32_e32 v67, v94, v94
	v_fmac_f32_e32 v68, v96, v96
	v_add_f32_e32 v67, v67, v68
	v_add_f32_e32 v66, v66, v67
	v_mul_f32_e32 v67, v87, v87
	v_mul_f32_e32 v68, v89, v89
	v_fmac_f32_e32 v67, v86, v86
	v_fmac_f32_e32 v68, v88, v88
	v_add_f32_e32 v67, v67, v68
	v_add_f32_e32 v66, v66, v67
	v_mov_b32_e32 v67, v66
	s_nop 1
	v_permlane16_swap_b32_e32 v66, v67
	v_add_f32_e32 v98, v66, v67
	v_mov_b32_e32 v99, v98
	s_nop 1
	v_permlane32_swap_b32_e32 v98, v99
	v_mov_b32_e32 v105, 1.0
	v_mov_b32_e32 v112, 1.0
	v_mov_b32_e32 v113, 1.0
	v_mov_b32_e32 v102, 1.0
	v_mov_b32_e32 v103, 1.0
	v_mov_b32_e32 v108, 1.0
	v_mov_b32_e32 v109, 1.0
	s_cbranch_vccnz .LBB0_133
	global_load_dwordx4 v[66:69], v[132:133], off
	global_load_dwordx4 v[100:103], v[132:133], off offset:16
	v_mov_b32_e32 v106, v130
	v_mov_b32_e32 v107, v130
	s_waitcnt vmcnt(0)
	v_pk_mul_f32 v[112:113], v[106:107], v[68:69]
	v_pk_mul_f32 v[104:105], v[130:131], v[66:67]
	v_pk_mul_f32 v[108:109], v[106:107], v[102:103]
	v_pk_mul_f32 v[102:103], v[130:131], v[100:101]

.LBB0_135:
	v_add_f32_e32 v66, v98, v99
	v_fmamk_f32 v66, v66, 0x37800000, v225
	v_mul_f32_e32 v66, 0x3c800000, v66
	v_rsq_f32_e32 v66, v66
	v_mov_b32_e32 v98, 1.0
	s_and_b64 vcc, exec, s[42:43]
	v_cndmask_b32_e64 v66, 1.0, v66, s[44:45]
	v_mul_f32_e32 v66, v154, v66
	v_pk_mul_f32 v[90:91], v[90:91], v[66:67] op_sel_hi:[1,0]
	v_pk_mul_f32 v[68:69], v[92:93], v[66:67] op_sel_hi:[1,0]
	v_pk_mul_f32 v[90:91], v[90:91], v[104:105]
	v_pk_mul_f32 v[84:85], v[84:85], v[66:67] op_sel_hi:[1,0]
	v_pk_mul_f32 v[82:83], v[82:83], v[66:67] op_sel_hi:[1,0]
	v_min_f32_e64 v67, |v90|, s33
	v_bfi_b32 v67, s2, v67, v90
	v_min_f32_e64 v90, |v91|, s33
	v_bfi_b32 v90, s2, v90, v91
	v_mov_b32_e32 v92, v207
	v_pk_mul_f32 v[68:69], v[68:69], v[112:113]
	v_cvt_pk_fp8_f32 v92, v67, v90
	v_min_f32_e64 v91, |v68|, s33
	v_bfi_b32 v67, s2, v91, v68
	v_min_f32_e64 v68, |v69|, s33
	v_pk_mul_f32 v[82:83], v[82:83], v[102:103]
	v_bfi_b32 v68, s2, v68, v69
	v_cvt_pk_fp8_f32 v92, v67, v68 op_sel:[0,0,1]
	v_min_f32_e64 v67, |v82|, s33
	v_min_f32_e64 v68, |v83|, s33
	v_pk_mul_f32 v[84:85], v[84:85], v[108:109]
	v_bfi_b32 v67, s2, v67, v82
	v_bfi_b32 v68, s2, v68, v83
	v_mov_b32_e32 v90, v207
	v_min_f32_e64 v69, |v84|, s33
	v_cvt_pk_fp8_f32 v90, v67, v68
	v_bfi_b32 v67, s2, v69, v84
	v_min_f32_e64 v68, |v85|, s33
	v_pk_mul_f32 v[82:83], v[94:95], v[66:67] op_sel_hi:[1,0]
	v_bfi_b32 v68, s2, v68, v85
	v_pk_mul_f32 v[82:83], v[82:83], v[116:117]
	v_cvt_pk_fp8_f32 v90, v67, v68 op_sel:[0,0,1]
	v_pk_mul_f32 v[68:69], v[96:97], v[66:67] op_sel_hi:[1,0]
	v_pk_mul_f32 v[84:85], v[88:89], v[66:67] op_sel_hi:[1,0]
	v_pk_mul_f32 v[66:67], v[86:87], v[66:67] op_sel_hi:[1,0]
	v_min_f32_e64 v86, |v82|, s33
	v_bfi_b32 v86, s2, v86, v82
	v_min_f32_e64 v82, |v83|, s33
	v_bfi_b32 v83, s2, v82, v83
	v_mov_b32_e32 v82, v207
	v_cvt_pk_fp8_f32 v82, v86, v83
	v_pk_mul_f32 v[68:69], v[68:69], v[110:111]
	v_pk_mul_f32 v[66:67], v[66:67], v[100:101]
	v_min_f32_e64 v87, |v68|, s33
	v_min_f32_e64 v83, |v69|, s33
	v_bfi_b32 v68, s2, v87, v68
	v_bfi_b32 v69, s2, v83, v69
	v_cvt_pk_fp8_f32 v82, v68, v69 op_sel:[0,0,1]
	v_min_f32_e64 v68, |v66|, s33
	v_bfi_b32 v66, s2, v68, v66
	v_min_f32_e64 v68, |v67|, s33
	v_bfi_b32 v67, s2, v68, v67
	v_mov_b32_e32 v83, v207
	v_cvt_pk_fp8_f32 v83, v66, v67
	v_pk_mul_f32 v[84:85], v[84:85], v[106:107]
	v_mov_b32_e32 v88, 1.0
	v_min_f32_e64 v68, |v84|, s33
	v_min_f32_e64 v67, |v85|, s33
	v_bfi_b32 v66, s2, v68, v84
	v_bfi_b32 v67, s2, v67, v85
	v_cvt_pk_fp8_f32 v83, v66, v67 op_sel:[0,0,1]
	v_mov_b32_e32 v66, v92
	v_mov_b32_e32 v67, v90
	v_mul_f32_e32 v68, v177, v177
	v_mov_b32_dpp v66, v82 row_ror:8 row_mask:0xf bank_mask:0xc
	v_mov_b32_dpp v67, v83 row_ror:8 row_mask:0xf bank_mask:0xc
	v_mov_b32_dpp v82, v92 row_ror:8 row_mask:0xf bank_mask:0x3
	v_mov_b32_dpp v83, v90 row_ror:8 row_mask:0xf bank_mask:0x3
	global_store_dwordx2 v[114:115], v[66:67], off offset:2048 nt
	global_store_dwordx2 v[114:115], v[82:83], off offset:2560 nt
	v_mul_f32_e32 v66, v75, v75
	v_mul_f32_e32 v67, v77, v77
	v_fmac_f32_e32 v66, v74, v74
	v_fmac_f32_e32 v67, v76, v76
	v_add_f32_e32 v66, v66, v67
	v_mul_f32_e32 v67, v175, v175
	v_fmac_f32_e32 v67, v174, v174
	v_fmac_f32_e32 v68, v176, v176
	v_add_f32_e32 v67, v67, v68
	v_add_f32_e32 v66, v66, v67
	v_mul_f32_e32 v67, v79, v79
	v_mul_f32_e32 v68, v81, v81
	v_fmac_f32_e32 v67, v78, v78
	v_fmac_f32_e32 v68, v80, v80
	v_add_f32_e32 v67, v67, v68
	v_add_f32_e32 v66, v66, v67
	v_mul_f32_e32 v67, v71, v71
	v_mul_f32_e32 v68, v73, v73
	v_fmac_f32_e32 v67, v70, v70
	v_fmac_f32_e32 v68, v72, v72
	v_add_f32_e32 v67, v67, v68
	v_add_f32_e32 v66, v66, v67
	v_mov_b32_e32 v67, v66
	s_nop 1
	v_permlane16_swap_b32_e32 v66, v67
	v_add_f32_e32 v82, v66, v67
	v_mov_b32_e32 v83, v82
	s_nop 1
	v_permlane32_swap_b32_e32 v82, v83
	v_mov_b32_e32 v89, 1.0
	v_mov_b32_e32 v96, 1.0
	v_mov_b32_e32 v97, 1.0
	v_mov_b32_e32 v86, 1.0
	v_mov_b32_e32 v87, 1.0
	v_mov_b32_e32 v92, 1.0
	v_mov_b32_e32 v93, 1.0
	s_cbranch_vccnz .LBB0_137
	global_load_dwordx4 v[66:69], v[132:133], off
	global_load_dwordx4 v[84:87], v[132:133], off offset:16
	v_mov_b32_e32 v90, v130
	v_mov_b32_e32 v91, v130
	s_waitcnt vmcnt(0)
	v_pk_mul_f32 v[96:97], v[90:91], v[68:69]
	v_pk_mul_f32 v[88:89], v[130:131], v[66:67]
	v_pk_mul_f32 v[92:93], v[90:91], v[86:87]
	v_pk_mul_f32 v[86:87], v[130:131], v[84:85]

.LBB0_139:
	v_add_f32_e32 v66, v82, v83
	v_fmamk_f32 v66, v66, 0x37800000, v225
	v_mul_f32_e32 v66, 0x3c800000, v66
	v_rsq_f32_e32 v66, v66
	v_mov_b32_e32 v83, v207
	v_mov_b32_e32 v82, 1.0
	s_and_b64 vcc, exec, s[42:43]
	v_cndmask_b32_e64 v66, 1.0, v66, s[44:45]
	v_mul_f32_e32 v66, v154, v66
	v_pk_mul_f32 v[74:75], v[74:75], v[66:67] op_sel_hi:[1,0]
	v_pk_mul_f32 v[68:69], v[76:77], v[66:67] op_sel_hi:[1,0]
	v_pk_mul_f32 v[74:75], v[74:75], v[88:89]
	v_pk_mul_f32 v[76:77], v[176:177], v[66:67] op_sel_hi:[1,0]
	v_pk_mul_f32 v[88:89], v[174:175], v[66:67] op_sel_hi:[1,0]
	v_min_f32_e64 v67, |v74|, s33
	v_bfi_b32 v67, s2, v67, v74
	v_min_f32_e64 v74, |v75|, s33
	v_bfi_b32 v74, s2, v74, v75
	v_pk_mul_f32 v[68:69], v[68:69], v[96:97]
	v_cvt_pk_fp8_f32 v83, v67, v74
	v_min_f32_e64 v75, |v68|, s33
	v_bfi_b32 v67, s2, v75, v68
	v_min_f32_e64 v68, |v69|, s33
	v_pk_mul_f32 v[86:87], v[88:89], v[86:87]
	v_bfi_b32 v68, s2, v68, v69
	v_cvt_pk_fp8_f32 v83, v67, v68 op_sel:[0,0,1]
	v_min_f32_e64 v67, |v86|, s33
	v_min_f32_e64 v68, |v87|, s33
	v_pk_mul_f32 v[76:77], v[76:77], v[92:93]
	v_bfi_b32 v67, s2, v67, v86
	v_bfi_b32 v68, s2, v68, v87
	v_mov_b32_e32 v86, v207
	v_min_f32_e64 v69, |v76|, s33
	v_cvt_pk_fp8_f32 v86, v67, v68
	v_bfi_b32 v67, s2, v69, v76
	v_min_f32_e64 v68, |v77|, s33
	v_pk_mul_f32 v[74:75], v[78:79], v[66:67] op_sel_hi:[1,0]
	v_bfi_b32 v68, s2, v68, v77
	v_pk_mul_f32 v[74:75], v[74:75], v[98:99]
	v_pk_mul_f32 v[72:73], v[72:73], v[66:67] op_sel_hi:[1,0]
	v_cvt_pk_fp8_f32 v86, v67, v68 op_sel:[0,0,1]
	v_pk_mul_f32 v[68:69], v[80:81], v[66:67] op_sel_hi:[1,0]
	v_pk_mul_f32 v[66:67], v[70:71], v[66:67] op_sel_hi:[1,0]
	v_pk_mul_f32 v[70:71], v[72:73], v[90:91]
	v_min_f32_e64 v72, |v74|, s33
	v_bfi_b32 v73, s2, v72, v74
	v_min_f32_e64 v72, |v75|, s33
	v_bfi_b32 v74, s2, v72, v75
	v_mov_b32_e32 v72, v207
	v_cvt_pk_fp8_f32 v72, v73, v74
	v_pk_mul_f32 v[68:69], v[68:69], v[94:95]
	v_pk_mul_f32 v[66:67], v[66:67], v[84:85]
	v_min_f32_e64 v75, |v68|, s33
	v_min_f32_e64 v73, |v69|, s33
	v_bfi_b32 v68, s2, v75, v68
	v_bfi_b32 v69, s2, v73, v69
	v_cvt_pk_fp8_f32 v72, v68, v69 op_sel:[0,0,1]
	v_min_f32_e64 v68, |v66|, s33
	v_bfi_b32 v66, s2, v68, v66
	v_min_f32_e64 v68, |v67|, s33
	v_bfi_b32 v67, s2, v68, v67
	v_mov_b32_e32 v73, v207
	v_cvt_pk_fp8_f32 v73, v66, v67
	v_min_f32_e64 v68, |v70|, s33
	v_min_f32_e64 v67, |v71|, s33
	v_bfi_b32 v66, s2, v68, v70
	v_bfi_b32 v67, s2, v67, v71
	v_cvt_pk_fp8_f32 v73, v66, v67 op_sel:[0,0,1]
	v_mov_b32_e32 v66, v83
	v_mov_b32_e32 v67, v86
	v_mul_f32_e32 v68, v61, v61
	v_mov_b32_dpp v66, v72 row_ror:8 row_mask:0xf bank_mask:0xc
	v_mov_b32_dpp v67, v73 row_ror:8 row_mask:0xf bank_mask:0xc
	v_mov_b32_dpp v72, v83 row_ror:8 row_mask:0xf bank_mask:0x3
	v_mov_b32_dpp v73, v86 row_ror:8 row_mask:0xf bank_mask:0x3
	global_store_dwordx2 v[114:115], v[66:67], off offset:3072 nt
	global_store_dwordx2 v[114:115], v[72:73], off offset:3584 nt
	v_mul_f32_e32 v66, v63, v63
	v_mul_f32_e32 v67, v65, v65
	v_fmac_f32_e32 v66, v62, v62
	v_fmac_f32_e32 v67, v64, v64
	v_add_f32_e32 v66, v66, v67
	v_mul_f32_e32 v67, v59, v59
	v_fmac_f32_e32 v67, v58, v58
	v_fmac_f32_e32 v68, v60, v60
	v_add_f32_e32 v67, v67, v68
	v_add_f32_e32 v66, v66, v67
	v_mul_f32_e32 v67, v55, v55
	v_mul_f32_e32 v68, v57, v57
	v_fmac_f32_e32 v67, v54, v54
	v_fmac_f32_e32 v68, v56, v56
	v_add_f32_e32 v67, v67, v68
	v_add_f32_e32 v66, v66, v67
	v_mul_f32_e32 v67, v51, v51
	v_mul_f32_e32 v68, v53, v53
	v_fmac_f32_e32 v67, v50, v50
	v_fmac_f32_e32 v68, v52, v52
	v_add_f32_e32 v67, v67, v68
	v_add_f32_e32 v66, v66, v67
	v_mov_b32_e32 v67, v66
	s_nop 1
	v_permlane16_swap_b32_e32 v66, v67
	v_add_f32_e32 v66, v66, v67
	v_mov_b32_e32 v67, v66
	s_nop 1
	v_permlane32_swap_b32_e32 v66, v67
	v_mov_b32_e32 v76, 1.0
	v_mov_b32_e32 v77, 1.0
	v_mov_b32_e32 v80, 1.0
	v_mov_b32_e32 v81, 1.0
	v_mov_b32_e32 v74, 1.0
	v_mov_b32_e32 v75, 1.0
	v_mov_b32_e32 v78, 1.0
	v_mov_b32_e32 v79, 1.0
	s_cbranch_vccnz .LBB0_141
	global_load_dwordx4 v[68:71], v[132:133], off
	global_load_dwordx4 v[72:75], v[132:133], off offset:16
	v_mov_b32_e32 v78, v130
	v_mov_b32_e32 v79, v130
	s_waitcnt vmcnt(0)
	v_pk_mul_f32 v[80:81], v[78:79], v[70:71]
	v_pk_mul_f32 v[76:77], v[130:131], v[68:69]
	v_pk_mul_f32 v[78:79], v[78:79], v[74:75]
	v_pk_mul_f32 v[74:75], v[130:131], v[72:73]

.LBB0_143:
	v_add_f32_e32 v66, v66, v67
	v_fmamk_f32 v66, v66, 0x37800000, v225
	v_mul_f32_e32 v66, 0x3c800000, v66
	v_rsq_f32_e32 v67, v66
	s_addk_i32 s0, 0x80
	v_mov_b32_e32 v66, 1.0
	s_and_b64 vcc, exec, s[42:43]
	v_cndmask_b32_e64 v67, 1.0, v67, s[44:45]
	v_mul_f32_e32 v84, v154, v67
	v_pk_mul_f32 v[62:63], v[62:63], v[84:85] op_sel_hi:[1,0]
	v_pk_mul_f32 v[58:59], v[58:59], v[84:85] op_sel_hi:[1,0]
	v_pk_mul_f32 v[62:63], v[62:63], v[76:77]
	v_pk_mul_f32 v[58:59], v[58:59], v[74:75]
	v_min_f32_e64 v67, |v62|, s33
	v_bfi_b32 v62, s2, v67, v62
	v_min_f32_e64 v67, |v63|, s33
	v_bfi_b32 v63, s2, v67, v63
	v_mov_b32_e32 v74, v207
	v_pk_mul_f32 v[64:65], v[64:65], v[84:85] op_sel_hi:[1,0]
	v_cvt_pk_fp8_f32 v74, v62, v63
	v_pk_mul_f32 v[64:65], v[64:65], v[80:81]
	v_pk_mul_f32 v[60:61], v[60:61], v[84:85] op_sel_hi:[1,0]
	v_min_f32_e64 v67, |v64|, s33
	v_min_f32_e64 v63, |v65|, s33
	v_bfi_b32 v62, s2, v67, v64
	v_bfi_b32 v63, s2, v63, v65
	v_cvt_pk_fp8_f32 v74, v62, v63 op_sel:[0,0,1]
	v_min_f32_e64 v62, |v58|, s33
	v_bfi_b32 v58, s2, v62, v58
	v_min_f32_e64 v62, |v59|, s33
	v_pk_mul_f32 v[60:61], v[60:61], v[78:79]
	v_bfi_b32 v59, s2, v62, v59
	v_mov_b32_e32 v63, v207
	v_pk_mul_f32 v[54:55], v[54:55], v[84:85] op_sel_hi:[1,0]
	v_cvt_pk_fp8_f32 v63, v58, v59
	v_min_f32_e64 v59, |v61|, s33
	v_pk_mul_f32 v[54:55], v[54:55], v[82:83]
	v_bfi_b32 v59, s2, v59, v61
	v_min_f32_e64 v61, |v54|, s33
	v_bfi_b32 v61, s2, v61, v54
	v_min_f32_e64 v54, |v55|, s33
	v_pk_mul_f32 v[56:57], v[56:57], v[84:85] op_sel_hi:[1,0]
	v_bfi_b32 v55, s2, v54, v55
	v_mov_b32_e32 v54, v207
	v_min_f32_e64 v62, |v60|, s33
	v_pk_mul_f32 v[56:57], v[56:57], v[72:73]
	v_cvt_pk_fp8_f32 v54, v61, v55
	v_bfi_b32 v58, s2, v62, v60
	v_min_f32_e64 v62, |v56|, s33
	v_pk_mul_f32 v[50:51], v[50:51], v[84:85] op_sel_hi:[1,0]
	v_bfi_b32 v55, s2, v62, v56
	v_min_f32_e64 v56, |v57|, s33
	v_pk_mul_f32 v[50:51], v[50:51], v[68:69]
	v_bfi_b32 v56, s2, v56, v57
	v_cvt_pk_fp8_f32 v54, v55, v56 op_sel:[0,0,1]
	v_min_f32_e64 v55, |v50|, s33
	v_bfi_b32 v50, s2, v55, v50
	v_min_f32_e64 v55, |v51|, s33
	v_bfi_b32 v51, s2, v55, v51
	v_mov_b32_e32 v55, v207
	v_pk_mul_f32 v[52:53], v[52:53], v[84:85] op_sel_hi:[1,0]
	v_cvt_pk_fp8_f32 v55, v50, v51
	v_pk_mul_f32 v[52:53], v[52:53], v[70:71]
	v_cvt_pk_fp8_f32 v63, v58, v59 op_sel:[0,0,1]
	v_min_f32_e64 v56, |v52|, s33
	v_min_f32_e64 v51, |v53|, s33
	v_bfi_b32 v50, s2, v56, v52
	v_bfi_b32 v51, s2, v51, v53
	v_or_b32_e32 v60, s0, v146
	s_ashr_i32 s0, s0, 12
	v_cvt_pk_fp8_f32 v55, v50, v51 op_sel:[0,0,1]
	s_ashr_i32 s1, s0, 31
	s_lshl_b64 s[0:1], s[0:1], 21
	v_lshlrev_b32_e32 v50, 6, v60
	v_lshl_add_u64 v[58:59], v[122:123], 0, s[0:1]
	v_mov_b32_e32 v52, v74
	v_mov_b32_e32 v53, v63
	v_and_b32_e32 v206, 0x3f1c0, v50
	v_mov_b32_dpp v52, v54 row_ror:8 row_mask:0xf bank_mask:0xc
	v_mov_b32_dpp v53, v55 row_ror:8 row_mask:0xf bank_mask:0xc
	v_lshl_add_u64 v[50:51], v[58:59], 0, v[206:207]
	v_mov_b32_dpp v54, v74 row_ror:8 row_mask:0xf bank_mask:0x3
	v_mov_b32_dpp v55, v63 row_ror:8 row_mask:0xf bank_mask:0x3
	global_store_dwordx2 v[50:51], v[52:53], off nt
	global_store_dwordx2 v[50:51], v[54:55], off offset:512 nt
	v_mul_f32_e32 v52, v47, v47
	v_mul_f32_e32 v53, v49, v49
	v_fmac_f32_e32 v52, v46, v46
	v_fmac_f32_e32 v53, v48, v48
	v_add_f32_e32 v52, v52, v53
	v_mul_f32_e32 v53, v43, v43
	v_mul_f32_e32 v54, v45, v45
	v_fmac_f32_e32 v53, v42, v42
	v_fmac_f32_e32 v54, v44, v44
	v_add_f32_e32 v53, v53, v54
	v_add_f32_e32 v52, v52, v53
	v_mul_f32_e32 v53, v39, v39
	v_mul_f32_e32 v54, v41, v41
	v_fmac_f32_e32 v53, v38, v38
	v_fmac_f32_e32 v54, v40, v40
	v_add_f32_e32 v53, v53, v54
	v_add_f32_e32 v52, v52, v53
	v_mul_f32_e32 v53, v35, v35
	v_mul_f32_e32 v54, v37, v37
	v_fmac_f32_e32 v53, v34, v34
	v_fmac_f32_e32 v54, v36, v36
	v_add_f32_e32 v53, v53, v54
	v_add_f32_e32 v52, v52, v53
	v_mov_b32_e32 v53, v52
	s_nop 1
	v_permlane16_swap_b32_e32 v52, v53
	v_add_f32_e32 v52, v52, v53
	v_mov_b32_e32 v53, v52
	s_nop 1
	v_permlane32_swap_b32_e32 v52, v53
	v_mov_b32_e32 v58, 1.0
	v_mov_b32_e32 v59, 1.0
	v_mov_b32_e32 v68, 1.0
	v_mov_b32_e32 v69, 1.0
	v_mov_b32_e32 v56, 1.0
	v_mov_b32_e32 v57, 1.0
	v_mov_b32_e32 v62, 1.0
	v_mov_b32_e32 v63, 1.0
	s_cbranch_vccnz .LBB0_145
	global_load_dwordx4 v[54:57], v[132:133], off
	global_load_dwordx4 v[60:63], v[132:133], off offset:16
	v_mov_b32_e32 v64, v130
	v_mov_b32_e32 v65, v130
	s_waitcnt vmcnt(0)
	v_pk_mul_f32 v[68:69], v[64:65], v[56:57]
	v_pk_mul_f32 v[58:59], v[130:131], v[54:55]
	v_pk_mul_f32 v[62:63], v[64:65], v[62:63]
	v_pk_mul_f32 v[56:57], v[130:131], v[60:61]

.LBB0_147:
	v_add_f32_e32 v52, v52, v53
	v_fmamk_f32 v52, v52, 0x37800000, v225
	v_mul_f32_e32 v52, 0x3c800000, v52
	v_rsq_f32_e32 v53, v52
	v_mov_b32_e32 v52, 1.0
	s_and_b64 vcc, exec, s[42:43]
	v_cndmask_b32_e64 v53, 1.0, v53, s[44:45]
	v_mul_f32_e32 v70, v154, v53
	v_pk_mul_f32 v[46:47], v[46:47], v[70:71] op_sel_hi:[1,0]
	v_pk_mul_f32 v[42:43], v[42:43], v[70:71] op_sel_hi:[1,0]
	v_pk_mul_f32 v[46:47], v[46:47], v[58:59]
	v_pk_mul_f32 v[42:43], v[42:43], v[56:57]
	v_min_f32_e64 v53, |v46|, s33
	v_bfi_b32 v46, s2, v53, v46
	v_min_f32_e64 v53, |v47|, s33
	v_bfi_b32 v47, s2, v53, v47
	v_mov_b32_e32 v56, v207
	v_pk_mul_f32 v[48:49], v[48:49], v[70:71] op_sel_hi:[1,0]
	v_cvt_pk_fp8_f32 v56, v46, v47
	v_pk_mul_f32 v[48:49], v[48:49], v[68:69]
	v_pk_mul_f32 v[44:45], v[44:45], v[70:71] op_sel_hi:[1,0]
	v_min_f32_e64 v53, |v48|, s33
	v_min_f32_e64 v47, |v49|, s33
	v_bfi_b32 v46, s2, v53, v48
	v_bfi_b32 v47, s2, v47, v49
	v_cvt_pk_fp8_f32 v56, v46, v47 op_sel:[0,0,1]
	v_min_f32_e64 v46, |v42|, s33
	v_bfi_b32 v42, s2, v46, v42
	v_min_f32_e64 v46, |v43|, s33
	v_bfi_b32 v43, s2, v46, v43
	v_mov_b32_e32 v47, v207
	v_cvt_pk_fp8_f32 v47, v42, v43
	v_pk_mul_f32 v[44:45], v[44:45], v[62:63]
	v_pk_mul_f32 v[38:39], v[38:39], v[70:71] op_sel_hi:[1,0]
	v_min_f32_e64 v46, |v44|, s33
	v_min_f32_e64 v43, |v45|, s33
	v_bfi_b32 v42, s2, v46, v44
	v_bfi_b32 v43, s2, v43, v45
	v_pk_mul_f32 v[38:39], v[38:39], v[66:67]
	v_cvt_pk_fp8_f32 v47, v42, v43 op_sel:[0,0,1]
	v_min_f32_e64 v42, |v38|, s33
	v_bfi_b32 v42, s2, v42, v38
	v_min_f32_e64 v38, |v39|, s33
	v_pk_mul_f32 v[40:41], v[40:41], v[70:71] op_sel_hi:[1,0]
	v_bfi_b32 v39, s2, v38, v39
	v_mov_b32_e32 v38, v207
	v_pk_mul_f32 v[40:41], v[40:41], v[64:65]
	v_cvt_pk_fp8_f32 v38, v42, v39
	v_min_f32_e64 v43, |v40|, s33
	v_pk_mul_f32 v[34:35], v[34:35], v[70:71] op_sel_hi:[1,0]
	v_bfi_b32 v39, s2, v43, v40
	v_min_f32_e64 v40, |v41|, s33
	v_pk_mul_f32 v[34:35], v[34:35], v[54:55]
	v_bfi_b32 v40, s2, v40, v41
	v_cvt_pk_fp8_f32 v38, v39, v40 op_sel:[0,0,1]
	v_min_f32_e64 v39, |v34|, s33
	v_bfi_b32 v34, s2, v39, v34
	v_min_f32_e64 v39, |v35|, s33
	v_bfi_b32 v35, s2, v39, v35
	v_mov_b32_e32 v39, v207
	v_pk_mul_f32 v[36:37], v[36:37], v[70:71] op_sel_hi:[1,0]
	v_cvt_pk_fp8_f32 v39, v34, v35
	v_pk_mul_f32 v[36:37], v[36:37], v[60:61]
	v_mov_b32_e32 v46, 1.0
	v_min_f32_e64 v40, |v36|, s33
	v_min_f32_e64 v35, |v37|, s33
	v_bfi_b32 v34, s2, v40, v36
	v_bfi_b32 v35, s2, v35, v37
	v_cvt_pk_fp8_f32 v39, v34, v35 op_sel:[0,0,1]
	v_mov_b32_e32 v34, v56
	v_mov_b32_e32 v35, v47
	v_mul_f32_e32 v36, v29, v29
	v_mov_b32_dpp v34, v38 row_ror:8 row_mask:0xf bank_mask:0xc
	v_mov_b32_dpp v35, v39 row_ror:8 row_mask:0xf bank_mask:0xc
	v_mov_b32_dpp v38, v56 row_ror:8 row_mask:0xf bank_mask:0x3
	v_mov_b32_dpp v39, v47 row_ror:8 row_mask:0xf bank_mask:0x3
	global_store_dwordx2 v[50:51], v[34:35], off offset:1024 nt
	global_store_dwordx2 v[50:51], v[38:39], off offset:1536 nt
	v_mul_f32_e32 v34, v31, v31
	v_mul_f32_e32 v35, v33, v33
	v_fmac_f32_e32 v34, v30, v30
	v_fmac_f32_e32 v35, v32, v32
	v_add_f32_e32 v34, v34, v35
	v_mul_f32_e32 v35, v27, v27
	v_fmac_f32_e32 v35, v26, v26
	v_fmac_f32_e32 v36, v28, v28
	v_add_f32_e32 v35, v35, v36
	v_add_f32_e32 v34, v34, v35
	v_mul_f32_e32 v35, v23, v23
	v_mul_f32_e32 v36, v25, v25
	v_fmac_f32_e32 v35, v22, v22
	v_fmac_f32_e32 v36, v24, v24
	v_add_f32_e32 v35, v35, v36
	v_add_f32_e32 v34, v34, v35
	v_mul_f32_e32 v35, v19, v19
	v_mul_f32_e32 v36, v21, v21
	v_fmac_f32_e32 v35, v18, v18
	v_fmac_f32_e32 v36, v20, v20
	v_add_f32_e32 v35, v35, v36
	v_add_f32_e32 v34, v34, v35
	v_mov_b32_e32 v35, v34
	s_nop 1
	v_permlane16_swap_b32_e32 v34, v35
	v_add_f32_e32 v48, v34, v35
	v_mov_b32_e32 v49, v48
	s_nop 1
	v_permlane32_swap_b32_e32 v48, v49
	v_mov_b32_e32 v38, 1.0
	v_mov_b32_e32 v39, 1.0
	v_mov_b32_e32 v47, 1.0
	v_mov_b32_e32 v36, 1.0
	v_mov_b32_e32 v37, 1.0
	v_mov_b32_e32 v42, 1.0
	v_mov_b32_e32 v43, 1.0
	s_cbranch_vccnz .LBB0_149
	global_load_dwordx4 v[34:37], v[132:133], off
	global_load_dwordx4 v[40:43], v[132:133], off offset:16
	v_mov_b32_e32 v44, v130
	v_mov_b32_e32 v45, v130
	s_waitcnt vmcnt(0)
	v_pk_mul_f32 v[46:47], v[44:45], v[36:37]
	v_pk_mul_f32 v[38:39], v[130:131], v[34:35]
	v_pk_mul_f32 v[42:43], v[44:45], v[42:43]
	v_pk_mul_f32 v[36:37], v[130:131], v[40:41]

.LBB0_151:
	v_add_f32_e32 v48, v48, v49
	v_fmamk_f32 v48, v48, 0x37800000, v225
	v_mul_f32_e32 v48, 0x3c800000, v48
	v_rsq_f32_e32 v49, v48
	v_mov_b32_e32 v48, 1.0
	s_and_b64 vcc, exec, s[42:43]
	v_cndmask_b32_e64 v49, 1.0, v49, s[44:45]
	v_mul_f32_e32 v54, v154, v49
	v_pk_mul_f32 v[30:31], v[30:31], v[54:55] op_sel_hi:[1,0]
	v_pk_mul_f32 v[26:27], v[26:27], v[54:55] op_sel_hi:[1,0]
	v_pk_mul_f32 v[30:31], v[30:31], v[38:39]
	v_pk_mul_f32 v[26:27], v[26:27], v[36:37]
	v_min_f32_e64 v36, |v30|, s33
	v_bfi_b32 v30, s2, v36, v30
	v_min_f32_e64 v36, |v31|, s33
	v_bfi_b32 v31, s2, v36, v31
	v_mov_b32_e32 v37, v207
	v_pk_mul_f32 v[32:33], v[32:33], v[54:55] op_sel_hi:[1,0]
	v_cvt_pk_fp8_f32 v37, v30, v31
	v_pk_mul_f32 v[32:33], v[32:33], v[46:47]
	v_pk_mul_f32 v[28:29], v[28:29], v[54:55] op_sel_hi:[1,0]
	v_min_f32_e64 v36, |v32|, s33
	v_min_f32_e64 v31, |v33|, s33
	v_bfi_b32 v30, s2, v36, v32
	v_bfi_b32 v31, s2, v31, v33
	v_cvt_pk_fp8_f32 v37, v30, v31 op_sel:[0,0,1]
	v_min_f32_e64 v30, |v26|, s33
	v_bfi_b32 v26, s2, v30, v26
	v_min_f32_e64 v30, |v27|, s33
	v_bfi_b32 v27, s2, v30, v27
	v_mov_b32_e32 v31, v207
	v_cvt_pk_fp8_f32 v31, v26, v27
	v_pk_mul_f32 v[28:29], v[28:29], v[42:43]
	v_pk_mul_f32 v[22:23], v[22:23], v[54:55] op_sel_hi:[1,0]
	v_min_f32_e64 v30, |v28|, s33
	v_min_f32_e64 v27, |v29|, s33
	v_bfi_b32 v26, s2, v30, v28
	v_bfi_b32 v27, s2, v27, v29
	v_pk_mul_f32 v[22:23], v[22:23], v[52:53]
	v_cvt_pk_fp8_f32 v31, v26, v27 op_sel:[0,0,1]
	v_min_f32_e64 v26, |v22|, s33
	v_bfi_b32 v26, s2, v26, v22
	v_min_f32_e64 v22, |v23|, s33
	v_pk_mul_f32 v[24:25], v[24:25], v[54:55] op_sel_hi:[1,0]
	v_bfi_b32 v23, s2, v22, v23
	v_mov_b32_e32 v22, v207
	v_pk_mul_f32 v[24:25], v[24:25], v[44:45]
	v_cvt_pk_fp8_f32 v22, v26, v23
	v_min_f32_e64 v27, |v24|, s33
	v_pk_mul_f32 v[18:19], v[18:19], v[54:55] op_sel_hi:[1,0]
	v_bfi_b32 v23, s2, v27, v24
	v_min_f32_e64 v24, |v25|, s33
	v_pk_mul_f32 v[18:19], v[18:19], v[34:35]
	v_bfi_b32 v24, s2, v24, v25
	v_cvt_pk_fp8_f32 v22, v23, v24 op_sel:[0,0,1]
	v_min_f32_e64 v23, |v18|, s33
	v_bfi_b32 v18, s2, v23, v18
	v_min_f32_e64 v23, |v19|, s33
	v_bfi_b32 v19, s2, v23, v19
	v_mov_b32_e32 v23, v207
	v_pk_mul_f32 v[20:21], v[20:21], v[54:55] op_sel_hi:[1,0]
	v_cvt_pk_fp8_f32 v23, v18, v19
	v_pk_mul_f32 v[20:21], v[20:21], v[40:41]
	v_mov_b32_e32 v30, 1.0
	v_min_f32_e64 v24, |v20|, s33
	v_min_f32_e64 v19, |v21|, s33
	v_bfi_b32 v18, s2, v24, v20
	v_bfi_b32 v19, s2, v19, v21
	v_cvt_pk_fp8_f32 v23, v18, v19 op_sel:[0,0,1]
	v_mov_b32_e32 v18, v37
	v_mov_b32_e32 v19, v31
	v_mul_f32_e32 v20, v17, v17
	v_mov_b32_dpp v18, v22 row_ror:8 row_mask:0xf bank_mask:0xc
	v_mov_b32_dpp v19, v23 row_ror:8 row_mask:0xf bank_mask:0xc
	v_mov_b32_dpp v22, v37 row_ror:8 row_mask:0xf bank_mask:0x3
	v_mov_b32_dpp v23, v31 row_ror:8 row_mask:0xf bank_mask:0x3
	global_store_dwordx2 v[50:51], v[18:19], off offset:2048 nt
	global_store_dwordx2 v[50:51], v[22:23], off offset:2560 nt
	v_mul_f32_e32 v18, v3, v3
	v_mul_f32_e32 v19, v5, v5
	v_fmac_f32_e32 v18, v2, v2
	v_fmac_f32_e32 v19, v4, v4
	v_add_f32_e32 v18, v18, v19
	v_mul_f32_e32 v19, v15, v15
	v_fmac_f32_e32 v19, v14, v14
	v_fmac_f32_e32 v20, v16, v16
	v_add_f32_e32 v19, v19, v20
	v_add_f32_e32 v18, v18, v19
	v_mul_f32_e32 v19, v11, v11
	v_mul_f32_e32 v20, v13, v13
	v_fmac_f32_e32 v19, v10, v10
	v_fmac_f32_e32 v20, v12, v12
	v_add_f32_e32 v19, v19, v20
	v_add_f32_e32 v18, v18, v19
	v_mul_f32_e32 v19, v7, v7
	v_mul_f32_e32 v20, v9, v9
	v_fmac_f32_e32 v19, v6, v6
	v_fmac_f32_e32 v20, v8, v8
	v_add_f32_e32 v19, v19, v20
	v_add_f32_e32 v18, v18, v19
	v_mov_b32_e32 v19, v18
	s_nop 1
	v_permlane16_swap_b32_e32 v18, v19
	v_add_f32_e32 v34, v18, v19
	v_mov_b32_e32 v35, v34
	s_nop 1
	v_permlane32_swap_b32_e32 v34, v35
	v_mov_b32_e32 v20, 1.0
	v_mov_b32_e32 v21, 1.0
	v_mov_b32_e32 v18, 1.0
	v_mov_b32_e32 v19, 1.0
	v_mov_b32_e32 v31, 1.0
	v_mov_b32_e32 v26, 1.0
	v_mov_b32_e32 v27, 1.0
	s_cbranch_vccnz .LBB0_153
	global_load_dwordx4 v[20:23], v[132:133], off
	global_load_dwordx4 v[24:27], v[132:133], off offset:16
	v_mov_b32_e32 v28, v130
	v_mov_b32_e32 v29, v130
	s_waitcnt vmcnt(0)
	v_pk_mul_f32 v[18:19], v[28:29], v[22:23]
	v_pk_mul_f32 v[20:21], v[130:131], v[20:21]
	v_pk_mul_f32 v[26:27], v[28:29], v[26:27]
	v_pk_mul_f32 v[30:31], v[130:131], v[24:25]

.LBB0_155:
	v_mul_f32_e32 v34, v154, v48
	v_pk_mul_f32 v[14:15], v[14:15], v[34:35] op_sel_hi:[1,0]
	v_pk_mul_f32 v[16:17], v[16:17], v[34:35] op_sel_hi:[1,0]
	v_pk_mul_f32 v[14:15], v[30:31], v[14:15]
	v_pk_mul_f32 v[16:17], v[26:27], v[16:17]
	v_min_f32_e64 v27, |v14|, s33
	v_bfi_b32 v14, s2, v27, v14
	v_min_f32_e64 v27, |v15|, s33
	v_bfi_b32 v15, s2, v27, v15
	v_mov_b32_e32 v27, v207
	v_cvt_pk_fp8_f32 v27, v14, v15
	v_min_f32_e64 v26, |v16|, s33
	v_min_f32_e64 v15, |v17|, s33
	v_pk_mul_f32 v[2:3], v[2:3], v[34:35] op_sel_hi:[1,0]
	v_bfi_b32 v14, s2, v26, v16
	v_bfi_b32 v15, s2, v15, v17
	v_pk_mul_f32 v[2:3], v[20:21], v[2:3]
	v_cvt_pk_fp8_f32 v27, v14, v15 op_sel:[0,0,1]
	v_min_f32_e64 v15, |v2|, s33
	v_pk_mul_f32 v[4:5], v[4:5], v[34:35] op_sel_hi:[1,0]
	v_bfi_b32 v2, s2, v15, v2
	v_min_f32_e64 v15, |v3|, s33
	v_pk_mul_f32 v[4:5], v[18:19], v[4:5]
	v_bfi_b32 v3, s2, v15, v3
	v_mov_b32_e32 v15, v207
	v_min_f32_e64 v14, |v4|, s33
	v_cvt_pk_fp8_f32 v15, v2, v3
	v_min_f32_e64 v3, |v5|, s33
	v_bfi_b32 v2, s2, v14, v4
	v_bfi_b32 v3, s2, v3, v5
	v_pk_mul_f32 v[4:5], v[10:11], v[34:35] op_sel_hi:[1,0]
	v_cvt_pk_fp8_f32 v15, v2, v3 op_sel:[0,0,1]
	v_pk_mul_f32 v[4:5], v[24:25], v[4:5]
	v_pk_mul_f32 v[2:3], v[12:13], v[34:35] op_sel_hi:[1,0]
	v_min_f32_e64 v10, |v4|, s33
	v_bfi_b32 v10, s2, v10, v4
	v_min_f32_e64 v4, |v5|, s33
	v_bfi_b32 v5, s2, v4, v5
	v_mov_b32_e32 v4, v207
	v_cvt_pk_fp8_f32 v4, v10, v5
	v_pk_mul_f32 v[2:3], v[32:33], v[2:3]
	v_pk_mul_f32 v[6:7], v[6:7], v[34:35] op_sel_hi:[1,0]
	v_min_f32_e64 v11, |v2|, s33
	v_min_f32_e64 v5, |v3|, s33
	v_pk_mul_f32 v[6:7], v[22:23], v[6:7]
	v_bfi_b32 v2, s2, v11, v2
	v_bfi_b32 v3, s2, v5, v3
	v_cvt_pk_fp8_f32 v4, v2, v3 op_sel:[0,0,1]
	v_min_f32_e64 v2, |v6|, s33
	v_min_f32_e64 v3, |v7|, s33
	v_bfi_b32 v2, s2, v2, v6
	v_bfi_b32 v3, s2, v3, v7
	v_mov_b32_e32 v5, v207
	v_pk_mul_f32 v[8:9], v[8:9], v[34:35] op_sel_hi:[1,0]
	v_cvt_pk_fp8_f32 v5, v2, v3
	v_pk_mul_f32 v[8:9], v[28:29], v[8:9]
	s_andn2_b64 vcc, exec, s[40:41]
	v_min_f32_e64 v6, |v8|, s33
	v_min_f32_e64 v3, |v9|, s33
	v_bfi_b32 v2, s2, v6, v8
	v_bfi_b32 v3, s2, v3, v9
	v_cvt_pk_fp8_f32 v5, v2, v3 op_sel:[0,0,1]
	v_mov_b32_e32 v2, v15
	v_mov_b32_e32 v3, v27
	s_mov_b64 s[0:1], -1
	v_mov_b32_dpp v2, v4 row_ror:8 row_mask:0xf bank_mask:0xc
	v_mov_b32_dpp v3, v5 row_ror:8 row_mask:0xf bank_mask:0xc
	v_mov_b32_dpp v4, v15 row_ror:8 row_mask:0xf bank_mask:0x3
	v_mov_b32_dpp v5, v27 row_ror:8 row_mask:0xf bank_mask:0x3
	global_store_dwordx2 v[50:51], v[2:3], off offset:3072 nt
	global_store_dwordx2 v[50:51], v[4:5], off offset:3584 nt
	s_cbranch_vccnz .LBB0_118
	s_andn2_b64 vcc, exec, s[52:53]
	s_cbranch_vccnz .LBB0_117
	s_barrier
	s_branch .LBB0_117

.LBB0_435:
	s_waitcnt vmcnt(0)
	v_pk_add_f32 v[128:129], v[128:129], v[146:147]
	v_pk_add_f32 v[126:127], v[126:127], v[144:145]
	v_pk_add_f32 v[128:129], v[128:129], 0 op_sel_hi:[1,0]
	v_pk_add_f32 v[126:127], v[126:127], 0 op_sel_hi:[1,0]
	v_pk_add_f32 v[122:123], v[130:131], v[122:123]
	v_cvt_pk_bf16_f32 v130, v126, v127
	v_cvt_pk_bf16_f32 v131, v128, v129
	v_lshl_add_u64 v[126:127], v[142:143], 1, s[52:53]
	s_movk_i32 s0, 0x4000
	v_pk_add_f32 v[124:125], v[132:133], v[124:125]
	global_store_dwordx2 v[126:127], v[130:131], off nt
	v_add_co_u32_e32 v128, vcc, s0, v126
	v_mov_b32_e32 v130, v118
	v_pk_add_f32 v[124:125], v[124:125], 0 op_sel_hi:[1,0]
	v_pk_add_f32 v[122:123], v[122:123], 0 op_sel_hi:[1,0]
	v_addc_co_u32_e32 v129, vcc, 0, v127, vcc
	v_mov_b32_dpp v130, v114 row_ror:8 row_mask:0xf bank_mask:0xc
	v_mov_b32_dpp v114, v118 row_ror:8 row_mask:0xf bank_mask:0x3
	v_mov_b32_e32 v131, v119
	v_mov_b32_e32 v132, v120
	v_mov_b32_e32 v133, v121
	v_cndmask_b32_e64 v118, 0, 1, s[46:47]
	v_cvt_pk_bf16_f32 v122, v122, v123
	v_cvt_pk_bf16_f32 v123, v124, v125
	v_mov_b32_dpp v131, v115 row_ror:8 row_mask:0xf bank_mask:0xc
	v_mov_b32_dpp v115, v119 row_ror:8 row_mask:0xf bank_mask:0x3
	v_mov_b32_dpp v132, v116 row_ror:8 row_mask:0xf bank_mask:0xc
	v_mov_b32_dpp v116, v120 row_ror:8 row_mask:0xf bank_mask:0x3
	v_mov_b32_dpp v133, v117 row_ror:8 row_mask:0xf bank_mask:0xc
	v_cmp_ne_u32_e64 s[42:43], 1, v118
	s_andn2_b64 vcc, exec, s[46:47]
	v_mov_b32_dpp v117, v121 row_ror:8 row_mask:0xf bank_mask:0x3
	global_store_dwordx2 v[128:129], v[122:123], off nt
	s_cbranch_vccnz .LBB0_484
	v_add_co_u32_e32 v118, vcc, 0x4000, v140
	global_load_dwordx2 v[120:121], v[140:141], off offset:64 nt
	s_nop 0
	v_addc_co_u32_e32 v119, vcc, 0, v141, vcc
	global_load_dwordx2 v[124:125], v[118:119], off offset:64 nt
	s_waitcnt vmcnt(1)
	v_lshlrev_b32_e32 v118, 16, v120
	v_and_b32_e32 v119, 0xffff0000, v120
	v_lshlrev_b32_e32 v120, 16, v121
	v_and_b32_e32 v121, 0xffff0000, v121
	s_waitcnt vmcnt(0)
	v_lshlrev_b32_e32 v122, 16, v124
	v_and_b32_e32 v123, 0xffff0000, v124
	v_lshlrev_b32_e32 v124, 16, v125
	v_and_b32_e32 v125, 0xffff0000, v125
	s_cbranch_execnz .LBB0_438

.LBB0_438:
	s_waitcnt vmcnt(1)
	v_pk_add_f32 v[120:121], v[120:121], v[132:133]
	v_pk_add_f32 v[118:119], v[118:119], v[130:131]
	s_waitcnt vmcnt(0)
	v_pk_add_f32 v[114:115], v[122:123], v[114:115]
	v_pk_add_f32 v[120:121], v[120:121], 0 op_sel_hi:[1,0]
	v_pk_add_f32 v[118:119], v[118:119], 0 op_sel_hi:[1,0]
	v_pk_add_f32 v[116:117], v[124:125], v[116:117]
	v_pk_add_f32 v[114:115], v[114:115], 0 op_sel_hi:[1,0]
	v_pk_add_f32 v[116:117], v[116:117], 0 op_sel_hi:[1,0]
	v_cvt_pk_bf16_f32 v118, v118, v119
	v_cvt_pk_bf16_f32 v119, v120, v121
	v_cvt_pk_bf16_f32 v114, v114, v115
	v_cvt_pk_bf16_f32 v115, v116, v117
	global_store_dwordx2 v[126:127], v[118:119], off offset:64 nt
	global_store_dwordx2 v[128:129], v[114:115], off offset:64 nt
	v_or_b32_e32 v114, 16, v136
	v_ashrrev_i32_e32 v115, 31, v114
	v_lshlrev_b64 v[114:115], 10, v[114:115]
	v_lshl_add_u64 v[122:123], v[114:115], 0, v[134:135]
	v_mov_b32_e32 v124, v110
	v_mov_b32_e32 v125, v111
	v_mov_b32_e32 v126, v112
	v_mov_b32_e32 v127, v113
	v_mov_b32_dpp v124, v106 row_ror:8 row_mask:0xf bank_mask:0xc
	v_mov_b32_dpp v106, v110 row_ror:8 row_mask:0xf bank_mask:0x3
	v_mov_b32_dpp v125, v107 row_ror:8 row_mask:0xf bank_mask:0xc
	v_mov_b32_dpp v107, v111 row_ror:8 row_mask:0xf bank_mask:0x3
	v_mov_b32_dpp v126, v108 row_ror:8 row_mask:0xf bank_mask:0xc
	v_mov_b32_dpp v108, v112 row_ror:8 row_mask:0xf bank_mask:0x3
	v_mov_b32_dpp v127, v109 row_ror:8 row_mask:0xf bank_mask:0xc
	v_mov_b32_dpp v109, v113 row_ror:8 row_mask:0xf bank_mask:0x3
	s_and_b64 vcc, exec, s[42:43]
	v_lshl_add_u64 v[120:121], v[122:123], 1, s[48:49]
	s_cbranch_vccnz .LBB0_485
	v_add_co_u32_e32 v110, vcc, 0x4000, v120
	global_load_dwordx2 v[112:113], v[120:121], off nt
	s_nop 0
	v_addc_co_u32_e32 v111, vcc, 0, v121, vcc
	global_load_dwordx2 v[116:117], v[110:111], off nt
	s_waitcnt vmcnt(1)
	v_lshlrev_b32_e32 v110, 16, v112
	v_and_b32_e32 v111, 0xffff0000, v112
	v_lshlrev_b32_e32 v112, 16, v113
	v_and_b32_e32 v113, 0xffff0000, v113
	s_waitcnt vmcnt(0)
	v_lshlrev_b32_e32 v114, 16, v116
	v_and_b32_e32 v115, 0xffff0000, v116
	v_lshlrev_b32_e32 v116, 16, v117
	v_and_b32_e32 v117, 0xffff0000, v117
	v_lshl_add_u64 v[118:119], v[122:123], 2, s[48:49]
	s_cbranch_execnz .LBB0_441

.LBB0_441:
	s_waitcnt vmcnt(1)
	v_pk_add_f32 v[110:111], v[110:111], v[124:125]
	v_pk_add_f32 v[112:113], v[112:113], v[126:127]
	v_pk_add_f32 v[110:111], v[110:111], 0 op_sel_hi:[1,0]
	v_pk_add_f32 v[112:113], v[112:113], 0 op_sel_hi:[1,0]
	s_waitcnt vmcnt(0)
	v_pk_add_f32 v[106:107], v[114:115], v[106:107]
	v_cvt_pk_bf16_f32 v114, v110, v111
	v_lshl_add_u64 v[110:111], v[122:123], 1, s[52:53]
	s_movk_i32 s0, 0x4000
	v_pk_add_f32 v[108:109], v[116:117], v[108:109]
	v_cvt_pk_bf16_f32 v115, v112, v113
	v_add_co_u32_e32 v112, vcc, s0, v110
	v_pk_add_f32 v[108:109], v[108:109], 0 op_sel_hi:[1,0]
	v_pk_add_f32 v[106:107], v[106:107], 0 op_sel_hi:[1,0]
	global_store_dwordx2 v[110:111], v[114:115], off nt
	v_addc_co_u32_e32 v113, vcc, 0, v111, vcc
	v_mov_b32_e32 v114, v102
	v_mov_b32_e32 v115, v103
	v_mov_b32_e32 v116, v104
	v_mov_b32_e32 v117, v105
	v_cvt_pk_bf16_f32 v106, v106, v107
	v_cvt_pk_bf16_f32 v107, v108, v109
	v_mov_b32_dpp v114, v98 row_ror:8 row_mask:0xf bank_mask:0xc
	v_mov_b32_dpp v98, v102 row_ror:8 row_mask:0xf bank_mask:0x3
	v_mov_b32_dpp v115, v99 row_ror:8 row_mask:0xf bank_mask:0xc
	v_mov_b32_dpp v99, v103 row_ror:8 row_mask:0xf bank_mask:0x3
	v_mov_b32_dpp v116, v100 row_ror:8 row_mask:0xf bank_mask:0xc
	v_mov_b32_dpp v100, v104 row_ror:8 row_mask:0xf bank_mask:0x3
	v_mov_b32_dpp v117, v101 row_ror:8 row_mask:0xf bank_mask:0xc
	s_and_b64 vcc, exec, s[42:43]
	v_mov_b32_dpp v101, v105 row_ror:8 row_mask:0xf bank_mask:0x3
	global_store_dwordx2 v[112:113], v[106:107], off nt
	s_cbranch_vccnz .LBB0_486
	v_add_co_u32_e32 v102, vcc, 0x4000, v120
	global_load_dwordx2 v[104:105], v[120:121], off offset:64 nt
	s_nop 0
	v_addc_co_u32_e32 v103, vcc, 0, v121, vcc
	global_load_dwordx2 v[108:109], v[102:103], off offset:64 nt
	s_waitcnt vmcnt(1)
	v_lshlrev_b32_e32 v102, 16, v104
	v_and_b32_e32 v103, 0xffff0000, v104
	v_lshlrev_b32_e32 v104, 16, v105
	v_and_b32_e32 v105, 0xffff0000, v105
	s_waitcnt vmcnt(0)
	v_lshlrev_b32_e32 v106, 16, v108
	v_and_b32_e32 v107, 0xffff0000, v108
	v_lshlrev_b32_e32 v108, 16, v109
	v_and_b32_e32 v109, 0xffff0000, v109
	s_cbranch_execnz .LBB0_444

.LBB0_444:
	s_waitcnt vmcnt(1)
	v_pk_add_f32 v[104:105], v[104:105], v[116:117]
	v_pk_add_f32 v[102:103], v[102:103], v[114:115]
	s_waitcnt vmcnt(0)
	v_pk_add_f32 v[98:99], v[106:107], v[98:99]
	v_pk_add_f32 v[104:105], v[104:105], 0 op_sel_hi:[1,0]
	v_pk_add_f32 v[102:103], v[102:103], 0 op_sel_hi:[1,0]
	v_pk_add_f32 v[100:101], v[108:109], v[100:101]
	v_pk_add_f32 v[98:99], v[98:99], 0 op_sel_hi:[1,0]
	v_pk_add_f32 v[100:101], v[100:101], 0 op_sel_hi:[1,0]
	v_cvt_pk_bf16_f32 v102, v102, v103
	v_cvt_pk_bf16_f32 v103, v104, v105
	v_cvt_pk_bf16_f32 v98, v98, v99
	v_cvt_pk_bf16_f32 v99, v100, v101
	global_store_dwordx2 v[110:111], v[102:103], off offset:64 nt
	global_store_dwordx2 v[112:113], v[98:99], off offset:64 nt
	v_or_b32_e32 v98, 32, v136
	v_ashrrev_i32_e32 v99, 31, v98
	v_lshlrev_b64 v[98:99], 10, v[98:99]
	v_lshl_add_u64 v[106:107], v[98:99], 0, v[134:135]
	v_mov_b32_e32 v108, v94
	v_mov_b32_e32 v109, v95
	v_mov_b32_e32 v110, v96
	v_mov_b32_e32 v111, v97
	v_mov_b32_dpp v108, v90 row_ror:8 row_mask:0xf bank_mask:0xc
	v_mov_b32_dpp v90, v94 row_ror:8 row_mask:0xf bank_mask:0x3
	v_mov_b32_dpp v109, v91 row_ror:8 row_mask:0xf bank_mask:0xc
	v_mov_b32_dpp v91, v95 row_ror:8 row_mask:0xf bank_mask:0x3
	v_mov_b32_dpp v110, v92 row_ror:8 row_mask:0xf bank_mask:0xc
	v_mov_b32_dpp v92, v96 row_ror:8 row_mask:0xf bank_mask:0x3
	v_mov_b32_dpp v111, v93 row_ror:8 row_mask:0xf bank_mask:0xc
	v_mov_b32_dpp v93, v97 row_ror:8 row_mask:0xf bank_mask:0x3
	s_and_b64 vcc, exec, s[42:43]
	v_lshl_add_u64 v[104:105], v[106:107], 1, s[48:49]
	s_cbranch_vccnz .LBB0_487
	v_add_co_u32_e32 v94, vcc, 0x4000, v104
	global_load_dwordx2 v[96:97], v[104:105], off nt
	s_nop 0
	v_addc_co_u32_e32 v95, vcc, 0, v105, vcc
	global_load_dwordx2 v[100:101], v[94:95], off nt
	s_waitcnt vmcnt(1)
	v_lshlrev_b32_e32 v94, 16, v96
	v_and_b32_e32 v95, 0xffff0000, v96
	v_lshlrev_b32_e32 v96, 16, v97
	v_and_b32_e32 v97, 0xffff0000, v97
	s_waitcnt vmcnt(0)
	v_lshlrev_b32_e32 v98, 16, v100
	v_and_b32_e32 v99, 0xffff0000, v100
	v_lshlrev_b32_e32 v100, 16, v101
	v_and_b32_e32 v101, 0xffff0000, v101
	v_lshl_add_u64 v[102:103], v[106:107], 2, s[48:49]
	s_cbranch_execnz .LBB0_447

.LBB0_447:
	s_waitcnt vmcnt(1)
	v_pk_add_f32 v[94:95], v[94:95], v[108:109]
	v_pk_add_f32 v[96:97], v[96:97], v[110:111]
	v_pk_add_f32 v[94:95], v[94:95], 0 op_sel_hi:[1,0]
	v_pk_add_f32 v[96:97], v[96:97], 0 op_sel_hi:[1,0]
	s_waitcnt vmcnt(0)
	v_pk_add_f32 v[90:91], v[98:99], v[90:91]
	v_cvt_pk_bf16_f32 v98, v94, v95
	v_lshl_add_u64 v[94:95], v[106:107], 1, s[52:53]
	s_movk_i32 s0, 0x4000
	v_pk_add_f32 v[92:93], v[100:101], v[92:93]
	v_cvt_pk_bf16_f32 v99, v96, v97
	v_add_co_u32_e32 v96, vcc, s0, v94
	v_pk_add_f32 v[92:93], v[92:93], 0 op_sel_hi:[1,0]
	v_pk_add_f32 v[90:91], v[90:91], 0 op_sel_hi:[1,0]
	global_store_dwordx2 v[94:95], v[98:99], off nt
	v_addc_co_u32_e32 v97, vcc, 0, v95, vcc
	v_mov_b32_e32 v98, v86
	v_mov_b32_e32 v99, v87
	v_mov_b32_e32 v100, v88
	v_mov_b32_e32 v101, v89
	v_cvt_pk_bf16_f32 v90, v90, v91
	v_cvt_pk_bf16_f32 v91, v92, v93
	v_mov_b32_dpp v98, v82 row_ror:8 row_mask:0xf bank_mask:0xc
	v_mov_b32_dpp v82, v86 row_ror:8 row_mask:0xf bank_mask:0x3
	v_mov_b32_dpp v99, v83 row_ror:8 row_mask:0xf bank_mask:0xc
	v_mov_b32_dpp v83, v87 row_ror:8 row_mask:0xf bank_mask:0x3
	v_mov_b32_dpp v100, v84 row_ror:8 row_mask:0xf bank_mask:0xc
	v_mov_b32_dpp v84, v88 row_ror:8 row_mask:0xf bank_mask:0x3
	v_mov_b32_dpp v101, v85 row_ror:8 row_mask:0xf bank_mask:0xc
	s_and_b64 vcc, exec, s[42:43]
	v_mov_b32_dpp v85, v89 row_ror:8 row_mask:0xf bank_mask:0x3
	global_store_dwordx2 v[96:97], v[90:91], off nt
	s_cbranch_vccnz .LBB0_488
	v_add_co_u32_e32 v86, vcc, 0x4000, v104
	global_load_dwordx2 v[88:89], v[104:105], off offset:64 nt
	s_nop 0
	v_addc_co_u32_e32 v87, vcc, 0, v105, vcc
	global_load_dwordx2 v[92:93], v[86:87], off offset:64 nt
	s_waitcnt vmcnt(1)
	v_lshlrev_b32_e32 v86, 16, v88
	v_and_b32_e32 v87, 0xffff0000, v88
	v_lshlrev_b32_e32 v88, 16, v89
	v_and_b32_e32 v89, 0xffff0000, v89
	s_waitcnt vmcnt(0)
	v_lshlrev_b32_e32 v90, 16, v92
	v_and_b32_e32 v91, 0xffff0000, v92
	v_lshlrev_b32_e32 v92, 16, v93
	v_and_b32_e32 v93, 0xffff0000, v93
	s_cbranch_execnz .LBB0_450

.LBB0_450:
	s_waitcnt vmcnt(1)
	v_pk_add_f32 v[88:89], v[88:89], v[100:101]
	v_pk_add_f32 v[86:87], v[86:87], v[98:99]
	s_waitcnt vmcnt(0)
	v_pk_add_f32 v[82:83], v[90:91], v[82:83]
	v_pk_add_f32 v[88:89], v[88:89], 0 op_sel_hi:[1,0]
	v_pk_add_f32 v[86:87], v[86:87], 0 op_sel_hi:[1,0]
	v_pk_add_f32 v[84:85], v[92:93], v[84:85]
	v_pk_add_f32 v[82:83], v[82:83], 0 op_sel_hi:[1,0]
	v_pk_add_f32 v[84:85], v[84:85], 0 op_sel_hi:[1,0]
	v_cvt_pk_bf16_f32 v86, v86, v87
	v_cvt_pk_bf16_f32 v87, v88, v89
	v_cvt_pk_bf16_f32 v82, v82, v83
	v_cvt_pk_bf16_f32 v83, v84, v85
	global_store_dwordx2 v[94:95], v[86:87], off offset:64 nt
	global_store_dwordx2 v[96:97], v[82:83], off offset:64 nt
	v_or_b32_e32 v82, 48, v136
	v_ashrrev_i32_e32 v83, 31, v82
	v_lshlrev_b64 v[82:83], 10, v[82:83]
	v_lshl_add_u64 v[90:91], v[82:83], 0, v[134:135]
	v_mov_b32_e32 v92, v78
	v_mov_b32_e32 v93, v79
	v_mov_b32_e32 v94, v80
	v_mov_b32_e32 v95, v81
	v_mov_b32_dpp v92, v74 row_ror:8 row_mask:0xf bank_mask:0xc
	v_mov_b32_dpp v74, v78 row_ror:8 row_mask:0xf bank_mask:0x3
	v_mov_b32_dpp v93, v75 row_ror:8 row_mask:0xf bank_mask:0xc
	v_mov_b32_dpp v75, v79 row_ror:8 row_mask:0xf bank_mask:0x3
	v_mov_b32_dpp v94, v76 row_ror:8 row_mask:0xf bank_mask:0xc
	v_mov_b32_dpp v76, v80 row_ror:8 row_mask:0xf bank_mask:0x3
	v_mov_b32_dpp v95, v77 row_ror:8 row_mask:0xf bank_mask:0xc
	v_mov_b32_dpp v77, v81 row_ror:8 row_mask:0xf bank_mask:0x3
	s_and_b64 vcc, exec, s[42:43]
	v_lshl_add_u64 v[88:89], v[90:91], 1, s[48:49]
	s_cbranch_vccnz .LBB0_489
	v_add_co_u32_e32 v78, vcc, 0x4000, v88
	global_load_dwordx2 v[80:81], v[88:89], off nt
	s_nop 0
	v_addc_co_u32_e32 v79, vcc, 0, v89, vcc
	global_load_dwordx2 v[84:85], v[78:79], off nt
	s_waitcnt vmcnt(1)
	v_lshlrev_b32_e32 v78, 16, v80
	v_and_b32_e32 v79, 0xffff0000, v80
	v_lshlrev_b32_e32 v80, 16, v81
	v_and_b32_e32 v81, 0xffff0000, v81
	s_waitcnt vmcnt(0)
	v_lshlrev_b32_e32 v82, 16, v84
	v_and_b32_e32 v83, 0xffff0000, v84
	v_lshlrev_b32_e32 v84, 16, v85
	v_and_b32_e32 v85, 0xffff0000, v85
	v_lshl_add_u64 v[86:87], v[90:91], 2, s[48:49]
	s_cbranch_execnz .LBB0_453

.LBB0_453:
	s_waitcnt vmcnt(1)
	v_pk_add_f32 v[78:79], v[78:79], v[92:93]
	v_pk_add_f32 v[80:81], v[80:81], v[94:95]
	v_pk_add_f32 v[78:79], v[78:79], 0 op_sel_hi:[1,0]
	v_pk_add_f32 v[80:81], v[80:81], 0 op_sel_hi:[1,0]
	s_waitcnt vmcnt(0)
	v_pk_add_f32 v[74:75], v[82:83], v[74:75]
	v_cvt_pk_bf16_f32 v82, v78, v79
	v_lshl_add_u64 v[78:79], v[90:91], 1, s[52:53]
	s_movk_i32 s0, 0x4000
	v_pk_add_f32 v[76:77], v[84:85], v[76:77]
	v_cvt_pk_bf16_f32 v83, v80, v81
	v_add_co_u32_e32 v80, vcc, s0, v78
	v_pk_add_f32 v[76:77], v[76:77], 0 op_sel_hi:[1,0]
	v_pk_add_f32 v[74:75], v[74:75], 0 op_sel_hi:[1,0]
	global_store_dwordx2 v[78:79], v[82:83], off nt
	v_addc_co_u32_e32 v81, vcc, 0, v79, vcc
	v_mov_b32_e32 v82, v70
	v_mov_b32_e32 v83, v71
	v_mov_b32_e32 v84, v72
	v_mov_b32_e32 v85, v73
	v_cvt_pk_bf16_f32 v74, v74, v75
	v_cvt_pk_bf16_f32 v75, v76, v77
	v_mov_b32_dpp v82, v66 row_ror:8 row_mask:0xf bank_mask:0xc
	v_mov_b32_dpp v66, v70 row_ror:8 row_mask:0xf bank_mask:0x3
	v_mov_b32_dpp v83, v67 row_ror:8 row_mask:0xf bank_mask:0xc
	v_mov_b32_dpp v67, v71 row_ror:8 row_mask:0xf bank_mask:0x3
	v_mov_b32_dpp v84, v68 row_ror:8 row_mask:0xf bank_mask:0xc
	v_mov_b32_dpp v68, v72 row_ror:8 row_mask:0xf bank_mask:0x3
	v_mov_b32_dpp v85, v69 row_ror:8 row_mask:0xf bank_mask:0xc
	s_and_b64 vcc, exec, s[42:43]
	v_mov_b32_dpp v69, v73 row_ror:8 row_mask:0xf bank_mask:0x3
	global_store_dwordx2 v[80:81], v[74:75], off nt
	s_cbranch_vccnz .LBB0_490
	v_add_co_u32_e32 v70, vcc, 0x4000, v88
	global_load_dwordx2 v[72:73], v[88:89], off offset:64 nt
	s_nop 0
	v_addc_co_u32_e32 v71, vcc, 0, v89, vcc
	global_load_dwordx2 v[76:77], v[70:71], off offset:64 nt
	s_waitcnt vmcnt(1)
	v_lshlrev_b32_e32 v70, 16, v72
	v_and_b32_e32 v71, 0xffff0000, v72
	v_lshlrev_b32_e32 v72, 16, v73
	v_and_b32_e32 v73, 0xffff0000, v73
	s_waitcnt vmcnt(0)
	v_lshlrev_b32_e32 v74, 16, v76
	v_and_b32_e32 v75, 0xffff0000, v76
	v_lshlrev_b32_e32 v76, 16, v77
	v_and_b32_e32 v77, 0xffff0000, v77
	s_cbranch_execnz .LBB0_456

.LBB0_456:
	s_waitcnt vmcnt(1)
	v_pk_add_f32 v[72:73], v[72:73], v[84:85]
	v_pk_add_f32 v[70:71], v[70:71], v[82:83]
	s_waitcnt vmcnt(0)
	v_pk_add_f32 v[66:67], v[74:75], v[66:67]
	v_pk_add_f32 v[72:73], v[72:73], 0 op_sel_hi:[1,0]
	v_pk_add_f32 v[70:71], v[70:71], 0 op_sel_hi:[1,0]
	v_pk_add_f32 v[68:69], v[76:77], v[68:69]
	v_pk_add_f32 v[66:67], v[66:67], 0 op_sel_hi:[1,0]
	v_pk_add_f32 v[68:69], v[68:69], 0 op_sel_hi:[1,0]
	v_cvt_pk_bf16_f32 v70, v70, v71
	v_cvt_pk_bf16_f32 v71, v72, v73
	v_cvt_pk_bf16_f32 v66, v66, v67
	v_cvt_pk_bf16_f32 v67, v68, v69
	global_store_dwordx2 v[78:79], v[70:71], off offset:64 nt
	global_store_dwordx2 v[80:81], v[66:67], off offset:64 nt
	v_add_u32_e32 v66, 0x80, v136
	v_ashrrev_i32_e32 v67, 31, v66
	v_lshlrev_b64 v[66:67], 10, v[66:67]
	v_lshl_add_u64 v[74:75], v[66:67], 0, v[134:135]
	v_mov_b32_e32 v76, v62
	v_mov_b32_e32 v77, v63
	v_mov_b32_e32 v78, v64
	v_mov_b32_e32 v79, v65
	v_mov_b32_dpp v76, v58 row_ror:8 row_mask:0xf bank_mask:0xc
	v_mov_b32_dpp v58, v62 row_ror:8 row_mask:0xf bank_mask:0x3
	v_mov_b32_dpp v77, v59 row_ror:8 row_mask:0xf bank_mask:0xc
	v_mov_b32_dpp v59, v63 row_ror:8 row_mask:0xf bank_mask:0x3
	v_mov_b32_dpp v78, v60 row_ror:8 row_mask:0xf bank_mask:0xc
	v_mov_b32_dpp v60, v64 row_ror:8 row_mask:0xf bank_mask:0x3
	v_mov_b32_dpp v79, v61 row_ror:8 row_mask:0xf bank_mask:0xc
	v_mov_b32_dpp v61, v65 row_ror:8 row_mask:0xf bank_mask:0x3
	s_and_b64 vcc, exec, s[42:43]
	v_lshl_add_u64 v[72:73], v[74:75], 1, s[48:49]
	s_cbranch_vccnz .LBB0_491
	v_add_co_u32_e32 v62, vcc, 0x4000, v72
	global_load_dwordx2 v[64:65], v[72:73], off nt
	s_nop 0
	v_addc_co_u32_e32 v63, vcc, 0, v73, vcc
	global_load_dwordx2 v[68:69], v[62:63], off nt
	s_waitcnt vmcnt(1)
	v_lshlrev_b32_e32 v62, 16, v64
	v_and_b32_e32 v63, 0xffff0000, v64
	v_lshlrev_b32_e32 v64, 16, v65
	v_and_b32_e32 v65, 0xffff0000, v65
	s_waitcnt vmcnt(0)
	v_lshlrev_b32_e32 v66, 16, v68
	v_and_b32_e32 v67, 0xffff0000, v68
	v_lshlrev_b32_e32 v68, 16, v69
	v_and_b32_e32 v69, 0xffff0000, v69
	v_lshl_add_u64 v[70:71], v[74:75], 2, s[48:49]
	s_cbranch_execnz .LBB0_459

.LBB0_459:
	s_waitcnt vmcnt(1)
	v_pk_add_f32 v[62:63], v[62:63], v[76:77]
	v_pk_add_f32 v[64:65], v[64:65], v[78:79]
	v_pk_add_f32 v[62:63], v[62:63], 0 op_sel_hi:[1,0]
	v_pk_add_f32 v[64:65], v[64:65], 0 op_sel_hi:[1,0]
	s_waitcnt vmcnt(0)
	v_pk_add_f32 v[58:59], v[66:67], v[58:59]
	v_cvt_pk_bf16_f32 v66, v62, v63
	v_lshl_add_u64 v[62:63], v[74:75], 1, s[52:53]
	s_movk_i32 s0, 0x4000
	v_pk_add_f32 v[60:61], v[68:69], v[60:61]
	v_cvt_pk_bf16_f32 v67, v64, v65
	v_add_co_u32_e32 v64, vcc, s0, v62
	v_pk_add_f32 v[60:61], v[60:61], 0 op_sel_hi:[1,0]
	v_pk_add_f32 v[58:59], v[58:59], 0 op_sel_hi:[1,0]
	global_store_dwordx2 v[62:63], v[66:67], off nt
	v_addc_co_u32_e32 v65, vcc, 0, v63, vcc
	v_mov_b32_e32 v66, v54
	v_mov_b32_e32 v67, v55
	v_mov_b32_e32 v68, v56
	v_mov_b32_e32 v69, v57
	v_cvt_pk_bf16_f32 v58, v58, v59
	v_cvt_pk_bf16_f32 v59, v60, v61
	v_mov_b32_dpp v66, v50 row_ror:8 row_mask:0xf bank_mask:0xc
	v_mov_b32_dpp v50, v54 row_ror:8 row_mask:0xf bank_mask:0x3
	v_mov_b32_dpp v67, v51 row_ror:8 row_mask:0xf bank_mask:0xc
	v_mov_b32_dpp v51, v55 row_ror:8 row_mask:0xf bank_mask:0x3
	v_mov_b32_dpp v68, v52 row_ror:8 row_mask:0xf bank_mask:0xc
	v_mov_b32_dpp v52, v56 row_ror:8 row_mask:0xf bank_mask:0x3
	v_mov_b32_dpp v69, v53 row_ror:8 row_mask:0xf bank_mask:0xc
	s_and_b64 vcc, exec, s[42:43]
	v_mov_b32_dpp v53, v57 row_ror:8 row_mask:0xf bank_mask:0x3
	global_store_dwordx2 v[64:65], v[58:59], off nt
	s_cbranch_vccnz .LBB0_492
	v_add_co_u32_e32 v54, vcc, 0x4000, v72
	global_load_dwordx2 v[56:57], v[72:73], off offset:64 nt
	s_nop 0
	v_addc_co_u32_e32 v55, vcc, 0, v73, vcc
	global_load_dwordx2 v[60:61], v[54:55], off offset:64 nt
	s_waitcnt vmcnt(1)
	v_lshlrev_b32_e32 v54, 16, v56
	v_and_b32_e32 v55, 0xffff0000, v56
	v_lshlrev_b32_e32 v56, 16, v57
	v_and_b32_e32 v57, 0xffff0000, v57
	s_waitcnt vmcnt(0)
	v_lshlrev_b32_e32 v58, 16, v60
	v_and_b32_e32 v59, 0xffff0000, v60
	v_lshlrev_b32_e32 v60, 16, v61
	v_and_b32_e32 v61, 0xffff0000, v61
	s_cbranch_execnz .LBB0_462

.LBB0_462:
	s_waitcnt vmcnt(1)
	v_pk_add_f32 v[56:57], v[56:57], v[68:69]
	v_pk_add_f32 v[54:55], v[54:55], v[66:67]
	s_waitcnt vmcnt(0)
	v_pk_add_f32 v[50:51], v[58:59], v[50:51]
	v_pk_add_f32 v[56:57], v[56:57], 0 op_sel_hi:[1,0]
	v_pk_add_f32 v[54:55], v[54:55], 0 op_sel_hi:[1,0]
	v_pk_add_f32 v[52:53], v[60:61], v[52:53]
	v_pk_add_f32 v[50:51], v[50:51], 0 op_sel_hi:[1,0]
	v_pk_add_f32 v[52:53], v[52:53], 0 op_sel_hi:[1,0]
	v_cvt_pk_bf16_f32 v54, v54, v55
	v_cvt_pk_bf16_f32 v55, v56, v57
	v_cvt_pk_bf16_f32 v50, v50, v51
	v_cvt_pk_bf16_f32 v51, v52, v53
	global_store_dwordx2 v[62:63], v[54:55], off offset:64 nt
	global_store_dwordx2 v[64:65], v[50:51], off offset:64 nt
	v_add_u32_e32 v50, 0x90, v136
	v_ashrrev_i32_e32 v51, 31, v50
	v_lshlrev_b64 v[50:51], 10, v[50:51]
	v_lshl_add_u64 v[58:59], v[50:51], 0, v[134:135]
	v_mov_b32_e32 v60, v46
	v_mov_b32_e32 v61, v47
	v_mov_b32_e32 v62, v48
	v_mov_b32_e32 v63, v49
	v_mov_b32_dpp v60, v42 row_ror:8 row_mask:0xf bank_mask:0xc
	v_mov_b32_dpp v42, v46 row_ror:8 row_mask:0xf bank_mask:0x3
	v_mov_b32_dpp v61, v43 row_ror:8 row_mask:0xf bank_mask:0xc
	v_mov_b32_dpp v43, v47 row_ror:8 row_mask:0xf bank_mask:0x3
	v_mov_b32_dpp v62, v44 row_ror:8 row_mask:0xf bank_mask:0xc
	v_mov_b32_dpp v44, v48 row_ror:8 row_mask:0xf bank_mask:0x3
	v_mov_b32_dpp v63, v45 row_ror:8 row_mask:0xf bank_mask:0xc
	v_mov_b32_dpp v45, v49 row_ror:8 row_mask:0xf bank_mask:0x3
	s_and_b64 vcc, exec, s[42:43]
	v_lshl_add_u64 v[56:57], v[58:59], 1, s[48:49]
	s_cbranch_vccnz .LBB0_493
	v_add_co_u32_e32 v46, vcc, 0x4000, v56
	global_load_dwordx2 v[48:49], v[56:57], off nt
	s_nop 0
	v_addc_co_u32_e32 v47, vcc, 0, v57, vcc
	global_load_dwordx2 v[52:53], v[46:47], off nt
	s_waitcnt vmcnt(1)
	v_lshlrev_b32_e32 v46, 16, v48
	v_and_b32_e32 v47, 0xffff0000, v48
	v_lshlrev_b32_e32 v48, 16, v49
	v_and_b32_e32 v49, 0xffff0000, v49
	s_waitcnt vmcnt(0)
	v_lshlrev_b32_e32 v50, 16, v52
	v_and_b32_e32 v51, 0xffff0000, v52
	v_lshlrev_b32_e32 v52, 16, v53
	v_and_b32_e32 v53, 0xffff0000, v53
	v_lshl_add_u64 v[54:55], v[58:59], 2, s[48:49]
	s_cbranch_execnz .LBB0_465

.LBB0_465:
	s_waitcnt vmcnt(1)
	v_pk_add_f32 v[46:47], v[46:47], v[60:61]
	v_pk_add_f32 v[48:49], v[48:49], v[62:63]
	v_pk_add_f32 v[46:47], v[46:47], 0 op_sel_hi:[1,0]
	v_pk_add_f32 v[48:49], v[48:49], 0 op_sel_hi:[1,0]
	s_waitcnt vmcnt(0)
	v_pk_add_f32 v[42:43], v[50:51], v[42:43]
	v_cvt_pk_bf16_f32 v50, v46, v47
	v_lshl_add_u64 v[46:47], v[58:59], 1, s[52:53]
	s_movk_i32 s0, 0x4000
	v_pk_add_f32 v[44:45], v[52:53], v[44:45]
	v_cvt_pk_bf16_f32 v51, v48, v49
	v_add_co_u32_e32 v48, vcc, s0, v46
	v_pk_add_f32 v[44:45], v[44:45], 0 op_sel_hi:[1,0]
	v_pk_add_f32 v[42:43], v[42:43], 0 op_sel_hi:[1,0]
	global_store_dwordx2 v[46:47], v[50:51], off nt
	v_addc_co_u32_e32 v49, vcc, 0, v47, vcc
	v_mov_b32_e32 v50, v38
	v_mov_b32_e32 v51, v39
	v_mov_b32_e32 v52, v40
	v_mov_b32_e32 v53, v41
	v_cvt_pk_bf16_f32 v42, v42, v43
	v_cvt_pk_bf16_f32 v43, v44, v45
	v_mov_b32_dpp v50, v34 row_ror:8 row_mask:0xf bank_mask:0xc
	v_mov_b32_dpp v34, v38 row_ror:8 row_mask:0xf bank_mask:0x3
	v_mov_b32_dpp v51, v35 row_ror:8 row_mask:0xf bank_mask:0xc
	v_mov_b32_dpp v35, v39 row_ror:8 row_mask:0xf bank_mask:0x3
	v_mov_b32_dpp v52, v36 row_ror:8 row_mask:0xf bank_mask:0xc
	v_mov_b32_dpp v36, v40 row_ror:8 row_mask:0xf bank_mask:0x3
	v_mov_b32_dpp v53, v37 row_ror:8 row_mask:0xf bank_mask:0xc
	s_and_b64 vcc, exec, s[42:43]
	v_mov_b32_dpp v37, v41 row_ror:8 row_mask:0xf bank_mask:0x3
	global_store_dwordx2 v[48:49], v[42:43], off nt
	s_cbranch_vccnz .LBB0_494
	v_add_co_u32_e32 v38, vcc, 0x4000, v56
	global_load_dwordx2 v[40:41], v[56:57], off offset:64 nt
	s_nop 0
	v_addc_co_u32_e32 v39, vcc, 0, v57, vcc
	global_load_dwordx2 v[44:45], v[38:39], off offset:64 nt
	s_waitcnt vmcnt(1)
	v_lshlrev_b32_e32 v38, 16, v40
	v_and_b32_e32 v39, 0xffff0000, v40
	v_lshlrev_b32_e32 v40, 16, v41
	v_and_b32_e32 v41, 0xffff0000, v41
	s_waitcnt vmcnt(0)
	v_lshlrev_b32_e32 v42, 16, v44
	v_and_b32_e32 v43, 0xffff0000, v44
	v_lshlrev_b32_e32 v44, 16, v45
	v_and_b32_e32 v45, 0xffff0000, v45
	s_cbranch_execnz .LBB0_468

.LBB0_468:
	s_waitcnt vmcnt(1)
	v_pk_add_f32 v[40:41], v[40:41], v[52:53]
	v_pk_add_f32 v[38:39], v[38:39], v[50:51]
	s_waitcnt vmcnt(0)
	v_pk_add_f32 v[34:35], v[42:43], v[34:35]
	v_pk_add_f32 v[40:41], v[40:41], 0 op_sel_hi:[1,0]
	v_pk_add_f32 v[38:39], v[38:39], 0 op_sel_hi:[1,0]
	v_pk_add_f32 v[36:37], v[44:45], v[36:37]
	v_pk_add_f32 v[34:35], v[34:35], 0 op_sel_hi:[1,0]
	v_pk_add_f32 v[36:37], v[36:37], 0 op_sel_hi:[1,0]
	v_cvt_pk_bf16_f32 v38, v38, v39
	v_cvt_pk_bf16_f32 v39, v40, v41
	v_cvt_pk_bf16_f32 v34, v34, v35
	v_cvt_pk_bf16_f32 v35, v36, v37
	global_store_dwordx2 v[46:47], v[38:39], off offset:64 nt
	global_store_dwordx2 v[48:49], v[34:35], off offset:64 nt
	v_add_u32_e32 v34, 0xa0, v136
	v_ashrrev_i32_e32 v35, 31, v34
	v_lshlrev_b64 v[34:35], 10, v[34:35]
	v_lshl_add_u64 v[42:43], v[34:35], 0, v[134:135]
	v_mov_b32_e32 v44, v30
	v_mov_b32_e32 v45, v31
	v_mov_b32_e32 v46, v32
	v_mov_b32_e32 v47, v33
	v_mov_b32_dpp v44, v26 row_ror:8 row_mask:0xf bank_mask:0xc
	v_mov_b32_dpp v26, v30 row_ror:8 row_mask:0xf bank_mask:0x3
	v_mov_b32_dpp v45, v27 row_ror:8 row_mask:0xf bank_mask:0xc
	v_mov_b32_dpp v27, v31 row_ror:8 row_mask:0xf bank_mask:0x3
	v_mov_b32_dpp v46, v28 row_ror:8 row_mask:0xf bank_mask:0xc
	v_mov_b32_dpp v28, v32 row_ror:8 row_mask:0xf bank_mask:0x3
	v_mov_b32_dpp v47, v29 row_ror:8 row_mask:0xf bank_mask:0xc
	v_mov_b32_dpp v29, v33 row_ror:8 row_mask:0xf bank_mask:0x3
	s_and_b64 vcc, exec, s[42:43]
	v_lshl_add_u64 v[40:41], v[42:43], 1, s[48:49]
	s_cbranch_vccnz .LBB0_495
	v_add_co_u32_e32 v30, vcc, 0x4000, v40
	global_load_dwordx2 v[32:33], v[40:41], off nt
	s_nop 0
	v_addc_co_u32_e32 v31, vcc, 0, v41, vcc
	global_load_dwordx2 v[36:37], v[30:31], off nt
	s_waitcnt vmcnt(1)
	v_lshlrev_b32_e32 v30, 16, v32
	v_and_b32_e32 v31, 0xffff0000, v32
	v_lshlrev_b32_e32 v32, 16, v33
	v_and_b32_e32 v33, 0xffff0000, v33
	s_waitcnt vmcnt(0)
	v_lshlrev_b32_e32 v34, 16, v36
	v_and_b32_e32 v35, 0xffff0000, v36
	v_lshlrev_b32_e32 v36, 16, v37
	v_and_b32_e32 v37, 0xffff0000, v37
	v_lshl_add_u64 v[38:39], v[42:43], 2, s[48:49]
	s_cbranch_execnz .LBB0_471

.LBB0_471:
	s_waitcnt vmcnt(1)
	v_pk_add_f32 v[30:31], v[30:31], v[44:45]
	v_pk_add_f32 v[32:33], v[32:33], v[46:47]
	v_pk_add_f32 v[30:31], v[30:31], 0 op_sel_hi:[1,0]
	v_pk_add_f32 v[32:33], v[32:33], 0 op_sel_hi:[1,0]
	s_waitcnt vmcnt(0)
	v_pk_add_f32 v[26:27], v[34:35], v[26:27]
	v_cvt_pk_bf16_f32 v34, v30, v31
	v_lshl_add_u64 v[30:31], v[42:43], 1, s[52:53]
	s_movk_i32 s0, 0x4000
	v_pk_add_f32 v[28:29], v[36:37], v[28:29]
	v_cvt_pk_bf16_f32 v35, v32, v33
	v_add_co_u32_e32 v32, vcc, s0, v30
	v_pk_add_f32 v[28:29], v[28:29], 0 op_sel_hi:[1,0]
	v_pk_add_f32 v[26:27], v[26:27], 0 op_sel_hi:[1,0]
	global_store_dwordx2 v[30:31], v[34:35], off nt
	v_addc_co_u32_e32 v33, vcc, 0, v31, vcc
	v_mov_b32_e32 v34, v22
	v_mov_b32_e32 v35, v23
	v_mov_b32_e32 v36, v24
	v_mov_b32_e32 v37, v25
	v_cvt_pk_bf16_f32 v26, v26, v27
	v_cvt_pk_bf16_f32 v27, v28, v29
	v_mov_b32_dpp v34, v18 row_ror:8 row_mask:0xf bank_mask:0xc
	v_mov_b32_dpp v18, v22 row_ror:8 row_mask:0xf bank_mask:0x3
	v_mov_b32_dpp v35, v19 row_ror:8 row_mask:0xf bank_mask:0xc
	v_mov_b32_dpp v19, v23 row_ror:8 row_mask:0xf bank_mask:0x3
	v_mov_b32_dpp v36, v20 row_ror:8 row_mask:0xf bank_mask:0xc
	v_mov_b32_dpp v20, v24 row_ror:8 row_mask:0xf bank_mask:0x3
	v_mov_b32_dpp v37, v21 row_ror:8 row_mask:0xf bank_mask:0xc
	s_and_b64 vcc, exec, s[42:43]
	v_mov_b32_dpp v21, v25 row_ror:8 row_mask:0xf bank_mask:0x3
	global_store_dwordx2 v[32:33], v[26:27], off nt
	s_cbranch_vccnz .LBB0_496
	v_add_co_u32_e32 v22, vcc, 0x4000, v40
	global_load_dwordx2 v[24:25], v[40:41], off offset:64 nt
	s_nop 0
	v_addc_co_u32_e32 v23, vcc, 0, v41, vcc
	global_load_dwordx2 v[28:29], v[22:23], off offset:64 nt
	s_waitcnt vmcnt(1)
	v_lshlrev_b32_e32 v22, 16, v24
	v_and_b32_e32 v23, 0xffff0000, v24
	v_lshlrev_b32_e32 v24, 16, v25
	v_and_b32_e32 v25, 0xffff0000, v25
	s_waitcnt vmcnt(0)
	v_lshlrev_b32_e32 v26, 16, v28
	v_and_b32_e32 v27, 0xffff0000, v28
	v_lshlrev_b32_e32 v28, 16, v29
	v_and_b32_e32 v29, 0xffff0000, v29
	s_cbranch_execnz .LBB0_474

.LBB0_474:
	s_waitcnt vmcnt(1)
	v_pk_add_f32 v[24:25], v[24:25], v[36:37]
	v_pk_add_f32 v[22:23], v[22:23], v[34:35]
	s_waitcnt vmcnt(0)
	v_pk_add_f32 v[18:19], v[26:27], v[18:19]
	v_pk_add_f32 v[24:25], v[24:25], 0 op_sel_hi:[1,0]
	v_pk_add_f32 v[22:23], v[22:23], 0 op_sel_hi:[1,0]
	v_pk_add_f32 v[20:21], v[28:29], v[20:21]
	v_pk_add_f32 v[18:19], v[18:19], 0 op_sel_hi:[1,0]
	v_pk_add_f32 v[20:21], v[20:21], 0 op_sel_hi:[1,0]
	v_cvt_pk_bf16_f32 v22, v22, v23
	v_cvt_pk_bf16_f32 v23, v24, v25
	v_cvt_pk_bf16_f32 v18, v18, v19
	v_cvt_pk_bf16_f32 v19, v20, v21
	global_store_dwordx2 v[30:31], v[22:23], off offset:64 nt
	global_store_dwordx2 v[32:33], v[18:19], off offset:64 nt
	v_add_u32_e32 v18, 0xb0, v136
	v_ashrrev_i32_e32 v19, 31, v18
	v_lshlrev_b64 v[18:19], 10, v[18:19]
	v_lshl_add_u64 v[26:27], v[18:19], 0, v[134:135]
	v_mov_b32_e32 v28, v14
	v_mov_b32_e32 v29, v15
	v_mov_b32_e32 v30, v16
	v_mov_b32_e32 v31, v17
	v_mov_b32_dpp v28, v10 row_ror:8 row_mask:0xf bank_mask:0xc
	v_mov_b32_dpp v10, v14 row_ror:8 row_mask:0xf bank_mask:0x3
	v_mov_b32_dpp v29, v11 row_ror:8 row_mask:0xf bank_mask:0xc
	v_mov_b32_dpp v11, v15 row_ror:8 row_mask:0xf bank_mask:0x3
	v_mov_b32_dpp v30, v12 row_ror:8 row_mask:0xf bank_mask:0xc
	v_mov_b32_dpp v12, v16 row_ror:8 row_mask:0xf bank_mask:0x3
	v_mov_b32_dpp v31, v13 row_ror:8 row_mask:0xf bank_mask:0xc
	v_mov_b32_dpp v13, v17 row_ror:8 row_mask:0xf bank_mask:0x3
	s_and_b64 vcc, exec, s[42:43]
	v_lshl_add_u64 v[24:25], v[26:27], 1, s[48:49]
	s_cbranch_vccnz .LBB0_497
	v_add_co_u32_e32 v14, vcc, 0x4000, v24
	global_load_dwordx2 v[16:17], v[24:25], off nt
	s_nop 0
	v_addc_co_u32_e32 v15, vcc, 0, v25, vcc
	global_load_dwordx2 v[20:21], v[14:15], off nt
	s_waitcnt vmcnt(1)
	v_lshlrev_b32_e32 v14, 16, v16
	v_and_b32_e32 v15, 0xffff0000, v16
	v_lshlrev_b32_e32 v16, 16, v17
	v_and_b32_e32 v17, 0xffff0000, v17
	s_waitcnt vmcnt(0)
	v_lshlrev_b32_e32 v18, 16, v20
	v_and_b32_e32 v19, 0xffff0000, v20
	v_lshlrev_b32_e32 v20, 16, v21
	v_and_b32_e32 v21, 0xffff0000, v21
	v_lshl_add_u64 v[22:23], v[26:27], 2, s[48:49]
	s_cbranch_execnz .LBB0_477

.LBB0_477:
	s_waitcnt vmcnt(1)
	v_pk_add_f32 v[14:15], v[14:15], v[28:29]
	v_pk_add_f32 v[16:17], v[16:17], v[30:31]
	v_pk_add_f32 v[14:15], v[14:15], 0 op_sel_hi:[1,0]
	s_waitcnt vmcnt(0)
	v_pk_add_f32 v[12:13], v[20:21], v[12:13]
	v_pk_add_f32 v[10:11], v[18:19], v[10:11]
	v_pk_add_f32 v[16:17], v[16:17], 0 op_sel_hi:[1,0]
	v_pk_add_f32 v[12:13], v[12:13], 0 op_sel_hi:[1,0]
	v_pk_add_f32 v[10:11], v[10:11], 0 op_sel_hi:[1,0]
	v_cvt_pk_bf16_f32 v18, v14, v15
	v_lshl_add_u64 v[14:15], v[26:27], 1, s[52:53]
	s_movk_i32 s0, 0x4000
	v_cvt_pk_bf16_f32 v19, v16, v17
	v_cvt_pk_bf16_f32 v10, v10, v11
	v_cvt_pk_bf16_f32 v11, v12, v13
	v_add_co_u32_e32 v12, vcc, s0, v14
	global_store_dwordx2 v[14:15], v[18:19], off nt
	s_nop 0
	v_addc_co_u32_e32 v13, vcc, 0, v15, vcc
	v_mov_b32_e32 v16, v6
	v_mov_b32_e32 v17, v7
	v_mov_b32_e32 v18, v8
	v_mov_b32_e32 v19, v9
	v_mov_b32_dpp v16, v2 row_ror:8 row_mask:0xf bank_mask:0xc
	v_mov_b32_dpp v2, v6 row_ror:8 row_mask:0xf bank_mask:0x3
	v_mov_b32_dpp v17, v3 row_ror:8 row_mask:0xf bank_mask:0xc
	v_mov_b32_dpp v3, v7 row_ror:8 row_mask:0xf bank_mask:0x3
	v_mov_b32_dpp v18, v4 row_ror:8 row_mask:0xf bank_mask:0xc
	v_mov_b32_dpp v4, v8 row_ror:8 row_mask:0xf bank_mask:0x3
	v_mov_b32_dpp v19, v5 row_ror:8 row_mask:0xf bank_mask:0xc
	s_and_b64 vcc, exec, s[42:43]
	v_mov_b32_dpp v5, v9 row_ror:8 row_mask:0xf bank_mask:0x3
	global_store_dwordx2 v[12:13], v[10:11], off nt
	s_cbranch_vccnz .LBB0_498
	v_add_co_u32_e32 v6, vcc, 0x4000, v24
	global_load_dwordx2 v[8:9], v[24:25], off offset:64 nt
	s_nop 0
	v_addc_co_u32_e32 v7, vcc, 0, v25, vcc
	global_load_dwordx2 v[12:13], v[6:7], off offset:64 nt
	s_waitcnt vmcnt(1)
	v_lshlrev_b32_e32 v6, 16, v8
	v_and_b32_e32 v7, 0xffff0000, v8
	v_lshlrev_b32_e32 v8, 16, v9
	v_and_b32_e32 v9, 0xffff0000, v9
	s_waitcnt vmcnt(0)
	v_lshlrev_b32_e32 v10, 16, v12
	v_and_b32_e32 v11, 0xffff0000, v12
	v_lshlrev_b32_e32 v12, 16, v13
	v_and_b32_e32 v13, 0xffff0000, v13
	s_cbranch_execnz .LBB0_480

.LBB0_480:
	s_waitcnt vmcnt(0)
	v_pk_add_f32 v[4:5], v[12:13], v[4:5]
	v_pk_add_f32 v[2:3], v[10:11], v[2:3]
	v_pk_add_f32 v[8:9], v[8:9], v[18:19]
	v_pk_add_f32 v[6:7], v[6:7], v[16:17]
	v_pk_add_f32 v[4:5], v[4:5], 0 op_sel_hi:[1,0]
	v_pk_add_f32 v[2:3], v[2:3], 0 op_sel_hi:[1,0]
	v_pk_add_f32 v[8:9], v[8:9], 0 op_sel_hi:[1,0]
	v_pk_add_f32 v[6:7], v[6:7], 0 op_sel_hi:[1,0]
	v_cvt_pk_bf16_f32 v2, v2, v3
	v_cvt_pk_bf16_f32 v3, v4, v5
	v_add_co_u32_e32 v4, vcc, 0x4000, v14
	v_cvt_pk_bf16_f32 v6, v6, v7
	v_cvt_pk_bf16_f32 v7, v8, v9
	v_addc_co_u32_e32 v5, vcc, 0, v15, vcc
	global_store_dwordx2 v[14:15], v[6:7], off offset:64 nt
	global_store_dwordx2 v[4:5], v[2:3], off offset:64 nt
	s_andn2_b64 vcc, exec, s[40:41]
	s_mov_b64 s[0:1], -1
	s_cbranch_vccnz .LBB0_421
	s_andn2_b64 vcc, exec, s[50:51]
	s_cbranch_vccnz .LBB0_420
	s_barrier
	s_branch .LBB0_420

.LBB0_583:
	s_lshl_b32 s0, s67, 8
	s_or_b32 s0, s0, s65
	v_mov_b32_e32 v152, v0
	s_ashr_i32 s1, s0, 31
	s_lshl_b64 s[4:5], s[0:1], 2
	v_lshrrev_b32_e32 v34, 1, v152
	s_add_u32 s4, s36, s4
	v_and_b32_e32 v153, 24, v34
	s_addc_u32 s5, s37, s5
	v_lshlrev_b32_e32 v38, 2, v153
	global_load_dwordx4 v[50:53], v38, s[4:5] offset:16
	global_load_dwordx4 v[54:57], v38, s[4:5]
	global_load_dwordx4 v[34:37], v38, s[4:5] offset:144
	s_nop 0
	global_load_dwordx4 v[38:41], v38, s[4:5] offset:128
	s_lshl_b32 s4, s23, 8
	s_add_i32 s4, s4, s34
	v_and_or_b32 v154, v152, 7, s4
	v_mov_b64_e32 v[146:147], s[48:49]
	v_mad_i64_i32 v[146:147], s[4:5], v154, s3, v[146:147]
	v_lshlrev_b32_e32 v152, 3, v152
	v_lshl_add_u64 v[146:147], s[0:1], 1, v[146:147]
	v_and_b32_e32 v206, 64, v152
	v_lshl_add_u64 v[146:147], v[146:147], 0, v[206:207]
	v_lshlrev_b32_e32 v206, 1, v153
	v_lshl_add_u64 v[146:147], v[146:147], 0, v[206:207]
	s_mov_b32 s0, 0xc000
	s_waitcnt vmcnt(0)
	v_pk_add_f32 v[152:153], v[140:141], v[52:53]
	v_pk_add_f32 v[142:143], v[142:143], v[54:55]
	v_pk_add_f32 v[144:145], v[144:145], v[56:57]
	v_mul_f32_e32 v140, 0x3d372713, v142
	v_mul_f32_e32 v141, 0x3d372713, v143
	v_fma_f32 v140, v142, v140, 1.0
	v_fma_f32 v141, v143, v141, 1.0
	v_mul_f32_e32 v140, v142, v140
	v_mul_f32_e32 v141, v143, v141
	v_mul_f32_e32 v140, 0xc0135761, v140
	v_mul_f32_e32 v141, 0xc0135761, v141
	v_exp_f32_e32 v140, v140
	v_exp_f32_e32 v141, v141
	v_pk_add_f32 v[138:139], v[138:139], v[50:51]
	v_pk_add_f32 v[134:135], v[134:135], v[38:39]
	v_add_f32_e32 v140, 1.0, v140
	v_add_f32_e32 v141, 1.0, v141
	v_rcp_f32_e32 v140, v140
	v_rcp_f32_e32 v141, v141
	v_pk_add_f32 v[136:137], v[136:137], v[40:41]
	v_pk_add_f32 v[130:131], v[130:131], v[34:35]
	v_pk_add_f32 v[132:133], v[132:133], v[36:37]
	v_pk_mul_f32 v[140:141], v[142:143], v[140:141]
	v_pk_add_f32 v[126:127], v[126:127], v[54:55]
	v_cvt_pk_bf16_f32 v140, v140, v141
	v_mul_f32_e32 v141, 0x3d372713, v144
	v_fma_f32 v141, v144, v141, 1.0
	v_mul_f32_e32 v141, v144, v141
	v_mul_f32_e32 v141, 0xc0135761, v141
	v_exp_f32_e32 v141, v141
	v_pk_add_f32 v[128:129], v[128:129], v[56:57]
	v_pk_add_f32 v[122:123], v[122:123], v[50:51]
	v_pk_add_f32 v[124:125], v[124:125], v[52:53]
	v_add_f32_e32 v141, 1.0, v141
	v_rcp_f32_e32 v142, v141
	v_mul_f32_e32 v141, 0x3d372713, v145
	v_fma_f32 v141, v145, v141, 1.0
	v_mul_f32_e32 v141, v145, v141
	v_mul_f32_e32 v141, 0xc0135761, v141
	v_exp_f32_e32 v141, v141
	v_pk_add_f32 v[118:119], v[118:119], v[38:39]
	v_pk_add_f32 v[120:121], v[120:121], v[40:41]
	v_pk_add_f32 v[110:111], v[110:111], v[54:55]
	v_add_f32_e32 v141, 1.0, v141
	v_rcp_f32_e32 v143, v141
	v_pk_add_f32 v[112:113], v[112:113], v[56:57]
	v_pk_add_f32 v[106:107], v[106:107], v[50:51]
	v_pk_add_f32 v[108:109], v[108:109], v[52:53]
	v_pk_mul_f32 v[142:143], v[144:145], v[142:143]
	v_pk_add_f32 v[102:103], v[102:103], v[38:39]
	v_cvt_pk_bf16_f32 v141, v142, v143
	v_mul_f32_e32 v142, 0x3d372713, v138
	v_mul_f32_e32 v143, 0x3d372713, v139
	v_fma_f32 v142, v138, v142, 1.0
	v_fma_f32 v143, v139, v143, 1.0
	v_mul_f32_e32 v142, v138, v142
	v_mul_f32_e32 v143, v139, v143
	v_mul_f32_e32 v142, 0xc0135761, v142
	v_mul_f32_e32 v143, 0xc0135761, v143
	v_exp_f32_e32 v142, v142
	v_exp_f32_e32 v143, v143
	v_pk_add_f32 v[104:105], v[104:105], v[40:41]
	v_pk_add_f32 v[94:95], v[94:95], v[54:55]
	v_add_f32_e32 v142, 1.0, v142
	v_add_f32_e32 v143, 1.0, v143
	v_rcp_f32_e32 v142, v142
	v_rcp_f32_e32 v143, v143
	v_pk_add_f32 v[96:97], v[96:97], v[56:57]
	v_pk_add_f32 v[90:91], v[90:91], v[50:51]
	v_pk_add_f32 v[92:93], v[92:93], v[52:53]
	v_pk_mul_f32 v[138:139], v[138:139], v[142:143]
	v_pk_add_f32 v[86:87], v[86:87], v[38:39]
	v_cvt_pk_bf16_f32 v142, v138, v139
	v_mul_f32_e32 v138, 0x3d372713, v152
	v_mul_f32_e32 v139, 0x3d372713, v153
	v_fma_f32 v138, v152, v138, 1.0
	v_fma_f32 v139, v153, v139, 1.0
	v_mul_f32_e32 v138, v152, v138
	v_mul_f32_e32 v139, v153, v139
	v_mul_f32_e32 v138, 0xc0135761, v138
	v_mul_f32_e32 v139, 0xc0135761, v139
	v_exp_f32_e32 v138, v138
	v_exp_f32_e32 v139, v139
	v_pk_add_f32 v[88:89], v[88:89], v[40:41]
	v_pk_add_f32 v[78:79], v[78:79], v[54:55]
	v_add_f32_e32 v138, 1.0, v138
	v_add_f32_e32 v139, 1.0, v139
	v_rcp_f32_e32 v138, v138
	v_rcp_f32_e32 v139, v139
	v_pk_add_f32 v[80:81], v[80:81], v[56:57]
	v_pk_add_f32 v[74:75], v[74:75], v[50:51]
	v_pk_add_f32 v[76:77], v[76:77], v[52:53]
	v_pk_mul_f32 v[138:139], v[152:153], v[138:139]
	v_pk_add_f32 v[70:71], v[70:71], v[38:39]
	v_cvt_pk_bf16_f32 v143, v138, v139
	v_mul_f32_e32 v138, 0x3d372713, v134
	v_mul_f32_e32 v139, 0x3d372713, v135
	v_fma_f32 v138, v134, v138, 1.0
	v_fma_f32 v139, v135, v139, 1.0
	v_mul_f32_e32 v138, v134, v138
	v_mul_f32_e32 v139, v135, v139
	v_mul_f32_e32 v138, 0xc0135761, v138
	v_mul_f32_e32 v139, 0xc0135761, v139
	v_exp_f32_e32 v138, v138
	v_exp_f32_e32 v139, v139
	v_pk_add_f32 v[72:73], v[72:73], v[40:41]
	v_pk_add_f32 v[62:63], v[62:63], v[54:55]
	v_add_f32_e32 v138, 1.0, v138
	v_add_f32_e32 v139, 1.0, v139
	v_rcp_f32_e32 v138, v138
	v_rcp_f32_e32 v139, v139
	v_pk_add_f32 v[64:65], v[64:65], v[56:57]
	v_pk_add_f32 v[58:59], v[58:59], v[50:51]
	v_pk_add_f32 v[60:61], v[60:61], v[52:53]
	v_pk_mul_f32 v[134:135], v[134:135], v[138:139]
	v_pk_add_f32 v[46:47], v[46:47], v[38:39]
	v_cvt_pk_bf16_f32 v134, v134, v135
	v_mul_f32_e32 v135, 0x3d372713, v136
	v_fma_f32 v135, v136, v135, 1.0
	v_mul_f32_e32 v135, v136, v135
	v_mul_f32_e32 v135, 0xc0135761, v135
	v_exp_f32_e32 v135, v135
	v_pk_add_f32 v[48:49], v[48:49], v[40:41]
	v_pk_add_f32 v[30:31], v[30:31], v[54:55]
	v_pk_add_f32 v[32:33], v[32:33], v[56:57]
	v_add_f32_e32 v135, 1.0, v135
	v_rcp_f32_e32 v138, v135
	v_mul_f32_e32 v135, 0x3d372713, v137
	v_fma_f32 v135, v137, v135, 1.0
	v_mul_f32_e32 v135, v137, v135
	v_mul_f32_e32 v135, 0xc0135761, v135
	v_exp_f32_e32 v135, v135
	v_pk_add_f32 v[26:27], v[26:27], v[50:51]
	v_pk_add_f32 v[28:29], v[28:29], v[52:53]
	v_pk_add_f32 v[22:23], v[22:23], v[38:39]
	v_add_f32_e32 v135, 1.0, v135
	v_rcp_f32_e32 v139, v135
	v_pk_add_f32 v[24:25], v[24:25], v[40:41]
	v_pk_add_f32 v[14:15], v[14:15], v[54:55]
	v_pk_add_f32 v[16:17], v[16:17], v[56:57]
	v_pk_mul_f32 v[136:137], v[136:137], v[138:139]
	v_pk_add_f32 v[10:11], v[10:11], v[50:51]
	v_cvt_pk_bf16_f32 v135, v136, v137
	v_mul_f32_e32 v136, 0x3d372713, v130
	v_mul_f32_e32 v137, 0x3d372713, v131
	v_fma_f32 v136, v130, v136, 1.0
	v_fma_f32 v137, v131, v137, 1.0
	v_mul_f32_e32 v136, v130, v136
	v_mul_f32_e32 v137, v131, v137
	v_mul_f32_e32 v136, 0xc0135761, v136
	v_mul_f32_e32 v137, 0xc0135761, v137
	v_exp_f32_e32 v136, v136
	v_exp_f32_e32 v137, v137
	v_pk_add_f32 v[12:13], v[12:13], v[52:53]
	v_pk_add_f32 v[6:7], v[6:7], v[38:39]
	v_add_f32_e32 v136, 1.0, v136
	v_add_f32_e32 v137, 1.0, v137
	v_rcp_f32_e32 v136, v136
	v_rcp_f32_e32 v137, v137
	v_pk_add_f32 v[8:9], v[8:9], v[40:41]
	v_pk_mul_f32 v[130:131], v[130:131], v[136:137]
	s_nop 0
	v_cvt_pk_bf16_f32 v136, v130, v131
	v_mul_f32_e32 v130, 0x3d372713, v132
	v_mul_f32_e32 v131, 0x3d372713, v133
	v_fma_f32 v130, v132, v130, 1.0
	v_fma_f32 v131, v133, v131, 1.0
	v_mul_f32_e32 v130, v132, v130
	v_mul_f32_e32 v131, v133, v131
	v_mul_f32_e32 v130, 0xc0135761, v130
	v_mul_f32_e32 v131, 0xc0135761, v131
	v_exp_f32_e32 v130, v130
	v_exp_f32_e32 v131, v131
	v_add_f32_e32 v130, 1.0, v130
	v_add_f32_e32 v131, 1.0, v131
	v_rcp_f32_e32 v130, v130
	v_rcp_f32_e32 v131, v131
	s_nop 0
	v_pk_mul_f32 v[130:131], v[132:133], v[130:131]
	s_nop 0
	v_cvt_pk_bf16_f32 v137, v130, v131
	v_mov_b32_e32 v130, v140
	v_mov_b32_e32 v131, v141
	v_mov_b32_e32 v132, v142
	v_mov_b32_e32 v133, v143
	v_mov_b32_dpp v130, v134 row_ror:8 row_mask:0xf bank_mask:0xc
	v_mov_b32_dpp v131, v135 row_ror:8 row_mask:0xf bank_mask:0xc
	v_mov_b32_dpp v132, v136 row_ror:8 row_mask:0xf bank_mask:0xc
	v_mov_b32_dpp v133, v137 row_ror:8 row_mask:0xf bank_mask:0xc
	global_store_dwordx4 v[146:147], v[130:133], off nt
	v_mov_b32_dpp v134, v140 row_ror:8 row_mask:0xf bank_mask:0x3
	v_mov_b32_dpp v135, v141 row_ror:8 row_mask:0xf bank_mask:0x3
	v_add_co_u32_e32 v130, vcc, s0, v146
	v_mov_b32_dpp v136, v142 row_ror:8 row_mask:0xf bank_mask:0x3
	v_mov_b32_dpp v137, v143 row_ror:8 row_mask:0xf bank_mask:0x3
	v_addc_co_u32_e32 v131, vcc, 0, v147, vcc
	global_store_dwordx4 v[130:131], v[134:137], off nt
	v_mul_f32_e32 v130, 0x3d372713, v126
	v_mul_f32_e32 v131, 0x3d372713, v127
	v_fma_f32 v130, v126, v130, 1.0
	v_fma_f32 v131, v127, v131, 1.0
	v_mul_f32_e32 v130, v126, v130
	v_mul_f32_e32 v131, v127, v131
	v_mul_f32_e32 v130, 0xc0135761, v130
	v_mul_f32_e32 v131, 0xc0135761, v131
	v_exp_f32_e32 v130, v130
	v_exp_f32_e32 v131, v131
	s_mov_b32 s0, 0x18000
	v_add_f32_e32 v130, 1.0, v130
	v_add_f32_e32 v131, 1.0, v131
	v_rcp_f32_e32 v130, v130
	v_rcp_f32_e32 v131, v131
	s_nop 0
	v_pk_mul_f32 v[126:127], v[126:127], v[130:131]
	s_nop 0
	v_cvt_pk_bf16_f32 v130, v126, v127
	v_mul_f32_e32 v126, 0x3d372713, v128
	v_mul_f32_e32 v127, 0x3d372713, v129
	v_fma_f32 v126, v128, v126, 1.0
	v_fma_f32 v127, v129, v127, 1.0
	v_mul_f32_e32 v126, v128, v126
	v_mul_f32_e32 v127, v129, v127
	v_mul_f32_e32 v126, 0xc0135761, v126
	v_mul_f32_e32 v127, 0xc0135761, v127
	v_exp_f32_e32 v126, v126
	v_exp_f32_e32 v127, v127
	v_add_f32_e32 v126, 1.0, v126
	v_add_f32_e32 v127, 1.0, v127
	v_rcp_f32_e32 v126, v126
	v_rcp_f32_e32 v127, v127
	s_nop 0
	v_pk_mul_f32 v[126:127], v[128:129], v[126:127]
	s_nop 0
	v_cvt_pk_bf16_f32 v128, v126, v127
	v_mul_f32_e32 v126, 0x3d372713, v122
	v_mul_f32_e32 v127, 0x3d372713, v123
	v_fma_f32 v126, v122, v126, 1.0
	v_fma_f32 v127, v123, v127, 1.0
	v_mul_f32_e32 v126, v122, v126
	v_mul_f32_e32 v127, v123, v127
	v_mul_f32_e32 v126, 0xc0135761, v126
	v_mul_f32_e32 v127, 0xc0135761, v127
	v_exp_f32_e32 v126, v126
	v_exp_f32_e32 v127, v127
	v_add_f32_e32 v126, 1.0, v126
	v_add_f32_e32 v127, 1.0, v127
	v_rcp_f32_e32 v126, v126
	v_rcp_f32_e32 v127, v127
	s_nop 0
	v_pk_mul_f32 v[122:123], v[122:123], v[126:127]
	s_nop 0
	v_cvt_pk_bf16_f32 v126, v122, v123
	v_mul_f32_e32 v122, 0x3d372713, v124
	v_mul_f32_e32 v123, 0x3d372713, v125
	v_fma_f32 v122, v124, v122, 1.0
	v_fma_f32 v123, v125, v123, 1.0
	v_mul_f32_e32 v122, v124, v122
	v_mul_f32_e32 v123, v125, v123
	v_mul_f32_e32 v122, 0xc0135761, v122
	v_mul_f32_e32 v123, 0xc0135761, v123
	v_exp_f32_e32 v122, v122
	v_exp_f32_e32 v123, v123
	v_add_f32_e32 v122, 1.0, v122
	v_add_f32_e32 v123, 1.0, v123
	v_rcp_f32_e32 v122, v122
	v_rcp_f32_e32 v123, v123
	s_nop 0
	v_pk_mul_f32 v[122:123], v[124:125], v[122:123]
	s_nop 0
	v_cvt_pk_bf16_f32 v124, v122, v123
	v_pk_add_f32 v[122:123], v[116:117], v[36:37]
	v_pk_add_f32 v[116:117], v[114:115], v[34:35]
	v_mul_f32_e32 v114, 0x3d372713, v118
	v_mul_f32_e32 v115, 0x3d372713, v119
	v_fma_f32 v114, v118, v114, 1.0
	v_fma_f32 v115, v119, v115, 1.0
	v_mul_f32_e32 v114, v118, v114
	v_mul_f32_e32 v115, v119, v115
	v_mul_f32_e32 v114, 0xc0135761, v114
	v_mul_f32_e32 v115, 0xc0135761, v115
	v_exp_f32_e32 v114, v114
	v_exp_f32_e32 v115, v115
	v_add_f32_e32 v114, 1.0, v114
	v_add_f32_e32 v115, 1.0, v115
	v_rcp_f32_e32 v114, v114
	v_rcp_f32_e32 v115, v115
	s_nop 0
	v_pk_mul_f32 v[114:115], v[118:119], v[114:115]
	s_nop 0
	v_cvt_pk_bf16_f32 v114, v114, v115
	v_mul_f32_e32 v115, 0x3d372713, v120
	v_fma_f32 v115, v120, v115, 1.0
	v_mul_f32_e32 v115, v120, v115
	v_mul_f32_e32 v115, 0xc0135761, v115
	v_exp_f32_e32 v115, v115
	s_nop 0
	v_add_f32_e32 v115, 1.0, v115
	v_rcp_f32_e32 v118, v115
	v_mul_f32_e32 v115, 0x3d372713, v121
	v_fma_f32 v115, v121, v115, 1.0
	v_mul_f32_e32 v115, v121, v115
	v_mul_f32_e32 v115, 0xc0135761, v115
	v_exp_f32_e32 v115, v115
	s_nop 0
	v_add_f32_e32 v115, 1.0, v115
	v_rcp_f32_e32 v119, v115
	s_nop 0
	v_pk_mul_f32 v[118:119], v[120:121], v[118:119]
	s_nop 0
	v_cvt_pk_bf16_f32 v115, v118, v119
	v_mul_f32_e32 v118, 0x3d372713, v116
	v_mul_f32_e32 v119, 0x3d372713, v117
	v_fma_f32 v118, v116, v118, 1.0
	v_fma_f32 v119, v117, v119, 1.0
	v_mul_f32_e32 v118, v116, v118
	v_mul_f32_e32 v119, v117, v119
	v_mul_f32_e32 v118, 0xc0135761, v118
	v_mul_f32_e32 v119, 0xc0135761, v119
	v_exp_f32_e32 v118, v118
	v_exp_f32_e32 v119, v119
	v_mov_b32_e32 v120, v126
	v_mov_b32_e32 v121, v124
	v_add_f32_e32 v118, 1.0, v118
	v_add_f32_e32 v119, 1.0, v119
	v_rcp_f32_e32 v118, v118
	v_rcp_f32_e32 v119, v119
	s_nop 0
	v_pk_mul_f32 v[116:117], v[116:117], v[118:119]
	s_nop 0
	v_cvt_pk_bf16_f32 v116, v116, v117
	v_mul_f32_e32 v117, 0x3d372713, v122
	v_fma_f32 v117, v122, v117, 1.0
	v_mul_f32_e32 v117, v122, v117
	v_mul_f32_e32 v117, 0xc0135761, v117
	v_exp_f32_e32 v117, v117
	v_mov_b32_dpp v120, v116 row_ror:8 row_mask:0xf bank_mask:0xc
	v_mov_b32_dpp v116, v126 row_ror:8 row_mask:0xf bank_mask:0x3
	v_add_f32_e32 v117, 1.0, v117
	v_rcp_f32_e32 v118, v117
	v_mul_f32_e32 v117, 0x3d372713, v123
	v_fma_f32 v117, v123, v117, 1.0
	v_mul_f32_e32 v117, v123, v117
	v_mul_f32_e32 v117, 0xc0135761, v117
	v_exp_f32_e32 v117, v117
	s_nop 0
	v_add_f32_e32 v117, 1.0, v117
	v_rcp_f32_e32 v119, v117
	s_nop 0
	v_pk_mul_f32 v[118:119], v[122:123], v[118:119]
	s_nop 0
	v_cvt_pk_bf16_f32 v117, v118, v119
	v_mov_b32_e32 v118, v130
	v_mov_b32_e32 v119, v128
	v_add_co_u32_e32 v122, vcc, s0, v146
	v_mov_b32_dpp v118, v114 row_ror:8 row_mask:0xf bank_mask:0xc
	v_mov_b32_dpp v119, v115 row_ror:8 row_mask:0xf bank_mask:0xc
	v_mov_b32_dpp v121, v117 row_ror:8 row_mask:0xf bank_mask:0xc
	v_addc_co_u32_e32 v123, vcc, 0, v147, vcc
	s_mov_b32 s0, 0x24000
	global_store_dwordx4 v[122:123], v[118:121], off nt
	v_mov_b32_dpp v114, v130 row_ror:8 row_mask:0xf bank_mask:0x3
	v_mov_b32_dpp v115, v128 row_ror:8 row_mask:0xf bank_mask:0x3
	v_add_co_u32_e32 v118, vcc, s0, v146
	v_mov_b32_dpp v117, v124 row_ror:8 row_mask:0xf bank_mask:0x3
	s_nop 0
	v_addc_co_u32_e32 v119, vcc, 0, v147, vcc
	global_store_dwordx4 v[118:119], v[114:117], off nt
	s_mov_b32 s0, 0x30000
	s_nop 0
	v_mul_f32_e32 v114, 0x3d372713, v110
	v_mul_f32_e32 v115, 0x3d372713, v111
	v_fma_f32 v114, v110, v114, 1.0
	v_fma_f32 v115, v111, v115, 1.0
	v_mul_f32_e32 v114, v110, v114
	v_mul_f32_e32 v115, v111, v115
	v_mul_f32_e32 v114, 0xc0135761, v114
	v_mul_f32_e32 v115, 0xc0135761, v115
	v_exp_f32_e32 v114, v114
	v_exp_f32_e32 v115, v115
	v_add_f32_e32 v114, 1.0, v114
	v_add_f32_e32 v115, 1.0, v115
	v_rcp_f32_e32 v114, v114
	v_rcp_f32_e32 v115, v115
	s_nop 0
	v_pk_mul_f32 v[110:111], v[110:111], v[114:115]
	s_nop 0
	v_cvt_pk_bf16_f32 v114, v110, v111
	v_mul_f32_e32 v110, 0x3d372713, v112
	v_mul_f32_e32 v111, 0x3d372713, v113
	v_fma_f32 v110, v112, v110, 1.0
	v_fma_f32 v111, v113, v111, 1.0
	v_mul_f32_e32 v110, v112, v110
	v_mul_f32_e32 v111, v113, v111
	v_mul_f32_e32 v110, 0xc0135761, v110
	v_mul_f32_e32 v111, 0xc0135761, v111
	v_exp_f32_e32 v110, v110
	v_exp_f32_e32 v111, v111
	v_add_f32_e32 v110, 1.0, v110
	v_add_f32_e32 v111, 1.0, v111
	v_rcp_f32_e32 v110, v110
	v_rcp_f32_e32 v111, v111
	s_nop 0
	v_pk_mul_f32 v[110:111], v[112:113], v[110:111]
	s_nop 0
	v_cvt_pk_bf16_f32 v112, v110, v111
	v_mul_f32_e32 v110, 0x3d372713, v106
	v_mul_f32_e32 v111, 0x3d372713, v107
	v_fma_f32 v110, v106, v110, 1.0
	v_fma_f32 v111, v107, v111, 1.0
	v_mul_f32_e32 v110, v106, v110
	v_mul_f32_e32 v111, v107, v111
	v_mul_f32_e32 v110, 0xc0135761, v110
	v_mul_f32_e32 v111, 0xc0135761, v111
	v_exp_f32_e32 v110, v110
	v_exp_f32_e32 v111, v111
	v_add_f32_e32 v110, 1.0, v110
	v_add_f32_e32 v111, 1.0, v111
	v_rcp_f32_e32 v110, v110
	v_rcp_f32_e32 v111, v111
	s_nop 0
	v_pk_mul_f32 v[106:107], v[106:107], v[110:111]
	s_nop 0
	v_cvt_pk_bf16_f32 v110, v106, v107
	v_mul_f32_e32 v106, 0x3d372713, v108
	v_mul_f32_e32 v107, 0x3d372713, v109
	v_fma_f32 v106, v108, v106, 1.0
	v_fma_f32 v107, v109, v107, 1.0
	v_mul_f32_e32 v106, v108, v106
	v_mul_f32_e32 v107, v109, v107
	v_mul_f32_e32 v106, 0xc0135761, v106
	v_mul_f32_e32 v107, 0xc0135761, v107
	v_exp_f32_e32 v106, v106
	v_exp_f32_e32 v107, v107
	v_add_f32_e32 v106, 1.0, v106
	v_add_f32_e32 v107, 1.0, v107
	v_rcp_f32_e32 v106, v106
	v_rcp_f32_e32 v107, v107
	s_nop 0
	v_pk_mul_f32 v[106:107], v[108:109], v[106:107]
	s_nop 0
	v_cvt_pk_bf16_f32 v108, v106, v107
	v_pk_add_f32 v[106:107], v[100:101], v[36:37]
	v_pk_add_f32 v[100:101], v[98:99], v[34:35]
	v_mul_f32_e32 v98, 0x3d372713, v102
	v_mul_f32_e32 v99, 0x3d372713, v103
	v_fma_f32 v98, v102, v98, 1.0
	v_fma_f32 v99, v103, v99, 1.0
	v_mul_f32_e32 v98, v102, v98
	v_mul_f32_e32 v99, v103, v99
	v_mul_f32_e32 v98, 0xc0135761, v98
	v_mul_f32_e32 v99, 0xc0135761, v99
	v_exp_f32_e32 v98, v98
	v_exp_f32_e32 v99, v99
	v_add_f32_e32 v98, 1.0, v98
	v_add_f32_e32 v99, 1.0, v99
	v_rcp_f32_e32 v98, v98
	v_rcp_f32_e32 v99, v99
	s_nop 0
	v_pk_mul_f32 v[98:99], v[102:103], v[98:99]
	s_nop 0
	v_cvt_pk_bf16_f32 v98, v98, v99
	v_mul_f32_e32 v99, 0x3d372713, v104
	v_fma_f32 v99, v104, v99, 1.0
	v_mul_f32_e32 v99, v104, v99
	v_mul_f32_e32 v99, 0xc0135761, v99
	v_exp_f32_e32 v99, v99
	s_nop 0
	v_add_f32_e32 v99, 1.0, v99
	v_rcp_f32_e32 v102, v99
	v_mul_f32_e32 v99, 0x3d372713, v105
	v_fma_f32 v99, v105, v99, 1.0
	v_mul_f32_e32 v99, v105, v99
	v_mul_f32_e32 v99, 0xc0135761, v99
	v_exp_f32_e32 v99, v99
	s_nop 0
	v_add_f32_e32 v99, 1.0, v99
	v_rcp_f32_e32 v103, v99
	s_nop 0
	v_pk_mul_f32 v[102:103], v[104:105], v[102:103]
	s_nop 0
	v_cvt_pk_bf16_f32 v99, v102, v103
	v_mul_f32_e32 v102, 0x3d372713, v100
	v_mul_f32_e32 v103, 0x3d372713, v101
	v_fma_f32 v102, v100, v102, 1.0
	v_fma_f32 v103, v101, v103, 1.0
	v_mul_f32_e32 v102, v100, v102
	v_mul_f32_e32 v103, v101, v103
	v_mul_f32_e32 v102, 0xc0135761, v102
	v_mul_f32_e32 v103, 0xc0135761, v103
	v_exp_f32_e32 v102, v102
	v_exp_f32_e32 v103, v103
	v_mov_b32_e32 v104, v110
	v_mov_b32_e32 v105, v108
	v_add_f32_e32 v102, 1.0, v102
	v_add_f32_e32 v103, 1.0, v103
	v_rcp_f32_e32 v102, v102
	v_rcp_f32_e32 v103, v103
	s_nop 0
	v_pk_mul_f32 v[100:101], v[100:101], v[102:103]
	s_nop 0
	v_cvt_pk_bf16_f32 v100, v100, v101
	v_mul_f32_e32 v101, 0x3d372713, v106
	v_fma_f32 v101, v106, v101, 1.0
	v_mul_f32_e32 v101, v106, v101
	v_mul_f32_e32 v101, 0xc0135761, v101
	v_exp_f32_e32 v101, v101
	v_mov_b32_dpp v104, v100 row_ror:8 row_mask:0xf bank_mask:0xc
	v_mov_b32_dpp v100, v110 row_ror:8 row_mask:0xf bank_mask:0x3
	v_add_f32_e32 v101, 1.0, v101
	v_rcp_f32_e32 v102, v101
	v_mul_f32_e32 v101, 0x3d372713, v107
	v_fma_f32 v101, v107, v101, 1.0
	v_mul_f32_e32 v101, v107, v101
	v_mul_f32_e32 v101, 0xc0135761, v101
	v_exp_f32_e32 v101, v101
	s_nop 0
	v_add_f32_e32 v101, 1.0, v101
	v_rcp_f32_e32 v103, v101
	s_nop 0
	v_pk_mul_f32 v[102:103], v[106:107], v[102:103]
	s_nop 0
	v_cvt_pk_bf16_f32 v101, v102, v103
	v_mov_b32_e32 v102, v114
	v_mov_b32_e32 v103, v112
	v_add_co_u32_e32 v106, vcc, s0, v146
	v_mov_b32_dpp v102, v98 row_ror:8 row_mask:0xf bank_mask:0xc
	v_mov_b32_dpp v103, v99 row_ror:8 row_mask:0xf bank_mask:0xc
	v_mov_b32_dpp v105, v101 row_ror:8 row_mask:0xf bank_mask:0xc
	v_addc_co_u32_e32 v107, vcc, 0, v147, vcc
	s_mov_b32 s0, 0x3c000
	global_store_dwordx4 v[106:107], v[102:105], off nt
	v_mov_b32_dpp v98, v114 row_ror:8 row_mask:0xf bank_mask:0x3
	v_mov_b32_dpp v99, v112 row_ror:8 row_mask:0xf bank_mask:0x3
	v_add_co_u32_e32 v102, vcc, s0, v146
	v_mov_b32_dpp v101, v108 row_ror:8 row_mask:0xf bank_mask:0x3
	s_nop 0
	v_addc_co_u32_e32 v103, vcc, 0, v147, vcc
	global_store_dwordx4 v[102:103], v[98:101], off nt
	s_mov_b32 s0, 0x48000
	s_nop 0
	v_mul_f32_e32 v98, 0x3d372713, v94
	v_mul_f32_e32 v99, 0x3d372713, v95
	v_fma_f32 v98, v94, v98, 1.0
	v_fma_f32 v99, v95, v99, 1.0
	v_mul_f32_e32 v98, v94, v98
	v_mul_f32_e32 v99, v95, v99
	v_mul_f32_e32 v98, 0xc0135761, v98
	v_mul_f32_e32 v99, 0xc0135761, v99
	v_exp_f32_e32 v98, v98
	v_exp_f32_e32 v99, v99
	v_add_f32_e32 v98, 1.0, v98
	v_add_f32_e32 v99, 1.0, v99
	v_rcp_f32_e32 v98, v98
	v_rcp_f32_e32 v99, v99
	s_nop 0
	v_pk_mul_f32 v[94:95], v[94:95], v[98:99]
	s_nop 0
	v_cvt_pk_bf16_f32 v98, v94, v95
	v_mul_f32_e32 v94, 0x3d372713, v96
	v_mul_f32_e32 v95, 0x3d372713, v97
	v_fma_f32 v94, v96, v94, 1.0
	v_fma_f32 v95, v97, v95, 1.0
	v_mul_f32_e32 v94, v96, v94
	v_mul_f32_e32 v95, v97, v95
	v_mul_f32_e32 v94, 0xc0135761, v94
	v_mul_f32_e32 v95, 0xc0135761, v95
	v_exp_f32_e32 v94, v94
	v_exp_f32_e32 v95, v95
	v_add_f32_e32 v94, 1.0, v94
	v_add_f32_e32 v95, 1.0, v95
	v_rcp_f32_e32 v94, v94
	v_rcp_f32_e32 v95, v95
	s_nop 0
	v_pk_mul_f32 v[94:95], v[96:97], v[94:95]
	s_nop 0
	v_cvt_pk_bf16_f32 v96, v94, v95
	v_mul_f32_e32 v94, 0x3d372713, v90
	v_mul_f32_e32 v95, 0x3d372713, v91
	v_fma_f32 v94, v90, v94, 1.0
	v_fma_f32 v95, v91, v95, 1.0
	v_mul_f32_e32 v94, v90, v94
	v_mul_f32_e32 v95, v91, v95
	v_mul_f32_e32 v94, 0xc0135761, v94
	v_mul_f32_e32 v95, 0xc0135761, v95
	v_exp_f32_e32 v94, v94
	v_exp_f32_e32 v95, v95
	v_add_f32_e32 v94, 1.0, v94
	v_add_f32_e32 v95, 1.0, v95
	v_rcp_f32_e32 v94, v94
	v_rcp_f32_e32 v95, v95
	s_nop 0
	v_pk_mul_f32 v[90:91], v[90:91], v[94:95]
	s_nop 0
	v_cvt_pk_bf16_f32 v94, v90, v91
	v_mul_f32_e32 v90, 0x3d372713, v92
	v_mul_f32_e32 v91, 0x3d372713, v93
	v_fma_f32 v90, v92, v90, 1.0
	v_fma_f32 v91, v93, v91, 1.0
	v_mul_f32_e32 v90, v92, v90
	v_mul_f32_e32 v91, v93, v91
	v_mul_f32_e32 v90, 0xc0135761, v90
	v_mul_f32_e32 v91, 0xc0135761, v91
	v_exp_f32_e32 v90, v90
	v_exp_f32_e32 v91, v91
	v_add_f32_e32 v90, 1.0, v90
	v_add_f32_e32 v91, 1.0, v91
	v_rcp_f32_e32 v90, v90
	v_rcp_f32_e32 v91, v91
	s_nop 0
	v_pk_mul_f32 v[90:91], v[92:93], v[90:91]
	s_nop 0
	v_cvt_pk_bf16_f32 v92, v90, v91
	v_pk_add_f32 v[90:91], v[84:85], v[36:37]
	v_pk_add_f32 v[84:85], v[82:83], v[34:35]
	v_mul_f32_e32 v82, 0x3d372713, v86
	v_mul_f32_e32 v83, 0x3d372713, v87
	v_fma_f32 v82, v86, v82, 1.0
	v_fma_f32 v83, v87, v83, 1.0
	v_mul_f32_e32 v82, v86, v82
	v_mul_f32_e32 v83, v87, v83
	v_mul_f32_e32 v82, 0xc0135761, v82
	v_mul_f32_e32 v83, 0xc0135761, v83
	v_exp_f32_e32 v82, v82
	v_exp_f32_e32 v83, v83
	v_add_f32_e32 v82, 1.0, v82
	v_add_f32_e32 v83, 1.0, v83
	v_rcp_f32_e32 v82, v82
	v_rcp_f32_e32 v83, v83
	s_nop 0
	v_pk_mul_f32 v[82:83], v[86:87], v[82:83]
	s_nop 0
	v_cvt_pk_bf16_f32 v82, v82, v83
	v_mul_f32_e32 v83, 0x3d372713, v88
	v_fma_f32 v83, v88, v83, 1.0
	v_mul_f32_e32 v83, v88, v83
	v_mul_f32_e32 v83, 0xc0135761, v83
	v_exp_f32_e32 v83, v83
	s_nop 0
	v_add_f32_e32 v83, 1.0, v83
	v_rcp_f32_e32 v86, v83
	v_mul_f32_e32 v83, 0x3d372713, v89
	v_fma_f32 v83, v89, v83, 1.0
	v_mul_f32_e32 v83, v89, v83
	v_mul_f32_e32 v83, 0xc0135761, v83
	v_exp_f32_e32 v83, v83
	s_nop 0
	v_add_f32_e32 v83, 1.0, v83
	v_rcp_f32_e32 v87, v83
	s_nop 0
	v_pk_mul_f32 v[86:87], v[88:89], v[86:87]
	s_nop 0
	v_cvt_pk_bf16_f32 v83, v86, v87
	v_mul_f32_e32 v86, 0x3d372713, v84
	v_mul_f32_e32 v87, 0x3d372713, v85
	v_fma_f32 v86, v84, v86, 1.0
	v_fma_f32 v87, v85, v87, 1.0
	v_mul_f32_e32 v86, v84, v86
	v_mul_f32_e32 v87, v85, v87
	v_mul_f32_e32 v86, 0xc0135761, v86
	v_mul_f32_e32 v87, 0xc0135761, v87
	v_exp_f32_e32 v86, v86
	v_exp_f32_e32 v87, v87
	v_mov_b32_e32 v88, v94
	v_mov_b32_e32 v89, v92
	v_add_f32_e32 v86, 1.0, v86
	v_add_f32_e32 v87, 1.0, v87
	v_rcp_f32_e32 v86, v86
	v_rcp_f32_e32 v87, v87
	s_nop 0
	v_pk_mul_f32 v[84:85], v[84:85], v[86:87]
	s_nop 0
	v_cvt_pk_bf16_f32 v84, v84, v85
	v_mul_f32_e32 v85, 0x3d372713, v90
	v_fma_f32 v85, v90, v85, 1.0
	v_mul_f32_e32 v85, v90, v85
	v_mul_f32_e32 v85, 0xc0135761, v85
	v_exp_f32_e32 v85, v85
	v_mov_b32_dpp v88, v84 row_ror:8 row_mask:0xf bank_mask:0xc
	v_mov_b32_dpp v84, v94 row_ror:8 row_mask:0xf bank_mask:0x3
	v_add_f32_e32 v85, 1.0, v85
	v_rcp_f32_e32 v86, v85
	v_mul_f32_e32 v85, 0x3d372713, v91
	v_fma_f32 v85, v91, v85, 1.0
	v_mul_f32_e32 v85, v91, v85
	v_mul_f32_e32 v85, 0xc0135761, v85
	v_exp_f32_e32 v85, v85
	s_nop 0
	v_add_f32_e32 v85, 1.0, v85
	v_rcp_f32_e32 v87, v85
	s_nop 0
	v_pk_mul_f32 v[86:87], v[90:91], v[86:87]
	s_nop 0
	v_cvt_pk_bf16_f32 v85, v86, v87
	v_mov_b32_e32 v86, v98
	v_mov_b32_e32 v87, v96
	v_add_co_u32_e32 v90, vcc, s0, v146
	v_mov_b32_dpp v86, v82 row_ror:8 row_mask:0xf bank_mask:0xc
	v_mov_b32_dpp v87, v83 row_ror:8 row_mask:0xf bank_mask:0xc
	v_mov_b32_dpp v89, v85 row_ror:8 row_mask:0xf bank_mask:0xc
	v_addc_co_u32_e32 v91, vcc, 0, v147, vcc
	s_mov_b32 s0, 0x54000
	global_store_dwordx4 v[90:91], v[86:89], off nt
	v_mov_b32_dpp v82, v98 row_ror:8 row_mask:0xf bank_mask:0x3
	v_mov_b32_dpp v83, v96 row_ror:8 row_mask:0xf bank_mask:0x3
	v_add_co_u32_e32 v86, vcc, s0, v146
	v_mov_b32_dpp v85, v92 row_ror:8 row_mask:0xf bank_mask:0x3
	s_nop 0
	v_addc_co_u32_e32 v87, vcc, 0, v147, vcc
	global_store_dwordx4 v[86:87], v[82:85], off nt
	s_mov_b32 s0, 0xc0000
	s_nop 0
	v_mul_f32_e32 v82, 0x3d372713, v78
	v_mul_f32_e32 v83, 0x3d372713, v79
	v_fma_f32 v82, v78, v82, 1.0
	v_fma_f32 v83, v79, v83, 1.0
	v_mul_f32_e32 v82, v78, v82
	v_mul_f32_e32 v83, v79, v83
	v_mul_f32_e32 v82, 0xc0135761, v82
	v_mul_f32_e32 v83, 0xc0135761, v83
	v_exp_f32_e32 v82, v82
	v_exp_f32_e32 v83, v83
	v_add_f32_e32 v82, 1.0, v82
	v_add_f32_e32 v83, 1.0, v83
	v_rcp_f32_e32 v82, v82
	v_rcp_f32_e32 v83, v83
	s_nop 0
	v_pk_mul_f32 v[78:79], v[78:79], v[82:83]
	s_nop 0
	v_cvt_pk_bf16_f32 v82, v78, v79
	v_mul_f32_e32 v78, 0x3d372713, v80
	v_mul_f32_e32 v79, 0x3d372713, v81
	v_fma_f32 v78, v80, v78, 1.0
	v_fma_f32 v79, v81, v79, 1.0
	v_mul_f32_e32 v78, v80, v78
	v_mul_f32_e32 v79, v81, v79
	v_mul_f32_e32 v78, 0xc0135761, v78
	v_mul_f32_e32 v79, 0xc0135761, v79
	v_exp_f32_e32 v78, v78
	v_exp_f32_e32 v79, v79
	v_add_f32_e32 v78, 1.0, v78
	v_add_f32_e32 v79, 1.0, v79
	v_rcp_f32_e32 v78, v78
	v_rcp_f32_e32 v79, v79
	s_nop 0
	v_pk_mul_f32 v[78:79], v[80:81], v[78:79]
	s_nop 0
	v_cvt_pk_bf16_f32 v80, v78, v79
	v_mul_f32_e32 v78, 0x3d372713, v74
	v_mul_f32_e32 v79, 0x3d372713, v75
	v_fma_f32 v78, v74, v78, 1.0
	v_fma_f32 v79, v75, v79, 1.0
	v_mul_f32_e32 v78, v74, v78
	v_mul_f32_e32 v79, v75, v79
	v_mul_f32_e32 v78, 0xc0135761, v78
	v_mul_f32_e32 v79, 0xc0135761, v79
	v_exp_f32_e32 v78, v78
	v_exp_f32_e32 v79, v79
	v_add_f32_e32 v78, 1.0, v78
	v_add_f32_e32 v79, 1.0, v79
	v_rcp_f32_e32 v78, v78
	v_rcp_f32_e32 v79, v79
	s_nop 0
	v_pk_mul_f32 v[74:75], v[74:75], v[78:79]
	s_nop 0
	v_cvt_pk_bf16_f32 v78, v74, v75
	v_mul_f32_e32 v74, 0x3d372713, v76
	v_mul_f32_e32 v75, 0x3d372713, v77
	v_fma_f32 v74, v76, v74, 1.0
	v_fma_f32 v75, v77, v75, 1.0
	v_mul_f32_e32 v74, v76, v74
	v_mul_f32_e32 v75, v77, v75
	v_mul_f32_e32 v74, 0xc0135761, v74
	v_mul_f32_e32 v75, 0xc0135761, v75
	v_exp_f32_e32 v74, v74
	v_exp_f32_e32 v75, v75
	v_add_f32_e32 v74, 1.0, v74
	v_add_f32_e32 v75, 1.0, v75
	v_rcp_f32_e32 v74, v74
	v_rcp_f32_e32 v75, v75
	s_nop 0
	v_pk_mul_f32 v[74:75], v[76:77], v[74:75]
	s_nop 0
	v_cvt_pk_bf16_f32 v76, v74, v75
	v_pk_add_f32 v[74:75], v[68:69], v[36:37]
	v_pk_add_f32 v[68:69], v[66:67], v[34:35]
	v_mul_f32_e32 v66, 0x3d372713, v70
	v_mul_f32_e32 v67, 0x3d372713, v71
	v_fma_f32 v66, v70, v66, 1.0
	v_fma_f32 v67, v71, v67, 1.0
	v_mul_f32_e32 v66, v70, v66
	v_mul_f32_e32 v67, v71, v67
	v_mul_f32_e32 v66, 0xc0135761, v66
	v_mul_f32_e32 v67, 0xc0135761, v67
	v_exp_f32_e32 v66, v66
	v_exp_f32_e32 v67, v67
	v_add_f32_e32 v66, 1.0, v66
	v_add_f32_e32 v67, 1.0, v67
	v_rcp_f32_e32 v66, v66
	v_rcp_f32_e32 v67, v67
	s_nop 0
	v_pk_mul_f32 v[66:67], v[70:71], v[66:67]
	s_nop 0
	v_cvt_pk_bf16_f32 v66, v66, v67
	v_mul_f32_e32 v67, 0x3d372713, v72
	v_fma_f32 v67, v72, v67, 1.0
	v_mul_f32_e32 v67, v72, v67
	v_mul_f32_e32 v67, 0xc0135761, v67
	v_exp_f32_e32 v67, v67
	s_nop 0
	v_add_f32_e32 v67, 1.0, v67
	v_rcp_f32_e32 v70, v67
	v_mul_f32_e32 v67, 0x3d372713, v73
	v_fma_f32 v67, v73, v67, 1.0
	v_mul_f32_e32 v67, v73, v67
	v_mul_f32_e32 v67, 0xc0135761, v67
	v_exp_f32_e32 v67, v67
	s_nop 0
	v_add_f32_e32 v67, 1.0, v67
	v_rcp_f32_e32 v71, v67
	s_nop 0
	v_pk_mul_f32 v[70:71], v[72:73], v[70:71]
	s_nop 0
	v_cvt_pk_bf16_f32 v67, v70, v71
	v_mul_f32_e32 v70, 0x3d372713, v68
	v_mul_f32_e32 v71, 0x3d372713, v69
	v_fma_f32 v70, v68, v70, 1.0
	v_fma_f32 v71, v69, v71, 1.0
	v_mul_f32_e32 v70, v68, v70
	v_mul_f32_e32 v71, v69, v71
	v_mul_f32_e32 v70, 0xc0135761, v70
	v_mul_f32_e32 v71, 0xc0135761, v71
	v_exp_f32_e32 v70, v70
	v_exp_f32_e32 v71, v71
	v_mov_b32_e32 v72, v78
	v_mov_b32_e32 v73, v76
	v_add_f32_e32 v70, 1.0, v70
	v_add_f32_e32 v71, 1.0, v71
	v_rcp_f32_e32 v70, v70
	v_rcp_f32_e32 v71, v71
	s_nop 0
	v_pk_mul_f32 v[68:69], v[68:69], v[70:71]
	s_nop 0
	v_cvt_pk_bf16_f32 v68, v68, v69
	v_mul_f32_e32 v69, 0x3d372713, v74
	v_fma_f32 v69, v74, v69, 1.0
	v_mul_f32_e32 v69, v74, v69
	v_mul_f32_e32 v69, 0xc0135761, v69
	v_exp_f32_e32 v69, v69
	v_mov_b32_dpp v72, v68 row_ror:8 row_mask:0xf bank_mask:0xc
	v_mov_b32_dpp v68, v78 row_ror:8 row_mask:0xf bank_mask:0x3
	v_add_f32_e32 v69, 1.0, v69
	v_rcp_f32_e32 v70, v69
	v_mul_f32_e32 v69, 0x3d372713, v75
	v_fma_f32 v69, v75, v69, 1.0
	v_mul_f32_e32 v69, v75, v69
	v_mul_f32_e32 v69, 0xc0135761, v69
	v_exp_f32_e32 v69, v69
	s_nop 0
	v_add_f32_e32 v69, 1.0, v69
	v_rcp_f32_e32 v71, v69
	s_nop 0
	v_pk_mul_f32 v[70:71], v[74:75], v[70:71]
	s_nop 0
	v_cvt_pk_bf16_f32 v69, v70, v71
	v_mov_b32_e32 v70, v82
	v_mov_b32_e32 v71, v80
	v_add_co_u32_e32 v74, vcc, s0, v146
	v_mov_b32_dpp v70, v66 row_ror:8 row_mask:0xf bank_mask:0xc
	v_mov_b32_dpp v71, v67 row_ror:8 row_mask:0xf bank_mask:0xc
	v_mov_b32_dpp v73, v69 row_ror:8 row_mask:0xf bank_mask:0xc
	v_addc_co_u32_e32 v75, vcc, 0, v147, vcc
	s_mov_b32 s0, 0xcc000
	global_store_dwordx4 v[74:75], v[70:73], off nt
	v_mov_b32_dpp v66, v82 row_ror:8 row_mask:0xf bank_mask:0x3
	v_mov_b32_dpp v67, v80 row_ror:8 row_mask:0xf bank_mask:0x3
	v_add_co_u32_e32 v70, vcc, s0, v146
	v_mov_b32_dpp v69, v76 row_ror:8 row_mask:0xf bank_mask:0x3
	s_nop 0
	v_addc_co_u32_e32 v71, vcc, 0, v147, vcc
	global_store_dwordx4 v[70:71], v[66:69], off nt
	s_mov_b32 s0, 0xd8000
	s_nop 0
	v_mul_f32_e32 v66, 0x3d372713, v62
	v_mul_f32_e32 v67, 0x3d372713, v63
	v_fma_f32 v66, v62, v66, 1.0
	v_fma_f32 v67, v63, v67, 1.0
	v_mul_f32_e32 v66, v62, v66
	v_mul_f32_e32 v67, v63, v67
	v_mul_f32_e32 v66, 0xc0135761, v66
	v_mul_f32_e32 v67, 0xc0135761, v67
	v_exp_f32_e32 v66, v66
	v_exp_f32_e32 v67, v67
	v_add_f32_e32 v66, 1.0, v66
	v_add_f32_e32 v67, 1.0, v67
	v_rcp_f32_e32 v66, v66
	v_rcp_f32_e32 v67, v67
	s_nop 0
	v_pk_mul_f32 v[62:63], v[62:63], v[66:67]
	s_nop 0
	v_cvt_pk_bf16_f32 v66, v62, v63
	v_mul_f32_e32 v62, 0x3d372713, v64
	v_mul_f32_e32 v63, 0x3d372713, v65
	v_fma_f32 v62, v64, v62, 1.0
	v_fma_f32 v63, v65, v63, 1.0
	v_mul_f32_e32 v62, v64, v62
	v_mul_f32_e32 v63, v65, v63
	v_mul_f32_e32 v62, 0xc0135761, v62
	v_mul_f32_e32 v63, 0xc0135761, v63
	v_exp_f32_e32 v62, v62
	v_exp_f32_e32 v63, v63
	v_add_f32_e32 v62, 1.0, v62
	v_add_f32_e32 v63, 1.0, v63
	v_rcp_f32_e32 v62, v62
	v_rcp_f32_e32 v63, v63
	s_nop 0
	v_pk_mul_f32 v[62:63], v[64:65], v[62:63]
	s_nop 0
	v_cvt_pk_bf16_f32 v64, v62, v63
	v_mul_f32_e32 v62, 0x3d372713, v58
	v_mul_f32_e32 v63, 0x3d372713, v59
	v_fma_f32 v62, v58, v62, 1.0
	v_fma_f32 v63, v59, v63, 1.0
	v_mul_f32_e32 v62, v58, v62
	v_mul_f32_e32 v63, v59, v63
	v_mul_f32_e32 v62, 0xc0135761, v62
	v_mul_f32_e32 v63, 0xc0135761, v63
	v_exp_f32_e32 v62, v62
	v_exp_f32_e32 v63, v63
	v_add_f32_e32 v62, 1.0, v62
	v_add_f32_e32 v63, 1.0, v63
	v_rcp_f32_e32 v62, v62
	v_rcp_f32_e32 v63, v63
	s_nop 0
	v_pk_mul_f32 v[58:59], v[58:59], v[62:63]
	s_nop 0
	v_cvt_pk_bf16_f32 v62, v58, v59
	v_mul_f32_e32 v58, 0x3d372713, v60
	v_mul_f32_e32 v59, 0x3d372713, v61
	v_fma_f32 v58, v60, v58, 1.0
	v_fma_f32 v59, v61, v59, 1.0
	v_mul_f32_e32 v58, v60, v58
	v_mul_f32_e32 v59, v61, v59
	v_mul_f32_e32 v58, 0xc0135761, v58
	v_mul_f32_e32 v59, 0xc0135761, v59
	v_exp_f32_e32 v58, v58
	v_exp_f32_e32 v59, v59
	v_add_f32_e32 v58, 1.0, v58
	v_add_f32_e32 v59, 1.0, v59
	v_rcp_f32_e32 v58, v58
	v_rcp_f32_e32 v59, v59
	s_nop 0
	v_pk_mul_f32 v[58:59], v[60:61], v[58:59]
	s_nop 0
	v_cvt_pk_bf16_f32 v60, v58, v59
	v_pk_add_f32 v[58:59], v[44:45], v[36:37]
	v_pk_add_f32 v[44:45], v[42:43], v[34:35]
	v_mul_f32_e32 v42, 0x3d372713, v46
	v_mul_f32_e32 v43, 0x3d372713, v47
	v_fma_f32 v42, v46, v42, 1.0
	v_fma_f32 v43, v47, v43, 1.0
	v_mul_f32_e32 v42, v46, v42
	v_mul_f32_e32 v43, v47, v43
	v_mul_f32_e32 v42, 0xc0135761, v42
	v_mul_f32_e32 v43, 0xc0135761, v43
	v_exp_f32_e32 v42, v42
	v_exp_f32_e32 v43, v43
	v_add_f32_e32 v42, 1.0, v42
	v_add_f32_e32 v43, 1.0, v43
	v_rcp_f32_e32 v42, v42
	v_rcp_f32_e32 v43, v43
	s_nop 0
	v_pk_mul_f32 v[42:43], v[46:47], v[42:43]
	s_nop 0
	v_cvt_pk_bf16_f32 v42, v42, v43
	v_mul_f32_e32 v43, 0x3d372713, v48
	v_fma_f32 v43, v48, v43, 1.0
	v_mul_f32_e32 v43, v48, v43
	v_mul_f32_e32 v43, 0xc0135761, v43
	v_exp_f32_e32 v43, v43
	s_nop 0
	v_add_f32_e32 v43, 1.0, v43
	v_rcp_f32_e32 v46, v43
	v_mul_f32_e32 v43, 0x3d372713, v49
	v_fma_f32 v43, v49, v43, 1.0
	v_mul_f32_e32 v43, v49, v43
	v_mul_f32_e32 v43, 0xc0135761, v43
	v_exp_f32_e32 v43, v43
	s_nop 0
	v_add_f32_e32 v43, 1.0, v43
	v_rcp_f32_e32 v47, v43
	s_nop 0
	v_pk_mul_f32 v[46:47], v[48:49], v[46:47]
	s_nop 0
	v_cvt_pk_bf16_f32 v43, v46, v47
	v_mul_f32_e32 v46, 0x3d372713, v44
	v_mul_f32_e32 v47, 0x3d372713, v45
	v_fma_f32 v46, v44, v46, 1.0
	v_fma_f32 v47, v45, v47, 1.0
	v_mul_f32_e32 v46, v44, v46
	v_mul_f32_e32 v47, v45, v47
	v_mul_f32_e32 v46, 0xc0135761, v46
	v_mul_f32_e32 v47, 0xc0135761, v47
	v_exp_f32_e32 v46, v46
	v_exp_f32_e32 v47, v47
	v_mov_b32_e32 v48, v62
	v_mov_b32_e32 v49, v60
	v_add_f32_e32 v46, 1.0, v46
	v_add_f32_e32 v47, 1.0, v47
	v_rcp_f32_e32 v46, v46
	v_rcp_f32_e32 v47, v47
	s_nop 0
	v_pk_mul_f32 v[44:45], v[44:45], v[46:47]
	s_nop 0
	v_cvt_pk_bf16_f32 v44, v44, v45
	v_mul_f32_e32 v45, 0x3d372713, v58
	v_fma_f32 v45, v58, v45, 1.0
	v_mul_f32_e32 v45, v58, v45
	v_mul_f32_e32 v45, 0xc0135761, v45
	v_exp_f32_e32 v45, v45
	v_mov_b32_dpp v48, v44 row_ror:8 row_mask:0xf bank_mask:0xc
	v_mov_b32_dpp v44, v62 row_ror:8 row_mask:0xf bank_mask:0x3
	v_add_f32_e32 v45, 1.0, v45
	v_rcp_f32_e32 v46, v45
	v_mul_f32_e32 v45, 0x3d372713, v59
	v_fma_f32 v45, v59, v45, 1.0
	v_mul_f32_e32 v45, v59, v45
	v_mul_f32_e32 v45, 0xc0135761, v45
	v_exp_f32_e32 v45, v45
	s_nop 0
	v_add_f32_e32 v45, 1.0, v45
	v_rcp_f32_e32 v47, v45
	s_nop 0
	v_pk_mul_f32 v[46:47], v[58:59], v[46:47]
	s_nop 0
	v_cvt_pk_bf16_f32 v45, v46, v47
	v_mov_b32_e32 v46, v66
	v_mov_b32_e32 v47, v64
	v_add_co_u32_e32 v58, vcc, s0, v146
	v_mov_b32_dpp v46, v42 row_ror:8 row_mask:0xf bank_mask:0xc
	v_mov_b32_dpp v47, v43 row_ror:8 row_mask:0xf bank_mask:0xc
	v_mov_b32_dpp v49, v45 row_ror:8 row_mask:0xf bank_mask:0xc
	v_addc_co_u32_e32 v59, vcc, 0, v147, vcc
	s_mov_b32 s0, 0xe4000
	global_store_dwordx4 v[58:59], v[46:49], off nt
	v_mov_b32_dpp v42, v66 row_ror:8 row_mask:0xf bank_mask:0x3
	v_mov_b32_dpp v43, v64 row_ror:8 row_mask:0xf bank_mask:0x3
	v_add_co_u32_e32 v46, vcc, s0, v146
	v_mov_b32_dpp v45, v60 row_ror:8 row_mask:0xf bank_mask:0x3
	s_nop 0
	v_addc_co_u32_e32 v47, vcc, 0, v147, vcc
	global_store_dwordx4 v[46:47], v[42:45], off nt
	s_mov_b32 s0, 0xf0000
	s_nop 0
	v_mul_f32_e32 v42, 0x3d372713, v30
	v_mul_f32_e32 v43, 0x3d372713, v31
	v_fma_f32 v42, v30, v42, 1.0
	v_fma_f32 v43, v31, v43, 1.0
	v_mul_f32_e32 v42, v30, v42
	v_mul_f32_e32 v43, v31, v43
	v_mul_f32_e32 v42, 0xc0135761, v42
	v_mul_f32_e32 v43, 0xc0135761, v43
	v_exp_f32_e32 v42, v42
	v_exp_f32_e32 v43, v43
	v_add_f32_e32 v42, 1.0, v42
	v_add_f32_e32 v43, 1.0, v43
	v_rcp_f32_e32 v42, v42
	v_rcp_f32_e32 v43, v43
	s_nop 0
	v_pk_mul_f32 v[30:31], v[30:31], v[42:43]
	s_nop 0
	v_cvt_pk_bf16_f32 v42, v30, v31
	v_mul_f32_e32 v30, 0x3d372713, v32
	v_mul_f32_e32 v31, 0x3d372713, v33
	v_fma_f32 v30, v32, v30, 1.0
	v_fma_f32 v31, v33, v31, 1.0
	v_mul_f32_e32 v30, v32, v30
	v_mul_f32_e32 v31, v33, v31
	v_mul_f32_e32 v30, 0xc0135761, v30
	v_mul_f32_e32 v31, 0xc0135761, v31
	v_exp_f32_e32 v30, v30
	v_exp_f32_e32 v31, v31
	v_add_f32_e32 v30, 1.0, v30
	v_add_f32_e32 v31, 1.0, v31
	v_rcp_f32_e32 v30, v30
	v_rcp_f32_e32 v31, v31
	s_nop 0
	v_pk_mul_f32 v[30:31], v[32:33], v[30:31]
	s_nop 0
	v_cvt_pk_bf16_f32 v32, v30, v31
	v_mul_f32_e32 v30, 0x3d372713, v26
	v_mul_f32_e32 v31, 0x3d372713, v27
	v_fma_f32 v30, v26, v30, 1.0
	v_fma_f32 v31, v27, v31, 1.0
	v_mul_f32_e32 v30, v26, v30
	v_mul_f32_e32 v31, v27, v31
	v_mul_f32_e32 v30, 0xc0135761, v30
	v_mul_f32_e32 v31, 0xc0135761, v31
	v_exp_f32_e32 v30, v30
	v_exp_f32_e32 v31, v31
	v_add_f32_e32 v30, 1.0, v30
	v_add_f32_e32 v31, 1.0, v31
	v_rcp_f32_e32 v30, v30
	v_rcp_f32_e32 v31, v31
	s_nop 0
	v_pk_mul_f32 v[26:27], v[26:27], v[30:31]
	s_nop 0
	v_cvt_pk_bf16_f32 v30, v26, v27
	v_mul_f32_e32 v26, 0x3d372713, v28
	v_mul_f32_e32 v27, 0x3d372713, v29
	v_fma_f32 v26, v28, v26, 1.0
	v_fma_f32 v27, v29, v27, 1.0
	v_mul_f32_e32 v26, v28, v26
	v_mul_f32_e32 v27, v29, v27
	v_mul_f32_e32 v26, 0xc0135761, v26
	v_mul_f32_e32 v27, 0xc0135761, v27
	v_exp_f32_e32 v26, v26
	v_exp_f32_e32 v27, v27
	v_add_f32_e32 v26, 1.0, v26
	v_add_f32_e32 v27, 1.0, v27
	v_rcp_f32_e32 v26, v26
	v_rcp_f32_e32 v27, v27
	s_nop 0
	v_pk_mul_f32 v[26:27], v[28:29], v[26:27]
	s_nop 0
	v_cvt_pk_bf16_f32 v28, v26, v27
	v_pk_add_f32 v[26:27], v[20:21], v[36:37]
	v_pk_add_f32 v[20:21], v[18:19], v[34:35]
	v_mul_f32_e32 v18, 0x3d372713, v22
	v_mul_f32_e32 v19, 0x3d372713, v23
	v_fma_f32 v18, v22, v18, 1.0
	v_fma_f32 v19, v23, v19, 1.0
	v_mul_f32_e32 v18, v22, v18
	v_mul_f32_e32 v19, v23, v19
	v_mul_f32_e32 v18, 0xc0135761, v18
	v_mul_f32_e32 v19, 0xc0135761, v19
	v_exp_f32_e32 v18, v18
	v_exp_f32_e32 v19, v19
	v_add_f32_e32 v18, 1.0, v18
	v_add_f32_e32 v19, 1.0, v19
	v_rcp_f32_e32 v18, v18
	v_rcp_f32_e32 v19, v19
	s_nop 0
	v_pk_mul_f32 v[18:19], v[22:23], v[18:19]
	s_nop 0
	v_cvt_pk_bf16_f32 v18, v18, v19
	v_mul_f32_e32 v19, 0x3d372713, v24
	v_fma_f32 v19, v24, v19, 1.0
	v_mul_f32_e32 v19, v24, v19
	v_mul_f32_e32 v19, 0xc0135761, v19
	v_exp_f32_e32 v19, v19
	s_nop 0
	v_add_f32_e32 v19, 1.0, v19
	v_rcp_f32_e32 v22, v19
	v_mul_f32_e32 v19, 0x3d372713, v25
	v_fma_f32 v19, v25, v19, 1.0
	v_mul_f32_e32 v19, v25, v19
	v_mul_f32_e32 v19, 0xc0135761, v19
	v_exp_f32_e32 v19, v19
	s_nop 0
	v_add_f32_e32 v19, 1.0, v19
	v_rcp_f32_e32 v23, v19
	s_nop 0
	v_pk_mul_f32 v[22:23], v[24:25], v[22:23]
	s_nop 0
	v_cvt_pk_bf16_f32 v19, v22, v23
	v_mul_f32_e32 v22, 0x3d372713, v20
	v_mul_f32_e32 v23, 0x3d372713, v21
	v_fma_f32 v22, v20, v22, 1.0
	v_fma_f32 v23, v21, v23, 1.0
	v_mul_f32_e32 v22, v20, v22
	v_mul_f32_e32 v23, v21, v23
	v_mul_f32_e32 v22, 0xc0135761, v22
	v_mul_f32_e32 v23, 0xc0135761, v23
	v_exp_f32_e32 v22, v22
	v_exp_f32_e32 v23, v23
	v_mov_b32_e32 v24, v30
	v_mov_b32_e32 v25, v28
	v_add_f32_e32 v22, 1.0, v22
	v_add_f32_e32 v23, 1.0, v23
	v_rcp_f32_e32 v22, v22
	v_rcp_f32_e32 v23, v23
	s_nop 0
	v_pk_mul_f32 v[20:21], v[20:21], v[22:23]
	s_nop 0
	v_cvt_pk_bf16_f32 v20, v20, v21
	v_mul_f32_e32 v21, 0x3d372713, v26
	v_fma_f32 v21, v26, v21, 1.0
	v_mul_f32_e32 v21, v26, v21
	v_mul_f32_e32 v21, 0xc0135761, v21
	v_exp_f32_e32 v21, v21
	v_mov_b32_dpp v24, v20 row_ror:8 row_mask:0xf bank_mask:0xc
	v_mov_b32_dpp v20, v30 row_ror:8 row_mask:0xf bank_mask:0x3
	v_add_f32_e32 v21, 1.0, v21
	v_rcp_f32_e32 v22, v21
	v_mul_f32_e32 v21, 0x3d372713, v27
	v_fma_f32 v21, v27, v21, 1.0
	v_mul_f32_e32 v21, v27, v21
	v_mul_f32_e32 v21, 0xc0135761, v21
	v_exp_f32_e32 v21, v21
	s_nop 0
	v_add_f32_e32 v21, 1.0, v21
	v_rcp_f32_e32 v23, v21
	s_nop 0
	v_pk_mul_f32 v[22:23], v[26:27], v[22:23]
	s_nop 0
	v_cvt_pk_bf16_f32 v21, v22, v23
	v_mov_b32_e32 v22, v42
	v_mov_b32_e32 v23, v32
	v_add_co_u32_e32 v26, vcc, s0, v146
	v_mov_b32_dpp v22, v18 row_ror:8 row_mask:0xf bank_mask:0xc
	v_mov_b32_dpp v23, v19 row_ror:8 row_mask:0xf bank_mask:0xc
	v_mov_b32_dpp v25, v21 row_ror:8 row_mask:0xf bank_mask:0xc
	v_addc_co_u32_e32 v27, vcc, 0, v147, vcc
	s_mov_b32 s0, 0xfc000
	global_store_dwordx4 v[26:27], v[22:25], off nt
	v_mov_b32_dpp v18, v42 row_ror:8 row_mask:0xf bank_mask:0x3
	v_mov_b32_dpp v19, v32 row_ror:8 row_mask:0xf bank_mask:0x3
	v_add_co_u32_e32 v22, vcc, s0, v146
	v_mov_b32_dpp v21, v28 row_ror:8 row_mask:0xf bank_mask:0x3
	s_nop 0
	v_addc_co_u32_e32 v23, vcc, 0, v147, vcc
	global_store_dwordx4 v[22:23], v[18:21], off nt
	s_mov_b64 s[0:1], -1
	s_nop 0
	v_mul_f32_e32 v18, 0x3d372713, v14
	v_mul_f32_e32 v19, 0x3d372713, v15
	v_fma_f32 v18, v14, v18, 1.0
	v_fma_f32 v19, v15, v19, 1.0
	v_mul_f32_e32 v18, v14, v18
	v_mul_f32_e32 v19, v15, v19
	v_mul_f32_e32 v18, 0xc0135761, v18
	v_mul_f32_e32 v19, 0xc0135761, v19
	v_exp_f32_e32 v18, v18
	v_exp_f32_e32 v19, v19
	v_add_f32_e32 v18, 1.0, v18
	v_add_f32_e32 v19, 1.0, v19
	v_rcp_f32_e32 v18, v18
	v_rcp_f32_e32 v19, v19
	s_nop 0
	v_pk_mul_f32 v[14:15], v[14:15], v[18:19]
	s_nop 0
	v_cvt_pk_bf16_f32 v18, v14, v15
	v_mul_f32_e32 v14, 0x3d372713, v16
	v_mul_f32_e32 v15, 0x3d372713, v17
	v_fma_f32 v14, v16, v14, 1.0
	v_fma_f32 v15, v17, v15, 1.0
	v_mul_f32_e32 v14, v16, v14
	v_mul_f32_e32 v15, v17, v15
	v_mul_f32_e32 v14, 0xc0135761, v14
	v_mul_f32_e32 v15, 0xc0135761, v15
	v_exp_f32_e32 v14, v14
	v_exp_f32_e32 v15, v15
	v_add_f32_e32 v14, 1.0, v14
	v_add_f32_e32 v15, 1.0, v15
	v_rcp_f32_e32 v14, v14
	v_rcp_f32_e32 v15, v15
	s_nop 0
	v_pk_mul_f32 v[14:15], v[16:17], v[14:15]
	s_nop 0
	v_cvt_pk_bf16_f32 v16, v14, v15
	v_mul_f32_e32 v14, 0x3d372713, v10
	v_mul_f32_e32 v15, 0x3d372713, v11
	v_fma_f32 v14, v10, v14, 1.0
	v_fma_f32 v15, v11, v15, 1.0
	v_mul_f32_e32 v14, v10, v14
	v_mul_f32_e32 v15, v11, v15
	v_mul_f32_e32 v14, 0xc0135761, v14
	v_mul_f32_e32 v15, 0xc0135761, v15
	v_exp_f32_e32 v14, v14
	v_exp_f32_e32 v15, v15
	v_add_f32_e32 v14, 1.0, v14
	v_add_f32_e32 v15, 1.0, v15
	v_rcp_f32_e32 v14, v14
	v_rcp_f32_e32 v15, v15
	s_nop 0
	v_pk_mul_f32 v[10:11], v[10:11], v[14:15]
	s_nop 0
	v_cvt_pk_bf16_f32 v14, v10, v11
	v_mul_f32_e32 v10, 0x3d372713, v12
	v_mul_f32_e32 v11, 0x3d372713, v13
	v_fma_f32 v10, v12, v10, 1.0
	v_fma_f32 v11, v13, v11, 1.0
	v_mul_f32_e32 v10, v12, v10
	v_mul_f32_e32 v11, v13, v11
	v_mul_f32_e32 v10, 0xc0135761, v10
	v_mul_f32_e32 v11, 0xc0135761, v11
	v_exp_f32_e32 v10, v10
	v_exp_f32_e32 v11, v11
	v_add_f32_e32 v10, 1.0, v10
	v_add_f32_e32 v11, 1.0, v11
	v_rcp_f32_e32 v10, v10
	v_rcp_f32_e32 v11, v11
	s_nop 0
	v_pk_mul_f32 v[10:11], v[12:13], v[10:11]
	s_nop 0
	v_cvt_pk_bf16_f32 v12, v10, v11
	v_pk_add_f32 v[10:11], v[4:5], v[36:37]
	v_pk_add_f32 v[4:5], v[2:3], v[34:35]
	v_mul_f32_e32 v2, 0x3d372713, v6
	v_mul_f32_e32 v3, 0x3d372713, v7
	v_fma_f32 v2, v6, v2, 1.0
	v_fma_f32 v3, v7, v3, 1.0
	v_mul_f32_e32 v2, v6, v2
	v_mul_f32_e32 v3, v7, v3
	v_mul_f32_e32 v2, 0xc0135761, v2
	v_mul_f32_e32 v3, 0xc0135761, v3
	v_exp_f32_e32 v2, v2
	v_exp_f32_e32 v3, v3
	v_add_f32_e32 v2, 1.0, v2
	v_add_f32_e32 v3, 1.0, v3
	v_rcp_f32_e32 v2, v2
	v_rcp_f32_e32 v3, v3
	s_nop 0
	v_pk_mul_f32 v[2:3], v[6:7], v[2:3]
	s_nop 0
	v_cvt_pk_bf16_f32 v2, v2, v3
	v_mul_f32_e32 v3, 0x3d372713, v8
	v_fma_f32 v3, v8, v3, 1.0
	v_mul_f32_e32 v3, v8, v3
	v_mul_f32_e32 v3, 0xc0135761, v3
	v_exp_f32_e32 v3, v3
	s_nop 0
	v_add_f32_e32 v3, 1.0, v3
	v_rcp_f32_e32 v6, v3
	v_mul_f32_e32 v3, 0x3d372713, v9
	v_fma_f32 v3, v9, v3, 1.0
	v_mul_f32_e32 v3, v9, v3
	v_mul_f32_e32 v3, 0xc0135761, v3
	v_exp_f32_e32 v3, v3
	s_nop 0
	v_add_f32_e32 v3, 1.0, v3
	v_rcp_f32_e32 v7, v3
	s_nop 0
	v_pk_mul_f32 v[6:7], v[8:9], v[6:7]
	s_nop 0
	v_cvt_pk_bf16_f32 v3, v6, v7
	v_mul_f32_e32 v6, 0x3d372713, v4
	v_mul_f32_e32 v7, 0x3d372713, v5
	v_fma_f32 v6, v4, v6, 1.0
	v_fma_f32 v7, v5, v7, 1.0
	v_mul_f32_e32 v6, v4, v6
	v_mul_f32_e32 v7, v5, v7
	v_mul_f32_e32 v6, 0xc0135761, v6
	v_mul_f32_e32 v7, 0xc0135761, v7
	v_exp_f32_e32 v6, v6
	v_exp_f32_e32 v7, v7
	v_mov_b32_e32 v8, v14
	v_mov_b32_e32 v9, v12
	v_add_f32_e32 v6, 1.0, v6
	v_add_f32_e32 v7, 1.0, v7
	v_rcp_f32_e32 v6, v6
	v_rcp_f32_e32 v7, v7
	s_nop 0
	v_pk_mul_f32 v[4:5], v[4:5], v[6:7]
	s_nop 0
	v_cvt_pk_bf16_f32 v4, v4, v5
	v_mul_f32_e32 v5, 0x3d372713, v10
	v_fma_f32 v5, v10, v5, 1.0
	v_mul_f32_e32 v5, v10, v5
	v_mul_f32_e32 v5, 0xc0135761, v5
	v_exp_f32_e32 v5, v5
	v_mov_b32_dpp v8, v4 row_ror:8 row_mask:0xf bank_mask:0xc
	v_mov_b32_dpp v4, v14 row_ror:8 row_mask:0xf bank_mask:0x3
	v_add_f32_e32 v5, 1.0, v5
	v_rcp_f32_e32 v6, v5
	v_mul_f32_e32 v5, 0x3d372713, v11
	v_fma_f32 v5, v11, v5, 1.0
	v_mul_f32_e32 v5, v11, v5
	v_mul_f32_e32 v5, 0xc0135761, v5
	v_exp_f32_e32 v5, v5
	s_nop 0
	v_add_f32_e32 v5, 1.0, v5
	v_rcp_f32_e32 v7, v5
	s_nop 0
	v_pk_mul_f32 v[6:7], v[10:11], v[6:7]
	s_nop 0
	v_cvt_pk_bf16_f32 v5, v6, v7
	v_mov_b32_e32 v6, v18
	v_mov_b32_e32 v7, v16
	v_add_co_u32_e32 v10, vcc, 0x108000, v146
	v_mov_b32_dpp v6, v2 row_ror:8 row_mask:0xf bank_mask:0xc
	v_mov_b32_dpp v7, v3 row_ror:8 row_mask:0xf bank_mask:0xc
	v_mov_b32_dpp v9, v5 row_ror:8 row_mask:0xf bank_mask:0xc
	v_addc_co_u32_e32 v11, vcc, 0, v147, vcc
	global_store_dwordx4 v[10:11], v[6:9], off nt
	v_mov_b32_dpp v2, v18 row_ror:8 row_mask:0xf bank_mask:0x3
	v_mov_b32_dpp v3, v16 row_ror:8 row_mask:0xf bank_mask:0x3
	v_add_co_u32_e32 v6, vcc, 0x114000, v146
	v_mov_b32_dpp v5, v12 row_ror:8 row_mask:0xf bank_mask:0x3
	s_nop 0
	v_addc_co_u32_e32 v7, vcc, 0, v147, vcc
	s_andn2_b64 vcc, exec, s[40:41]
	global_store_dwordx4 v[6:7], v[2:5], off nt
	s_cbranch_vccnz .LBB0_576
	s_andn2_b64 vcc, exec, s[44:45]
	s_cbranch_vccnz .LBB0_575
	s_barrier
	s_branch .LBB0_575

.LBB0_599:
	s_lshl_b32 s0, s67, 8
	s_lshl_b32 s1, s68, 1
	s_add_i32 s0, s0, s35
	s_or_b32 s1, s1, s65
	v_mov_b32_e32 v132, v0
	s_mul_hi_i32 s4, s1, 0xc00
	s_mulk_i32 s1, 0xc00
	s_ashr_i32 s5, s0, 31
	s_add_u32 s1, s1, s0
	v_and_b32_e32 v142, 15, v132
	v_and_or_b32 v130, v132, 7, s1
	v_lshlrev_b32_e32 v133, 3, v132
	v_lshrrev_b32_e32 v132, 1, v132
	v_and_b32_e32 v141, 24, v132
	v_or_b32_e32 v132, s0, v142
	v_and_b32_e32 v206, 64, v133
	v_ashrrev_i32_e32 v133, 31, v132
	v_lshl_add_u64 v[132:133], v[132:133], 2, s[44:45]
	global_load_dword v134, v[132:133], off
	s_addc_u32 s4, s4, s5
	v_mov_b32_e32 v131, s4
	v_lshlrev_b64 v[130:131], 8, v[130:131]
	v_lshl_add_u64 v[130:131], s[46:47], 0, v[130:131]
	v_lshl_add_u64 v[130:131], v[130:131], 0, v[206:207]
	v_lshlrev_b32_e32 v206, 1, v141
	v_lshl_add_u64 v[130:131], v[130:131], 0, v[206:207]
	s_movk_i32 s0, 0x1000
	s_waitcnt vmcnt(0)
	v_pk_add_f32 v[136:137], v[124:125], v[134:135] op_sel_hi:[1,0]
	v_pk_add_f32 v[124:125], v[122:123], v[134:135] op_sel_hi:[1,0]
	v_pk_add_f32 v[126:127], v[126:127], v[134:135] op_sel_hi:[1,0]
	v_mul_f32_e32 v123, 0x3d372713, v124
	v_fma_f32 v123, v124, v123, 1.0
	v_mul_f32_e32 v123, v124, v123
	v_mul_f32_e32 v123, 0xc0135761, v123
	v_exp_f32_e32 v123, v123
	v_mul_f32_e32 v122, 0x3d372713, v126
	v_fma_f32 v122, v126, v122, 1.0
	v_mul_f32_e32 v122, v126, v122
	v_add_f32_e32 v123, 1.0, v123
	v_rcp_f32_e32 v144, v123
	v_mul_f32_e32 v123, 0x3d372713, v127
	v_fma_f32 v123, v127, v123, 1.0
	v_mul_f32_e32 v123, v127, v123
	v_mul_f32_e32 v122, 0xc0135761, v122
	v_mul_f32_e32 v123, 0xc0135761, v123
	v_exp_f32_e32 v122, v122
	v_exp_f32_e32 v123, v123
	v_pk_add_f32 v[128:129], v[128:129], v[134:135] op_sel_hi:[1,0]
	v_pk_add_f32 v[118:119], v[118:119], v[134:135] op_sel_hi:[1,0]
	v_add_f32_e32 v122, 1.0, v122
	v_add_f32_e32 v123, 1.0, v123
	v_rcp_f32_e32 v122, v122
	v_rcp_f32_e32 v123, v123
	s_nop 0
	v_pk_mul_f32 v[122:123], v[126:127], v[122:123]
	v_mul_f32_e32 v126, 0x3d372713, v125
	v_fma_f32 v126, v125, v126, 1.0
	v_mul_f32_e32 v126, v125, v126
	v_mul_f32_e32 v126, 0xc0135761, v126
	v_exp_f32_e32 v126, v126
	v_mul_f32_e32 v127, 0x3d372713, v136
	v_fma_f32 v127, v136, v127, 1.0
	v_mul_f32_e32 v127, v136, v127
	v_mul_f32_e32 v127, 0xc0135761, v127
	v_add_f32_e32 v126, 1.0, v126
	v_exp_f32_e32 v127, v127
	v_rcp_f32_e32 v145, v126
	v_mul_f32_e32 v126, 0x3d372713, v128
	v_fma_f32 v126, v128, v126, 1.0
	v_add_f32_e32 v127, 1.0, v127
	v_pk_mul_f32 v[124:125], v[124:125], v[144:145]
	v_rcp_f32_e32 v144, v127
	v_mul_f32_e32 v127, 0x3d372713, v129
	v_fma_f32 v127, v129, v127, 1.0
	v_mul_f32_e32 v126, v128, v126
	v_mul_f32_e32 v127, v129, v127
	v_mul_f32_e32 v126, 0xc0135761, v126
	v_mul_f32_e32 v127, 0xc0135761, v127
	v_exp_f32_e32 v126, v126
	v_exp_f32_e32 v127, v127
	v_cvt_pk_bf16_f32 v146, v122, v123
	v_mov_b32_e32 v152, v146
	v_add_f32_e32 v126, 1.0, v126
	v_add_f32_e32 v127, 1.0, v127
	v_rcp_f32_e32 v126, v126
	v_rcp_f32_e32 v127, v127
	s_nop 0
	v_pk_mul_f32 v[126:127], v[128:129], v[126:127]
	v_mul_f32_e32 v128, 0x3d372713, v137
	v_fma_f32 v128, v137, v128, 1.0
	v_mul_f32_e32 v128, v137, v128
	v_mul_f32_e32 v128, 0xc0135761, v128
	v_exp_f32_e32 v128, v128
	s_nop 0
	v_add_f32_e32 v128, 1.0, v128
	v_rcp_f32_e32 v145, v128
	s_nop 0
	v_pk_mul_f32 v[128:129], v[136:137], v[144:145]
	v_pk_add_f32 v[136:137], v[120:121], v[134:135] op_sel_hi:[1,0]
	v_pk_add_f32 v[120:121], v[116:117], v[134:135] op_sel_hi:[1,0]
	v_pk_add_f32 v[116:117], v[114:115], v[134:135] op_sel_hi:[1,0]
	v_mul_f32_e32 v114, 0x3d372713, v118
	v_mul_f32_e32 v115, 0x3d372713, v116
	v_fma_f32 v115, v116, v115, 1.0
	v_mul_f32_e32 v115, v116, v115
	v_mul_f32_e32 v115, 0xc0135761, v115
	v_exp_f32_e32 v115, v115
	v_fma_f32 v114, v118, v114, 1.0
	v_mul_f32_e32 v114, v118, v114
	v_mul_f32_e32 v114, 0xc0135761, v114
	v_add_f32_e32 v115, 1.0, v115
	v_rcp_f32_e32 v148, v115
	v_mul_f32_e32 v115, 0x3d372713, v119
	v_fma_f32 v115, v119, v115, 1.0
	v_mul_f32_e32 v115, v119, v115
	v_mul_f32_e32 v115, 0xc0135761, v115
	v_exp_f32_e32 v114, v114
	v_exp_f32_e32 v115, v115
	v_mul_f32_e32 v134, 0x3d372713, v121
	v_fma_f32 v134, v121, v134, 1.0
	v_add_f32_e32 v114, 1.0, v114
	v_add_f32_e32 v115, 1.0, v115
	v_rcp_f32_e32 v114, v114
	v_rcp_f32_e32 v115, v115
	v_mul_f32_e32 v134, v121, v134
	v_mul_f32_e32 v134, 0xc0135761, v134
	v_exp_f32_e32 v134, v134
	v_pk_mul_f32 v[114:115], v[118:119], v[114:115]
	v_mul_f32_e32 v118, 0x3d372713, v117
	v_fma_f32 v118, v117, v118, 1.0
	v_mul_f32_e32 v118, v117, v118
	v_mul_f32_e32 v118, 0xc0135761, v118
	v_exp_f32_e32 v118, v118
	v_mul_f32_e32 v119, 0x3d372713, v120
	v_fma_f32 v119, v120, v119, 1.0
	v_mul_f32_e32 v119, v120, v119
	v_mul_f32_e32 v119, 0xc0135761, v119
	v_add_f32_e32 v118, 1.0, v118
	v_exp_f32_e32 v119, v119
	v_rcp_f32_e32 v149, v118
	v_mul_f32_e32 v118, 0x3d372713, v136
	v_fma_f32 v118, v136, v118, 1.0
	v_add_f32_e32 v119, 1.0, v119
	v_pk_mul_f32 v[116:117], v[116:117], v[148:149]
	v_rcp_f32_e32 v148, v119
	v_mul_f32_e32 v119, 0x3d372713, v137
	v_fma_f32 v119, v137, v119, 1.0
	v_mul_f32_e32 v118, v136, v118
	v_mul_f32_e32 v119, v137, v119
	v_mul_f32_e32 v118, 0xc0135761, v118
	v_mul_f32_e32 v119, 0xc0135761, v119
	v_exp_f32_e32 v118, v118
	v_exp_f32_e32 v119, v119
	v_add_f32_e32 v134, 1.0, v134
	v_rcp_f32_e32 v149, v134
	v_add_f32_e32 v118, 1.0, v118
	v_add_f32_e32 v119, 1.0, v119
	v_rcp_f32_e32 v118, v118
	v_rcp_f32_e32 v119, v119
	v_cvt_pk_bf16_f32 v145, v126, v127
	v_cvt_pk_bf16_f32 v144, v124, v125
	v_cvt_pk_bf16_f32 v143, v128, v129
	v_pk_mul_f32 v[118:119], v[136:137], v[118:119]
	v_pk_mul_f32 v[120:121], v[120:121], v[148:149]
	v_cvt_pk_bf16_f32 v148, v114, v115
	v_cvt_pk_bf16_f32 v149, v118, v119
	v_cvt_pk_bf16_f32 v150, v116, v117
	v_cvt_pk_bf16_f32 v151, v120, v121
	v_mov_b32_e32 v153, v145
	v_mov_b32_e32 v154, v144
	v_mov_b32_e32 v155, v143
	v_mov_b32_dpp v152, v148 row_ror:8 row_mask:0xf bank_mask:0xc
	v_mov_b32_dpp v153, v149 row_ror:8 row_mask:0xf bank_mask:0xc
	v_mov_b32_dpp v154, v150 row_ror:8 row_mask:0xf bank_mask:0xc
	v_mov_b32_dpp v155, v151 row_ror:8 row_mask:0xf bank_mask:0xc
	v_mov_b32_dpp v148, v146 row_ror:8 row_mask:0xf bank_mask:0x3
	v_mov_b32_dpp v149, v145 row_ror:8 row_mask:0xf bank_mask:0x3
	v_mov_b32_dpp v150, v144 row_ror:8 row_mask:0xf bank_mask:0x3
	v_mov_b32_dpp v151, v143 row_ror:8 row_mask:0xf bank_mask:0x3
	global_store_dwordx4 v[130:131], v[152:155], off nt
	global_store_dwordx4 v[130:131], v[148:151], off offset:2048 nt
	global_load_dword v134, v[132:133], off offset:64
	s_waitcnt vmcnt(0)
	v_pk_add_f32 v[106:107], v[106:107], v[134:135] op_sel_hi:[1,0]
	s_nop 0
	v_mul_f32_e32 v137, 0x3d372713, v106
	v_fma_f32 v137, v106, v137, 1.0
	v_mul_f32_e32 v137, v106, v137
	v_mul_f32_e32 v137, 0xc0135761, v137
	v_exp_f32_e32 v137, v137
	v_pk_add_f32 v[110:111], v[110:111], v[134:135] op_sel_hi:[1,0]
	v_pk_add_f32 v[108:109], v[108:109], v[134:135] op_sel_hi:[1,0]
	v_mul_f32_e32 v136, 0x3d372713, v110
	v_add_f32_e32 v137, 1.0, v137
	v_rcp_f32_e32 v144, v137
	v_mul_f32_e32 v137, 0x3d372713, v111
	v_fma_f32 v136, v110, v136, 1.0
	v_fma_f32 v137, v111, v137, 1.0
	v_mul_f32_e32 v136, v110, v136
	v_mul_f32_e32 v137, v111, v137
	v_mul_f32_e32 v136, 0xc0135761, v136
	v_mul_f32_e32 v137, 0xc0135761, v137
	v_exp_f32_e32 v136, v136
	v_exp_f32_e32 v137, v137
	v_pk_add_f32 v[112:113], v[112:113], v[134:135] op_sel_hi:[1,0]
	v_pk_add_f32 v[98:99], v[98:99], v[134:135] op_sel_hi:[1,0]
	v_add_f32_e32 v136, 1.0, v136
	v_add_f32_e32 v137, 1.0, v137
	v_rcp_f32_e32 v136, v136
	v_rcp_f32_e32 v137, v137
	v_pk_add_f32 v[102:103], v[102:103], v[134:135] op_sel_hi:[1,0]
	v_pk_add_f32 v[100:101], v[100:101], v[134:135] op_sel_hi:[1,0]
	v_pk_add_f32 v[104:105], v[104:105], v[134:135] op_sel_hi:[1,0]
	v_pk_mul_f32 v[136:137], v[110:111], v[136:137]
	v_mul_f32_e32 v110, 0x3d372713, v107
	v_fma_f32 v110, v107, v110, 1.0
	v_mul_f32_e32 v110, v107, v110
	v_mul_f32_e32 v110, 0xc0135761, v110
	v_exp_f32_e32 v110, v110
	s_nop 0
	v_add_f32_e32 v110, 1.0, v110
	v_rcp_f32_e32 v145, v110
	s_nop 0
	v_pk_mul_f32 v[144:145], v[106:107], v[144:145]
	v_mul_f32_e32 v107, 0x3d372713, v108
	v_fma_f32 v107, v108, v107, 1.0
	v_mul_f32_e32 v107, v108, v107
	v_mul_f32_e32 v107, 0xc0135761, v107
	v_exp_f32_e32 v107, v107
	v_mul_f32_e32 v106, 0x3d372713, v112
	v_fma_f32 v106, v112, v106, 1.0
	v_mul_f32_e32 v106, v112, v106
	v_add_f32_e32 v107, 1.0, v107
	v_rcp_f32_e32 v110, v107
	v_mul_f32_e32 v107, 0x3d372713, v113
	v_fma_f32 v107, v113, v107, 1.0
	v_mul_f32_e32 v107, v113, v107
	v_mul_f32_e32 v106, 0xc0135761, v106
	v_mul_f32_e32 v107, 0xc0135761, v107
	v_exp_f32_e32 v106, v106
	v_exp_f32_e32 v107, v107
	v_cvt_pk_bf16_f32 v143, v144, v145
	v_add_f32_e32 v106, 1.0, v106
	v_add_f32_e32 v107, 1.0, v107
	v_rcp_f32_e32 v106, v106
	v_rcp_f32_e32 v107, v107
	s_nop 0
	v_pk_mul_f32 v[146:147], v[112:113], v[106:107]
	v_mul_f32_e32 v106, 0x3d372713, v109
	v_fma_f32 v106, v109, v106, 1.0
	v_mul_f32_e32 v106, v109, v106
	v_mul_f32_e32 v106, 0xc0135761, v106
	v_exp_f32_e32 v106, v106
	v_pk_mul_f32 v[112:113], v[144:145], v[144:145]
	v_add_f32_e32 v106, 1.0, v106
	v_rcp_f32_e32 v111, v106
	v_pk_fma_f32 v[112:113], v[124:125], v[124:125], v[112:113]
	v_pk_mul_f32 v[106:107], v[146:147], v[146:147]
	v_pk_mul_f32 v[148:149], v[108:109], v[110:111]
	v_pk_mul_f32 v[108:109], v[136:137], v[136:137]
	v_pk_fma_f32 v[106:107], v[126:127], v[126:127], v[106:107]
	v_pk_fma_f32 v[108:109], v[122:123], v[122:123], v[108:109]
	v_mul_f32_e32 v123, 0x3d372713, v98
	v_fma_f32 v123, v98, v123, 1.0
	v_mul_f32_e32 v123, v98, v123
	v_mul_f32_e32 v123, 0xc0135761, v123
	v_exp_f32_e32 v123, v123
	v_mul_f32_e32 v122, 0x3d372713, v102
	v_fma_f32 v122, v102, v122, 1.0
	v_mul_f32_e32 v122, v102, v122
	v_add_f32_e32 v123, 1.0, v123
	v_rcp_f32_e32 v124, v123
	v_mul_f32_e32 v123, 0x3d372713, v103
	v_fma_f32 v123, v103, v123, 1.0
	v_mul_f32_e32 v123, v103, v123
	v_mul_f32_e32 v122, 0xc0135761, v122
	v_mul_f32_e32 v123, 0xc0135761, v123
	v_exp_f32_e32 v122, v122
	v_exp_f32_e32 v123, v123
	v_pk_mul_f32 v[110:111], v[148:149], v[148:149]
	v_cvt_pk_bf16_f32 v136, v136, v137
	v_add_f32_e32 v122, 1.0, v122
	v_add_f32_e32 v123, 1.0, v123
	v_rcp_f32_e32 v122, v122
	v_rcp_f32_e32 v123, v123
	v_pk_fma_f32 v[110:111], v[128:129], v[128:129], v[110:111]
	v_cvt_pk_bf16_f32 v137, v146, v147
	v_cvt_pk_bf16_f32 v144, v148, v149
	v_pk_mul_f32 v[122:123], v[102:103], v[122:123]
	v_mul_f32_e32 v102, 0x3d372713, v99
	v_fma_f32 v102, v99, v102, 1.0
	v_mul_f32_e32 v102, v99, v102
	v_mul_f32_e32 v102, 0xc0135761, v102
	v_exp_f32_e32 v102, v102
	s_nop 0
	v_add_f32_e32 v102, 1.0, v102
	v_rcp_f32_e32 v125, v102
	s_nop 0
	v_pk_mul_f32 v[124:125], v[98:99], v[124:125]
	v_mul_f32_e32 v99, 0x3d372713, v100
	v_fma_f32 v99, v100, v99, 1.0
	v_mul_f32_e32 v99, v100, v99
	v_mul_f32_e32 v99, 0xc0135761, v99
	v_exp_f32_e32 v99, v99
	v_mul_f32_e32 v98, 0x3d372713, v104
	v_fma_f32 v98, v104, v98, 1.0
	v_mul_f32_e32 v98, v104, v98
	v_add_f32_e32 v99, 1.0, v99
	v_rcp_f32_e32 v102, v99
	v_mul_f32_e32 v99, 0x3d372713, v105
	v_fma_f32 v99, v105, v99, 1.0
	v_mul_f32_e32 v99, v105, v99
	v_mul_f32_e32 v98, 0xc0135761, v98
	v_mul_f32_e32 v99, 0xc0135761, v99
	v_exp_f32_e32 v98, v98
	v_exp_f32_e32 v99, v99
	v_add_f32_e32 v98, 1.0, v98
	v_add_f32_e32 v99, 1.0, v99
	v_rcp_f32_e32 v98, v98
	v_rcp_f32_e32 v99, v99
	s_nop 0
	v_pk_mul_f32 v[126:127], v[104:105], v[98:99]
	v_mul_f32_e32 v98, 0x3d372713, v101
	v_fma_f32 v98, v101, v98, 1.0
	v_mul_f32_e32 v98, v101, v98
	v_mul_f32_e32 v98, 0xc0135761, v98
	v_exp_f32_e32 v98, v98
	v_pk_mul_f32 v[104:105], v[124:125], v[124:125]
	v_add_f32_e32 v98, 1.0, v98
	v_rcp_f32_e32 v103, v98
	v_pk_mul_f32 v[98:99], v[126:127], v[126:127]
	v_pk_fma_f32 v[104:105], v[116:117], v[116:117], v[104:105]
	v_pk_fma_f32 v[98:99], v[118:119], v[118:119], v[98:99]
	v_pk_mul_f32 v[128:129], v[100:101], v[102:103]
	v_cvt_pk_bf16_f32 v118, v124, v125
	v_add_co_u32_e32 v124, vcc, s0, v130
	v_pk_mul_f32 v[100:101], v[122:123], v[122:123]
	v_pk_mul_f32 v[102:103], v[128:129], v[128:129]
	v_addc_co_u32_e32 v125, vcc, 0, v131, vcc
	s_movk_i32 s0, 0x2000
	v_pk_fma_f32 v[100:101], v[114:115], v[114:115], v[100:101]
	v_pk_fma_f32 v[102:103], v[120:121], v[120:121], v[102:103]
	v_cvt_pk_bf16_f32 v116, v122, v123
	v_cvt_pk_bf16_f32 v117, v126, v127
	v_cvt_pk_bf16_f32 v119, v128, v129
	v_mov_b32_e32 v120, v136
	v_mov_b32_e32 v121, v137
	v_mov_b32_e32 v122, v143
	v_mov_b32_e32 v123, v144
	v_add_co_u32_e32 v114, vcc, s0, v130
	v_mov_b32_dpp v120, v116 row_ror:8 row_mask:0xf bank_mask:0xc
	v_mov_b32_dpp v121, v117 row_ror:8 row_mask:0xf bank_mask:0xc
	v_mov_b32_dpp v122, v118 row_ror:8 row_mask:0xf bank_mask:0xc
	v_mov_b32_dpp v123, v119 row_ror:8 row_mask:0xf bank_mask:0xc
	v_addc_co_u32_e32 v115, vcc, 0, v131, vcc
	v_mov_b32_dpp v116, v136 row_ror:8 row_mask:0xf bank_mask:0x3
	v_mov_b32_dpp v117, v137 row_ror:8 row_mask:0xf bank_mask:0x3
	v_mov_b32_dpp v118, v143 row_ror:8 row_mask:0xf bank_mask:0x3
	v_mov_b32_dpp v119, v144 row_ror:8 row_mask:0xf bank_mask:0x3
	global_store_dwordx4 v[114:115], v[120:123], off offset:-4096 nt
	global_store_dwordx4 v[124:125], v[116:119], off offset:2048 nt
	global_load_dword v116, v[132:133], off offset:128
	s_movk_i32 s0, 0x3000
	s_waitcnt vmcnt(0)
	v_pk_add_f32 v[94:95], v[94:95], v[116:117] op_sel_hi:[1,0]
	v_pk_add_f32 v[96:97], v[96:97], v[116:117] op_sel_hi:[1,0]
	v_pk_add_f32 v[92:93], v[92:93], v[116:117] op_sel_hi:[1,0]
	v_pk_add_f32 v[90:91], v[90:91], v[116:117] op_sel_hi:[1,0]
	v_mul_f32_e32 v117, 0x3d372713, v94
	v_fma_f32 v117, v94, v117, 1.0
	v_mul_f32_e32 v117, v94, v117
	v_mul_f32_e32 v117, 0xc0135761, v117
	v_exp_f32_e32 v117, v117
	s_nop 0
	v_add_f32_e32 v117, 1.0, v117
	v_rcp_f32_e32 v118, v117
	v_mul_f32_e32 v117, 0x3d372713, v90
	v_fma_f32 v117, v90, v117, 1.0
	v_mul_f32_e32 v117, v90, v117
	v_mul_f32_e32 v117, 0xc0135761, v117
	v_exp_f32_e32 v117, v117
	s_nop 0
	v_add_f32_e32 v117, 1.0, v117
	v_rcp_f32_e32 v120, v117
	v_mul_f32_e32 v117, 0x3d372713, v95
	v_fma_f32 v117, v95, v117, 1.0
	v_mul_f32_e32 v117, v95, v117
	v_mul_f32_e32 v117, 0xc0135761, v117
	v_exp_f32_e32 v117, v117
	s_nop 0
	v_add_f32_e32 v117, 1.0, v117
	v_rcp_f32_e32 v119, v117
	s_nop 0
	v_pk_mul_f32 v[118:119], v[94:95], v[118:119]
	v_mul_f32_e32 v94, 0x3d372713, v91
	v_fma_f32 v94, v91, v94, 1.0
	v_mul_f32_e32 v94, v91, v94
	v_mul_f32_e32 v94, 0xc0135761, v94
	v_exp_f32_e32 v94, v94
	v_cvt_pk_bf16_f32 v117, v118, v119
	v_pk_add_f32 v[82:83], v[82:83], v[116:117] op_sel_hi:[1,0]
	v_pk_add_f32 v[86:87], v[86:87], v[116:117] op_sel_hi:[1,0]
	v_add_f32_e32 v94, 1.0, v94
	v_rcp_f32_e32 v121, v94
	v_pk_add_f32 v[84:85], v[84:85], v[116:117] op_sel_hi:[1,0]
	v_pk_add_f32 v[88:89], v[88:89], v[116:117] op_sel_hi:[1,0]
	v_pk_mul_f32 v[120:121], v[90:91], v[120:121]
	v_mul_f32_e32 v91, 0x3d372713, v92
	v_fma_f32 v91, v92, v91, 1.0
	v_mul_f32_e32 v91, v92, v91
	v_mul_f32_e32 v91, 0xc0135761, v91
	v_exp_f32_e32 v91, v91
	v_mul_f32_e32 v90, 0x3d372713, v96
	v_fma_f32 v90, v96, v90, 1.0
	v_mul_f32_e32 v90, v96, v90
	v_add_f32_e32 v91, 1.0, v91
	v_rcp_f32_e32 v94, v91
	v_mul_f32_e32 v91, 0x3d372713, v97
	v_fma_f32 v91, v97, v91, 1.0
	v_mul_f32_e32 v91, v97, v91
	v_mul_f32_e32 v90, 0xc0135761, v90
	v_mul_f32_e32 v91, 0xc0135761, v91
	v_exp_f32_e32 v90, v90
	v_exp_f32_e32 v91, v91
	v_add_f32_e32 v90, 1.0, v90
	v_add_f32_e32 v91, 1.0, v91
	v_rcp_f32_e32 v90, v90
	v_rcp_f32_e32 v91, v91
	s_nop 0
	v_pk_mul_f32 v[122:123], v[96:97], v[90:91]
	v_mul_f32_e32 v90, 0x3d372713, v93
	v_fma_f32 v90, v93, v90, 1.0
	v_mul_f32_e32 v90, v93, v90
	v_mul_f32_e32 v90, 0xc0135761, v90
	v_exp_f32_e32 v90, v90
	s_nop 0
	v_add_f32_e32 v90, 1.0, v90
	v_rcp_f32_e32 v95, v90
	v_pk_fma_f32 v[90:91], v[118:119], v[118:119], v[108:109]
	v_cvt_pk_bf16_f32 v118, v122, v123
	v_cvt_pk_bf16_f32 v119, v120, v121
	v_pk_mul_f32 v[124:125], v[92:93], v[94:95]
	v_pk_fma_f32 v[94:95], v[122:123], v[122:123], v[106:107]
	v_mul_f32_e32 v107, 0x3d372713, v82
	v_fma_f32 v107, v82, v107, 1.0
	v_mul_f32_e32 v107, v82, v107
	v_mul_f32_e32 v107, 0xc0135761, v107
	v_exp_f32_e32 v107, v107
	v_mul_f32_e32 v106, 0x3d372713, v86
	v_fma_f32 v106, v86, v106, 1.0
	v_mul_f32_e32 v106, v86, v106
	v_add_f32_e32 v107, 1.0, v107
	v_rcp_f32_e32 v108, v107
	v_mul_f32_e32 v107, 0x3d372713, v87
	v_fma_f32 v107, v87, v107, 1.0
	v_mul_f32_e32 v107, v87, v107
	v_mul_f32_e32 v106, 0xc0135761, v106
	v_mul_f32_e32 v107, 0xc0135761, v107
	v_exp_f32_e32 v106, v106
	v_exp_f32_e32 v107, v107
	v_pk_fma_f32 v[96:97], v[124:125], v[124:125], v[110:111]
	v_pk_fma_f32 v[92:93], v[120:121], v[120:121], v[112:113]
	v_add_f32_e32 v106, 1.0, v106
	v_add_f32_e32 v107, 1.0, v107
	v_rcp_f32_e32 v106, v106
	v_rcp_f32_e32 v107, v107
	v_cvt_pk_bf16_f32 v120, v124, v125
	v_pk_mul_f32 v[106:107], v[86:87], v[106:107]
	v_mul_f32_e32 v86, 0x3d372713, v83
	v_fma_f32 v86, v83, v86, 1.0
	v_mul_f32_e32 v86, v83, v86
	v_mul_f32_e32 v86, 0xc0135761, v86
	v_exp_f32_e32 v86, v86
	s_nop 0
	v_add_f32_e32 v86, 1.0, v86
	v_rcp_f32_e32 v109, v86
	s_nop 0
	v_pk_mul_f32 v[108:109], v[82:83], v[108:109]
	v_mul_f32_e32 v83, 0x3d372713, v84
	v_fma_f32 v83, v84, v83, 1.0
	v_mul_f32_e32 v83, v84, v83
	v_mul_f32_e32 v83, 0xc0135761, v83
	v_exp_f32_e32 v83, v83
	v_mul_f32_e32 v82, 0x3d372713, v88
	v_fma_f32 v82, v88, v82, 1.0
	v_mul_f32_e32 v82, v88, v82
	v_add_f32_e32 v83, 1.0, v83
	v_rcp_f32_e32 v86, v83
	v_mul_f32_e32 v83, 0x3d372713, v89
	v_fma_f32 v83, v89, v83, 1.0
	v_mul_f32_e32 v83, v89, v83
	v_mul_f32_e32 v82, 0xc0135761, v82
	v_mul_f32_e32 v83, 0xc0135761, v83
	v_exp_f32_e32 v82, v82
	v_exp_f32_e32 v83, v83
	v_add_f32_e32 v82, 1.0, v82
	v_add_f32_e32 v83, 1.0, v83
	v_rcp_f32_e32 v82, v82
	v_rcp_f32_e32 v83, v83
	s_nop 0
	v_pk_mul_f32 v[110:111], v[88:89], v[82:83]
	v_mul_f32_e32 v82, 0x3d372713, v85
	v_fma_f32 v82, v85, v82, 1.0
	v_mul_f32_e32 v82, v85, v82
	v_mul_f32_e32 v82, 0xc0135761, v82
	v_exp_f32_e32 v82, v82
	s_nop 0
	v_add_f32_e32 v82, 1.0, v82
	v_rcp_f32_e32 v87, v82
	v_pk_fma_f32 v[82:83], v[106:107], v[106:107], v[100:101]
	v_cvt_pk_bf16_f32 v100, v108, v109
	v_pk_mul_f32 v[112:113], v[84:85], v[86:87]
	v_pk_fma_f32 v[86:87], v[110:111], v[110:111], v[98:99]
	v_pk_fma_f32 v[84:85], v[108:109], v[108:109], v[104:105]
	v_pk_fma_f32 v[88:89], v[112:113], v[112:113], v[102:103]
	v_cvt_pk_bf16_f32 v98, v106, v107
	v_cvt_pk_bf16_f32 v99, v110, v111
	v_cvt_pk_bf16_f32 v101, v112, v113
	v_mov_b32_e32 v102, v117
	v_mov_b32_e32 v103, v118
	v_mov_b32_e32 v104, v119
	v_mov_b32_e32 v105, v120
	v_mov_b32_dpp v102, v98 row_ror:8 row_mask:0xf bank_mask:0xc
	v_mov_b32_dpp v103, v99 row_ror:8 row_mask:0xf bank_mask:0xc
	v_mov_b32_dpp v104, v100 row_ror:8 row_mask:0xf bank_mask:0xc
	v_mov_b32_dpp v105, v101 row_ror:8 row_mask:0xf bank_mask:0xc
	v_mov_b32_dpp v98, v117 row_ror:8 row_mask:0xf bank_mask:0x3
	v_mov_b32_dpp v99, v118 row_ror:8 row_mask:0xf bank_mask:0x3
	v_mov_b32_dpp v100, v119 row_ror:8 row_mask:0xf bank_mask:0x3
	v_mov_b32_dpp v101, v120 row_ror:8 row_mask:0xf bank_mask:0x3
	global_store_dwordx4 v[114:115], v[102:105], off nt
	global_store_dwordx4 v[114:115], v[98:101], off offset:2048 nt
	global_load_dword v98, v[132:133], off offset:192
	s_waitcnt vmcnt(0)
	v_pk_add_f32 v[78:79], v[78:79], v[98:99] op_sel_hi:[1,0]
	v_pk_add_f32 v[80:81], v[80:81], v[98:99] op_sel_hi:[1,0]
	v_pk_add_f32 v[76:77], v[76:77], v[98:99] op_sel_hi:[1,0]
	v_pk_add_f32 v[74:75], v[74:75], v[98:99] op_sel_hi:[1,0]
	v_mul_f32_e32 v99, 0x3d372713, v78
	v_fma_f32 v99, v78, v99, 1.0
	v_mul_f32_e32 v99, v78, v99
	v_mul_f32_e32 v99, 0xc0135761, v99
	v_exp_f32_e32 v99, v99
	s_nop 0
	v_add_f32_e32 v99, 1.0, v99
	v_rcp_f32_e32 v100, v99
	v_mul_f32_e32 v99, 0x3d372713, v74
	v_fma_f32 v99, v74, v99, 1.0
	v_mul_f32_e32 v99, v74, v99
	v_mul_f32_e32 v99, 0xc0135761, v99
	v_exp_f32_e32 v99, v99
	s_nop 0
	v_add_f32_e32 v99, 1.0, v99
	v_rcp_f32_e32 v102, v99
	v_mul_f32_e32 v99, 0x3d372713, v79
	v_fma_f32 v99, v79, v99, 1.0
	v_mul_f32_e32 v99, v79, v99
	v_mul_f32_e32 v99, 0xc0135761, v99
	v_exp_f32_e32 v99, v99
	s_nop 0
	v_add_f32_e32 v99, 1.0, v99
	v_rcp_f32_e32 v101, v99
	s_nop 0
	v_pk_mul_f32 v[100:101], v[78:79], v[100:101]
	v_mul_f32_e32 v78, 0x3d372713, v75
	v_fma_f32 v78, v75, v78, 1.0
	v_mul_f32_e32 v78, v75, v78
	v_mul_f32_e32 v78, 0xc0135761, v78
	v_exp_f32_e32 v78, v78
	v_cvt_pk_bf16_f32 v99, v100, v101
	v_pk_add_f32 v[66:67], v[66:67], v[98:99] op_sel_hi:[1,0]
	v_pk_add_f32 v[70:71], v[70:71], v[98:99] op_sel_hi:[1,0]
	v_add_f32_e32 v78, 1.0, v78
	v_rcp_f32_e32 v103, v78
	v_pk_add_f32 v[68:69], v[68:69], v[98:99] op_sel_hi:[1,0]
	v_pk_add_f32 v[72:73], v[72:73], v[98:99] op_sel_hi:[1,0]
	v_pk_mul_f32 v[102:103], v[74:75], v[102:103]
	v_mul_f32_e32 v75, 0x3d372713, v76
	v_fma_f32 v75, v76, v75, 1.0
	v_mul_f32_e32 v75, v76, v75
	v_mul_f32_e32 v75, 0xc0135761, v75
	v_exp_f32_e32 v75, v75
	v_mul_f32_e32 v74, 0x3d372713, v80
	v_fma_f32 v74, v80, v74, 1.0
	v_mul_f32_e32 v74, v80, v74
	v_add_f32_e32 v75, 1.0, v75
	v_rcp_f32_e32 v78, v75
	v_mul_f32_e32 v75, 0x3d372713, v81
	v_fma_f32 v75, v81, v75, 1.0
	v_mul_f32_e32 v75, v81, v75
	v_mul_f32_e32 v74, 0xc0135761, v74
	v_mul_f32_e32 v75, 0xc0135761, v75
	v_exp_f32_e32 v74, v74
	v_exp_f32_e32 v75, v75
	v_add_f32_e32 v74, 1.0, v74
	v_add_f32_e32 v75, 1.0, v75
	v_rcp_f32_e32 v74, v74
	v_rcp_f32_e32 v75, v75
	s_nop 0
	v_pk_mul_f32 v[104:105], v[80:81], v[74:75]
	v_mul_f32_e32 v74, 0x3d372713, v77
	v_fma_f32 v74, v77, v74, 1.0
	v_mul_f32_e32 v74, v77, v74
	v_mul_f32_e32 v74, 0xc0135761, v74
	v_exp_f32_e32 v74, v74
	v_pk_fma_f32 v[80:81], v[102:103], v[102:103], v[92:93]
	v_add_f32_e32 v74, 1.0, v74
	v_rcp_f32_e32 v79, v74
	v_pk_fma_f32 v[74:75], v[104:105], v[104:105], v[94:95]
	v_pk_mul_f32 v[106:107], v[76:77], v[78:79]
	v_pk_fma_f32 v[78:79], v[100:101], v[100:101], v[90:91]
	v_mul_f32_e32 v91, 0x3d372713, v66
	v_fma_f32 v91, v66, v91, 1.0
	v_mul_f32_e32 v91, v66, v91
	v_mul_f32_e32 v91, 0xc0135761, v91
	v_exp_f32_e32 v91, v91
	v_mul_f32_e32 v90, 0x3d372713, v70
	v_fma_f32 v90, v70, v90, 1.0
	v_mul_f32_e32 v90, v70, v90
	v_add_f32_e32 v91, 1.0, v91
	v_rcp_f32_e32 v92, v91
	v_mul_f32_e32 v91, 0x3d372713, v71
	v_fma_f32 v91, v71, v91, 1.0
	v_mul_f32_e32 v91, v71, v91
	v_mul_f32_e32 v90, 0xc0135761, v90
	v_mul_f32_e32 v91, 0xc0135761, v91
	v_exp_f32_e32 v90, v90
	v_exp_f32_e32 v91, v91
	v_pk_fma_f32 v[76:77], v[106:107], v[106:107], v[96:97]
	v_cvt_pk_bf16_f32 v100, v104, v105
	v_add_f32_e32 v90, 1.0, v90
	v_add_f32_e32 v91, 1.0, v91
	v_rcp_f32_e32 v90, v90
	v_rcp_f32_e32 v91, v91
	v_cvt_pk_bf16_f32 v101, v102, v103
	v_cvt_pk_bf16_f32 v102, v106, v107
	v_pk_mul_f32 v[90:91], v[70:71], v[90:91]
	v_mul_f32_e32 v70, 0x3d372713, v67
	v_fma_f32 v70, v67, v70, 1.0
	v_mul_f32_e32 v70, v67, v70
	v_mul_f32_e32 v70, 0xc0135761, v70
	v_exp_f32_e32 v70, v70
	s_nop 0
	v_add_f32_e32 v70, 1.0, v70
	v_rcp_f32_e32 v93, v70
	s_nop 0
	v_pk_mul_f32 v[92:93], v[66:67], v[92:93]
	v_mul_f32_e32 v67, 0x3d372713, v68
	v_fma_f32 v67, v68, v67, 1.0
	v_mul_f32_e32 v67, v68, v67
	v_mul_f32_e32 v67, 0xc0135761, v67
	v_exp_f32_e32 v67, v67
	v_mul_f32_e32 v66, 0x3d372713, v72
	v_fma_f32 v66, v72, v66, 1.0
	v_mul_f32_e32 v66, v72, v66
	v_add_f32_e32 v67, 1.0, v67
	v_rcp_f32_e32 v70, v67
	v_mul_f32_e32 v67, 0x3d372713, v73
	v_fma_f32 v67, v73, v67, 1.0
	v_mul_f32_e32 v67, v73, v67
	v_mul_f32_e32 v66, 0xc0135761, v66
	v_mul_f32_e32 v67, 0xc0135761, v67
	v_exp_f32_e32 v66, v66
	v_exp_f32_e32 v67, v67
	v_add_f32_e32 v66, 1.0, v66
	v_add_f32_e32 v67, 1.0, v67
	v_rcp_f32_e32 v66, v66
	v_rcp_f32_e32 v67, v67
	s_nop 0
	v_pk_mul_f32 v[94:95], v[72:73], v[66:67]
	v_mul_f32_e32 v66, 0x3d372713, v69
	v_fma_f32 v66, v69, v66, 1.0
	v_mul_f32_e32 v66, v69, v66
	v_mul_f32_e32 v66, 0xc0135761, v66
	v_exp_f32_e32 v66, v66
	v_pk_fma_f32 v[72:73], v[92:93], v[92:93], v[84:85]
	v_cvt_pk_bf16_f32 v84, v92, v93
	v_add_f32_e32 v66, 1.0, v66
	v_rcp_f32_e32 v71, v66
	v_pk_fma_f32 v[66:67], v[94:95], v[94:95], v[86:87]
	v_mov_b32_e32 v86, v99
	v_mov_b32_e32 v87, v100
	v_pk_mul_f32 v[96:97], v[68:69], v[70:71]
	v_pk_fma_f32 v[70:71], v[90:91], v[90:91], v[82:83]
	v_pk_fma_f32 v[68:69], v[96:97], v[96:97], v[88:89]
	v_cvt_pk_bf16_f32 v82, v90, v91
	v_cvt_pk_bf16_f32 v83, v94, v95
	v_cvt_pk_bf16_f32 v85, v96, v97
	v_mov_b32_e32 v88, v101
	v_mov_b32_e32 v89, v102
	v_add_co_u32_e32 v90, vcc, s0, v130
	v_mov_b32_dpp v86, v82 row_ror:8 row_mask:0xf bank_mask:0xc
	v_mov_b32_dpp v87, v83 row_ror:8 row_mask:0xf bank_mask:0xc
	v_mov_b32_dpp v88, v84 row_ror:8 row_mask:0xf bank_mask:0xc
	v_mov_b32_dpp v89, v85 row_ror:8 row_mask:0xf bank_mask:0xc
	v_addc_co_u32_e32 v91, vcc, 0, v131, vcc
	v_mov_b32_dpp v82, v99 row_ror:8 row_mask:0xf bank_mask:0x3
	v_mov_b32_dpp v83, v100 row_ror:8 row_mask:0xf bank_mask:0x3
	v_mov_b32_dpp v84, v101 row_ror:8 row_mask:0xf bank_mask:0x3
	v_mov_b32_dpp v85, v102 row_ror:8 row_mask:0xf bank_mask:0x3
	global_store_dwordx4 v[90:91], v[86:89], off nt
	global_store_dwordx4 v[90:91], v[82:85], off offset:2048 nt
	global_load_dword v82, v[132:133], off offset:512
	s_mov_b32 s0, 0x8000
	s_waitcnt vmcnt(0)
	v_pk_add_f32 v[62:63], v[62:63], v[82:83] op_sel_hi:[1,0]
	v_pk_add_f32 v[64:65], v[64:65], v[82:83] op_sel_hi:[1,0]
	v_pk_add_f32 v[60:61], v[60:61], v[82:83] op_sel_hi:[1,0]
	v_pk_add_f32 v[58:59], v[58:59], v[82:83] op_sel_hi:[1,0]
	v_mul_f32_e32 v83, 0x3d372713, v62
	v_fma_f32 v83, v62, v83, 1.0
	v_mul_f32_e32 v83, v62, v83
	v_mul_f32_e32 v83, 0xc0135761, v83
	v_exp_f32_e32 v83, v83
	s_nop 0
	v_add_f32_e32 v83, 1.0, v83
	v_rcp_f32_e32 v84, v83
	v_mul_f32_e32 v83, 0x3d372713, v58
	v_fma_f32 v83, v58, v83, 1.0
	v_mul_f32_e32 v83, v58, v83
	v_mul_f32_e32 v83, 0xc0135761, v83
	v_exp_f32_e32 v83, v83
	s_nop 0
	v_add_f32_e32 v83, 1.0, v83
	v_rcp_f32_e32 v86, v83
	v_mul_f32_e32 v83, 0x3d372713, v63
	v_fma_f32 v83, v63, v83, 1.0
	v_mul_f32_e32 v83, v63, v83
	v_mul_f32_e32 v83, 0xc0135761, v83
	v_exp_f32_e32 v83, v83
	s_nop 0
	v_add_f32_e32 v83, 1.0, v83
	v_rcp_f32_e32 v85, v83
	s_nop 0
	v_pk_mul_f32 v[84:85], v[62:63], v[84:85]
	v_mul_f32_e32 v62, 0x3d372713, v59
	v_fma_f32 v62, v59, v62, 1.0
	v_mul_f32_e32 v62, v59, v62
	v_mul_f32_e32 v62, 0xc0135761, v62
	v_exp_f32_e32 v62, v62
	v_cvt_pk_bf16_f32 v83, v84, v85
	v_pk_add_f32 v[50:51], v[50:51], v[82:83] op_sel_hi:[1,0]
	v_pk_add_f32 v[54:55], v[54:55], v[82:83] op_sel_hi:[1,0]
	v_add_f32_e32 v62, 1.0, v62
	v_rcp_f32_e32 v87, v62
	v_pk_add_f32 v[52:53], v[52:53], v[82:83] op_sel_hi:[1,0]
	v_pk_add_f32 v[56:57], v[56:57], v[82:83] op_sel_hi:[1,0]
	v_pk_mul_f32 v[86:87], v[58:59], v[86:87]
	v_mul_f32_e32 v59, 0x3d372713, v60
	v_fma_f32 v59, v60, v59, 1.0
	v_mul_f32_e32 v59, v60, v59
	v_mul_f32_e32 v59, 0xc0135761, v59
	v_exp_f32_e32 v59, v59
	v_mul_f32_e32 v58, 0x3d372713, v64
	v_fma_f32 v58, v64, v58, 1.0
	v_mul_f32_e32 v58, v64, v58
	v_add_f32_e32 v59, 1.0, v59
	v_rcp_f32_e32 v62, v59
	v_mul_f32_e32 v59, 0x3d372713, v65
	v_fma_f32 v59, v65, v59, 1.0
	v_mul_f32_e32 v59, v65, v59
	v_mul_f32_e32 v58, 0xc0135761, v58
	v_mul_f32_e32 v59, 0xc0135761, v59
	v_exp_f32_e32 v58, v58
	v_exp_f32_e32 v59, v59
	v_add_f32_e32 v58, 1.0, v58
	v_add_f32_e32 v59, 1.0, v59
	v_rcp_f32_e32 v58, v58
	v_rcp_f32_e32 v59, v59
	s_nop 0
	v_pk_mul_f32 v[88:89], v[64:65], v[58:59]
	v_mul_f32_e32 v58, 0x3d372713, v61
	v_fma_f32 v58, v61, v58, 1.0
	v_mul_f32_e32 v58, v61, v58
	v_mul_f32_e32 v58, 0xc0135761, v58
	v_exp_f32_e32 v58, v58
	s_nop 0
	v_add_f32_e32 v58, 1.0, v58
	v_rcp_f32_e32 v63, v58
	v_pk_fma_f32 v[58:59], v[84:85], v[84:85], v[78:79]
	v_cvt_pk_bf16_f32 v84, v88, v89
	v_cvt_pk_bf16_f32 v85, v86, v87
	v_pk_mul_f32 v[90:91], v[60:61], v[62:63]
	v_pk_fma_f32 v[62:63], v[88:89], v[88:89], v[74:75]
	v_mul_f32_e32 v75, 0x3d372713, v50
	v_fma_f32 v75, v50, v75, 1.0
	v_mul_f32_e32 v75, v50, v75
	v_mul_f32_e32 v75, 0xc0135761, v75
	v_exp_f32_e32 v75, v75
	v_pk_fma_f32 v[64:65], v[90:91], v[90:91], v[76:77]
	v_mul_f32_e32 v74, 0x3d372713, v54
	v_fma_f32 v74, v54, v74, 1.0
	v_add_f32_e32 v75, 1.0, v75
	v_rcp_f32_e32 v76, v75
	v_mul_f32_e32 v75, 0x3d372713, v55
	v_fma_f32 v75, v55, v75, 1.0
	v_mul_f32_e32 v74, v54, v74
	v_mul_f32_e32 v75, v55, v75
	v_mul_f32_e32 v74, 0xc0135761, v74
	v_mul_f32_e32 v75, 0xc0135761, v75
	v_exp_f32_e32 v74, v74
	v_exp_f32_e32 v75, v75
	v_pk_fma_f32 v[60:61], v[86:87], v[86:87], v[80:81]
	v_cvt_pk_bf16_f32 v86, v90, v91
	v_add_f32_e32 v74, 1.0, v74
	v_add_f32_e32 v75, 1.0, v75
	v_rcp_f32_e32 v74, v74
	v_rcp_f32_e32 v75, v75
	s_nop 0
	v_pk_mul_f32 v[74:75], v[54:55], v[74:75]
	v_mul_f32_e32 v54, 0x3d372713, v51
	v_fma_f32 v54, v51, v54, 1.0
	v_mul_f32_e32 v54, v51, v54
	v_mul_f32_e32 v54, 0xc0135761, v54
	v_exp_f32_e32 v54, v54
	s_nop 0
	v_add_f32_e32 v54, 1.0, v54
	v_rcp_f32_e32 v77, v54
	s_nop 0
	v_pk_mul_f32 v[76:77], v[50:51], v[76:77]
	v_mul_f32_e32 v51, 0x3d372713, v52
	v_fma_f32 v51, v52, v51, 1.0
	v_mul_f32_e32 v51, v52, v51
	v_mul_f32_e32 v51, 0xc0135761, v51
	v_exp_f32_e32 v51, v51
	v_mul_f32_e32 v50, 0x3d372713, v56
	v_fma_f32 v50, v56, v50, 1.0
	v_mul_f32_e32 v50, v56, v50
	v_add_f32_e32 v51, 1.0, v51
	v_rcp_f32_e32 v54, v51
	v_mul_f32_e32 v51, 0x3d372713, v57
	v_fma_f32 v51, v57, v51, 1.0
	v_mul_f32_e32 v51, v57, v51
	v_mul_f32_e32 v50, 0xc0135761, v50
	v_mul_f32_e32 v51, 0xc0135761, v51
	v_exp_f32_e32 v50, v50
	v_exp_f32_e32 v51, v51
	v_add_f32_e32 v50, 1.0, v50
	v_add_f32_e32 v51, 1.0, v51
	v_rcp_f32_e32 v50, v50
	v_rcp_f32_e32 v51, v51
	s_nop 0
	v_pk_mul_f32 v[78:79], v[56:57], v[50:51]
	v_mul_f32_e32 v50, 0x3d372713, v53
	v_fma_f32 v50, v53, v50, 1.0
	v_mul_f32_e32 v50, v53, v50
	v_mul_f32_e32 v50, 0xc0135761, v50
	v_exp_f32_e32 v50, v50
	s_nop 0
	v_add_f32_e32 v50, 1.0, v50
	v_rcp_f32_e32 v55, v50
	v_pk_fma_f32 v[50:51], v[74:75], v[74:75], v[70:71]
	v_cvt_pk_bf16_f32 v70, v76, v77
	v_pk_mul_f32 v[80:81], v[52:53], v[54:55]
	v_pk_fma_f32 v[52:53], v[76:77], v[76:77], v[72:73]
	v_add_co_u32_e32 v76, vcc, s0, v130
	s_mov_b32 s0, 0x9000
	s_nop 0
	v_addc_co_u32_e32 v77, vcc, 0, v131, vcc
	v_pk_fma_f32 v[54:55], v[78:79], v[78:79], v[66:67]
	v_pk_fma_f32 v[56:57], v[80:81], v[80:81], v[68:69]
	v_cvt_pk_bf16_f32 v68, v74, v75
	v_cvt_pk_bf16_f32 v69, v78, v79
	v_cvt_pk_bf16_f32 v71, v80, v81
	v_mov_b32_e32 v72, v83
	v_mov_b32_e32 v73, v84
	v_mov_b32_e32 v74, v85
	v_mov_b32_e32 v75, v86
	v_add_co_u32_e32 v66, vcc, s0, v130
	v_mov_b32_dpp v72, v68 row_ror:8 row_mask:0xf bank_mask:0xc
	v_mov_b32_dpp v73, v69 row_ror:8 row_mask:0xf bank_mask:0xc
	v_mov_b32_dpp v74, v70 row_ror:8 row_mask:0xf bank_mask:0xc
	v_mov_b32_dpp v75, v71 row_ror:8 row_mask:0xf bank_mask:0xc
	v_addc_co_u32_e32 v67, vcc, 0, v131, vcc
	v_mov_b32_dpp v68, v83 row_ror:8 row_mask:0xf bank_mask:0x3
	v_mov_b32_dpp v69, v84 row_ror:8 row_mask:0xf bank_mask:0x3
	v_mov_b32_dpp v70, v85 row_ror:8 row_mask:0xf bank_mask:0x3
	v_mov_b32_dpp v71, v86 row_ror:8 row_mask:0xf bank_mask:0x3
	global_store_dwordx4 v[66:67], v[72:75], off offset:-4096 nt
	global_store_dwordx4 v[76:77], v[68:71], off offset:2048 nt
	global_load_dword v68, v[132:133], off offset:576
	s_mov_b32 s0, 0xa000
	s_waitcnt vmcnt(0)
	v_pk_add_f32 v[46:47], v[46:47], v[68:69] op_sel_hi:[1,0]
	v_pk_add_f32 v[48:49], v[48:49], v[68:69] op_sel_hi:[1,0]
	v_pk_add_f32 v[44:45], v[44:45], v[68:69] op_sel_hi:[1,0]
	v_pk_add_f32 v[42:43], v[42:43], v[68:69] op_sel_hi:[1,0]
	v_mul_f32_e32 v69, 0x3d372713, v46
	v_fma_f32 v69, v46, v69, 1.0
	v_mul_f32_e32 v69, v46, v69
	v_mul_f32_e32 v69, 0xc0135761, v69
	v_exp_f32_e32 v69, v69
	s_nop 0
	v_add_f32_e32 v69, 1.0, v69
	v_rcp_f32_e32 v70, v69
	v_mul_f32_e32 v69, 0x3d372713, v42
	v_fma_f32 v69, v42, v69, 1.0
	v_mul_f32_e32 v69, v42, v69
	v_mul_f32_e32 v69, 0xc0135761, v69
	v_exp_f32_e32 v69, v69
	s_nop 0
	v_add_f32_e32 v69, 1.0, v69
	v_rcp_f32_e32 v72, v69
	v_mul_f32_e32 v69, 0x3d372713, v47
	v_fma_f32 v69, v47, v69, 1.0
	v_mul_f32_e32 v69, v47, v69
	v_mul_f32_e32 v69, 0xc0135761, v69
	v_exp_f32_e32 v69, v69
	s_nop 0
	v_add_f32_e32 v69, 1.0, v69
	v_rcp_f32_e32 v71, v69
	s_nop 0
	v_pk_mul_f32 v[70:71], v[46:47], v[70:71]
	v_mul_f32_e32 v46, 0x3d372713, v43
	v_fma_f32 v46, v43, v46, 1.0
	v_mul_f32_e32 v46, v43, v46
	v_mul_f32_e32 v46, 0xc0135761, v46
	v_exp_f32_e32 v46, v46
	v_cvt_pk_bf16_f32 v69, v70, v71
	v_pk_add_f32 v[34:35], v[34:35], v[68:69] op_sel_hi:[1,0]
	v_pk_add_f32 v[38:39], v[38:39], v[68:69] op_sel_hi:[1,0]
	v_add_f32_e32 v46, 1.0, v46
	v_rcp_f32_e32 v73, v46
	v_pk_add_f32 v[36:37], v[36:37], v[68:69] op_sel_hi:[1,0]
	v_pk_add_f32 v[40:41], v[40:41], v[68:69] op_sel_hi:[1,0]
	v_pk_mul_f32 v[72:73], v[42:43], v[72:73]
	v_mul_f32_e32 v43, 0x3d372713, v44
	v_fma_f32 v43, v44, v43, 1.0
	v_mul_f32_e32 v43, v44, v43
	v_mul_f32_e32 v43, 0xc0135761, v43
	v_exp_f32_e32 v43, v43
	v_mul_f32_e32 v42, 0x3d372713, v48
	v_fma_f32 v42, v48, v42, 1.0
	v_mul_f32_e32 v42, v48, v42
	v_add_f32_e32 v43, 1.0, v43
	v_rcp_f32_e32 v46, v43
	v_mul_f32_e32 v43, 0x3d372713, v49
	v_fma_f32 v43, v49, v43, 1.0
	v_mul_f32_e32 v43, v49, v43
	v_mul_f32_e32 v42, 0xc0135761, v42
	v_mul_f32_e32 v43, 0xc0135761, v43
	v_exp_f32_e32 v42, v42
	v_exp_f32_e32 v43, v43
	v_add_f32_e32 v42, 1.0, v42
	v_add_f32_e32 v43, 1.0, v43
	v_rcp_f32_e32 v42, v42
	v_rcp_f32_e32 v43, v43
	s_nop 0
	v_pk_mul_f32 v[74:75], v[48:49], v[42:43]
	v_mul_f32_e32 v42, 0x3d372713, v45
	v_fma_f32 v42, v45, v42, 1.0
	v_mul_f32_e32 v42, v45, v42
	v_mul_f32_e32 v42, 0xc0135761, v42
	v_exp_f32_e32 v42, v42
	v_pk_fma_f32 v[48:49], v[72:73], v[72:73], v[60:61]
	v_add_f32_e32 v42, 1.0, v42
	v_rcp_f32_e32 v47, v42
	v_pk_fma_f32 v[42:43], v[74:75], v[74:75], v[62:63]
	v_pk_mul_f32 v[76:77], v[44:45], v[46:47]
	v_pk_fma_f32 v[46:47], v[70:71], v[70:71], v[58:59]
	v_mul_f32_e32 v59, 0x3d372713, v34
	v_fma_f32 v59, v34, v59, 1.0
	v_mul_f32_e32 v59, v34, v59
	v_mul_f32_e32 v59, 0xc0135761, v59
	v_exp_f32_e32 v59, v59
	v_mul_f32_e32 v58, 0x3d372713, v38
	v_fma_f32 v58, v38, v58, 1.0
	v_mul_f32_e32 v58, v38, v58
	v_add_f32_e32 v59, 1.0, v59
	v_rcp_f32_e32 v60, v59
	v_mul_f32_e32 v59, 0x3d372713, v39
	v_fma_f32 v59, v39, v59, 1.0
	v_mul_f32_e32 v59, v39, v59
	v_mul_f32_e32 v58, 0xc0135761, v58
	v_mul_f32_e32 v59, 0xc0135761, v59
	v_exp_f32_e32 v58, v58
	v_exp_f32_e32 v59, v59
	v_pk_fma_f32 v[44:45], v[76:77], v[76:77], v[64:65]
	v_cvt_pk_bf16_f32 v70, v74, v75
	v_add_f32_e32 v58, 1.0, v58
	v_add_f32_e32 v59, 1.0, v59
	v_rcp_f32_e32 v58, v58
	v_rcp_f32_e32 v59, v59
	v_cvt_pk_bf16_f32 v71, v72, v73
	v_cvt_pk_bf16_f32 v72, v76, v77
	v_pk_mul_f32 v[58:59], v[38:39], v[58:59]
	v_mul_f32_e32 v38, 0x3d372713, v35
	v_fma_f32 v38, v35, v38, 1.0
	v_mul_f32_e32 v38, v35, v38
	v_mul_f32_e32 v38, 0xc0135761, v38
	v_exp_f32_e32 v38, v38
	s_nop 0
	v_add_f32_e32 v38, 1.0, v38
	v_rcp_f32_e32 v61, v38
	s_nop 0
	v_pk_mul_f32 v[60:61], v[34:35], v[60:61]
	v_mul_f32_e32 v35, 0x3d372713, v36
	v_fma_f32 v35, v36, v35, 1.0
	v_mul_f32_e32 v35, v36, v35
	v_mul_f32_e32 v35, 0xc0135761, v35
	v_exp_f32_e32 v35, v35
	v_mul_f32_e32 v34, 0x3d372713, v40
	v_fma_f32 v34, v40, v34, 1.0
	v_mul_f32_e32 v34, v40, v34
	v_add_f32_e32 v35, 1.0, v35
	v_rcp_f32_e32 v38, v35
	v_mul_f32_e32 v35, 0x3d372713, v41
	v_fma_f32 v35, v41, v35, 1.0
	v_mul_f32_e32 v35, v41, v35
	v_mul_f32_e32 v34, 0xc0135761, v34
	v_mul_f32_e32 v35, 0xc0135761, v35
	v_exp_f32_e32 v34, v34
	v_exp_f32_e32 v35, v35
	v_add_f32_e32 v34, 1.0, v34
	v_add_f32_e32 v35, 1.0, v35
	v_rcp_f32_e32 v34, v34
	v_rcp_f32_e32 v35, v35
	s_nop 0
	v_pk_mul_f32 v[62:63], v[40:41], v[34:35]
	v_mul_f32_e32 v34, 0x3d372713, v37
	v_fma_f32 v34, v37, v34, 1.0
	v_mul_f32_e32 v34, v37, v34
	v_mul_f32_e32 v34, 0xc0135761, v34
	v_exp_f32_e32 v34, v34
	v_pk_fma_f32 v[40:41], v[60:61], v[60:61], v[52:53]
	v_cvt_pk_bf16_f32 v52, v60, v61
	v_add_f32_e32 v34, 1.0, v34
	v_rcp_f32_e32 v39, v34
	v_pk_fma_f32 v[34:35], v[62:63], v[62:63], v[54:55]
	v_mov_b32_e32 v54, v69
	v_mov_b32_e32 v55, v70
	v_pk_mul_f32 v[64:65], v[36:37], v[38:39]
	v_pk_fma_f32 v[38:39], v[58:59], v[58:59], v[50:51]
	v_pk_fma_f32 v[36:37], v[64:65], v[64:65], v[56:57]
	v_cvt_pk_bf16_f32 v50, v58, v59
	v_cvt_pk_bf16_f32 v51, v62, v63
	v_cvt_pk_bf16_f32 v53, v64, v65
	v_mov_b32_e32 v56, v71
	v_mov_b32_e32 v57, v72
	v_mov_b32_dpp v54, v50 row_ror:8 row_mask:0xf bank_mask:0xc
	v_mov_b32_dpp v55, v51 row_ror:8 row_mask:0xf bank_mask:0xc
	v_mov_b32_dpp v56, v52 row_ror:8 row_mask:0xf bank_mask:0xc
	v_mov_b32_dpp v57, v53 row_ror:8 row_mask:0xf bank_mask:0xc
	v_mov_b32_dpp v50, v69 row_ror:8 row_mask:0xf bank_mask:0x3
	v_mov_b32_dpp v51, v70 row_ror:8 row_mask:0xf bank_mask:0x3
	v_mov_b32_dpp v52, v71 row_ror:8 row_mask:0xf bank_mask:0x3
	v_mov_b32_dpp v53, v72 row_ror:8 row_mask:0xf bank_mask:0x3
	global_store_dwordx4 v[66:67], v[54:57], off nt
	global_store_dwordx4 v[66:67], v[50:53], off offset:2048 nt
	global_load_dword v50, v[132:133], off offset:640
	s_waitcnt vmcnt(0)
	v_pk_add_f32 v[30:31], v[30:31], v[50:51] op_sel_hi:[1,0]
	v_pk_add_f32 v[32:33], v[32:33], v[50:51] op_sel_hi:[1,0]
	v_pk_add_f32 v[28:29], v[28:29], v[50:51] op_sel_hi:[1,0]
	v_pk_add_f32 v[26:27], v[26:27], v[50:51] op_sel_hi:[1,0]
	v_mul_f32_e32 v51, 0x3d372713, v30
	v_fma_f32 v51, v30, v51, 1.0
	v_mul_f32_e32 v51, v30, v51
	v_mul_f32_e32 v51, 0xc0135761, v51
	v_exp_f32_e32 v51, v51
	s_nop 0
	v_add_f32_e32 v51, 1.0, v51
	v_rcp_f32_e32 v52, v51
	v_mul_f32_e32 v51, 0x3d372713, v26
	v_fma_f32 v51, v26, v51, 1.0
	v_mul_f32_e32 v51, v26, v51
	v_mul_f32_e32 v51, 0xc0135761, v51
	v_exp_f32_e32 v51, v51
	s_nop 0
	v_add_f32_e32 v51, 1.0, v51
	v_rcp_f32_e32 v54, v51
	v_mul_f32_e32 v51, 0x3d372713, v31
	v_fma_f32 v51, v31, v51, 1.0
	v_mul_f32_e32 v51, v31, v51
	v_mul_f32_e32 v51, 0xc0135761, v51
	v_exp_f32_e32 v51, v51
	s_nop 0
	v_add_f32_e32 v51, 1.0, v51
	v_rcp_f32_e32 v53, v51
	s_nop 0
	v_pk_mul_f32 v[52:53], v[30:31], v[52:53]
	v_mul_f32_e32 v30, 0x3d372713, v27
	v_fma_f32 v30, v27, v30, 1.0
	v_mul_f32_e32 v30, v27, v30
	v_mul_f32_e32 v30, 0xc0135761, v30
	v_exp_f32_e32 v30, v30
	v_cvt_pk_bf16_f32 v51, v52, v53
	v_pk_add_f32 v[18:19], v[18:19], v[50:51] op_sel_hi:[1,0]
	v_pk_add_f32 v[22:23], v[22:23], v[50:51] op_sel_hi:[1,0]
	v_add_f32_e32 v30, 1.0, v30
	v_rcp_f32_e32 v55, v30
	v_pk_add_f32 v[20:21], v[20:21], v[50:51] op_sel_hi:[1,0]
	v_pk_add_f32 v[24:25], v[24:25], v[50:51] op_sel_hi:[1,0]
	v_pk_mul_f32 v[54:55], v[26:27], v[54:55]
	v_mul_f32_e32 v27, 0x3d372713, v28
	v_fma_f32 v27, v28, v27, 1.0
	v_mul_f32_e32 v27, v28, v27
	v_mul_f32_e32 v27, 0xc0135761, v27
	v_exp_f32_e32 v27, v27
	v_mul_f32_e32 v26, 0x3d372713, v32
	v_fma_f32 v26, v32, v26, 1.0
	v_mul_f32_e32 v26, v32, v26
	v_add_f32_e32 v27, 1.0, v27
	v_rcp_f32_e32 v30, v27
	v_mul_f32_e32 v27, 0x3d372713, v33
	v_fma_f32 v27, v33, v27, 1.0
	v_mul_f32_e32 v27, v33, v27
	v_mul_f32_e32 v26, 0xc0135761, v26
	v_mul_f32_e32 v27, 0xc0135761, v27
	v_exp_f32_e32 v26, v26
	v_exp_f32_e32 v27, v27
	v_add_f32_e32 v26, 1.0, v26
	v_add_f32_e32 v27, 1.0, v27
	v_rcp_f32_e32 v26, v26
	v_rcp_f32_e32 v27, v27
	s_nop 0
	v_pk_mul_f32 v[56:57], v[32:33], v[26:27]
	v_mul_f32_e32 v26, 0x3d372713, v29
	v_fma_f32 v26, v29, v26, 1.0
	v_mul_f32_e32 v26, v29, v26
	v_mul_f32_e32 v26, 0xc0135761, v26
	v_exp_f32_e32 v26, v26
	s_nop 0
	v_add_f32_e32 v26, 1.0, v26
	v_rcp_f32_e32 v31, v26
	v_pk_fma_f32 v[26:27], v[52:53], v[52:53], v[46:47]
	v_cvt_pk_bf16_f32 v52, v56, v57
	v_cvt_pk_bf16_f32 v53, v54, v55
	v_pk_mul_f32 v[58:59], v[28:29], v[30:31]
	v_pk_fma_f32 v[30:31], v[56:57], v[56:57], v[42:43]
	v_mul_f32_e32 v43, 0x3d372713, v18
	v_fma_f32 v43, v18, v43, 1.0
	v_mul_f32_e32 v43, v18, v43
	v_mul_f32_e32 v43, 0xc0135761, v43
	v_exp_f32_e32 v43, v43
	v_pk_fma_f32 v[32:33], v[58:59], v[58:59], v[44:45]
	v_mul_f32_e32 v42, 0x3d372713, v22
	v_fma_f32 v42, v22, v42, 1.0
	v_add_f32_e32 v43, 1.0, v43
	v_rcp_f32_e32 v44, v43
	v_mul_f32_e32 v43, 0x3d372713, v23
	v_fma_f32 v43, v23, v43, 1.0
	v_mul_f32_e32 v42, v22, v42
	v_mul_f32_e32 v43, v23, v43
	v_mul_f32_e32 v42, 0xc0135761, v42
	v_mul_f32_e32 v43, 0xc0135761, v43
	v_exp_f32_e32 v42, v42
	v_exp_f32_e32 v43, v43
	v_pk_fma_f32 v[28:29], v[54:55], v[54:55], v[48:49]
	v_cvt_pk_bf16_f32 v54, v58, v59
	v_add_f32_e32 v42, 1.0, v42
	v_add_f32_e32 v43, 1.0, v43
	v_rcp_f32_e32 v42, v42
	v_rcp_f32_e32 v43, v43
	s_nop 0
	v_pk_mul_f32 v[42:43], v[22:23], v[42:43]
	v_mul_f32_e32 v22, 0x3d372713, v19
	v_fma_f32 v22, v19, v22, 1.0
	v_mul_f32_e32 v22, v19, v22
	v_mul_f32_e32 v22, 0xc0135761, v22
	v_exp_f32_e32 v22, v22
	s_nop 0
	v_add_f32_e32 v22, 1.0, v22
	v_rcp_f32_e32 v45, v22
	s_nop 0
	v_pk_mul_f32 v[44:45], v[18:19], v[44:45]
	v_mul_f32_e32 v19, 0x3d372713, v20
	v_fma_f32 v19, v20, v19, 1.0
	v_mul_f32_e32 v19, v20, v19
	v_mul_f32_e32 v19, 0xc0135761, v19
	v_exp_f32_e32 v19, v19
	v_mul_f32_e32 v18, 0x3d372713, v24
	v_fma_f32 v18, v24, v18, 1.0
	v_mul_f32_e32 v18, v24, v18
	v_add_f32_e32 v19, 1.0, v19
	v_rcp_f32_e32 v22, v19
	v_mul_f32_e32 v19, 0x3d372713, v25
	v_fma_f32 v19, v25, v19, 1.0
	v_mul_f32_e32 v19, v25, v19
	v_mul_f32_e32 v18, 0xc0135761, v18
	v_mul_f32_e32 v19, 0xc0135761, v19
	v_exp_f32_e32 v18, v18
	v_exp_f32_e32 v19, v19
	v_add_f32_e32 v18, 1.0, v18
	v_add_f32_e32 v19, 1.0, v19
	v_rcp_f32_e32 v18, v18
	v_rcp_f32_e32 v19, v19
	s_nop 0
	v_pk_mul_f32 v[46:47], v[24:25], v[18:19]
	v_mul_f32_e32 v18, 0x3d372713, v21
	v_fma_f32 v18, v21, v18, 1.0
	v_mul_f32_e32 v18, v21, v18
	v_mul_f32_e32 v18, 0xc0135761, v18
	v_exp_f32_e32 v18, v18
	s_nop 0
	v_add_f32_e32 v18, 1.0, v18
	v_rcp_f32_e32 v23, v18
	v_pk_fma_f32 v[18:19], v[42:43], v[42:43], v[38:39]
	v_cvt_pk_bf16_f32 v38, v44, v45
	v_pk_mul_f32 v[48:49], v[20:21], v[22:23]
	v_pk_fma_f32 v[20:21], v[44:45], v[44:45], v[40:41]
	v_add_co_u32_e32 v44, vcc, s0, v130
	s_mov_b32 s0, 0xb000
	s_nop 0
	v_addc_co_u32_e32 v45, vcc, 0, v131, vcc
	v_pk_fma_f32 v[22:23], v[46:47], v[46:47], v[34:35]
	v_pk_fma_f32 v[24:25], v[48:49], v[48:49], v[36:37]
	v_cvt_pk_bf16_f32 v36, v42, v43
	v_cvt_pk_bf16_f32 v37, v46, v47
	v_cvt_pk_bf16_f32 v39, v48, v49
	v_mov_b32_e32 v40, v51
	v_mov_b32_e32 v41, v52
	v_mov_b32_e32 v42, v53
	v_mov_b32_e32 v43, v54
	v_add_co_u32_e32 v34, vcc, s0, v130
	v_mov_b32_dpp v40, v36 row_ror:8 row_mask:0xf bank_mask:0xc
	v_mov_b32_dpp v41, v37 row_ror:8 row_mask:0xf bank_mask:0xc
	v_mov_b32_dpp v42, v38 row_ror:8 row_mask:0xf bank_mask:0xc
	v_mov_b32_dpp v43, v39 row_ror:8 row_mask:0xf bank_mask:0xc
	v_addc_co_u32_e32 v35, vcc, 0, v131, vcc
	v_mov_b32_dpp v36, v51 row_ror:8 row_mask:0xf bank_mask:0x3
	v_mov_b32_dpp v37, v52 row_ror:8 row_mask:0xf bank_mask:0x3
	v_mov_b32_dpp v38, v53 row_ror:8 row_mask:0xf bank_mask:0x3
	v_mov_b32_dpp v39, v54 row_ror:8 row_mask:0xf bank_mask:0x3
	global_store_dwordx4 v[34:35], v[40:43], off offset:-4096 nt
	global_store_dwordx4 v[44:45], v[36:39], off offset:2048 nt
	global_load_dword v36, v[132:133], off offset:704
	v_cmp_eq_u32_e32 vcc, 0, v142
	s_waitcnt vmcnt(0)
	v_pk_add_f32 v[14:15], v[14:15], v[36:37] op_sel_hi:[1,0]
	v_pk_add_f32 v[16:17], v[16:17], v[36:37] op_sel_hi:[1,0]
	v_pk_add_f32 v[12:13], v[12:13], v[36:37] op_sel_hi:[1,0]
	v_pk_add_f32 v[10:11], v[10:11], v[36:37] op_sel_hi:[1,0]
	v_mul_f32_e32 v37, 0x3d372713, v14
	v_fma_f32 v37, v14, v37, 1.0
	v_mul_f32_e32 v37, v14, v37
	v_mul_f32_e32 v37, 0xc0135761, v37
	v_exp_f32_e32 v37, v37
	s_nop 0
	v_add_f32_e32 v37, 1.0, v37
	v_rcp_f32_e32 v38, v37
	v_mul_f32_e32 v37, 0x3d372713, v10
	v_fma_f32 v37, v10, v37, 1.0
	v_mul_f32_e32 v37, v10, v37
	v_mul_f32_e32 v37, 0xc0135761, v37
	v_exp_f32_e32 v37, v37
	s_nop 0
	v_add_f32_e32 v37, 1.0, v37
	v_rcp_f32_e32 v40, v37
	v_mul_f32_e32 v37, 0x3d372713, v15
	v_fma_f32 v37, v15, v37, 1.0
	v_mul_f32_e32 v37, v15, v37
	v_mul_f32_e32 v37, 0xc0135761, v37
	v_exp_f32_e32 v37, v37
	s_nop 0
	v_add_f32_e32 v37, 1.0, v37
	v_rcp_f32_e32 v39, v37
	s_nop 0
	v_pk_mul_f32 v[38:39], v[14:15], v[38:39]
	v_mul_f32_e32 v14, 0x3d372713, v11
	v_fma_f32 v14, v11, v14, 1.0
	v_mul_f32_e32 v14, v11, v14
	v_mul_f32_e32 v14, 0xc0135761, v14
	v_exp_f32_e32 v14, v14
	v_cvt_pk_bf16_f32 v37, v38, v39
	v_pk_add_f32 v[2:3], v[2:3], v[36:37] op_sel_hi:[1,0]
	v_pk_fma_f32 v[26:27], v[38:39], v[38:39], v[26:27]
	v_add_f32_e32 v14, 1.0, v14
	v_rcp_f32_e32 v41, v14
	v_pk_add_f32 v[6:7], v[6:7], v[36:37] op_sel_hi:[1,0]
	v_pk_add_f32 v[4:5], v[4:5], v[36:37] op_sel_hi:[1,0]
	v_pk_add_f32 v[8:9], v[8:9], v[36:37] op_sel_hi:[1,0]
	v_pk_mul_f32 v[40:41], v[10:11], v[40:41]
	v_mul_f32_e32 v11, 0x3d372713, v12
	v_fma_f32 v11, v12, v11, 1.0
	v_mul_f32_e32 v11, v12, v11
	v_mul_f32_e32 v11, 0xc0135761, v11
	v_exp_f32_e32 v11, v11
	v_mul_f32_e32 v10, 0x3d372713, v16
	v_fma_f32 v10, v16, v10, 1.0
	v_mul_f32_e32 v10, v16, v10
	v_add_f32_e32 v11, 1.0, v11
	v_rcp_f32_e32 v14, v11
	v_mul_f32_e32 v11, 0x3d372713, v17
	v_fma_f32 v11, v17, v11, 1.0
	v_mul_f32_e32 v11, v17, v11
	v_mul_f32_e32 v10, 0xc0135761, v10
	v_mul_f32_e32 v11, 0xc0135761, v11
	v_exp_f32_e32 v10, v10
	v_exp_f32_e32 v11, v11
	v_cvt_pk_bf16_f32 v39, v40, v41
	v_add_f32_e32 v10, 1.0, v10
	v_add_f32_e32 v11, 1.0, v11
	v_rcp_f32_e32 v10, v10
	v_rcp_f32_e32 v11, v11
	s_nop 0
	v_pk_mul_f32 v[16:17], v[16:17], v[10:11]
	v_mul_f32_e32 v10, 0x3d372713, v13
	v_fma_f32 v10, v13, v10, 1.0
	v_mul_f32_e32 v10, v13, v10
	v_mul_f32_e32 v10, 0xc0135761, v10
	v_exp_f32_e32 v10, v10
	v_cvt_pk_bf16_f32 v38, v16, v17
	v_add_f32_e32 v10, 1.0, v10
	v_rcp_f32_e32 v15, v10
	s_nop 0
	v_pk_mul_f32 v[42:43], v[12:13], v[14:15]
	v_pk_fma_f32 v[14:15], v[16:17], v[16:17], v[30:31]
	v_mul_f32_e32 v17, 0x3d372713, v2
	v_fma_f32 v17, v2, v17, 1.0
	v_mul_f32_e32 v17, v2, v17
	v_mul_f32_e32 v17, 0xc0135761, v17
	v_exp_f32_e32 v17, v17
	v_pk_fma_f32 v[12:13], v[40:41], v[40:41], v[28:29]
	v_mul_f32_e32 v16, 0x3d372713, v6
	v_fma_f32 v16, v6, v16, 1.0
	v_add_f32_e32 v17, 1.0, v17
	v_rcp_f32_e32 v28, v17
	v_mul_f32_e32 v17, 0x3d372713, v7
	v_fma_f32 v17, v7, v17, 1.0
	v_mul_f32_e32 v16, v6, v16
	v_mul_f32_e32 v17, v7, v17
	v_mul_f32_e32 v16, 0xc0135761, v16
	v_mul_f32_e32 v17, 0xc0135761, v17
	v_exp_f32_e32 v16, v16
	v_exp_f32_e32 v17, v17
	v_cvt_pk_bf16_f32 v40, v42, v43
	v_pk_fma_f32 v[10:11], v[42:43], v[42:43], v[32:33]
	v_add_f32_e32 v16, 1.0, v16
	v_add_f32_e32 v17, 1.0, v17
	v_rcp_f32_e32 v16, v16
	v_rcp_f32_e32 v17, v17
	s_nop 0
	v_pk_mul_f32 v[6:7], v[6:7], v[16:17]
	v_mul_f32_e32 v16, 0x3d372713, v3
	v_fma_f32 v16, v3, v16, 1.0
	v_mul_f32_e32 v16, v3, v16
	v_mul_f32_e32 v16, 0xc0135761, v16
	v_exp_f32_e32 v16, v16
	v_pk_fma_f32 v[18:19], v[6:7], v[6:7], v[18:19]
	v_add_f32_e32 v16, 1.0, v16
	v_rcp_f32_e32 v29, v16
	s_nop 0
	v_pk_mul_f32 v[16:17], v[2:3], v[28:29]
	v_mul_f32_e32 v3, 0x3d372713, v4
	v_fma_f32 v3, v4, v3, 1.0
	v_mul_f32_e32 v3, v4, v3
	v_mul_f32_e32 v3, 0xc0135761, v3
	v_exp_f32_e32 v3, v3
	v_mul_f32_e32 v2, 0x3d372713, v8
	v_fma_f32 v2, v8, v2, 1.0
	v_mul_f32_e32 v2, v8, v2
	v_add_f32_e32 v3, 1.0, v3
	v_rcp_f32_e32 v28, v3
	v_mul_f32_e32 v3, 0x3d372713, v9
	v_fma_f32 v3, v9, v3, 1.0
	v_mul_f32_e32 v3, v9, v3
	v_mul_f32_e32 v2, 0xc0135761, v2
	v_mul_f32_e32 v3, 0xc0135761, v3
	v_exp_f32_e32 v2, v2
	v_exp_f32_e32 v3, v3
	v_pk_fma_f32 v[32:33], v[16:17], v[16:17], v[20:21]
	v_mov_b32_dpp v20, v18 quad_perm:[1,0,3,2] row_mask:0xf bank_mask:0xf bound_ctrl:1
	v_add_f32_e32 v2, 1.0, v2
	v_add_f32_e32 v3, 1.0, v3
	v_rcp_f32_e32 v2, v2
	v_rcp_f32_e32 v3, v3
	v_mov_b32_dpp v21, v19 quad_perm:[1,0,3,2] row_mask:0xf bank_mask:0xf bound_ctrl:1
	v_pk_add_f32 v[18:19], v[18:19], v[20:21]
	v_pk_mul_f32 v[8:9], v[8:9], v[2:3]
	v_mul_f32_e32 v2, 0x3d372713, v5
	v_fma_f32 v2, v5, v2, 1.0
	v_mul_f32_e32 v2, v5, v2
	v_mul_f32_e32 v2, 0xc0135761, v2
	v_exp_f32_e32 v2, v2
	v_pk_fma_f32 v[22:23], v[8:9], v[8:9], v[22:23]
	v_cvt_pk_bf16_f32 v3, v8, v9
	v_mov_b32_e32 v8, v39
	v_add_f32_e32 v2, 1.0, v2
	v_rcp_f32_e32 v29, v2
	v_cvt_pk_bf16_f32 v2, v6, v7
	v_mov_b32_e32 v6, v37
	v_mov_b32_e32 v7, v38
	v_pk_mul_f32 v[28:29], v[4:5], v[28:29]
	v_cvt_pk_bf16_f32 v4, v16, v17
	v_cvt_pk_bf16_f32 v5, v28, v29
	v_mov_b32_e32 v9, v40
	v_mov_b32_dpp v6, v2 row_ror:8 row_mask:0xf bank_mask:0xc
	v_mov_b32_dpp v2, v37 row_ror:8 row_mask:0xf bank_mask:0x3
	v_mov_b32_dpp v7, v3 row_ror:8 row_mask:0xf bank_mask:0xc
	v_mov_b32_dpp v3, v38 row_ror:8 row_mask:0xf bank_mask:0x3
	v_mov_b32_dpp v8, v4 row_ror:8 row_mask:0xf bank_mask:0xc
	v_mov_b32_dpp v9, v5 row_ror:8 row_mask:0xf bank_mask:0xc
	v_mov_b32_dpp v4, v39 row_ror:8 row_mask:0xf bank_mask:0x3
	v_mov_b32_dpp v5, v40 row_ror:8 row_mask:0xf bank_mask:0x3
	global_store_dwordx4 v[34:35], v[6:9], off nt
	global_store_dwordx4 v[34:35], v[2:5], off offset:2048 nt
	v_pk_fma_f32 v[30:31], v[28:29], v[28:29], v[24:25]
	v_mov_b32_dpp v6, v14 quad_perm:[1,0,3,2] row_mask:0xf bank_mask:0xf bound_ctrl:1
	v_mov_b32_dpp v2, v26 quad_perm:[1,0,3,2] row_mask:0xf bank_mask:0xf bound_ctrl:1
	v_mov_b32_dpp v3, v27 quad_perm:[1,0,3,2] row_mask:0xf bank_mask:0xf bound_ctrl:1
	v_pk_add_f32 v[2:3], v[26:27], v[2:3]
	v_mov_b32_dpp v7, v15 quad_perm:[1,0,3,2] row_mask:0xf bank_mask:0xf bound_ctrl:1
	v_mov_b32_dpp v26, v32 quad_perm:[1,0,3,2] row_mask:0xf bank_mask:0xf bound_ctrl:1
	v_mov_b32_dpp v27, v33 quad_perm:[1,0,3,2] row_mask:0xf bank_mask:0xf bound_ctrl:1
	v_pk_add_f32 v[6:7], v[14:15], v[6:7]
	v_mov_b32_dpp v14, v12 quad_perm:[1,0,3,2] row_mask:0xf bank_mask:0xf bound_ctrl:1
	v_mov_b32_dpp v15, v13 quad_perm:[1,0,3,2] row_mask:0xf bank_mask:0xf bound_ctrl:1
	v_mov_b32_dpp v16, v10 quad_perm:[1,0,3,2] row_mask:0xf bank_mask:0xf bound_ctrl:1
	v_mov_b32_dpp v17, v11 quad_perm:[1,0,3,2] row_mask:0xf bank_mask:0xf bound_ctrl:1
	v_mov_b32_dpp v24, v22 quad_perm:[1,0,3,2] row_mask:0xf bank_mask:0xf bound_ctrl:1
	v_mov_b32_dpp v25, v23 quad_perm:[1,0,3,2] row_mask:0xf bank_mask:0xf bound_ctrl:1
	v_pk_add_f32 v[26:27], v[32:33], v[26:27]
	v_mov_b32_dpp v32, v30 quad_perm:[1,0,3,2] row_mask:0xf bank_mask:0xf bound_ctrl:1
	v_mov_b32_dpp v33, v31 quad_perm:[1,0,3,2] row_mask:0xf bank_mask:0xf bound_ctrl:1
	v_pk_add_f32 v[12:13], v[12:13], v[14:15]
	v_pk_add_f32 v[10:11], v[10:11], v[16:17]
	v_pk_add_f32 v[22:23], v[22:23], v[24:25]
	v_pk_add_f32 v[30:31], v[30:31], v[32:33]
	v_mov_b32_dpp v4, v2 quad_perm:[2,3,0,1] row_mask:0xf bank_mask:0xf bound_ctrl:1
	v_mov_b32_dpp v5, v3 quad_perm:[2,3,0,1] row_mask:0xf bank_mask:0xf bound_ctrl:1
	v_mov_b32_dpp v8, v6 quad_perm:[2,3,0,1] row_mask:0xf bank_mask:0xf bound_ctrl:1
	v_mov_b32_dpp v9, v7 quad_perm:[2,3,0,1] row_mask:0xf bank_mask:0xf bound_ctrl:1
	v_mov_b32_dpp v14, v12 quad_perm:[2,3,0,1] row_mask:0xf bank_mask:0xf bound_ctrl:1
	v_mov_b32_dpp v15, v13 quad_perm:[2,3,0,1] row_mask:0xf bank_mask:0xf bound_ctrl:1
	v_mov_b32_dpp v16, v10 quad_perm:[2,3,0,1] row_mask:0xf bank_mask:0xf bound_ctrl:1
	v_mov_b32_dpp v17, v11 quad_perm:[2,3,0,1] row_mask:0xf bank_mask:0xf bound_ctrl:1
	v_mov_b32_dpp v20, v18 quad_perm:[2,3,0,1] row_mask:0xf bank_mask:0xf bound_ctrl:1
	v_mov_b32_dpp v21, v19 quad_perm:[2,3,0,1] row_mask:0xf bank_mask:0xf bound_ctrl:1
	v_mov_b32_dpp v24, v22 quad_perm:[2,3,0,1] row_mask:0xf bank_mask:0xf bound_ctrl:1
	v_mov_b32_dpp v25, v23 quad_perm:[2,3,0,1] row_mask:0xf bank_mask:0xf bound_ctrl:1
	v_mov_b32_dpp v28, v26 quad_perm:[2,3,0,1] row_mask:0xf bank_mask:0xf bound_ctrl:1
	v_mov_b32_dpp v29, v27 quad_perm:[2,3,0,1] row_mask:0xf bank_mask:0xf bound_ctrl:1
	v_mov_b32_dpp v32, v30 quad_perm:[2,3,0,1] row_mask:0xf bank_mask:0xf bound_ctrl:1
	v_mov_b32_dpp v33, v31 quad_perm:[2,3,0,1] row_mask:0xf bank_mask:0xf bound_ctrl:1
	v_pk_add_f32 v[2:3], v[2:3], v[4:5]
	v_pk_add_f32 v[6:7], v[6:7], v[8:9]
	v_pk_add_f32 v[12:13], v[12:13], v[14:15]
	v_pk_add_f32 v[10:11], v[10:11], v[16:17]
	v_pk_add_f32 v[18:19], v[18:19], v[20:21]
	v_pk_add_f32 v[22:23], v[22:23], v[24:25]
	v_pk_add_f32 v[26:27], v[26:27], v[28:29]
	v_pk_add_f32 v[30:31], v[30:31], v[32:33]
	v_mov_b32_dpp v4, v2 row_half_mirror row_mask:0xf bank_mask:0xf bound_ctrl:1
	v_mov_b32_dpp v5, v3 row_half_mirror row_mask:0xf bank_mask:0xf bound_ctrl:1
	v_mov_b32_dpp v8, v6 row_half_mirror row_mask:0xf bank_mask:0xf bound_ctrl:1
	v_mov_b32_dpp v9, v7 row_half_mirror row_mask:0xf bank_mask:0xf bound_ctrl:1
	v_mov_b32_dpp v14, v12 row_half_mirror row_mask:0xf bank_mask:0xf bound_ctrl:1
	v_mov_b32_dpp v15, v13 row_half_mirror row_mask:0xf bank_mask:0xf bound_ctrl:1
	v_mov_b32_dpp v16, v10 row_half_mirror row_mask:0xf bank_mask:0xf bound_ctrl:1
	v_mov_b32_dpp v17, v11 row_half_mirror row_mask:0xf bank_mask:0xf bound_ctrl:1
	v_mov_b32_dpp v20, v18 row_half_mirror row_mask:0xf bank_mask:0xf bound_ctrl:1
	v_mov_b32_dpp v21, v19 row_half_mirror row_mask:0xf bank_mask:0xf bound_ctrl:1
	v_mov_b32_dpp v24, v22 row_half_mirror row_mask:0xf bank_mask:0xf bound_ctrl:1
	v_mov_b32_dpp v25, v23 row_half_mirror row_mask:0xf bank_mask:0xf bound_ctrl:1
	v_mov_b32_dpp v28, v26 row_half_mirror row_mask:0xf bank_mask:0xf bound_ctrl:1
	v_mov_b32_dpp v29, v27 row_half_mirror row_mask:0xf bank_mask:0xf bound_ctrl:1
	v_mov_b32_dpp v32, v30 row_half_mirror row_mask:0xf bank_mask:0xf bound_ctrl:1
	v_mov_b32_dpp v33, v31 row_half_mirror row_mask:0xf bank_mask:0xf bound_ctrl:1
	v_pk_add_f32 v[2:3], v[2:3], v[4:5]
	v_pk_add_f32 v[6:7], v[6:7], v[8:9]
	v_pk_add_f32 v[12:13], v[12:13], v[14:15]
	v_pk_add_f32 v[10:11], v[10:11], v[16:17]
	v_pk_add_f32 v[18:19], v[18:19], v[20:21]
	v_pk_add_f32 v[22:23], v[22:23], v[24:25]
	v_pk_add_f32 v[26:27], v[26:27], v[28:29]
	v_pk_add_f32 v[30:31], v[30:31], v[32:33]
	v_mov_b32_dpp v4, v2 row_mirror row_mask:0xf bank_mask:0xf bound_ctrl:1
	v_mov_b32_dpp v5, v3 row_mirror row_mask:0xf bank_mask:0xf bound_ctrl:1
	v_mov_b32_dpp v8, v6 row_mirror row_mask:0xf bank_mask:0xf bound_ctrl:1
	v_mov_b32_dpp v9, v7 row_mirror row_mask:0xf bank_mask:0xf bound_ctrl:1
	v_mov_b32_dpp v14, v12 row_mirror row_mask:0xf bank_mask:0xf bound_ctrl:1
	v_mov_b32_dpp v15, v13 row_mirror row_mask:0xf bank_mask:0xf bound_ctrl:1
	v_mov_b32_dpp v16, v10 row_mirror row_mask:0xf bank_mask:0xf bound_ctrl:1
	v_mov_b32_dpp v17, v11 row_mirror row_mask:0xf bank_mask:0xf bound_ctrl:1
	v_mov_b32_dpp v20, v18 row_mirror row_mask:0xf bank_mask:0xf bound_ctrl:1
	v_mov_b32_dpp v21, v19 row_mirror row_mask:0xf bank_mask:0xf bound_ctrl:1
	v_mov_b32_dpp v24, v22 row_mirror row_mask:0xf bank_mask:0xf bound_ctrl:1
	v_mov_b32_dpp v25, v23 row_mirror row_mask:0xf bank_mask:0xf bound_ctrl:1
	v_mov_b32_dpp v28, v26 row_mirror row_mask:0xf bank_mask:0xf bound_ctrl:1
	v_mov_b32_dpp v29, v27 row_mirror row_mask:0xf bank_mask:0xf bound_ctrl:1
	v_mov_b32_dpp v32, v30 row_mirror row_mask:0xf bank_mask:0xf bound_ctrl:1
	v_mov_b32_dpp v33, v31 row_mirror row_mask:0xf bank_mask:0xf bound_ctrl:1
	s_and_saveexec_b64 s[0:1], vcc
	s_cbranch_execz .LBB0_601
	s_lshl_b32 s5, s67, 1
	s_add_i32 s6, s5, s10
	s_lshl_b32 s4, s68, 8
	s_ashr_i32 s7, s6, 31
	s_or_b32 s4, s4, s64
	s_lshl_b64 s[6:7], s[6:7], 17
	s_add_u32 s6, s36, s6
	s_addc_u32 s7, s37, s7
	s_ashr_i32 s5, s4, 31
	s_lshl_b64 s[4:5], s[4:5], 2
	s_add_u32 s4, s6, s4
	v_pk_add_f32 v[6:7], v[6:7], v[8:9]
	v_pk_add_f32 v[4:5], v[2:3], v[4:5]
	s_addc_u32 s5, s7, s5
	v_lshlrev_b32_e32 v2, 2, v141
	v_pk_add_f32 v[30:31], v[30:31], v[32:33]
	v_pk_add_f32 v[28:29], v[26:27], v[28:29]
	v_pk_add_f32 v[22:23], v[22:23], v[24:25]
	v_pk_add_f32 v[20:21], v[18:19], v[20:21]
	v_pk_add_f32 v[16:17], v[10:11], v[16:17]
	v_pk_add_f32 v[14:15], v[12:13], v[14:15]
	global_store_dwordx4 v2, v[4:7], s[4:5] nt
	global_store_dwordx4 v2, v[14:17], s[4:5] offset:16 nt
	global_store_dwordx4 v2, v[20:23], s[4:5] offset:128 nt
	global_store_dwordx4 v2, v[28:31], s[4:5] offset:144 nt

.LBB0_787:
	s_waitcnt vmcnt(0)
	v_pk_add_f32 v[140:141], v[140:141], v[154:155]
	v_pk_add_f32 v[138:139], v[138:139], v[152:153]
	v_pk_add_f32 v[140:141], v[68:69], v[140:141]
	v_pk_add_f32 v[138:139], v[66:67], v[138:139]
	v_pk_add_f32 v[132:133], v[136:137], v[132:133]
	v_pk_add_f32 v[130:131], v[134:135], v[130:131]
	v_cvt_pk_bf16_f32 v136, v138, v139
	v_cvt_pk_bf16_f32 v137, v140, v141
	v_lshl_add_u64 v[134:135], v[150:151], 1, s[50:51]
	s_movk_i32 s0, 0x4000
	global_store_dwordx2 v[134:135], v[136:137], off nt
	v_add_co_u32_e32 v136, vcc, s0, v134
	v_mov_b32_e32 v138, v126
	v_pk_add_f32 v[132:133], v[68:69], v[132:133]
	v_pk_add_f32 v[130:131], v[66:67], v[130:131]
	v_addc_co_u32_e32 v137, vcc, 0, v135, vcc
	v_mov_b32_dpp v138, v122 row_ror:8 row_mask:0xf bank_mask:0xc
	v_mov_b32_dpp v122, v126 row_ror:8 row_mask:0xf bank_mask:0x3
	v_mov_b32_e32 v139, v127
	v_mov_b32_e32 v140, v128
	v_mov_b32_e32 v141, v129
	v_cndmask_b32_e64 v126, 0, 1, s[44:45]
	v_cvt_pk_bf16_f32 v130, v130, v131
	v_cvt_pk_bf16_f32 v131, v132, v133
	v_mov_b32_dpp v139, v123 row_ror:8 row_mask:0xf bank_mask:0xc
	v_mov_b32_dpp v123, v127 row_ror:8 row_mask:0xf bank_mask:0x3
	v_mov_b32_dpp v140, v124 row_ror:8 row_mask:0xf bank_mask:0xc
	v_mov_b32_dpp v124, v128 row_ror:8 row_mask:0xf bank_mask:0x3
	v_mov_b32_dpp v141, v125 row_ror:8 row_mask:0xf bank_mask:0xc
	v_cmp_ne_u32_e64 s[40:41], 1, v126
	s_andn2_b64 vcc, exec, s[44:45]
	v_mov_b32_dpp v125, v129 row_ror:8 row_mask:0xf bank_mask:0x3
	global_store_dwordx2 v[136:137], v[130:131], off nt
	s_cbranch_vccnz .LBB0_836
	v_add_co_u32_e32 v128, vcc, 0x4000, v148
	global_load_dwordx2 v[126:127], v[148:149], off offset:64 nt
	s_nop 0
	v_addc_co_u32_e32 v129, vcc, 0, v149, vcc
	global_load_dwordx2 v[128:129], v[128:129], off offset:64 nt
	s_waitcnt vmcnt(1)
	v_lshlrev_b32_e32 v130, 16, v126
	v_and_b32_e32 v131, 0xffff0000, v126
	v_lshlrev_b32_e32 v132, 16, v127
	v_and_b32_e32 v133, 0xffff0000, v127
	s_waitcnt vmcnt(0)
	v_lshlrev_b32_e32 v126, 16, v128
	v_and_b32_e32 v127, 0xffff0000, v128
	v_lshlrev_b32_e32 v128, 16, v129
	v_and_b32_e32 v129, 0xffff0000, v129
	s_cbranch_execnz .LBB0_790

.LBB0_790:
	s_waitcnt vmcnt(1)
	v_pk_add_f32 v[132:133], v[132:133], v[140:141]
	v_pk_add_f32 v[130:131], v[130:131], v[138:139]
	s_waitcnt vmcnt(0)
	v_pk_add_f32 v[122:123], v[126:127], v[122:123]
	v_pk_add_f32 v[132:133], v[56:57], v[132:133]
	v_pk_add_f32 v[130:131], v[54:55], v[130:131]
	v_pk_add_f32 v[124:125], v[128:129], v[124:125]
	v_pk_add_f32 v[122:123], v[54:55], v[122:123]
	v_pk_add_f32 v[124:125], v[56:57], v[124:125]
	v_cvt_pk_bf16_f32 v126, v130, v131
	v_cvt_pk_bf16_f32 v127, v132, v133
	v_cvt_pk_bf16_f32 v122, v122, v123
	v_cvt_pk_bf16_f32 v123, v124, v125
	global_store_dwordx2 v[134:135], v[126:127], off offset:64 nt
	global_store_dwordx2 v[136:137], v[122:123], off offset:64 nt
	v_or_b32_e32 v122, 16, v144
	v_ashrrev_i32_e32 v123, 31, v122
	v_lshlrev_b64 v[122:123], 10, v[122:123]
	v_lshl_add_u64 v[130:131], v[122:123], 0, v[142:143]
	v_mov_b32_e32 v132, v118
	v_mov_b32_e32 v133, v119
	v_mov_b32_e32 v134, v120
	v_mov_b32_e32 v135, v121
	v_mov_b32_dpp v132, v114 row_ror:8 row_mask:0xf bank_mask:0xc
	v_mov_b32_dpp v114, v118 row_ror:8 row_mask:0xf bank_mask:0x3
	v_mov_b32_dpp v133, v115 row_ror:8 row_mask:0xf bank_mask:0xc
	v_mov_b32_dpp v115, v119 row_ror:8 row_mask:0xf bank_mask:0x3
	v_mov_b32_dpp v134, v116 row_ror:8 row_mask:0xf bank_mask:0xc
	v_mov_b32_dpp v116, v120 row_ror:8 row_mask:0xf bank_mask:0x3
	v_mov_b32_dpp v135, v117 row_ror:8 row_mask:0xf bank_mask:0xc
	v_mov_b32_dpp v117, v121 row_ror:8 row_mask:0xf bank_mask:0x3
	s_and_b64 vcc, exec, s[40:41]
	v_lshl_add_u64 v[128:129], v[130:131], 1, s[46:47]
	s_cbranch_vccnz .LBB0_837
	v_add_co_u32_e32 v118, vcc, 0x4000, v128
	global_load_dwordx2 v[120:121], v[128:129], off nt
	s_nop 0
	v_addc_co_u32_e32 v119, vcc, 0, v129, vcc
	global_load_dwordx2 v[124:125], v[118:119], off nt
	s_waitcnt vmcnt(1)
	v_lshlrev_b32_e32 v118, 16, v120
	v_and_b32_e32 v119, 0xffff0000, v120
	v_lshlrev_b32_e32 v120, 16, v121
	v_and_b32_e32 v121, 0xffff0000, v121
	s_waitcnt vmcnt(0)
	v_lshlrev_b32_e32 v122, 16, v124
	v_and_b32_e32 v123, 0xffff0000, v124
	v_lshlrev_b32_e32 v124, 16, v125
	v_and_b32_e32 v125, 0xffff0000, v125
	v_lshl_add_u64 v[126:127], v[130:131], 2, s[46:47]
	s_cbranch_execnz .LBB0_793

.LBB0_793:
	s_waitcnt vmcnt(1)
	v_pk_add_f32 v[118:119], v[118:119], v[132:133]
	v_pk_add_f32 v[120:121], v[120:121], v[134:135]
	v_pk_add_f32 v[118:119], v[66:67], v[118:119]
	v_pk_add_f32 v[120:121], v[68:69], v[120:121]
	s_waitcnt vmcnt(0)
	v_pk_add_f32 v[114:115], v[122:123], v[114:115]
	v_cvt_pk_bf16_f32 v122, v118, v119
	v_lshl_add_u64 v[118:119], v[130:131], 1, s[50:51]
	s_movk_i32 s0, 0x4000
	v_pk_add_f32 v[116:117], v[124:125], v[116:117]
	v_cvt_pk_bf16_f32 v123, v120, v121
	v_add_co_u32_e32 v120, vcc, s0, v118
	v_pk_add_f32 v[116:117], v[68:69], v[116:117]
	v_pk_add_f32 v[114:115], v[66:67], v[114:115]
	global_store_dwordx2 v[118:119], v[122:123], off nt
	v_addc_co_u32_e32 v121, vcc, 0, v119, vcc
	v_mov_b32_e32 v122, v110
	v_mov_b32_e32 v123, v111
	v_mov_b32_e32 v124, v112
	v_mov_b32_e32 v125, v113
	v_cvt_pk_bf16_f32 v114, v114, v115
	v_cvt_pk_bf16_f32 v115, v116, v117
	v_mov_b32_dpp v122, v106 row_ror:8 row_mask:0xf bank_mask:0xc
	v_mov_b32_dpp v106, v110 row_ror:8 row_mask:0xf bank_mask:0x3
	v_mov_b32_dpp v123, v107 row_ror:8 row_mask:0xf bank_mask:0xc
	v_mov_b32_dpp v107, v111 row_ror:8 row_mask:0xf bank_mask:0x3
	v_mov_b32_dpp v124, v108 row_ror:8 row_mask:0xf bank_mask:0xc
	v_mov_b32_dpp v108, v112 row_ror:8 row_mask:0xf bank_mask:0x3
	v_mov_b32_dpp v125, v109 row_ror:8 row_mask:0xf bank_mask:0xc
	s_and_b64 vcc, exec, s[40:41]
	v_mov_b32_dpp v109, v113 row_ror:8 row_mask:0xf bank_mask:0x3
	global_store_dwordx2 v[120:121], v[114:115], off nt
	s_cbranch_vccnz .LBB0_838
	v_add_co_u32_e32 v110, vcc, 0x4000, v128
	global_load_dwordx2 v[112:113], v[128:129], off offset:64 nt
	s_nop 0
	v_addc_co_u32_e32 v111, vcc, 0, v129, vcc
	global_load_dwordx2 v[116:117], v[110:111], off offset:64 nt
	s_waitcnt vmcnt(1)
	v_lshlrev_b32_e32 v110, 16, v112
	v_and_b32_e32 v111, 0xffff0000, v112
	v_lshlrev_b32_e32 v112, 16, v113
	v_and_b32_e32 v113, 0xffff0000, v113
	s_waitcnt vmcnt(0)
	v_lshlrev_b32_e32 v114, 16, v116
	v_and_b32_e32 v115, 0xffff0000, v116
	v_lshlrev_b32_e32 v116, 16, v117
	v_and_b32_e32 v117, 0xffff0000, v117
	s_cbranch_execnz .LBB0_796

.LBB0_796:
	s_waitcnt vmcnt(1)
	v_pk_add_f32 v[112:113], v[112:113], v[124:125]
	v_pk_add_f32 v[110:111], v[110:111], v[122:123]
	s_waitcnt vmcnt(0)
	v_pk_add_f32 v[106:107], v[114:115], v[106:107]
	v_pk_add_f32 v[112:113], v[56:57], v[112:113]
	v_pk_add_f32 v[110:111], v[54:55], v[110:111]
	v_pk_add_f32 v[108:109], v[116:117], v[108:109]
	v_pk_add_f32 v[106:107], v[54:55], v[106:107]
	v_pk_add_f32 v[108:109], v[56:57], v[108:109]
	v_cvt_pk_bf16_f32 v110, v110, v111
	v_cvt_pk_bf16_f32 v111, v112, v113
	v_cvt_pk_bf16_f32 v106, v106, v107
	v_cvt_pk_bf16_f32 v107, v108, v109
	global_store_dwordx2 v[118:119], v[110:111], off offset:64 nt
	global_store_dwordx2 v[120:121], v[106:107], off offset:64 nt
	v_or_b32_e32 v106, 32, v144
	v_ashrrev_i32_e32 v107, 31, v106
	v_lshlrev_b64 v[106:107], 10, v[106:107]
	v_lshl_add_u64 v[114:115], v[106:107], 0, v[142:143]
	v_mov_b32_e32 v116, v102
	v_mov_b32_e32 v117, v103
	v_mov_b32_e32 v118, v104
	v_mov_b32_e32 v119, v105
	v_mov_b32_dpp v116, v98 row_ror:8 row_mask:0xf bank_mask:0xc
	v_mov_b32_dpp v98, v102 row_ror:8 row_mask:0xf bank_mask:0x3
	v_mov_b32_dpp v117, v99 row_ror:8 row_mask:0xf bank_mask:0xc
	v_mov_b32_dpp v99, v103 row_ror:8 row_mask:0xf bank_mask:0x3
	v_mov_b32_dpp v118, v100 row_ror:8 row_mask:0xf bank_mask:0xc
	v_mov_b32_dpp v100, v104 row_ror:8 row_mask:0xf bank_mask:0x3
	v_mov_b32_dpp v119, v101 row_ror:8 row_mask:0xf bank_mask:0xc
	v_mov_b32_dpp v101, v105 row_ror:8 row_mask:0xf bank_mask:0x3
	s_and_b64 vcc, exec, s[40:41]
	v_lshl_add_u64 v[112:113], v[114:115], 1, s[46:47]
	s_cbranch_vccnz .LBB0_839
	v_add_co_u32_e32 v102, vcc, 0x4000, v112
	global_load_dwordx2 v[104:105], v[112:113], off nt
	s_nop 0
	v_addc_co_u32_e32 v103, vcc, 0, v113, vcc
	global_load_dwordx2 v[108:109], v[102:103], off nt
	s_waitcnt vmcnt(1)
	v_lshlrev_b32_e32 v102, 16, v104
	v_and_b32_e32 v103, 0xffff0000, v104
	v_lshlrev_b32_e32 v104, 16, v105
	v_and_b32_e32 v105, 0xffff0000, v105
	s_waitcnt vmcnt(0)
	v_lshlrev_b32_e32 v106, 16, v108
	v_and_b32_e32 v107, 0xffff0000, v108
	v_lshlrev_b32_e32 v108, 16, v109
	v_and_b32_e32 v109, 0xffff0000, v109
	v_lshl_add_u64 v[110:111], v[114:115], 2, s[46:47]
	s_cbranch_execnz .LBB0_799

.LBB0_799:
	s_waitcnt vmcnt(1)
	v_pk_add_f32 v[102:103], v[102:103], v[116:117]
	v_pk_add_f32 v[104:105], v[104:105], v[118:119]
	v_pk_add_f32 v[102:103], v[66:67], v[102:103]
	v_pk_add_f32 v[104:105], v[68:69], v[104:105]
	s_waitcnt vmcnt(0)
	v_pk_add_f32 v[98:99], v[106:107], v[98:99]
	v_cvt_pk_bf16_f32 v106, v102, v103
	v_lshl_add_u64 v[102:103], v[114:115], 1, s[50:51]
	s_movk_i32 s0, 0x4000
	v_pk_add_f32 v[100:101], v[108:109], v[100:101]
	v_cvt_pk_bf16_f32 v107, v104, v105
	v_add_co_u32_e32 v104, vcc, s0, v102
	v_pk_add_f32 v[100:101], v[68:69], v[100:101]
	v_pk_add_f32 v[98:99], v[66:67], v[98:99]
	global_store_dwordx2 v[102:103], v[106:107], off nt
	v_addc_co_u32_e32 v105, vcc, 0, v103, vcc
	v_mov_b32_e32 v106, v94
	v_mov_b32_e32 v107, v95
	v_mov_b32_e32 v108, v96
	v_mov_b32_e32 v109, v97
	v_cvt_pk_bf16_f32 v98, v98, v99
	v_cvt_pk_bf16_f32 v99, v100, v101
	v_mov_b32_dpp v106, v90 row_ror:8 row_mask:0xf bank_mask:0xc
	v_mov_b32_dpp v90, v94 row_ror:8 row_mask:0xf bank_mask:0x3
	v_mov_b32_dpp v107, v91 row_ror:8 row_mask:0xf bank_mask:0xc
	v_mov_b32_dpp v91, v95 row_ror:8 row_mask:0xf bank_mask:0x3
	v_mov_b32_dpp v108, v92 row_ror:8 row_mask:0xf bank_mask:0xc
	v_mov_b32_dpp v92, v96 row_ror:8 row_mask:0xf bank_mask:0x3
	v_mov_b32_dpp v109, v93 row_ror:8 row_mask:0xf bank_mask:0xc
	s_and_b64 vcc, exec, s[40:41]
	v_mov_b32_dpp v93, v97 row_ror:8 row_mask:0xf bank_mask:0x3
	global_store_dwordx2 v[104:105], v[98:99], off nt
	s_cbranch_vccnz .LBB0_840
	v_add_co_u32_e32 v94, vcc, 0x4000, v112
	global_load_dwordx2 v[96:97], v[112:113], off offset:64 nt
	s_nop 0
	v_addc_co_u32_e32 v95, vcc, 0, v113, vcc
	global_load_dwordx2 v[100:101], v[94:95], off offset:64 nt
	s_waitcnt vmcnt(1)
	v_lshlrev_b32_e32 v94, 16, v96
	v_and_b32_e32 v95, 0xffff0000, v96
	v_lshlrev_b32_e32 v96, 16, v97
	v_and_b32_e32 v97, 0xffff0000, v97
	s_waitcnt vmcnt(0)
	v_lshlrev_b32_e32 v98, 16, v100
	v_and_b32_e32 v99, 0xffff0000, v100
	v_lshlrev_b32_e32 v100, 16, v101
	v_and_b32_e32 v101, 0xffff0000, v101
	s_cbranch_execnz .LBB0_802

.LBB0_802:
	s_waitcnt vmcnt(1)
	v_pk_add_f32 v[96:97], v[96:97], v[108:109]
	v_pk_add_f32 v[94:95], v[94:95], v[106:107]
	s_waitcnt vmcnt(0)
	v_pk_add_f32 v[90:91], v[98:99], v[90:91]
	v_pk_add_f32 v[96:97], v[56:57], v[96:97]
	v_pk_add_f32 v[94:95], v[54:55], v[94:95]
	v_pk_add_f32 v[92:93], v[100:101], v[92:93]
	v_pk_add_f32 v[90:91], v[54:55], v[90:91]
	v_pk_add_f32 v[92:93], v[56:57], v[92:93]
	v_cvt_pk_bf16_f32 v94, v94, v95
	v_cvt_pk_bf16_f32 v95, v96, v97
	v_cvt_pk_bf16_f32 v90, v90, v91
	v_cvt_pk_bf16_f32 v91, v92, v93
	global_store_dwordx2 v[102:103], v[94:95], off offset:64 nt
	global_store_dwordx2 v[104:105], v[90:91], off offset:64 nt
	v_or_b32_e32 v90, 48, v144
	v_ashrrev_i32_e32 v91, 31, v90
	v_lshlrev_b64 v[90:91], 10, v[90:91]
	v_lshl_add_u64 v[98:99], v[90:91], 0, v[142:143]
	v_mov_b32_e32 v100, v86
	v_mov_b32_e32 v101, v87
	v_mov_b32_e32 v102, v88
	v_mov_b32_e32 v103, v89
	v_mov_b32_dpp v100, v82 row_ror:8 row_mask:0xf bank_mask:0xc
	v_mov_b32_dpp v82, v86 row_ror:8 row_mask:0xf bank_mask:0x3
	v_mov_b32_dpp v101, v83 row_ror:8 row_mask:0xf bank_mask:0xc
	v_mov_b32_dpp v83, v87 row_ror:8 row_mask:0xf bank_mask:0x3
	v_mov_b32_dpp v102, v84 row_ror:8 row_mask:0xf bank_mask:0xc
	v_mov_b32_dpp v84, v88 row_ror:8 row_mask:0xf bank_mask:0x3
	v_mov_b32_dpp v103, v85 row_ror:8 row_mask:0xf bank_mask:0xc
	v_mov_b32_dpp v85, v89 row_ror:8 row_mask:0xf bank_mask:0x3
	s_and_b64 vcc, exec, s[40:41]
	v_lshl_add_u64 v[96:97], v[98:99], 1, s[46:47]
	s_cbranch_vccnz .LBB0_841
	v_add_co_u32_e32 v86, vcc, 0x4000, v96
	global_load_dwordx2 v[88:89], v[96:97], off nt
	s_nop 0
	v_addc_co_u32_e32 v87, vcc, 0, v97, vcc
	global_load_dwordx2 v[92:93], v[86:87], off nt
	s_waitcnt vmcnt(1)
	v_lshlrev_b32_e32 v86, 16, v88
	v_and_b32_e32 v87, 0xffff0000, v88
	v_lshlrev_b32_e32 v88, 16, v89
	v_and_b32_e32 v89, 0xffff0000, v89
	s_waitcnt vmcnt(0)
	v_lshlrev_b32_e32 v90, 16, v92
	v_and_b32_e32 v91, 0xffff0000, v92
	v_lshlrev_b32_e32 v92, 16, v93
	v_and_b32_e32 v93, 0xffff0000, v93
	v_lshl_add_u64 v[94:95], v[98:99], 2, s[46:47]
	s_cbranch_execnz .LBB0_805

.LBB0_805:
	s_waitcnt vmcnt(1)
	v_pk_add_f32 v[86:87], v[86:87], v[100:101]
	v_pk_add_f32 v[88:89], v[88:89], v[102:103]
	v_pk_add_f32 v[86:87], v[66:67], v[86:87]
	v_pk_add_f32 v[88:89], v[68:69], v[88:89]
	s_waitcnt vmcnt(0)
	v_pk_add_f32 v[82:83], v[90:91], v[82:83]
	v_cvt_pk_bf16_f32 v90, v86, v87
	v_lshl_add_u64 v[86:87], v[98:99], 1, s[50:51]
	s_movk_i32 s0, 0x4000
	v_pk_add_f32 v[84:85], v[92:93], v[84:85]
	v_cvt_pk_bf16_f32 v91, v88, v89
	v_add_co_u32_e32 v88, vcc, s0, v86
	v_pk_add_f32 v[84:85], v[68:69], v[84:85]
	v_pk_add_f32 v[82:83], v[66:67], v[82:83]
	global_store_dwordx2 v[86:87], v[90:91], off nt
	v_addc_co_u32_e32 v89, vcc, 0, v87, vcc
	v_mov_b32_e32 v90, v78
	v_mov_b32_e32 v91, v79
	v_mov_b32_e32 v92, v80
	v_mov_b32_e32 v93, v81
	v_cvt_pk_bf16_f32 v82, v82, v83
	v_cvt_pk_bf16_f32 v83, v84, v85
	v_mov_b32_dpp v90, v74 row_ror:8 row_mask:0xf bank_mask:0xc
	v_mov_b32_dpp v74, v78 row_ror:8 row_mask:0xf bank_mask:0x3
	v_mov_b32_dpp v91, v75 row_ror:8 row_mask:0xf bank_mask:0xc
	v_mov_b32_dpp v75, v79 row_ror:8 row_mask:0xf bank_mask:0x3
	v_mov_b32_dpp v92, v76 row_ror:8 row_mask:0xf bank_mask:0xc
	v_mov_b32_dpp v76, v80 row_ror:8 row_mask:0xf bank_mask:0x3
	v_mov_b32_dpp v93, v77 row_ror:8 row_mask:0xf bank_mask:0xc
	s_and_b64 vcc, exec, s[40:41]
	v_mov_b32_dpp v77, v81 row_ror:8 row_mask:0xf bank_mask:0x3
	global_store_dwordx2 v[88:89], v[82:83], off nt
	s_cbranch_vccnz .LBB0_842
	v_add_co_u32_e32 v78, vcc, 0x4000, v96
	global_load_dwordx2 v[80:81], v[96:97], off offset:64 nt
	s_nop 0
	v_addc_co_u32_e32 v79, vcc, 0, v97, vcc
	global_load_dwordx2 v[84:85], v[78:79], off offset:64 nt
	s_waitcnt vmcnt(1)
	v_lshlrev_b32_e32 v78, 16, v80
	v_and_b32_e32 v79, 0xffff0000, v80
	v_lshlrev_b32_e32 v80, 16, v81
	v_and_b32_e32 v81, 0xffff0000, v81
	s_waitcnt vmcnt(0)
	v_lshlrev_b32_e32 v82, 16, v84
	v_and_b32_e32 v83, 0xffff0000, v84
	v_lshlrev_b32_e32 v84, 16, v85
	v_and_b32_e32 v85, 0xffff0000, v85
	s_cbranch_execnz .LBB0_808

.LBB0_808:
	s_waitcnt vmcnt(1)
	v_pk_add_f32 v[80:81], v[80:81], v[92:93]
	v_pk_add_f32 v[78:79], v[78:79], v[90:91]
	s_waitcnt vmcnt(0)
	v_pk_add_f32 v[74:75], v[82:83], v[74:75]
	v_pk_add_f32 v[80:81], v[56:57], v[80:81]
	v_pk_add_f32 v[78:79], v[54:55], v[78:79]
	v_pk_add_f32 v[76:77], v[84:85], v[76:77]
	v_pk_add_f32 v[74:75], v[54:55], v[74:75]
	v_pk_add_f32 v[76:77], v[56:57], v[76:77]
	v_cvt_pk_bf16_f32 v78, v78, v79
	v_cvt_pk_bf16_f32 v79, v80, v81
	v_cvt_pk_bf16_f32 v74, v74, v75
	v_cvt_pk_bf16_f32 v75, v76, v77
	global_store_dwordx2 v[86:87], v[78:79], off offset:64 nt
	global_store_dwordx2 v[88:89], v[74:75], off offset:64 nt
	v_add_u32_e32 v74, 0x80, v144
	v_ashrrev_i32_e32 v75, 31, v74
	v_lshlrev_b64 v[74:75], 10, v[74:75]
	v_lshl_add_u64 v[82:83], v[74:75], 0, v[142:143]
	v_mov_b32_e32 v84, v70
	v_mov_b32_e32 v85, v71
	v_mov_b32_e32 v86, v72
	v_mov_b32_e32 v87, v73
	v_mov_b32_dpp v84, v62 row_ror:8 row_mask:0xf bank_mask:0xc
	v_mov_b32_dpp v62, v70 row_ror:8 row_mask:0xf bank_mask:0x3
	v_mov_b32_dpp v85, v63 row_ror:8 row_mask:0xf bank_mask:0xc
	v_mov_b32_dpp v63, v71 row_ror:8 row_mask:0xf bank_mask:0x3
	v_mov_b32_dpp v86, v64 row_ror:8 row_mask:0xf bank_mask:0xc
	v_mov_b32_dpp v64, v72 row_ror:8 row_mask:0xf bank_mask:0x3
	v_mov_b32_dpp v87, v65 row_ror:8 row_mask:0xf bank_mask:0xc
	v_mov_b32_dpp v65, v73 row_ror:8 row_mask:0xf bank_mask:0x3
	s_and_b64 vcc, exec, s[40:41]
	v_lshl_add_u64 v[80:81], v[82:83], 1, s[46:47]
	s_cbranch_vccnz .LBB0_843
	v_add_co_u32_e32 v70, vcc, 0x4000, v80
	global_load_dwordx2 v[72:73], v[80:81], off nt
	s_nop 0
	v_addc_co_u32_e32 v71, vcc, 0, v81, vcc
	global_load_dwordx2 v[76:77], v[70:71], off nt
	s_waitcnt vmcnt(1)
	v_lshlrev_b32_e32 v70, 16, v72
	v_and_b32_e32 v71, 0xffff0000, v72
	v_lshlrev_b32_e32 v72, 16, v73
	v_and_b32_e32 v73, 0xffff0000, v73
	s_waitcnt vmcnt(0)
	v_lshlrev_b32_e32 v74, 16, v76
	v_and_b32_e32 v75, 0xffff0000, v76
	v_lshlrev_b32_e32 v76, 16, v77
	v_and_b32_e32 v77, 0xffff0000, v77
	v_lshl_add_u64 v[78:79], v[82:83], 2, s[46:47]
	s_cbranch_execnz .LBB0_811

.LBB0_811:
	s_waitcnt vmcnt(1)
	v_pk_add_f32 v[70:71], v[70:71], v[84:85]
	v_pk_add_f32 v[72:73], v[72:73], v[86:87]
	v_pk_add_f32 v[70:71], v[66:67], v[70:71]
	v_pk_add_f32 v[72:73], v[68:69], v[72:73]
	s_waitcnt vmcnt(0)
	v_pk_add_f32 v[62:63], v[74:75], v[62:63]
	v_cvt_pk_bf16_f32 v74, v70, v71
	v_lshl_add_u64 v[70:71], v[82:83], 1, s[50:51]
	s_movk_i32 s0, 0x4000
	v_pk_add_f32 v[64:65], v[76:77], v[64:65]
	v_cvt_pk_bf16_f32 v75, v72, v73
	v_add_co_u32_e32 v72, vcc, s0, v70
	v_pk_add_f32 v[64:65], v[68:69], v[64:65]
	v_pk_add_f32 v[62:63], v[66:67], v[62:63]
	global_store_dwordx2 v[70:71], v[74:75], off nt
	v_addc_co_u32_e32 v73, vcc, 0, v71, vcc
	v_mov_b32_e32 v74, v58
	v_mov_b32_e32 v75, v59
	v_mov_b32_e32 v76, v60
	v_mov_b32_e32 v77, v61
	v_cvt_pk_bf16_f32 v62, v62, v63
	v_cvt_pk_bf16_f32 v63, v64, v65
	v_mov_b32_dpp v74, v50 row_ror:8 row_mask:0xf bank_mask:0xc
	v_mov_b32_dpp v50, v58 row_ror:8 row_mask:0xf bank_mask:0x3
	v_mov_b32_dpp v75, v51 row_ror:8 row_mask:0xf bank_mask:0xc
	v_mov_b32_dpp v51, v59 row_ror:8 row_mask:0xf bank_mask:0x3
	v_mov_b32_dpp v76, v52 row_ror:8 row_mask:0xf bank_mask:0xc
	v_mov_b32_dpp v52, v60 row_ror:8 row_mask:0xf bank_mask:0x3
	v_mov_b32_dpp v77, v53 row_ror:8 row_mask:0xf bank_mask:0xc
	s_and_b64 vcc, exec, s[40:41]
	v_mov_b32_dpp v53, v61 row_ror:8 row_mask:0xf bank_mask:0x3
	global_store_dwordx2 v[72:73], v[62:63], off nt
	s_cbranch_vccnz .LBB0_844
	v_add_co_u32_e32 v58, vcc, 0x4000, v80
	global_load_dwordx2 v[60:61], v[80:81], off offset:64 nt
	s_nop 0
	v_addc_co_u32_e32 v59, vcc, 0, v81, vcc
	global_load_dwordx2 v[64:65], v[58:59], off offset:64 nt
	s_waitcnt vmcnt(1)
	v_lshlrev_b32_e32 v58, 16, v60
	v_and_b32_e32 v59, 0xffff0000, v60
	v_lshlrev_b32_e32 v60, 16, v61
	v_and_b32_e32 v61, 0xffff0000, v61
	s_waitcnt vmcnt(0)
	v_lshlrev_b32_e32 v62, 16, v64
	v_and_b32_e32 v63, 0xffff0000, v64
	v_lshlrev_b32_e32 v64, 16, v65
	v_and_b32_e32 v65, 0xffff0000, v65
	s_cbranch_execnz .LBB0_814

.LBB0_814:
	s_waitcnt vmcnt(1)
	v_pk_add_f32 v[60:61], v[60:61], v[76:77]
	v_pk_add_f32 v[58:59], v[58:59], v[74:75]
	s_waitcnt vmcnt(0)
	v_pk_add_f32 v[50:51], v[62:63], v[50:51]
	v_pk_add_f32 v[60:61], v[56:57], v[60:61]
	v_pk_add_f32 v[58:59], v[54:55], v[58:59]
	v_pk_add_f32 v[52:53], v[64:65], v[52:53]
	v_pk_add_f32 v[50:51], v[54:55], v[50:51]
	v_pk_add_f32 v[52:53], v[56:57], v[52:53]
	v_cvt_pk_bf16_f32 v58, v58, v59
	v_cvt_pk_bf16_f32 v59, v60, v61
	v_cvt_pk_bf16_f32 v50, v50, v51
	v_cvt_pk_bf16_f32 v51, v52, v53
	global_store_dwordx2 v[70:71], v[58:59], off offset:64 nt
	global_store_dwordx2 v[72:73], v[50:51], off offset:64 nt
	v_add_u32_e32 v50, 0x90, v144
	v_ashrrev_i32_e32 v51, 31, v50
	v_lshlrev_b64 v[50:51], 10, v[50:51]
	v_lshl_add_u64 v[62:63], v[50:51], 0, v[142:143]
	v_mov_b32_e32 v64, v46
	v_mov_b32_e32 v65, v47
	v_mov_b32_e32 v70, v48
	v_mov_b32_e32 v71, v49
	v_mov_b32_dpp v64, v42 row_ror:8 row_mask:0xf bank_mask:0xc
	v_mov_b32_dpp v42, v46 row_ror:8 row_mask:0xf bank_mask:0x3
	v_mov_b32_dpp v65, v43 row_ror:8 row_mask:0xf bank_mask:0xc
	v_mov_b32_dpp v43, v47 row_ror:8 row_mask:0xf bank_mask:0x3
	v_mov_b32_dpp v70, v44 row_ror:8 row_mask:0xf bank_mask:0xc
	v_mov_b32_dpp v44, v48 row_ror:8 row_mask:0xf bank_mask:0x3
	v_mov_b32_dpp v71, v45 row_ror:8 row_mask:0xf bank_mask:0xc
	v_mov_b32_dpp v45, v49 row_ror:8 row_mask:0xf bank_mask:0x3
	s_and_b64 vcc, exec, s[40:41]
	v_lshl_add_u64 v[60:61], v[62:63], 1, s[46:47]
	s_cbranch_vccnz .LBB0_845
	v_add_co_u32_e32 v46, vcc, 0x4000, v60
	global_load_dwordx2 v[48:49], v[60:61], off nt
	s_nop 0
	v_addc_co_u32_e32 v47, vcc, 0, v61, vcc
	global_load_dwordx2 v[52:53], v[46:47], off nt
	s_waitcnt vmcnt(1)
	v_lshlrev_b32_e32 v46, 16, v48
	v_and_b32_e32 v47, 0xffff0000, v48
	v_lshlrev_b32_e32 v48, 16, v49
	v_and_b32_e32 v49, 0xffff0000, v49
	s_waitcnt vmcnt(0)
	v_lshlrev_b32_e32 v50, 16, v52
	v_and_b32_e32 v51, 0xffff0000, v52
	v_lshlrev_b32_e32 v52, 16, v53
	v_and_b32_e32 v53, 0xffff0000, v53
	v_lshl_add_u64 v[58:59], v[62:63], 2, s[46:47]
	s_cbranch_execnz .LBB0_817

.LBB0_817:
	s_waitcnt vmcnt(1)
	v_pk_add_f32 v[46:47], v[46:47], v[64:65]
	v_pk_add_f32 v[48:49], v[48:49], v[70:71]
	v_pk_add_f32 v[46:47], v[66:67], v[46:47]
	v_pk_add_f32 v[48:49], v[68:69], v[48:49]
	s_waitcnt vmcnt(0)
	v_pk_add_f32 v[42:43], v[50:51], v[42:43]
	v_cvt_pk_bf16_f32 v50, v46, v47
	v_lshl_add_u64 v[46:47], v[62:63], 1, s[50:51]
	s_movk_i32 s0, 0x4000
	v_pk_add_f32 v[44:45], v[52:53], v[44:45]
	v_cvt_pk_bf16_f32 v51, v48, v49
	v_add_co_u32_e32 v48, vcc, s0, v46
	v_pk_add_f32 v[44:45], v[68:69], v[44:45]
	v_pk_add_f32 v[42:43], v[66:67], v[42:43]
	global_store_dwordx2 v[46:47], v[50:51], off nt
	v_addc_co_u32_e32 v49, vcc, 0, v47, vcc
	v_mov_b32_e32 v50, v38
	v_mov_b32_e32 v51, v39
	v_mov_b32_e32 v52, v40
	v_mov_b32_e32 v53, v41
	v_cvt_pk_bf16_f32 v42, v42, v43
	v_cvt_pk_bf16_f32 v43, v44, v45
	v_mov_b32_dpp v50, v34 row_ror:8 row_mask:0xf bank_mask:0xc
	v_mov_b32_dpp v34, v38 row_ror:8 row_mask:0xf bank_mask:0x3
	v_mov_b32_dpp v51, v35 row_ror:8 row_mask:0xf bank_mask:0xc
	v_mov_b32_dpp v35, v39 row_ror:8 row_mask:0xf bank_mask:0x3
	v_mov_b32_dpp v52, v36 row_ror:8 row_mask:0xf bank_mask:0xc
	v_mov_b32_dpp v36, v40 row_ror:8 row_mask:0xf bank_mask:0x3
	v_mov_b32_dpp v53, v37 row_ror:8 row_mask:0xf bank_mask:0xc
	s_and_b64 vcc, exec, s[40:41]
	v_mov_b32_dpp v37, v41 row_ror:8 row_mask:0xf bank_mask:0x3
	global_store_dwordx2 v[48:49], v[42:43], off nt
	s_cbranch_vccnz .LBB0_846
	v_add_co_u32_e32 v38, vcc, 0x4000, v60
	global_load_dwordx2 v[40:41], v[60:61], off offset:64 nt
	s_nop 0
	v_addc_co_u32_e32 v39, vcc, 0, v61, vcc
	global_load_dwordx2 v[44:45], v[38:39], off offset:64 nt
	s_waitcnt vmcnt(1)
	v_lshlrev_b32_e32 v38, 16, v40
	v_and_b32_e32 v39, 0xffff0000, v40
	v_lshlrev_b32_e32 v40, 16, v41
	v_and_b32_e32 v41, 0xffff0000, v41
	s_waitcnt vmcnt(0)
	v_lshlrev_b32_e32 v42, 16, v44
	v_and_b32_e32 v43, 0xffff0000, v44
	v_lshlrev_b32_e32 v44, 16, v45
	v_and_b32_e32 v45, 0xffff0000, v45
	s_cbranch_execnz .LBB0_820

.LBB0_820:
	s_waitcnt vmcnt(1)
	v_pk_add_f32 v[40:41], v[40:41], v[52:53]
	v_pk_add_f32 v[38:39], v[38:39], v[50:51]
	s_waitcnt vmcnt(0)
	v_pk_add_f32 v[34:35], v[42:43], v[34:35]
	v_pk_add_f32 v[40:41], v[56:57], v[40:41]
	v_pk_add_f32 v[38:39], v[54:55], v[38:39]
	v_pk_add_f32 v[36:37], v[44:45], v[36:37]
	v_pk_add_f32 v[34:35], v[54:55], v[34:35]
	v_pk_add_f32 v[36:37], v[56:57], v[36:37]
	v_cvt_pk_bf16_f32 v38, v38, v39
	v_cvt_pk_bf16_f32 v39, v40, v41
	v_cvt_pk_bf16_f32 v34, v34, v35
	v_cvt_pk_bf16_f32 v35, v36, v37
	global_store_dwordx2 v[46:47], v[38:39], off offset:64 nt
	global_store_dwordx2 v[48:49], v[34:35], off offset:64 nt
	v_add_u32_e32 v34, 0xa0, v144
	v_ashrrev_i32_e32 v35, 31, v34
	v_lshlrev_b64 v[34:35], 10, v[34:35]
	v_lshl_add_u64 v[42:43], v[34:35], 0, v[142:143]
	v_mov_b32_e32 v44, v30
	v_mov_b32_e32 v45, v31
	v_mov_b32_e32 v46, v32
	v_mov_b32_e32 v47, v33
	v_mov_b32_dpp v44, v26 row_ror:8 row_mask:0xf bank_mask:0xc
	v_mov_b32_dpp v26, v30 row_ror:8 row_mask:0xf bank_mask:0x3
	v_mov_b32_dpp v45, v27 row_ror:8 row_mask:0xf bank_mask:0xc
	v_mov_b32_dpp v27, v31 row_ror:8 row_mask:0xf bank_mask:0x3
	v_mov_b32_dpp v46, v28 row_ror:8 row_mask:0xf bank_mask:0xc
	v_mov_b32_dpp v28, v32 row_ror:8 row_mask:0xf bank_mask:0x3
	v_mov_b32_dpp v47, v29 row_ror:8 row_mask:0xf bank_mask:0xc
	v_mov_b32_dpp v29, v33 row_ror:8 row_mask:0xf bank_mask:0x3
	s_and_b64 vcc, exec, s[40:41]
	v_lshl_add_u64 v[40:41], v[42:43], 1, s[46:47]
	s_cbranch_vccnz .LBB0_847
	v_add_co_u32_e32 v30, vcc, 0x4000, v40
	global_load_dwordx2 v[32:33], v[40:41], off nt
	s_nop 0
	v_addc_co_u32_e32 v31, vcc, 0, v41, vcc
	global_load_dwordx2 v[36:37], v[30:31], off nt
	s_waitcnt vmcnt(1)
	v_lshlrev_b32_e32 v30, 16, v32
	v_and_b32_e32 v31, 0xffff0000, v32
	v_lshlrev_b32_e32 v32, 16, v33
	v_and_b32_e32 v33, 0xffff0000, v33
	s_waitcnt vmcnt(0)
	v_lshlrev_b32_e32 v34, 16, v36
	v_and_b32_e32 v35, 0xffff0000, v36
	v_lshlrev_b32_e32 v36, 16, v37
	v_and_b32_e32 v37, 0xffff0000, v37
	v_lshl_add_u64 v[38:39], v[42:43], 2, s[46:47]
	s_cbranch_execnz .LBB0_823

.LBB0_823:
	s_waitcnt vmcnt(1)
	v_pk_add_f32 v[30:31], v[30:31], v[44:45]
	v_pk_add_f32 v[32:33], v[32:33], v[46:47]
	v_pk_add_f32 v[30:31], v[66:67], v[30:31]
	v_pk_add_f32 v[32:33], v[68:69], v[32:33]
	s_waitcnt vmcnt(0)
	v_pk_add_f32 v[26:27], v[34:35], v[26:27]
	v_cvt_pk_bf16_f32 v34, v30, v31
	v_lshl_add_u64 v[30:31], v[42:43], 1, s[50:51]
	s_movk_i32 s0, 0x4000
	v_pk_add_f32 v[28:29], v[36:37], v[28:29]
	v_cvt_pk_bf16_f32 v35, v32, v33
	v_add_co_u32_e32 v32, vcc, s0, v30
	v_pk_add_f32 v[28:29], v[68:69], v[28:29]
	v_pk_add_f32 v[26:27], v[66:67], v[26:27]
	global_store_dwordx2 v[30:31], v[34:35], off nt
	v_addc_co_u32_e32 v33, vcc, 0, v31, vcc
	v_mov_b32_e32 v34, v22
	v_mov_b32_e32 v35, v23
	v_mov_b32_e32 v36, v24
	v_mov_b32_e32 v37, v25
	v_cvt_pk_bf16_f32 v26, v26, v27
	v_cvt_pk_bf16_f32 v27, v28, v29
	v_mov_b32_dpp v34, v18 row_ror:8 row_mask:0xf bank_mask:0xc
	v_mov_b32_dpp v18, v22 row_ror:8 row_mask:0xf bank_mask:0x3
	v_mov_b32_dpp v35, v19 row_ror:8 row_mask:0xf bank_mask:0xc
	v_mov_b32_dpp v19, v23 row_ror:8 row_mask:0xf bank_mask:0x3
	v_mov_b32_dpp v36, v20 row_ror:8 row_mask:0xf bank_mask:0xc
	v_mov_b32_dpp v20, v24 row_ror:8 row_mask:0xf bank_mask:0x3
	v_mov_b32_dpp v37, v21 row_ror:8 row_mask:0xf bank_mask:0xc
	s_and_b64 vcc, exec, s[40:41]
	v_mov_b32_dpp v21, v25 row_ror:8 row_mask:0xf bank_mask:0x3
	global_store_dwordx2 v[32:33], v[26:27], off nt
	s_cbranch_vccnz .LBB0_848
	v_add_co_u32_e32 v22, vcc, 0x4000, v40
	global_load_dwordx2 v[24:25], v[40:41], off offset:64 nt
	s_nop 0
	v_addc_co_u32_e32 v23, vcc, 0, v41, vcc
	global_load_dwordx2 v[28:29], v[22:23], off offset:64 nt
	s_waitcnt vmcnt(1)
	v_lshlrev_b32_e32 v22, 16, v24
	v_and_b32_e32 v23, 0xffff0000, v24
	v_lshlrev_b32_e32 v24, 16, v25
	v_and_b32_e32 v25, 0xffff0000, v25
	s_waitcnt vmcnt(0)
	v_lshlrev_b32_e32 v26, 16, v28
	v_and_b32_e32 v27, 0xffff0000, v28
	v_lshlrev_b32_e32 v28, 16, v29
	v_and_b32_e32 v29, 0xffff0000, v29
	s_cbranch_execnz .LBB0_826

.LBB0_826:
	s_waitcnt vmcnt(1)
	v_pk_add_f32 v[24:25], v[24:25], v[36:37]
	v_pk_add_f32 v[22:23], v[22:23], v[34:35]
	s_waitcnt vmcnt(0)
	v_pk_add_f32 v[18:19], v[26:27], v[18:19]
	v_pk_add_f32 v[24:25], v[56:57], v[24:25]
	v_pk_add_f32 v[22:23], v[54:55], v[22:23]
	v_pk_add_f32 v[20:21], v[28:29], v[20:21]
	v_pk_add_f32 v[18:19], v[54:55], v[18:19]
	v_pk_add_f32 v[20:21], v[56:57], v[20:21]
	v_cvt_pk_bf16_f32 v22, v22, v23
	v_cvt_pk_bf16_f32 v23, v24, v25
	v_cvt_pk_bf16_f32 v18, v18, v19
	v_cvt_pk_bf16_f32 v19, v20, v21
	global_store_dwordx2 v[30:31], v[22:23], off offset:64 nt
	global_store_dwordx2 v[32:33], v[18:19], off offset:64 nt
	v_add_u32_e32 v18, 0xb0, v144
	v_ashrrev_i32_e32 v19, 31, v18
	v_lshlrev_b64 v[18:19], 10, v[18:19]
	v_lshl_add_u64 v[26:27], v[18:19], 0, v[142:143]
	v_mov_b32_e32 v28, v14
	v_mov_b32_e32 v29, v15
	v_mov_b32_e32 v30, v16
	v_mov_b32_e32 v31, v17
	v_mov_b32_dpp v28, v10 row_ror:8 row_mask:0xf bank_mask:0xc
	v_mov_b32_dpp v10, v14 row_ror:8 row_mask:0xf bank_mask:0x3
	v_mov_b32_dpp v29, v11 row_ror:8 row_mask:0xf bank_mask:0xc
	v_mov_b32_dpp v11, v15 row_ror:8 row_mask:0xf bank_mask:0x3
	v_mov_b32_dpp v30, v12 row_ror:8 row_mask:0xf bank_mask:0xc
	v_mov_b32_dpp v12, v16 row_ror:8 row_mask:0xf bank_mask:0x3
	v_mov_b32_dpp v31, v13 row_ror:8 row_mask:0xf bank_mask:0xc
	v_mov_b32_dpp v13, v17 row_ror:8 row_mask:0xf bank_mask:0x3
	s_and_b64 vcc, exec, s[40:41]
	v_lshl_add_u64 v[24:25], v[26:27], 1, s[46:47]
	s_cbranch_vccnz .LBB0_849
	v_add_co_u32_e32 v14, vcc, 0x4000, v24
	global_load_dwordx2 v[16:17], v[24:25], off nt
	s_nop 0
	v_addc_co_u32_e32 v15, vcc, 0, v25, vcc
	global_load_dwordx2 v[20:21], v[14:15], off nt
	s_waitcnt vmcnt(1)
	v_lshlrev_b32_e32 v14, 16, v16
	v_and_b32_e32 v15, 0xffff0000, v16
	v_lshlrev_b32_e32 v16, 16, v17
	v_and_b32_e32 v17, 0xffff0000, v17
	s_waitcnt vmcnt(0)
	v_lshlrev_b32_e32 v18, 16, v20
	v_and_b32_e32 v19, 0xffff0000, v20
	v_lshlrev_b32_e32 v20, 16, v21
	v_and_b32_e32 v21, 0xffff0000, v21
	v_lshl_add_u64 v[22:23], v[26:27], 2, s[46:47]
	s_cbranch_execnz .LBB0_829

.LBB0_829:
	s_waitcnt vmcnt(1)
	v_pk_add_f32 v[14:15], v[14:15], v[28:29]
	v_pk_add_f32 v[16:17], v[16:17], v[30:31]
	v_pk_add_f32 v[14:15], v[66:67], v[14:15]
	s_waitcnt vmcnt(0)
	v_pk_add_f32 v[12:13], v[20:21], v[12:13]
	v_pk_add_f32 v[10:11], v[18:19], v[10:11]
	v_pk_add_f32 v[16:17], v[68:69], v[16:17]
	v_pk_add_f32 v[12:13], v[68:69], v[12:13]
	v_pk_add_f32 v[10:11], v[66:67], v[10:11]
	v_cvt_pk_bf16_f32 v18, v14, v15
	v_lshl_add_u64 v[14:15], v[26:27], 1, s[50:51]
	s_movk_i32 s0, 0x4000
	v_cvt_pk_bf16_f32 v19, v16, v17
	v_cvt_pk_bf16_f32 v10, v10, v11
	v_cvt_pk_bf16_f32 v11, v12, v13
	v_add_co_u32_e32 v12, vcc, s0, v14
	global_store_dwordx2 v[14:15], v[18:19], off nt
	s_nop 0
	v_addc_co_u32_e32 v13, vcc, 0, v15, vcc
	v_mov_b32_e32 v16, v6
	v_mov_b32_e32 v17, v7
	v_mov_b32_e32 v18, v8
	v_mov_b32_e32 v19, v9
	v_mov_b32_dpp v16, v2 row_ror:8 row_mask:0xf bank_mask:0xc
	v_mov_b32_dpp v2, v6 row_ror:8 row_mask:0xf bank_mask:0x3
	v_mov_b32_dpp v17, v3 row_ror:8 row_mask:0xf bank_mask:0xc
	v_mov_b32_dpp v3, v7 row_ror:8 row_mask:0xf bank_mask:0x3
	v_mov_b32_dpp v18, v4 row_ror:8 row_mask:0xf bank_mask:0xc
	v_mov_b32_dpp v4, v8 row_ror:8 row_mask:0xf bank_mask:0x3
	v_mov_b32_dpp v19, v5 row_ror:8 row_mask:0xf bank_mask:0xc
	s_and_b64 vcc, exec, s[40:41]
	v_mov_b32_dpp v5, v9 row_ror:8 row_mask:0xf bank_mask:0x3
	global_store_dwordx2 v[12:13], v[10:11], off nt
	s_cbranch_vccnz .LBB0_850
	v_add_co_u32_e32 v6, vcc, 0x4000, v24
	global_load_dwordx2 v[8:9], v[24:25], off offset:64 nt
	s_nop 0
	v_addc_co_u32_e32 v7, vcc, 0, v25, vcc
	global_load_dwordx2 v[12:13], v[6:7], off offset:64 nt
	s_waitcnt vmcnt(1)
	v_lshlrev_b32_e32 v6, 16, v8
	v_and_b32_e32 v7, 0xffff0000, v8
	v_lshlrev_b32_e32 v8, 16, v9
	v_and_b32_e32 v9, 0xffff0000, v9
	s_waitcnt vmcnt(0)
	v_lshlrev_b32_e32 v10, 16, v12
	v_and_b32_e32 v11, 0xffff0000, v12
	v_lshlrev_b32_e32 v12, 16, v13
	v_and_b32_e32 v13, 0xffff0000, v13
	s_cbranch_execnz .LBB0_832

.LBB0_832:
	s_waitcnt vmcnt(0)
	v_pk_add_f32 v[4:5], v[12:13], v[4:5]
	v_pk_add_f32 v[2:3], v[10:11], v[2:3]
	v_pk_add_f32 v[8:9], v[8:9], v[18:19]
	v_pk_add_f32 v[6:7], v[6:7], v[16:17]
	v_pk_add_f32 v[4:5], v[56:57], v[4:5]
	v_pk_add_f32 v[2:3], v[54:55], v[2:3]
	v_pk_add_f32 v[8:9], v[56:57], v[8:9]
	v_pk_add_f32 v[6:7], v[54:55], v[6:7]
	v_cvt_pk_bf16_f32 v2, v2, v3
	v_cvt_pk_bf16_f32 v3, v4, v5
	v_add_co_u32_e32 v4, vcc, 0x4000, v14
	v_cvt_pk_bf16_f32 v6, v6, v7
	v_cvt_pk_bf16_f32 v7, v8, v9
	v_addc_co_u32_e32 v5, vcc, 0, v15, vcc
	global_store_dwordx2 v[14:15], v[6:7], off offset:64 nt
	global_store_dwordx2 v[4:5], v[2:3], off offset:64 nt
	s_and_b64 vcc, exec, s[38:39]
	s_mov_b64 s[0:1], -1
	s_cbranch_vccnz .LBB0_765
	s_andn2_b64 vcc, exec, s[48:49]
	s_cbranch_vccnz .LBB0_764
	s_barrier
	s_branch .LBB0_764

.LBB0_1251:
	s_nop 0
	v_mov_b32_e32 v56, v0
	s_and_b32 s1, s82, 0x400
	s_lshl_b32 s0, s85, 8
	v_and_b32_e32 v54, 15, v56
	s_add_i32 s1, s76, s1
	s_add_i32 s0, s0, s7
	v_lshl_add_u32 v132, v54, 2, s1
	v_or_b32_e32 v130, s0, v54
	ds_read2_b32 v[54:55], v132 offset1:16
	s_lshl_b32 s0, s84, 7
	s_and_b32 s0, s0, 0x780
	v_lshrrev_b32_e32 v56, 1, v56
	v_and_or_b32 v56, v56, 24, s0
	s_waitcnt lgkmcnt(0)
	v_mul_f32_e32 v54, 0x3b800000, v54
	v_pk_mul_f32 v[62:63], v[122:123], v[54:55] op_sel_hi:[1,0]
	v_pk_mul_f32 v[86:87], v[118:119], v[54:55] op_sel_hi:[1,0]
	v_mul_f32_e32 v92, 0xbfb8aa3b, v62
	v_exp_f32_e32 v118, v92
	v_pk_mul_f32 v[92:93], v[116:117], v[54:55] op_sel_hi:[1,0]
	v_mul_f32_e32 v116, 0xbfb8aa3b, v63
	v_exp_f32_e32 v116, v116
	v_or_b32_e32 v206, s6, v56
	v_pk_mul_f32 v[56:57], v[124:125], v[54:55] op_sel_hi:[1,0]
	v_pk_mul_f32 v[64:65], v[120:121], v[54:55] op_sel_hi:[1,0]
	v_pk_mul_f32 v[88:89], v[128:129], v[54:55] op_sel_hi:[1,0]
	v_pk_mul_f32 v[90:91], v[126:127], v[54:55] op_sel_hi:[1,0]
	v_add_f32_e32 v117, 1.0, v118
	v_pk_mul_f32 v[114:115], v[114:115], v[54:55] op_sel_hi:[1,0]
	v_add_f32_e32 v54, 1.0, v116
	v_rcp_f32_e32 v117, v117
	v_rcp_f32_e32 v54, v54
	v_ashrrev_i32_e32 v131, 31, v130
	s_mov_b32 s0, 0x40000
	v_mul_f32_e32 v62, v62, v117
	v_mul_f32_e32 v54, v63, v54
	v_mul_f32_e32 v63, 0xbfb8aa3b, v56
	v_mul_f32_e32 v62, v90, v62
	v_exp_f32_e32 v63, v63
	v_mul_f32_e32 v90, 0xbfb8aa3b, v57
	v_exp_f32_e32 v90, v90
	v_mul_f32_e32 v62, 0x41000000, v62
	v_add_f32_e32 v63, 1.0, v63
	v_rcp_f32_e32 v63, v63
	v_add_f32_e32 v90, 1.0, v90
	v_rcp_f32_e32 v90, v90
	v_mul_f32_e32 v54, v91, v54
	v_mul_f32_e32 v56, v56, v63
	v_mul_f32_e32 v54, 0x41000000, v54
	v_mul_f32_e32 v56, v88, v56
	v_mul_f32_e32 v57, v57, v90
	v_min_f32_e64 v63, |v62|, s33
	v_mul_f32_e32 v88, 0xbfb8aa3b, v86
	v_mul_f32_e32 v56, 0x41000000, v56
	v_mul_f32_e32 v57, v89, v57
	v_bfi_b32 v62, s2, v63, v62
	v_min_f32_e64 v63, |v54|, s33
	v_exp_f32_e32 v88, v88
	v_mul_f32_e32 v57, 0x41000000, v57
	v_bfi_b32 v54, s2, v63, v54
	v_min_f32_e64 v63, |v56|, s33
	v_bfi_b32 v63, s2, v63, v56
	v_min_f32_e64 v56, |v57|, s33
	v_bfi_b32 v57, s2, v56, v57
	v_mov_b32_e32 v56, v207
	v_cvt_pk_fp8_f32 v56, v62, v54
	v_add_f32_e32 v62, 1.0, v88
	v_rcp_f32_e32 v62, v62
	v_mul_f32_e32 v54, 0xbfb8aa3b, v87
	v_exp_f32_e32 v54, v54
	v_cvt_pk_fp8_f32 v56, v63, v57 op_sel:[0,0,1]
	v_mul_f32_e32 v57, v86, v62
	v_mul_f32_e32 v62, 0xbfb8aa3b, v64
	v_exp_f32_e32 v62, v62
	v_mul_f32_e32 v63, 0xbfb8aa3b, v65
	v_add_f32_e32 v54, 1.0, v54
	v_exp_f32_e32 v63, v63
	v_rcp_f32_e32 v54, v54
	v_add_f32_e32 v62, 1.0, v62
	v_rcp_f32_e32 v62, v62
	v_add_f32_e32 v63, 1.0, v63
	v_mul_f32_e32 v57, v114, v57
	v_mul_f32_e32 v54, v87, v54
	v_rcp_f32_e32 v63, v63
	v_mul_f32_e32 v57, 0x41000000, v57
	v_mul_f32_e32 v54, v115, v54
	v_mul_f32_e32 v54, 0x41000000, v54
	v_mul_f32_e32 v62, v64, v62
	v_min_f32_e64 v64, |v57|, s33
	v_bfi_b32 v64, s2, v64, v57
	v_min_f32_e64 v57, |v54|, s33
	v_mul_f32_e32 v62, v92, v62
	v_mul_f32_e32 v63, v65, v63
	v_bfi_b32 v54, s2, v57, v54
	v_mov_b32_e32 v57, v207
	v_mul_f32_e32 v62, 0x41000000, v62
	v_mul_f32_e32 v63, v93, v63
	v_cvt_pk_fp8_f32 v57, v64, v54
	v_mul_f32_e32 v63, 0x41000000, v63
	v_min_f32_e64 v65, |v62|, s33
	v_bfi_b32 v54, s2, v65, v62
	v_min_f32_e64 v62, |v63|, s33
	v_bfi_b32 v62, s2, v62, v63
	v_cvt_pk_fp8_f32 v57, v54, v62 op_sel:[0,0,1]
	v_lshlrev_b64 v[62:63], 11, v[130:131]
	v_mul_f32_e32 v54, 0x3b800000, v55
	v_lshl_add_u64 v[62:63], s[50:51], 0, v[62:63]
	v_pk_mul_f32 v[64:65], v[106:107], v[54:55] op_sel_hi:[1,0]
	v_lshl_add_u64 v[114:115], v[62:63], 0, v[206:207]
	v_pk_mul_f32 v[62:63], v[108:109], v[54:55] op_sel_hi:[1,0]
	v_pk_mul_f32 v[86:87], v[104:105], v[54:55] op_sel_hi:[1,0]
	v_pk_mul_f32 v[88:89], v[102:103], v[54:55] op_sel_hi:[1,0]
	v_pk_mul_f32 v[90:91], v[112:113], v[54:55] op_sel_hi:[1,0]
	v_pk_mul_f32 v[92:93], v[110:111], v[54:55] op_sel_hi:[1,0]
	v_mul_f32_e32 v55, 0xbfb8aa3b, v64
	v_exp_f32_e32 v55, v55
	v_mul_f32_e32 v102, 0xbfb8aa3b, v65
	v_exp_f32_e32 v102, v102
	global_store_dwordx2 v[114:115], v[56:57], off nt
	v_pk_mul_f32 v[100:101], v[100:101], v[54:55] op_sel_hi:[1,0]
	v_add_f32_e32 v55, 1.0, v55
	v_rcp_f32_e32 v103, v55
	v_pk_mul_f32 v[54:55], v[98:99], v[54:55] op_sel_hi:[1,0]
	v_add_f32_e32 v98, 1.0, v102
	v_rcp_f32_e32 v98, v98
	v_mul_f32_e32 v64, v64, v103
	v_mul_f32_e32 v64, v92, v64
	v_mul_f32_e32 v92, 0xbfb8aa3b, v62
	v_mul_f32_e32 v65, v65, v98
	v_exp_f32_e32 v92, v92
	v_mul_f32_e32 v65, v93, v65
	v_mul_f32_e32 v93, 0xbfb8aa3b, v63
	v_exp_f32_e32 v93, v93
	v_add_f32_e32 v92, 1.0, v92
	v_rcp_f32_e32 v92, v92
	v_mul_f32_e32 v64, 0x41000000, v64
	v_add_f32_e32 v93, 1.0, v93
	v_rcp_f32_e32 v93, v93
	v_mul_f32_e32 v62, v62, v92
	v_mul_f32_e32 v65, 0x41000000, v65
	v_mul_f32_e32 v62, v90, v62
	v_mul_f32_e32 v63, v63, v93
	v_min_f32_e64 v90, |v64|, s33
	v_mul_f32_e32 v62, 0x41000000, v62
	v_mul_f32_e32 v63, v91, v63
	v_bfi_b32 v64, s2, v90, v64
	v_min_f32_e64 v90, |v65|, s33
	v_mul_f32_e32 v63, 0x41000000, v63
	v_bfi_b32 v65, s2, v90, v65
	v_min_f32_e64 v90, |v62|, s33
	v_bfi_b32 v90, s2, v90, v62
	v_min_f32_e64 v62, |v63|, s33
	v_bfi_b32 v63, s2, v62, v63
	v_mov_b32_e32 v62, v207
	v_cvt_pk_fp8_f32 v62, v64, v65
	v_mul_f32_e32 v64, 0xbfb8aa3b, v89
	v_exp_f32_e32 v64, v64
	v_mul_f32_e32 v91, 0xbfb8aa3b, v88
	v_exp_f32_e32 v91, v91
	v_cvt_pk_fp8_f32 v62, v90, v63 op_sel:[0,0,1]
	v_add_f32_e32 v63, 1.0, v64
	v_rcp_f32_e32 v63, v63
	v_add_f32_e32 v65, 1.0, v91
	v_rcp_f32_e32 v65, v65
	v_or_b32_e32 v56, 16, v130
	v_mul_f32_e32 v63, v89, v63
	v_mul_f32_e32 v55, v55, v63
	v_mul_f32_e32 v63, 0xbfb8aa3b, v87
	v_exp_f32_e32 v63, v63
	v_mul_f32_e32 v64, v88, v65
	v_mul_f32_e32 v54, v54, v64
	v_mul_f32_e32 v64, 0xbfb8aa3b, v86
	v_exp_f32_e32 v64, v64
	v_add_f32_e32 v63, 1.0, v63
	v_rcp_f32_e32 v63, v63
	v_mul_f32_e32 v54, 0x41000000, v54
	v_add_f32_e32 v64, 1.0, v64
	v_rcp_f32_e32 v64, v64
	v_mul_f32_e32 v63, v87, v63
	v_mul_f32_e32 v63, v101, v63
	v_mul_f32_e32 v55, 0x41000000, v55
	v_mul_f32_e32 v65, 0x41000000, v63
	v_min_f32_e64 v63, |v54|, s33
	v_bfi_b32 v54, s2, v63, v54
	v_min_f32_e64 v63, |v55|, s33
	v_mul_f32_e32 v64, v86, v64
	v_bfi_b32 v55, s2, v63, v55
	v_mov_b32_e32 v63, v207
	v_mul_f32_e32 v64, v100, v64
	v_cvt_pk_fp8_f32 v63, v54, v55
	v_mul_f32_e32 v64, 0x41000000, v64
	v_ashrrev_i32_e32 v57, 31, v56
	v_min_f32_e64 v86, |v64|, s33
	v_min_f32_e64 v55, |v65|, s33
	v_lshlrev_b64 v[56:57], 11, v[56:57]
	v_bfi_b32 v54, s2, v86, v64
	v_bfi_b32 v55, s2, v55, v65
	v_cvt_pk_fp8_f32 v63, v54, v55 op_sel:[0,0,1]
	v_lshl_add_u64 v[54:55], s[50:51], 0, v[56:57]
	ds_read2_b32 v[56:57], v132 offset0:32 offset1:48
	v_lshl_add_u64 v[54:55], v[54:55], 0, v[206:207]
	global_store_dwordx2 v[54:55], v[62:63], off nt
	v_or_b32_e32 v54, 32, v130
	v_ashrrev_i32_e32 v55, 31, v54
	s_waitcnt lgkmcnt(0)
	v_mul_f32_e32 v56, 0x3b800000, v56
	v_pk_mul_f32 v[58:59], v[58:59], v[56:57] op_sel_hi:[1,0]
	v_pk_mul_f32 v[60:61], v[60:61], v[56:57] op_sel_hi:[1,0]
	v_mul_f32_e32 v86, 0xbfb8aa3b, v58
	v_mul_f32_e32 v87, 0xbfb8aa3b, v59
	v_exp_f32_e32 v86, v86
	v_exp_f32_e32 v87, v87
	v_pk_mul_f32 v[12:13], v[12:13], v[56:57] op_sel_hi:[1,0]
	v_pk_mul_f32 v[10:11], v[10:11], v[56:57] op_sel_hi:[1,0]
	v_pk_mul_f32 v[62:63], v[96:97], v[56:57] op_sel_hi:[1,0]
	v_pk_mul_f32 v[64:65], v[94:95], v[56:57] op_sel_hi:[1,0]
	v_pk_mul_f32 v[84:85], v[84:85], v[56:57] op_sel_hi:[1,0]
	v_add_f32_e32 v86, 1.0, v86
	v_pk_mul_f32 v[82:83], v[82:83], v[56:57] op_sel_hi:[1,0]
	v_add_f32_e32 v56, 1.0, v87
	v_rcp_f32_e32 v86, v86
	v_rcp_f32_e32 v56, v56
	v_mov_b64_e32 v[226:227], v[250:251]
	v_mov_b64_e32 v[250:251], v[232:233]
	v_mul_f32_e32 v58, v58, v86
	v_mul_f32_e32 v56, v59, v56
	v_mul_f32_e32 v59, 0xbfb8aa3b, v60
	v_mul_f32_e32 v58, v64, v58
	v_exp_f32_e32 v59, v59
	v_mul_f32_e32 v64, 0xbfb8aa3b, v61
	v_exp_f32_e32 v64, v64
	v_mul_f32_e32 v58, 0x41000000, v58
	v_add_f32_e32 v59, 1.0, v59
	v_rcp_f32_e32 v59, v59
	v_add_f32_e32 v64, 1.0, v64
	v_rcp_f32_e32 v64, v64
	v_mul_f32_e32 v56, v65, v56
	v_mul_f32_e32 v59, v60, v59
	v_mul_f32_e32 v56, 0x41000000, v56
	v_mul_f32_e32 v59, v62, v59
	v_mul_f32_e32 v60, v61, v64
	v_min_f32_e64 v61, |v58|, s33
	v_mul_f32_e32 v59, 0x41000000, v59
	v_mul_f32_e32 v60, v63, v60
	v_bfi_b32 v61, s2, v61, v58
	v_min_f32_e64 v58, |v56|, s33
	v_mul_f32_e32 v60, 0x41000000, v60
	v_bfi_b32 v56, s2, v58, v56
	v_min_f32_e64 v58, |v59|, s33
	v_bfi_b32 v59, s2, v58, v59
	v_min_f32_e64 v58, |v60|, s33
	v_bfi_b32 v60, s2, v58, v60
	v_mov_b32_e32 v58, v207
	v_cvt_pk_fp8_f32 v58, v61, v56
	v_mul_f32_e32 v56, 0xbfb8aa3b, v11
	v_exp_f32_e32 v56, v56
	v_mul_f32_e32 v62, 0xbfb8aa3b, v10
	v_exp_f32_e32 v62, v62
	v_cvt_pk_fp8_f32 v58, v59, v60 op_sel:[0,0,1]
	v_add_f32_e32 v56, 1.0, v56
	v_rcp_f32_e32 v56, v56
	v_add_f32_e32 v61, 1.0, v62
	v_mul_f32_e32 v59, 0xbfb8aa3b, v13
	v_rcp_f32_e32 v61, v61
	v_mul_f32_e32 v11, v11, v56
	v_mul_f32_e32 v56, 0xbfb8aa3b, v12
	v_exp_f32_e32 v56, v56
	v_exp_f32_e32 v59, v59
	v_mul_f32_e32 v10, v10, v61
	v_mul_f32_e32 v10, v82, v10
	v_add_f32_e32 v56, 1.0, v56
	v_rcp_f32_e32 v56, v56
	v_add_f32_e32 v59, 1.0, v59
	v_rcp_f32_e32 v59, v59
	v_mul_f32_e32 v10, 0x41000000, v10
	v_mul_f32_e32 v11, v83, v11
	v_mul_f32_e32 v11, 0x41000000, v11
	v_mul_f32_e32 v12, v12, v56
	v_min_f32_e64 v56, |v10|, s33
	v_bfi_b32 v10, s2, v56, v10
	v_min_f32_e64 v56, |v11|, s33
	v_mul_f32_e32 v13, v13, v59
	v_bfi_b32 v11, s2, v56, v11
	v_mov_b32_e32 v59, v207
	v_mul_f32_e32 v12, v84, v12
	v_mul_f32_e32 v13, v85, v13
	v_cvt_pk_fp8_f32 v59, v10, v11
	v_mul_f32_e32 v12, 0x41000000, v12
	v_mul_f32_e32 v13, 0x41000000, v13
	v_min_f32_e64 v56, |v12|, s33
	v_min_f32_e64 v11, |v13|, s33
	v_bfi_b32 v10, s2, v56, v12
	v_bfi_b32 v11, s2, v11, v13
	v_cvt_pk_fp8_f32 v59, v10, v11 op_sel:[0,0,1]
	v_lshlrev_b64 v[10:11], 11, v[54:55]
	v_lshl_add_u64 v[10:11], s[50:51], 0, v[10:11]
	v_mul_f32_e32 v12, 0x3b800000, v57
	v_lshl_add_u64 v[10:11], v[10:11], 0, v[206:207]
	v_pk_mul_f32 v[56:57], v[74:75], v[12:13] op_sel_hi:[1,0]
	global_store_dwordx2 v[10:11], v[58:59], off nt
	v_pk_mul_f32 v[54:55], v[76:77], v[12:13] op_sel_hi:[1,0]
	v_pk_mul_f32 v[58:59], v[72:73], v[12:13] op_sel_hi:[1,0]
	v_pk_mul_f32 v[60:61], v[70:71], v[12:13] op_sel_hi:[1,0]
	v_pk_mul_f32 v[62:63], v[80:81], v[12:13] op_sel_hi:[1,0]
	v_pk_mul_f32 v[64:65], v[78:79], v[12:13] op_sel_hi:[1,0]
	v_mul_f32_e32 v13, 0xbfb8aa3b, v56
	v_exp_f32_e32 v13, v13
	v_mul_f32_e32 v70, 0xbfb8aa3b, v57
	v_exp_f32_e32 v70, v70
	v_or_b32_e32 v10, 48, v130
	v_pk_mul_f32 v[68:69], v[68:69], v[12:13] op_sel_hi:[1,0]
	v_add_f32_e32 v13, 1.0, v13
	v_rcp_f32_e32 v71, v13
	v_pk_mul_f32 v[12:13], v[66:67], v[12:13] op_sel_hi:[1,0]
	v_add_f32_e32 v66, 1.0, v70
	v_rcp_f32_e32 v66, v66
	v_mul_f32_e32 v56, v56, v71
	v_mul_f32_e32 v56, v64, v56
	v_mul_f32_e32 v64, 0xbfb8aa3b, v54
	v_mul_f32_e32 v57, v57, v66
	v_exp_f32_e32 v64, v64
	v_mul_f32_e32 v57, v65, v57
	v_mul_f32_e32 v65, 0xbfb8aa3b, v55
	v_exp_f32_e32 v65, v65
	v_add_f32_e32 v64, 1.0, v64
	v_rcp_f32_e32 v64, v64
	v_mul_f32_e32 v56, 0x41000000, v56
	v_add_f32_e32 v65, 1.0, v65
	v_rcp_f32_e32 v65, v65
	v_mul_f32_e32 v54, v54, v64
	v_mul_f32_e32 v57, 0x41000000, v57
	v_mul_f32_e32 v54, v62, v54
	v_mul_f32_e32 v55, v55, v65
	v_min_f32_e64 v62, |v56|, s33
	v_mul_f32_e32 v54, 0x41000000, v54
	v_mul_f32_e32 v55, v63, v55
	v_bfi_b32 v56, s2, v62, v56
	v_min_f32_e64 v62, |v57|, s33
	v_mul_f32_e32 v55, 0x41000000, v55
	v_bfi_b32 v57, s2, v62, v57
	v_min_f32_e64 v62, |v54|, s33
	v_bfi_b32 v62, s2, v62, v54
	v_min_f32_e64 v54, |v55|, s33
	v_bfi_b32 v55, s2, v54, v55
	v_mov_b32_e32 v54, v207
	v_cvt_pk_fp8_f32 v54, v56, v57
	v_mul_f32_e32 v56, 0xbfb8aa3b, v61
	v_exp_f32_e32 v56, v56
	v_mul_f32_e32 v63, 0xbfb8aa3b, v60
	v_exp_f32_e32 v63, v63
	v_cvt_pk_fp8_f32 v54, v62, v55 op_sel:[0,0,1]
	v_add_f32_e32 v55, 1.0, v56
	v_rcp_f32_e32 v55, v55
	v_add_f32_e32 v57, 1.0, v63
	v_rcp_f32_e32 v57, v57
	v_ashrrev_i32_e32 v11, 31, v10
	v_mul_f32_e32 v55, v61, v55
	v_mul_f32_e32 v13, v13, v55
	v_mul_f32_e32 v55, 0xbfb8aa3b, v59
	v_exp_f32_e32 v55, v55
	v_mul_f32_e32 v56, v60, v57
	v_mul_f32_e32 v12, v12, v56
	v_mul_f32_e32 v56, 0xbfb8aa3b, v58
	v_exp_f32_e32 v56, v56
	v_add_f32_e32 v55, 1.0, v55
	v_rcp_f32_e32 v55, v55
	v_mul_f32_e32 v12, 0x41000000, v12
	v_add_f32_e32 v56, 1.0, v56
	v_rcp_f32_e32 v56, v56
	v_mul_f32_e32 v55, v59, v55
	v_mul_f32_e32 v55, v69, v55
	v_mul_f32_e32 v13, 0x41000000, v13
	v_mul_f32_e32 v57, 0x41000000, v55
	v_min_f32_e64 v55, |v12|, s33
	v_bfi_b32 v12, s2, v55, v12
	v_min_f32_e64 v55, |v13|, s33
	v_mul_f32_e32 v56, v58, v56
	v_bfi_b32 v13, s2, v55, v13
	v_mov_b32_e32 v55, v207
	v_mul_f32_e32 v56, v68, v56
	v_cvt_pk_fp8_f32 v55, v12, v13
	v_mul_f32_e32 v56, 0x41000000, v56
	v_min_f32_e64 v58, |v56|, s33
	v_min_f32_e64 v13, |v57|, s33
	v_bfi_b32 v12, s2, v58, v56
	v_bfi_b32 v13, s2, v13, v57
	v_cvt_pk_fp8_f32 v55, v12, v13 op_sel:[0,0,1]
	ds_read2_b32 v[12:13], v132 offset0:128 offset1:144
	v_lshlrev_b64 v[10:11], 11, v[10:11]
	v_lshl_add_u64 v[10:11], s[50:51], 0, v[10:11]
	v_lshl_add_u64 v[10:11], v[10:11], 0, v[206:207]
	global_store_dwordx2 v[10:11], v[54:55], off nt
	s_waitcnt lgkmcnt(0)
	v_mul_f32_e32 v10, 0x3b800000, v12
	v_pk_mul_f32 v[56:57], v[178:179], v[10:11] op_sel_hi:[1,0]
	v_pk_mul_f32 v[54:55], v[180:181], v[10:11] op_sel_hi:[1,0]
	v_pk_mul_f32 v[58:59], v[176:177], v[10:11] op_sel_hi:[1,0]
	v_pk_mul_f32 v[60:61], v[174:175], v[10:11] op_sel_hi:[1,0]
	v_pk_mul_f32 v[62:63], v[184:185], v[10:11] op_sel_hi:[1,0]
	v_pk_mul_f32 v[64:65], v[182:183], v[10:11] op_sel_hi:[1,0]
	v_mul_f32_e32 v11, 0xbfb8aa3b, v56
	v_exp_f32_e32 v11, v11
	v_mul_f32_e32 v12, 0xbfb8aa3b, v57
	v_exp_f32_e32 v12, v12
	v_pk_mul_f32 v[52:53], v[52:53], v[10:11] op_sel_hi:[1,0]
	v_add_f32_e32 v11, 1.0, v11
	v_rcp_f32_e32 v66, v11
	v_pk_mul_f32 v[10:11], v[50:51], v[10:11] op_sel_hi:[1,0]
	v_mul_f32_e32 v51, 0xbfb8aa3b, v54
	v_exp_f32_e32 v51, v51
	v_mul_f32_e32 v50, v56, v66
	v_mul_f32_e32 v56, 0xbfb8aa3b, v55
	v_exp_f32_e32 v56, v56
	v_add_f32_e32 v12, 1.0, v12
	v_rcp_f32_e32 v12, v12
	v_add_f32_e32 v51, 1.0, v51
	v_rcp_f32_e32 v51, v51
	v_add_f32_e32 v56, 1.0, v56
	v_rcp_f32_e32 v56, v56
	v_mul_f32_e32 v50, v64, v50
	v_mul_f32_e32 v12, v57, v12
	v_mul_f32_e32 v50, 0x41000000, v50
	v_mul_f32_e32 v12, v65, v12
	v_mul_f32_e32 v51, v54, v51
	v_mul_f32_e32 v12, 0x41000000, v12
	v_mul_f32_e32 v51, v62, v51
	v_mul_f32_e32 v54, v55, v56
	v_min_f32_e64 v55, |v50|, s33
	v_mul_f32_e32 v51, 0x41000000, v51
	v_mul_f32_e32 v54, v63, v54
	v_bfi_b32 v55, s2, v55, v50
	v_min_f32_e64 v50, |v12|, s33
	v_mul_f32_e32 v56, 0xbfb8aa3b, v60
	v_mul_f32_e32 v54, 0x41000000, v54
	v_bfi_b32 v12, s2, v50, v12
	v_min_f32_e64 v50, |v51|, s33
	v_exp_f32_e32 v56, v56
	v_bfi_b32 v51, s2, v50, v51
	v_min_f32_e64 v50, |v54|, s33
	v_bfi_b32 v54, s2, v50, v54
	v_mov_b32_e32 v50, v207
	v_cvt_pk_fp8_f32 v50, v55, v12
	v_mul_f32_e32 v12, 0xbfb8aa3b, v61
	v_exp_f32_e32 v12, v12
	v_add_f32_e32 v55, 1.0, v56
	v_rcp_f32_e32 v55, v55
	v_cvt_pk_fp8_f32 v50, v51, v54 op_sel:[0,0,1]
	v_add_f32_e32 v12, 1.0, v12
	v_rcp_f32_e32 v12, v12
	v_mul_f32_e32 v51, v60, v55
	v_mul_f32_e32 v10, v10, v51
	v_mul_f32_e32 v51, 0xbfb8aa3b, v58
	v_exp_f32_e32 v51, v51
	v_mul_f32_e32 v12, v61, v12
	v_mul_f32_e32 v11, v11, v12
	v_mul_f32_e32 v12, 0xbfb8aa3b, v59
	v_exp_f32_e32 v12, v12
	v_add_f32_e32 v51, 1.0, v51
	v_rcp_f32_e32 v51, v51
	v_mul_f32_e32 v10, 0x41000000, v10
	v_add_f32_e32 v12, 1.0, v12
	v_rcp_f32_e32 v12, v12
	v_mul_f32_e32 v51, v58, v51
	v_mul_f32_e32 v51, v52, v51
	v_mul_f32_e32 v11, 0x41000000, v11
	v_mul_f32_e32 v52, 0x41000000, v51
	v_min_f32_e64 v51, |v10|, s33
	v_bfi_b32 v10, s2, v51, v10
	v_min_f32_e64 v51, |v11|, s33
	v_mul_f32_e32 v12, v59, v12
	v_bfi_b32 v11, s2, v51, v11
	v_mov_b32_e32 v51, v207
	v_mul_f32_e32 v12, v53, v12
	v_cvt_pk_fp8_f32 v51, v10, v11
	v_mul_f32_e32 v12, 0x41000000, v12
	v_min_f32_e64 v53, |v52|, s33
	v_min_f32_e64 v11, |v12|, s33
	v_bfi_b32 v10, s2, v53, v52
	v_bfi_b32 v11, s2, v11, v12
	v_cvt_pk_fp8_f32 v51, v10, v11 op_sel:[0,0,1]
	v_add_co_u32_e32 v10, vcc, s0, v114
	s_mov_b32 s0, 0x48000
	s_nop 0
	v_addc_co_u32_e32 v11, vcc, 0, v115, vcc
	global_store_dwordx2 v[10:11], v[50:51], off nt
	v_mul_f32_e32 v10, 0x3b800000, v13
	v_pk_mul_f32 v[42:43], v[42:43], v[10:11] op_sel_hi:[1,0]
	v_pk_mul_f32 v[12:13], v[44:45], v[10:11] op_sel_hi:[1,0]
	v_pk_mul_f32 v[40:41], v[40:41], v[10:11] op_sel_hi:[1,0]
	v_pk_mul_f32 v[38:39], v[38:39], v[10:11] op_sel_hi:[1,0]
	v_pk_mul_f32 v[44:45], v[48:49], v[10:11] op_sel_hi:[1,0]
	v_pk_mul_f32 v[46:47], v[46:47], v[10:11] op_sel_hi:[1,0]
	v_mul_f32_e32 v11, 0xbfb8aa3b, v42
	v_exp_f32_e32 v11, v11
	v_mul_f32_e32 v48, 0xbfb8aa3b, v43
	v_exp_f32_e32 v48, v48
	v_pk_mul_f32 v[36:37], v[36:37], v[10:11] op_sel_hi:[1,0]
	v_add_f32_e32 v11, 1.0, v11
	v_rcp_f32_e32 v49, v11
	v_pk_mul_f32 v[10:11], v[34:35], v[10:11] op_sel_hi:[1,0]
	v_add_f32_e32 v34, 1.0, v48
	v_rcp_f32_e32 v34, v34
	v_mul_f32_e32 v35, v42, v49
	v_mul_f32_e32 v42, 0xbfb8aa3b, v12
	v_exp_f32_e32 v42, v42
	v_mul_f32_e32 v34, v43, v34
	v_mul_f32_e32 v43, 0xbfb8aa3b, v13
	v_exp_f32_e32 v43, v43
	v_add_f32_e32 v42, 1.0, v42
	v_rcp_f32_e32 v42, v42
	v_mul_f32_e32 v35, v46, v35
	v_add_f32_e32 v43, 1.0, v43
	v_rcp_f32_e32 v43, v43
	v_mul_f32_e32 v35, 0x41000000, v35
	v_mul_f32_e32 v34, v47, v34
	v_mul_f32_e32 v12, v12, v42
	v_mul_f32_e32 v34, 0x41000000, v34
	v_mul_f32_e32 v12, v44, v12
	v_mul_f32_e32 v13, v13, v43
	v_min_f32_e64 v42, |v35|, s33
	v_mul_f32_e32 v12, 0x41000000, v12
	v_mul_f32_e32 v13, v45, v13
	v_bfi_b32 v35, s2, v42, v35
	v_min_f32_e64 v42, |v34|, s33
	v_mul_f32_e32 v13, 0x41000000, v13
	v_bfi_b32 v34, s2, v42, v34
	v_min_f32_e64 v42, |v12|, s33
	v_bfi_b32 v42, s2, v42, v12
	v_min_f32_e64 v12, |v13|, s33
	v_bfi_b32 v13, s2, v12, v13
	v_mov_b32_e32 v12, v207
	v_cvt_pk_fp8_f32 v12, v35, v34
	v_mul_f32_e32 v34, 0xbfb8aa3b, v39
	v_exp_f32_e32 v34, v34
	v_mul_f32_e32 v43, 0xbfb8aa3b, v38
	v_exp_f32_e32 v43, v43
	v_cvt_pk_fp8_f32 v12, v42, v13 op_sel:[0,0,1]
	v_add_f32_e32 v13, 1.0, v34
	v_rcp_f32_e32 v13, v13
	v_add_f32_e32 v35, 1.0, v43
	v_rcp_f32_e32 v35, v35
	v_mul_f32_e32 v13, v39, v13
	v_mul_f32_e32 v11, v11, v13
	v_mul_f32_e32 v13, 0xbfb8aa3b, v41
	v_exp_f32_e32 v13, v13
	v_mul_f32_e32 v34, v38, v35
	v_mul_f32_e32 v10, v10, v34
	v_mul_f32_e32 v34, 0xbfb8aa3b, v40
	v_exp_f32_e32 v34, v34
	v_add_f32_e32 v13, 1.0, v13
	v_rcp_f32_e32 v13, v13
	v_mul_f32_e32 v10, 0x41000000, v10
	v_add_f32_e32 v34, 1.0, v34
	v_rcp_f32_e32 v34, v34
	v_mul_f32_e32 v13, v41, v13
	v_mul_f32_e32 v13, v37, v13
	v_mul_f32_e32 v11, 0x41000000, v11
	v_mul_f32_e32 v35, 0x41000000, v13
	v_min_f32_e64 v13, |v10|, s33
	v_bfi_b32 v10, s2, v13, v10
	v_min_f32_e64 v13, |v11|, s33
	v_mul_f32_e32 v34, v40, v34
	v_bfi_b32 v11, s2, v13, v11
	v_mov_b32_e32 v13, v207
	v_mul_f32_e32 v34, v36, v34
	v_cvt_pk_fp8_f32 v13, v10, v11
	v_mul_f32_e32 v34, 0x41000000, v34
	v_min_f32_e64 v36, |v34|, s33
	v_min_f32_e64 v11, |v35|, s33
	v_bfi_b32 v10, s2, v36, v34
	v_bfi_b32 v11, s2, v11, v35
	v_cvt_pk_fp8_f32 v13, v10, v11 op_sel:[0,0,1]
	ds_read2_b32 v[10:11], v132 offset0:160 offset1:176
	v_add_co_u32_e32 v34, vcc, s0, v114
	s_mov_b32 s0, 0x50000
	s_nop 0
	v_addc_co_u32_e32 v35, vcc, 0, v115, vcc
	s_waitcnt lgkmcnt(0)
	v_mul_f32_e32 v10, 0x3b800000, v10
	v_pk_mul_f32 v[26:27], v[26:27], v[10:11] op_sel_hi:[1,0]
	global_store_dwordx2 v[34:35], v[12:13], off nt
	v_pk_mul_f32 v[12:13], v[28:29], v[10:11] op_sel_hi:[1,0]
	v_pk_mul_f32 v[28:29], v[32:33], v[10:11] op_sel_hi:[1,0]
	v_mul_f32_e32 v32, 0xbfb8aa3b, v26
	v_mul_f32_e32 v33, 0xbfb8aa3b, v27
	v_exp_f32_e32 v32, v32
	v_exp_f32_e32 v33, v33
	v_pk_mul_f32 v[24:25], v[24:25], v[10:11] op_sel_hi:[1,0]
	v_pk_mul_f32 v[22:23], v[22:23], v[10:11] op_sel_hi:[1,0]
	v_pk_mul_f32 v[30:31], v[30:31], v[10:11] op_sel_hi:[1,0]
	v_pk_mul_f32 v[20:21], v[20:21], v[10:11] op_sel_hi:[1,0]
	v_add_f32_e32 v32, 1.0, v32
	v_pk_mul_f32 v[18:19], v[18:19], v[10:11] op_sel_hi:[1,0]
	v_add_f32_e32 v10, 1.0, v33
	v_rcp_f32_e32 v32, v32
	v_rcp_f32_e32 v10, v10
	v_mul_f32_e32 v26, v26, v32
	v_mul_f32_e32 v10, v27, v10
	v_mul_f32_e32 v27, 0xbfb8aa3b, v12
	v_mul_f32_e32 v26, v30, v26
	v_exp_f32_e32 v27, v27
	v_mul_f32_e32 v30, 0xbfb8aa3b, v13
	v_exp_f32_e32 v30, v30
	v_mul_f32_e32 v26, 0x41000000, v26
	v_add_f32_e32 v27, 1.0, v27
	v_rcp_f32_e32 v27, v27
	v_add_f32_e32 v30, 1.0, v30
	v_rcp_f32_e32 v30, v30
	v_mul_f32_e32 v10, v31, v10
	v_mul_f32_e32 v12, v12, v27
	v_mul_f32_e32 v10, 0x41000000, v10
	v_mul_f32_e32 v12, v28, v12
	v_mul_f32_e32 v13, v13, v30
	v_min_f32_e64 v27, |v26|, s33
	v_mul_f32_e32 v12, 0x41000000, v12
	v_mul_f32_e32 v13, v29, v13
	v_bfi_b32 v26, s2, v27, v26
	v_min_f32_e64 v27, |v10|, s33
	v_mul_f32_e32 v13, 0x41000000, v13
	v_bfi_b32 v10, s2, v27, v10
	v_min_f32_e64 v27, |v12|, s33
	v_mul_f32_e32 v28, 0xbfb8aa3b, v22
	v_bfi_b32 v27, s2, v27, v12
	v_min_f32_e64 v12, |v13|, s33
	v_exp_f32_e32 v28, v28
	v_bfi_b32 v13, s2, v12, v13
	v_mov_b32_e32 v12, v207
	v_cvt_pk_fp8_f32 v12, v26, v10
	v_mul_f32_e32 v10, 0xbfb8aa3b, v23
	v_exp_f32_e32 v10, v10
	v_add_f32_e32 v26, 1.0, v28
	v_rcp_f32_e32 v26, v26
	v_cvt_pk_fp8_f32 v12, v27, v13 op_sel:[0,0,1]
	v_add_f32_e32 v10, 1.0, v10
	v_rcp_f32_e32 v10, v10
	v_mul_f32_e32 v13, v22, v26
	v_mul_f32_e32 v13, v18, v13
	v_mul_f32_e32 v18, 0xbfb8aa3b, v24
	v_exp_f32_e32 v18, v18
	v_mul_f32_e32 v10, v23, v10
	v_mul_f32_e32 v10, v19, v10
	v_mul_f32_e32 v19, 0xbfb8aa3b, v25
	v_exp_f32_e32 v19, v19
	v_add_f32_e32 v18, 1.0, v18
	v_rcp_f32_e32 v18, v18
	v_mul_f32_e32 v13, 0x41000000, v13
	v_add_f32_e32 v19, 1.0, v19
	v_rcp_f32_e32 v19, v19
	v_mul_f32_e32 v18, v24, v18
	v_mul_f32_e32 v10, 0x41000000, v10
	v_mul_f32_e32 v18, v20, v18
	v_min_f32_e64 v20, |v13|, s33
	v_bfi_b32 v20, s2, v20, v13
	v_min_f32_e64 v13, |v10|, s33
	v_mul_f32_e32 v19, v25, v19
	v_bfi_b32 v10, s2, v13, v10
	v_mov_b32_e32 v13, v207
	v_mul_f32_e32 v18, 0x41000000, v18
	v_mul_f32_e32 v19, v21, v19
	v_cvt_pk_fp8_f32 v13, v20, v10
	v_mul_f32_e32 v19, 0x41000000, v19
	v_min_f32_e64 v21, |v18|, s33
	v_bfi_b32 v10, s2, v21, v18
	v_min_f32_e64 v18, |v19|, s33
	v_bfi_b32 v18, s2, v18, v19
	v_cvt_pk_fp8_f32 v13, v10, v18 op_sel:[0,0,1]
	v_add_co_u32_e32 v18, vcc, s0, v114
	v_mul_f32_e32 v10, 0x3b800000, v11
	s_nop 0
	v_addc_co_u32_e32 v19, vcc, 0, v115, vcc
	global_store_dwordx2 v[18:19], v[12:13], off nt
	v_pk_mul_f32 v[18:19], v[170:171], v[10:11] op_sel_hi:[1,0]
	v_pk_mul_f32 v[12:13], v[172:173], v[10:11] op_sel_hi:[1,0]
	v_pk_mul_f32 v[8:9], v[8:9], v[10:11] op_sel_hi:[1,0]
	v_pk_mul_f32 v[6:7], v[6:7], v[10:11] op_sel_hi:[1,0]
	v_pk_mul_f32 v[16:17], v[16:17], v[10:11] op_sel_hi:[1,0]
	v_pk_mul_f32 v[14:15], v[14:15], v[10:11] op_sel_hi:[1,0]
	v_mul_f32_e32 v11, 0xbfb8aa3b, v18
	v_exp_f32_e32 v11, v11
	v_mul_f32_e32 v20, 0xbfb8aa3b, v19
	v_exp_f32_e32 v20, v20
	s_mov_b64 s[0:1], -1
	v_pk_mul_f32 v[4:5], v[4:5], v[10:11] op_sel_hi:[1,0]
	v_add_f32_e32 v11, 1.0, v11
	v_rcp_f32_e32 v11, v11
	s_nop 0
	v_pk_mul_f32 v[2:3], v[2:3], v[10:11] op_sel_hi:[1,0]
	v_add_f32_e32 v10, 1.0, v20
	v_rcp_f32_e32 v10, v10
	v_mul_f32_e32 v11, v18, v11
	v_mul_f32_e32 v11, v14, v11
	v_mul_f32_e32 v14, 0xbfb8aa3b, v12
	v_mul_f32_e32 v10, v19, v10
	v_exp_f32_e32 v14, v14
	v_mul_f32_e32 v10, v15, v10
	v_mul_f32_e32 v15, 0xbfb8aa3b, v13
	v_exp_f32_e32 v15, v15
	v_add_f32_e32 v14, 1.0, v14
	v_rcp_f32_e32 v14, v14
	v_mul_f32_e32 v11, 0x41000000, v11
	v_add_f32_e32 v15, 1.0, v15
	v_rcp_f32_e32 v15, v15
	v_mul_f32_e32 v12, v12, v14
	v_mul_f32_e32 v10, 0x41000000, v10
	v_mul_f32_e32 v12, v16, v12
	v_mul_f32_e32 v13, v13, v15
	v_min_f32_e64 v14, |v11|, s33
	v_mul_f32_e32 v12, 0x41000000, v12
	v_mul_f32_e32 v13, v17, v13
	v_bfi_b32 v11, s2, v14, v11
	v_min_f32_e64 v14, |v10|, s33
	v_mul_f32_e32 v13, 0x41000000, v13
	v_bfi_b32 v14, s2, v14, v10
	v_min_f32_e64 v10, |v12|, s33
	v_bfi_b32 v12, s2, v10, v12
	v_min_f32_e64 v10, |v13|, s33
	v_bfi_b32 v13, s2, v10, v13
	v_mov_b32_e32 v10, v207
	v_mul_f32_e32 v15, 0xbfb8aa3b, v6
	v_exp_f32_e32 v15, v15
	v_cvt_pk_fp8_f32 v10, v11, v14
	v_mul_f32_e32 v11, 0xbfb8aa3b, v7
	v_exp_f32_e32 v11, v11
	v_add_f32_e32 v14, 1.0, v15
	v_rcp_f32_e32 v14, v14
	v_cvt_pk_fp8_f32 v10, v12, v13 op_sel:[0,0,1]
	v_add_f32_e32 v11, 1.0, v11
	v_rcp_f32_e32 v11, v11
	v_mul_f32_e32 v6, v6, v14
	v_mul_f32_e32 v2, v2, v6
	v_mul_f32_e32 v2, 0x41000000, v2
	v_mul_f32_e32 v6, v7, v11
	v_mul_f32_e32 v3, v3, v6
	v_mul_f32_e32 v6, 0xbfb8aa3b, v9
	v_exp_f32_e32 v6, v6
	v_mul_f32_e32 v7, 0xbfb8aa3b, v8
	v_exp_f32_e32 v7, v7
	v_mul_f32_e32 v3, 0x41000000, v3
	v_add_f32_e32 v6, 1.0, v6
	v_rcp_f32_e32 v6, v6
	v_add_f32_e32 v7, 1.0, v7
	v_rcp_f32_e32 v7, v7
	v_mov_b32_e32 v11, v207
	v_mul_f32_e32 v6, v9, v6
	v_mul_f32_e32 v5, v5, v6
	v_min_f32_e64 v6, |v2|, s33
	v_bfi_b32 v2, s2, v6, v2
	v_min_f32_e64 v6, |v3|, s33
	v_mul_f32_e32 v7, v8, v7
	v_bfi_b32 v3, s2, v6, v3
	v_mul_f32_e32 v4, v4, v7
	v_cvt_pk_fp8_f32 v11, v2, v3
	v_mul_f32_e32 v4, 0x41000000, v4
	v_mul_f32_e32 v5, 0x41000000, v5
	v_min_f32_e64 v6, |v4|, s33
	v_min_f32_e64 v3, |v5|, s33
	v_bfi_b32 v2, s2, v6, v4
	v_bfi_b32 v3, s2, v3, v5
	v_cvt_pk_fp8_f32 v11, v2, v3 op_sel:[0,0,1]
	v_add_co_u32_e32 v2, vcc, 0x58000, v114
	s_nop 1
	v_addc_co_u32_e32 v3, vcc, 0, v115, vcc
	s_and_b64 vcc, exec, s[38:39]
	global_store_dwordx2 v[2:3], v[10:11], off nt
	s_cbranch_vccnz .LBB0_1242
	s_andn2_b64 vcc, exec, s[48:49]
	s_cbranch_vccnz .LBB0_1241
	s_barrier
	s_branch .LBB0_1241

.LBB0_1353:
	v_mov_b32_e32 v4, v0
	s_lshl_b32 s0, s23, 8
	s_add_i32 s0, s0, s34
	v_lshlrev_b32_e32 v5, 2, v4
	v_and_or_b32 v2, v4, 7, s0
	v_and_b32_e32 v206, 32, v5
	v_lshrrev_b32_e32 v5, 1, v4
	v_and_or_b32 v4, v4, 15, s0
	v_and_b32_e32 v144, 24, v5
	v_ashrrev_i32_e32 v5, 31, v4
	v_lshl_add_u64 v[4:5], v[4:5], 2, s[42:43]
	global_load_dword v143, v[4:5], off
	global_load_dword v146, v[4:5], off offset:64
	global_load_dword v142, v[4:5], off offset:128
	global_load_dword v9, v[4:5], off offset:192
	global_load_dword v8, v[4:5], off offset:512
	global_load_dword v7, v[4:5], off offset:576
	global_load_dword v6, v[4:5], off offset:640
	s_nop 0
	global_load_dword v5, v[4:5], off offset:704
	s_lshl_b32 s1, s10, 8
	v_ashrrev_i32_e32 v3, 31, v2
	s_and_b32 s1, s1, 0x300
	v_lshlrev_b64 v[2:3], 10, v[2:3]
	s_or_b32 s10, s1, s59
	v_lshl_add_u64 v[2:3], s[40:41], 0, v[2:3]
	v_lshl_add_u64 v[2:3], v[2:3], 0, s[10:11]
	v_mov_b32_e32 v145, v207
	v_lshl_add_u64 v[2:3], v[2:3], 0, v[206:207]
	v_lshl_add_u64 v[2:3], v[2:3], 0, v[144:145]
	s_movk_i32 s0, 0x2000
	v_readlane_b32 s62, v253, 8
	v_readlane_b32 s63, v253, 9
	s_waitcnt vmcnt(0)
	v_mul_f32_e32 v4, 0x3d800000, v143
	v_pk_mul_f32 v[126:127], v[126:127], v[4:5] op_sel_hi:[1,0]
	v_pk_mul_f32 v[136:137], v[136:137], v[4:5] op_sel_hi:[1,0]
	v_pk_mul_f32 v[134:135], v[134:135], v[4:5] op_sel_hi:[1,0]
	v_pk_mul_f32 v[132:133], v[132:133], v[4:5] op_sel_hi:[1,0]
	v_pk_mul_f32 v[130:131], v[130:131], v[4:5] op_sel_hi:[1,0]
	v_pk_mul_f32 v[128:129], v[128:129], v[4:5] op_sel_hi:[1,0]
	v_pk_mul_f32 v[124:125], v[124:125], v[4:5] op_sel_hi:[1,0]
	v_pk_mul_f32 v[122:123], v[122:123], v[4:5] op_sel_hi:[1,0]
	v_min_f32_e64 v4, |v126|, s33
	v_bfi_b32 v4, s2, v4, v126
	v_min_f32_e64 v126, |v127|, s33
	v_bfi_b32 v127, s2, v126, v127
	v_min_f32_e64 v126, |v128|, s33
	v_bfi_b32 v128, s2, v126, v128
	v_min_f32_e64 v126, |v129|, s33
	v_bfi_b32 v129, s2, v126, v129
	v_mov_b32_e32 v126, v207
	v_cvt_pk_fp8_f32 v126, v4, v127
	v_min_f32_e64 v4, |v122|, s33
	v_bfi_b32 v4, s2, v4, v122
	v_min_f32_e64 v122, |v123|, s33
	v_bfi_b32 v122, s2, v122, v123
	v_mov_b32_e32 v127, v207
	v_cvt_pk_fp8_f32 v127, v4, v122
	v_mul_f32_e32 v4, 0x3d800000, v146
	v_pk_mul_f32 v[110:111], v[110:111], v[4:5] op_sel_hi:[1,0]
	v_pk_mul_f32 v[120:121], v[120:121], v[4:5] op_sel_hi:[1,0]
	v_pk_mul_f32 v[118:119], v[118:119], v[4:5] op_sel_hi:[1,0]
	v_pk_mul_f32 v[116:117], v[116:117], v[4:5] op_sel_hi:[1,0]
	v_pk_mul_f32 v[114:115], v[114:115], v[4:5] op_sel_hi:[1,0]
	v_pk_mul_f32 v[112:113], v[112:113], v[4:5] op_sel_hi:[1,0]
	v_pk_mul_f32 v[108:109], v[108:109], v[4:5] op_sel_hi:[1,0]
	v_pk_mul_f32 v[106:107], v[106:107], v[4:5] op_sel_hi:[1,0]
	v_min_f32_e64 v4, |v110|, s33
	v_bfi_b32 v4, s2, v4, v110
	v_min_f32_e64 v110, |v111|, s33
	v_min_f32_e64 v143, |v134|, s33
	v_bfi_b32 v111, s2, v110, v111
	v_min_f32_e64 v110, |v112|, s33
	v_bfi_b32 v134, s2, v143, v134
	v_min_f32_e64 v143, |v135|, s33
	v_bfi_b32 v112, s2, v110, v112
	v_min_f32_e64 v110, |v113|, s33
	v_bfi_b32 v135, s2, v143, v135
	v_min_f32_e64 v143, |v136|, s33
	v_bfi_b32 v113, s2, v110, v113
	v_mov_b32_e32 v110, v207
	v_bfi_b32 v136, s2, v143, v136
	v_min_f32_e64 v143, |v137|, s33
	v_cvt_pk_fp8_f32 v110, v4, v111
	v_min_f32_e64 v4, |v106|, s33
	v_bfi_b32 v137, s2, v143, v137
	v_mov_b32_e32 v143, v207
	v_bfi_b32 v4, s2, v4, v106
	v_min_f32_e64 v106, |v107|, s33
	v_cvt_pk_fp8_f32 v143, v134, v135
	v_min_f32_e64 v134, |v130|, s33
	v_bfi_b32 v106, s2, v106, v107
	v_mov_b32_e32 v111, v207
	v_bfi_b32 v130, s2, v134, v130
	v_min_f32_e64 v134, |v131|, s33
	v_cvt_pk_fp8_f32 v111, v4, v106
	v_mul_f32_e32 v4, 0x3d800000, v142
	v_bfi_b32 v131, s2, v134, v131
	v_min_f32_e64 v134, |v132|, s33
	v_pk_mul_f32 v[94:95], v[94:95], v[4:5] op_sel_hi:[1,0]
	v_bfi_b32 v132, s2, v134, v132
	v_min_f32_e64 v134, |v133|, s33
	v_pk_mul_f32 v[104:105], v[104:105], v[4:5] op_sel_hi:[1,0]
	v_pk_mul_f32 v[102:103], v[102:103], v[4:5] op_sel_hi:[1,0]
	v_pk_mul_f32 v[100:101], v[100:101], v[4:5] op_sel_hi:[1,0]
	v_pk_mul_f32 v[98:99], v[98:99], v[4:5] op_sel_hi:[1,0]
	v_pk_mul_f32 v[96:97], v[96:97], v[4:5] op_sel_hi:[1,0]
	v_pk_mul_f32 v[92:93], v[92:93], v[4:5] op_sel_hi:[1,0]
	v_pk_mul_f32 v[90:91], v[90:91], v[4:5] op_sel_hi:[1,0]
	v_min_f32_e64 v4, |v94|, s33
	v_bfi_b32 v133, s2, v134, v133
	v_mov_b32_e32 v134, v207
	v_bfi_b32 v4, s2, v4, v94
	v_min_f32_e64 v94, |v95|, s33
	v_cvt_pk_fp8_f32 v134, v130, v131
	v_bfi_b32 v95, s2, v94, v95
	v_min_f32_e64 v94, |v96|, s33
	v_bfi_b32 v96, s2, v94, v96
	v_min_f32_e64 v94, |v97|, s33
	v_min_f32_e64 v123, |v124|, s33
	v_bfi_b32 v97, s2, v94, v97
	v_mov_b32_e32 v94, v207
	v_bfi_b32 v123, s2, v123, v124
	v_min_f32_e64 v124, |v125|, s33
	v_cvt_pk_fp8_f32 v94, v4, v95
	v_min_f32_e64 v4, |v90|, s33
	v_cvt_pk_fp8_f32 v143, v136, v137 op_sel:[0,0,1]
	v_cvt_pk_fp8_f32 v134, v132, v133 op_sel:[0,0,1]
	v_bfi_b32 v124, s2, v124, v125
	v_bfi_b32 v4, s2, v4, v90
	v_min_f32_e64 v90, |v91|, s33
	v_cvt_pk_fp8_f32 v126, v128, v129 op_sel:[0,0,1]
	v_cvt_pk_fp8_f32 v127, v123, v124 op_sel:[0,0,1]
	v_bfi_b32 v90, s2, v90, v91
	v_mov_b32_e32 v95, v207
	v_cvt_pk_fp8_f32 v95, v4, v90
	v_mul_f32_e32 v4, 0x3d800000, v9
	v_pk_mul_f32 v[86:87], v[86:87], v[4:5] op_sel_hi:[1,0]
	v_mov_b32_e32 v122, v143
	v_mov_b32_e32 v123, v134
	v_min_f32_e64 v9, |v86|, s33
	v_mov_b32_dpp v122, v126 row_ror:8 row_mask:0xf bank_mask:0xc
	v_mov_b32_dpp v123, v127 row_ror:8 row_mask:0xf bank_mask:0xc
	v_pk_mul_f32 v[88:89], v[88:89], v[4:5] op_sel_hi:[1,0]
	v_bfi_b32 v9, s2, v9, v86
	v_min_f32_e64 v86, |v87|, s33
	global_store_dwordx2 v[2:3], v[122:123], off nt
	v_add_co_u32_e32 v122, vcc, s0, v2
	v_bfi_b32 v86, s2, v86, v87
	v_min_f32_e64 v87, |v88|, s33
	v_mov_b32_dpp v126, v143 row_ror:8 row_mask:0xf bank_mask:0x3
	v_mov_b32_dpp v127, v134 row_ror:8 row_mask:0xf bank_mask:0x3
	v_addc_co_u32_e32 v123, vcc, 0, v3, vcc
	v_bfi_b32 v87, s2, v87, v88
	v_min_f32_e64 v88, |v89|, s33
	global_store_dwordx2 v[122:123], v[126:127], off nt
	v_min_f32_e64 v122, |v118|, s33
	v_pk_mul_f32 v[82:83], v[82:83], v[4:5] op_sel_hi:[1,0]
	v_bfi_b32 v88, s2, v88, v89
	v_mov_b32_e32 v89, v207
	v_bfi_b32 v118, s2, v122, v118
	v_min_f32_e64 v122, |v119|, s33
	v_cvt_pk_fp8_f32 v89, v9, v86
	v_min_f32_e64 v9, |v82|, s33
	v_bfi_b32 v119, s2, v122, v119
	v_min_f32_e64 v122, |v120|, s33
	v_pk_mul_f32 v[84:85], v[84:85], v[4:5] op_sel_hi:[1,0]
	v_bfi_b32 v9, s2, v9, v82
	v_min_f32_e64 v82, |v83|, s33
	v_bfi_b32 v120, s2, v122, v120
	v_min_f32_e64 v122, |v121|, s33
	v_bfi_b32 v82, s2, v82, v83
	v_min_f32_e64 v83, |v84|, s33
	v_bfi_b32 v121, s2, v122, v121
	v_mov_b32_e32 v122, v207
	v_bfi_b32 v83, s2, v83, v84
	v_min_f32_e64 v84, |v85|, s33
	v_pk_mul_f32 v[78:79], v[78:79], v[4:5] op_sel_hi:[1,0]
	v_cvt_pk_fp8_f32 v122, v118, v119
	v_min_f32_e64 v118, |v114|, s33
	v_bfi_b32 v84, s2, v84, v85
	v_mov_b32_e32 v85, v207
	v_pk_mul_f32 v[80:81], v[80:81], v[4:5] op_sel_hi:[1,0]
	v_pk_mul_f32 v[76:77], v[76:77], v[4:5] op_sel_hi:[1,0]
	v_pk_mul_f32 v[74:75], v[74:75], v[4:5] op_sel_hi:[1,0]
	v_min_f32_e64 v4, |v78|, s33
	v_bfi_b32 v114, s2, v118, v114
	v_min_f32_e64 v118, |v115|, s33
	v_cvt_pk_fp8_f32 v85, v9, v82
	v_bfi_b32 v4, s2, v4, v78
	v_min_f32_e64 v9, |v79|, s33
	v_min_f32_e64 v78, |v80|, s33
	v_bfi_b32 v115, s2, v118, v115
	v_min_f32_e64 v118, |v116|, s33
	v_bfi_b32 v9, s2, v9, v79
	v_bfi_b32 v79, s2, v78, v80
	v_min_f32_e64 v78, |v81|, s33
	v_bfi_b32 v116, s2, v118, v116
	v_min_f32_e64 v118, |v117|, s33
	v_bfi_b32 v80, s2, v78, v81
	v_mov_b32_e32 v78, v207
	v_bfi_b32 v117, s2, v118, v117
	v_mov_b32_e32 v118, v207
	v_cvt_pk_fp8_f32 v78, v4, v9
	v_cvt_pk_fp8_f32 v118, v114, v115
	v_min_f32_e64 v107, |v108|, s33
	v_min_f32_e64 v4, |v74|, s33
	v_min_f32_e64 v9, |v75|, s33
	v_bfi_b32 v107, s2, v107, v108
	v_min_f32_e64 v108, |v109|, s33
	v_cvt_pk_fp8_f32 v78, v79, v80 op_sel:[0,0,1]
	v_bfi_b32 v4, s2, v4, v74
	v_bfi_b32 v9, s2, v9, v75
	v_mov_b32_e32 v79, v207
	v_cvt_pk_fp8_f32 v122, v120, v121 op_sel:[0,0,1]
	v_cvt_pk_fp8_f32 v118, v116, v117 op_sel:[0,0,1]
	v_bfi_b32 v108, s2, v108, v109
	v_cvt_pk_fp8_f32 v79, v4, v9
	v_mul_f32_e32 v4, 0x3d800000, v8
	v_cvt_pk_fp8_f32 v110, v112, v113 op_sel:[0,0,1]
	v_cvt_pk_fp8_f32 v111, v107, v108 op_sel:[0,0,1]
	v_pk_mul_f32 v[70:71], v[70:71], v[4:5] op_sel_hi:[1,0]
	v_pk_mul_f32 v[8:9], v[72:73], v[4:5] op_sel_hi:[1,0]
	v_min_f32_e64 v72, |v70|, s33
	s_movk_i32 s0, 0x4000
	v_bfi_b32 v70, s2, v72, v70
	v_min_f32_e64 v72, |v71|, s33
	v_mov_b32_e32 v106, v122
	v_mov_b32_e32 v107, v118
	v_add_co_u32_e32 v108, vcc, s0, v2
	v_bfi_b32 v71, s2, v72, v71
	v_min_f32_e64 v72, |v8|, s33
	v_mov_b32_dpp v106, v110 row_ror:8 row_mask:0xf bank_mask:0xc
	v_mov_b32_dpp v107, v111 row_ror:8 row_mask:0xf bank_mask:0xc
	v_addc_co_u32_e32 v109, vcc, 0, v3, vcc
	s_movk_i32 s0, 0x6000
	v_bfi_b32 v8, s2, v72, v8
	v_min_f32_e64 v72, |v9|, s33
	global_store_dwordx2 v[108:109], v[106:107], off nt
	v_add_co_u32_e32 v106, vcc, s0, v2
	v_bfi_b32 v9, s2, v72, v9
	v_mov_b32_e32 v72, v207
	v_mov_b32_dpp v110, v122 row_ror:8 row_mask:0xf bank_mask:0x3
	v_mov_b32_dpp v111, v118 row_ror:8 row_mask:0xf bank_mask:0x3
	v_addc_co_u32_e32 v107, vcc, 0, v3, vcc
	v_cvt_pk_fp8_f32 v72, v70, v71
	global_store_dwordx2 v[106:107], v[110:111], off nt
	v_min_f32_e64 v106, |v102|, s33
	v_bfi_b32 v102, s2, v106, v102
	v_min_f32_e64 v106, |v103|, s33
	v_bfi_b32 v103, s2, v106, v103
	v_min_f32_e64 v106, |v104|, s33
	v_pk_mul_f32 v[66:67], v[66:67], v[4:5] op_sel_hi:[1,0]
	v_bfi_b32 v104, s2, v106, v104
	v_min_f32_e64 v106, |v105|, s33
	v_pk_mul_f32 v[68:69], v[68:69], v[4:5] op_sel_hi:[1,0]
	v_cvt_pk_fp8_f32 v72, v8, v9 op_sel:[0,0,1]
	v_min_f32_e64 v8, |v66|, s33
	v_bfi_b32 v105, s2, v106, v105
	v_mov_b32_e32 v106, v207
	v_bfi_b32 v8, s2, v8, v66
	v_min_f32_e64 v9, |v67|, s33
	v_min_f32_e64 v66, |v68|, s33
	v_cvt_pk_fp8_f32 v106, v102, v103
	v_min_f32_e64 v102, |v98|, s33
	v_bfi_b32 v9, s2, v9, v67
	v_bfi_b32 v66, s2, v66, v68
	v_mov_b32_e32 v68, v207
	v_pk_mul_f32 v[62:63], v[62:63], v[4:5] op_sel_hi:[1,0]
	v_bfi_b32 v98, s2, v102, v98
	v_min_f32_e64 v102, |v99|, s33
	v_cvt_pk_fp8_f32 v68, v8, v9
	v_pk_mul_f32 v[8:9], v[64:65], v[4:5] op_sel_hi:[1,0]
	v_pk_mul_f32 v[60:61], v[60:61], v[4:5] op_sel_hi:[1,0]
	v_pk_mul_f32 v[58:59], v[58:59], v[4:5] op_sel_hi:[1,0]
	v_min_f32_e64 v4, |v62|, s33
	v_bfi_b32 v99, s2, v102, v99
	v_min_f32_e64 v102, |v100|, s33
	v_bfi_b32 v4, s2, v4, v62
	v_min_f32_e64 v62, |v63|, s33
	v_bfi_b32 v100, s2, v102, v100
	v_min_f32_e64 v102, |v101|, s33
	v_bfi_b32 v62, s2, v62, v63
	v_min_f32_e64 v63, |v8|, s33
	v_bfi_b32 v101, s2, v102, v101
	v_mov_b32_e32 v102, v207
	v_bfi_b32 v63, s2, v63, v8
	v_min_f32_e64 v8, |v9|, s33
	v_cvt_pk_fp8_f32 v102, v98, v99
	v_bfi_b32 v9, s2, v8, v9
	v_mov_b32_e32 v8, v207
	v_cvt_pk_fp8_f32 v8, v4, v62
	v_min_f32_e64 v91, |v92|, s33
	v_bfi_b32 v91, s2, v91, v92
	v_min_f32_e64 v92, |v93|, s33
	v_cvt_pk_fp8_f32 v106, v104, v105 op_sel:[0,0,1]
	v_cvt_pk_fp8_f32 v102, v100, v101 op_sel:[0,0,1]
	v_bfi_b32 v92, s2, v92, v93
	v_cvt_pk_fp8_f32 v94, v96, v97 op_sel:[0,0,1]
	v_cvt_pk_fp8_f32 v95, v91, v92 op_sel:[0,0,1]
	v_cvt_pk_fp8_f32 v8, v63, v9 op_sel:[0,0,1]
	v_min_f32_e64 v4, |v58|, s33
	v_min_f32_e64 v9, |v59|, s33
	v_bfi_b32 v4, s2, v4, v58
	v_bfi_b32 v58, s2, v9, v59
	v_min_f32_e64 v9, |v60|, s33
	s_mov_b32 s0, 0x8000
	v_min_f32_e64 v74, |v76|, s33
	v_min_f32_e64 v75, |v77|, s33
	v_bfi_b32 v59, s2, v9, v60
	v_min_f32_e64 v9, |v61|, s33
	v_mov_b32_e32 v90, v106
	v_mov_b32_e32 v91, v102
	v_add_co_u32_e32 v92, vcc, s0, v2
	v_cvt_pk_fp8_f32 v89, v87, v88 op_sel:[0,0,1]
	v_cvt_pk_fp8_f32 v85, v83, v84 op_sel:[0,0,1]
	v_bfi_b32 v74, s2, v74, v76
	v_bfi_b32 v75, s2, v75, v77
	v_bfi_b32 v60, s2, v9, v61
	v_mov_b32_e32 v9, v207
	v_mov_b32_dpp v90, v94 row_ror:8 row_mask:0xf bank_mask:0xc
	v_mov_b32_dpp v91, v95 row_ror:8 row_mask:0xf bank_mask:0xc
	v_addc_co_u32_e32 v93, vcc, 0, v3, vcc
	s_mov_b32 s0, 0xa000
	v_cvt_pk_fp8_f32 v79, v74, v75 op_sel:[0,0,1]
	v_cvt_pk_fp8_f32 v9, v4, v58
	global_store_dwordx2 v[92:93], v[90:91], off nt
	v_add_co_u32_e32 v90, vcc, s0, v2
	v_min_f32_e64 v67, |v69|, s33
	s_nop 0
	v_addc_co_u32_e32 v91, vcc, 0, v3, vcc
	s_mov_b32 s0, 0xc000
	v_bfi_b32 v67, s2, v67, v69
	v_mov_b32_e32 v74, v89
	v_mov_b32_e32 v75, v85
	v_add_co_u32_e32 v76, vcc, s0, v2
	v_cvt_pk_fp8_f32 v68, v66, v67 op_sel:[0,0,1]
	v_mov_b32_dpp v74, v78 row_ror:8 row_mask:0xf bank_mask:0xc
	v_mov_b32_dpp v75, v79 row_ror:8 row_mask:0xf bank_mask:0xc
	v_addc_co_u32_e32 v77, vcc, 0, v3, vcc
	s_mov_b32 s0, 0xe000
	v_cvt_pk_fp8_f32 v9, v59, v60 op_sel:[0,0,1]
	global_store_dwordx2 v[76:77], v[74:75], off nt
	v_add_co_u32_e32 v74, vcc, s0, v2
	s_mov_b32 s0, 0x20000
	s_nop 0
	v_addc_co_u32_e32 v75, vcc, 0, v3, vcc
	v_mov_b32_e32 v58, v72
	v_mov_b32_e32 v59, v68
	v_add_co_u32_e32 v60, vcc, s0, v2
	v_mov_b32_dpp v58, v8 row_ror:8 row_mask:0xf bank_mask:0xc
	v_mov_b32_dpp v59, v9 row_ror:8 row_mask:0xf bank_mask:0xc
	v_addc_co_u32_e32 v61, vcc, 0, v3, vcc
	s_mov_b32 s0, 0x22000
	v_mul_f32_e32 v4, 0x3d800000, v7
	global_store_dwordx2 v[60:61], v[58:59], off nt
	v_add_co_u32_e32 v58, vcc, s0, v2
	v_pk_mul_f32 v[54:55], v[54:55], v[4:5] op_sel_hi:[1,0]
	v_mov_b32_dpp v8, v72 row_ror:8 row_mask:0xf bank_mask:0x3
	v_mov_b32_dpp v9, v68 row_ror:8 row_mask:0xf bank_mask:0x3
	v_addc_co_u32_e32 v59, vcc, 0, v3, vcc
	v_min_f32_e64 v7, |v54|, s33
	global_store_dwordx2 v[58:59], v[8:9], off nt
	v_pk_mul_f32 v[8:9], v[56:57], v[4:5] op_sel_hi:[1,0]
	v_bfi_b32 v7, s2, v7, v54
	v_min_f32_e64 v54, |v55|, s33
	v_bfi_b32 v54, s2, v54, v55
	v_min_f32_e64 v55, |v8|, s33
	v_bfi_b32 v8, s2, v55, v8
	v_min_f32_e64 v55, |v9|, s33
	v_bfi_b32 v9, s2, v55, v9
	v_mov_b32_e32 v55, v207
	v_cvt_pk_fp8_f32 v55, v7, v54
	v_pk_mul_f32 v[50:51], v[50:51], v[4:5] op_sel_hi:[1,0]
	v_pk_mul_f32 v[52:53], v[52:53], v[4:5] op_sel_hi:[1,0]
	v_min_f32_e64 v7, |v50|, s33
	v_cvt_pk_fp8_f32 v55, v8, v9 op_sel:[0,0,1]
	v_min_f32_e64 v8, |v51|, s33
	v_bfi_b32 v7, s2, v7, v50
	v_bfi_b32 v8, s2, v8, v51
	v_mov_b32_e32 v51, v207
	v_cvt_pk_fp8_f32 v51, v7, v8
	v_min_f32_e64 v9, |v52|, s33
	v_min_f32_e64 v50, |v53|, s33
	v_bfi_b32 v9, s2, v9, v52
	v_bfi_b32 v50, s2, v50, v53
	v_pk_mul_f32 v[46:47], v[46:47], v[4:5] op_sel_hi:[1,0]
	v_cvt_pk_fp8_f32 v51, v9, v50 op_sel:[0,0,1]
	v_pk_mul_f32 v[8:9], v[48:49], v[4:5] op_sel_hi:[1,0]
	v_pk_mul_f32 v[44:45], v[44:45], v[4:5] op_sel_hi:[1,0]
	v_pk_mul_f32 v[42:43], v[42:43], v[4:5] op_sel_hi:[1,0]
	v_min_f32_e64 v4, |v46|, s33
	v_bfi_b32 v4, s2, v4, v46
	v_min_f32_e64 v46, |v8|, s33
	v_min_f32_e64 v7, |v47|, s33
	v_bfi_b32 v46, s2, v46, v8
	v_min_f32_e64 v8, |v9|, s33
	v_bfi_b32 v7, s2, v7, v47
	v_bfi_b32 v9, s2, v8, v9
	v_mov_b32_e32 v8, v207
	v_cvt_pk_fp8_f32 v8, v4, v7
	v_min_f32_e64 v4, |v42|, s33
	v_bfi_b32 v4, s2, v4, v42
	v_min_f32_e64 v7, |v43|, s33
	v_cvt_pk_fp8_f32 v8, v46, v9 op_sel:[0,0,1]
	v_min_f32_e64 v9, |v44|, s33
	v_bfi_b32 v42, s2, v9, v44
	v_min_f32_e64 v9, |v45|, s33
	v_bfi_b32 v7, s2, v7, v43
	v_bfi_b32 v43, s2, v9, v45
	v_mov_b32_e32 v9, v207
	v_cvt_pk_fp8_f32 v9, v4, v7
	s_mov_b32 s0, 0x24000
	v_add_co_u32_e32 v44, vcc, s0, v2
	v_cvt_pk_fp8_f32 v9, v42, v43 op_sel:[0,0,1]
	v_mov_b32_e32 v42, v55
	v_mov_b32_e32 v43, v51
	v_addc_co_u32_e32 v45, vcc, 0, v3, vcc
	v_mov_b32_dpp v42, v8 row_ror:8 row_mask:0xf bank_mask:0xc
	v_mov_b32_dpp v43, v9 row_ror:8 row_mask:0xf bank_mask:0xc
	s_mov_b32 s0, 0x26000
	global_store_dwordx2 v[44:45], v[42:43], off nt
	v_add_co_u32_e32 v42, vcc, s0, v2
	v_mov_b32_dpp v8, v55 row_ror:8 row_mask:0xf bank_mask:0x3
	v_mov_b32_dpp v9, v51 row_ror:8 row_mask:0xf bank_mask:0x3
	v_addc_co_u32_e32 v43, vcc, 0, v3, vcc
	v_mul_f32_e32 v4, 0x3d800000, v6
	global_store_dwordx2 v[42:43], v[8:9], off nt
	v_pk_mul_f32 v[8:9], v[38:39], v[4:5] op_sel_hi:[1,0]
	v_pk_mul_f32 v[6:7], v[40:41], v[4:5] op_sel_hi:[1,0]
	v_min_f32_e64 v38, |v8|, s33
	v_bfi_b32 v8, s2, v38, v8
	v_min_f32_e64 v38, |v9|, s33
	v_bfi_b32 v9, s2, v38, v9
	v_min_f32_e64 v38, |v6|, s33
	v_bfi_b32 v6, s2, v38, v6
	v_min_f32_e64 v38, |v7|, s33
	v_bfi_b32 v7, s2, v38, v7
	v_mov_b32_e32 v38, v207
	v_cvt_pk_fp8_f32 v38, v8, v9
	v_pk_mul_f32 v[34:35], v[34:35], v[4:5] op_sel_hi:[1,0]
	v_pk_mul_f32 v[36:37], v[36:37], v[4:5] op_sel_hi:[1,0]
	v_pk_mul_f32 v[28:29], v[28:29], v[4:5] op_sel_hi:[1,0]
	v_cvt_pk_fp8_f32 v38, v6, v7 op_sel:[0,0,1]
	v_min_f32_e64 v6, |v34|, s33
	v_min_f32_e64 v7, |v35|, s33
	v_bfi_b32 v6, s2, v6, v34
	v_bfi_b32 v7, s2, v7, v35
	v_mov_b32_e32 v34, v207
	v_cvt_pk_fp8_f32 v34, v6, v7
	v_min_f32_e64 v8, |v36|, s33
	v_min_f32_e64 v9, |v37|, s33
	v_bfi_b32 v8, s2, v8, v36
	v_bfi_b32 v9, s2, v9, v37
	v_cvt_pk_fp8_f32 v34, v8, v9 op_sel:[0,0,1]
	v_pk_mul_f32 v[8:9], v[30:31], v[4:5] op_sel_hi:[1,0]
	v_pk_mul_f32 v[6:7], v[32:33], v[4:5] op_sel_hi:[1,0]
	v_pk_mul_f32 v[26:27], v[26:27], v[4:5] op_sel_hi:[1,0]
	v_min_f32_e64 v4, |v8|, s33
	v_bfi_b32 v4, s2, v4, v8
	v_min_f32_e64 v8, |v9|, s33
	v_bfi_b32 v8, s2, v8, v9
	v_min_f32_e64 v9, |v6|, s33
	v_bfi_b32 v9, s2, v9, v6
	v_min_f32_e64 v6, |v7|, s33
	v_bfi_b32 v7, s2, v6, v7
	v_mov_b32_e32 v6, v207
	v_cvt_pk_fp8_f32 v6, v4, v8
	v_min_f32_e64 v4, |v26|, s33
	v_bfi_b32 v4, s2, v4, v26
	s_mov_b32 s0, 0x28000
	v_cvt_pk_fp8_f32 v6, v9, v7 op_sel:[0,0,1]
	v_min_f32_e64 v7, |v27|, s33
	v_bfi_b32 v8, s2, v7, v27
	v_min_f32_e64 v7, |v28|, s33
	v_bfi_b32 v9, s2, v7, v28
	v_min_f32_e64 v7, |v29|, s33
	v_bfi_b32 v26, s2, v7, v29
	v_mov_b32_e32 v7, v207
	v_cvt_pk_fp8_f32 v7, v4, v8
	v_mov_b32_e32 v8, v38
	v_mul_f32_e32 v4, 0x3d800000, v5
	v_pk_mul_f32 v[20:21], v[20:21], v[4:5] op_sel_hi:[1,0]
	v_cvt_pk_fp8_f32 v7, v9, v26 op_sel:[0,0,1]
	v_mov_b32_e32 v9, v34
	v_add_co_u32_e32 v26, vcc, s0, v2
	v_mov_b32_dpp v8, v6 row_ror:8 row_mask:0xf bank_mask:0xc
	v_mov_b32_dpp v9, v7 row_ror:8 row_mask:0xf bank_mask:0xc
	v_addc_co_u32_e32 v27, vcc, 0, v3, vcc
	s_mov_b32 s0, 0x2a000
	global_store_dwordx2 v[26:27], v[8:9], off nt
	v_add_co_u32_e32 v8, vcc, s0, v2
	v_mov_b32_dpp v6, v38 row_ror:8 row_mask:0xf bank_mask:0x3
	v_mov_b32_dpp v7, v34 row_ror:8 row_mask:0xf bank_mask:0x3
	v_addc_co_u32_e32 v9, vcc, 0, v3, vcc
	global_store_dwordx2 v[8:9], v[6:7], off nt
	v_pk_mul_f32 v[8:9], v[22:23], v[4:5] op_sel_hi:[1,0]
	v_pk_mul_f32 v[6:7], v[24:25], v[4:5] op_sel_hi:[1,0]
	v_pk_mul_f32 v[18:19], v[18:19], v[4:5] op_sel_hi:[1,0]
	v_min_f32_e64 v5, |v8|, s33
	v_bfi_b32 v5, s2, v5, v8
	v_min_f32_e64 v8, |v9|, s33
	v_bfi_b32 v8, s2, v8, v9
	v_mov_b32_e32 v22, v207
	v_cvt_pk_fp8_f32 v22, v5, v8
	v_min_f32_e64 v9, |v6|, s33
	v_bfi_b32 v6, s2, v9, v6
	v_min_f32_e64 v9, |v7|, s33
	v_bfi_b32 v7, s2, v9, v7
	v_cvt_pk_fp8_f32 v22, v6, v7 op_sel:[0,0,1]
	v_min_f32_e64 v5, |v18|, s33
	v_min_f32_e64 v6, |v19|, s33
	v_bfi_b32 v5, s2, v5, v18
	v_bfi_b32 v6, s2, v6, v19
	v_mov_b32_e32 v18, v207
	v_cvt_pk_fp8_f32 v18, v5, v6
	v_min_f32_e64 v7, |v20|, s33
	v_min_f32_e64 v8, |v21|, s33
	v_bfi_b32 v7, s2, v7, v20
	v_bfi_b32 v8, s2, v8, v21
	v_cvt_pk_fp8_f32 v18, v7, v8 op_sel:[0,0,1]
	v_pk_mul_f32 v[8:9], v[14:15], v[4:5] op_sel_hi:[1,0]
	v_pk_mul_f32 v[6:7], v[16:17], v[4:5] op_sel_hi:[1,0]
	v_pk_mul_f32 v[12:13], v[12:13], v[4:5] op_sel_hi:[1,0]
	v_pk_mul_f32 v[4:5], v[10:11], v[4:5] op_sel_hi:[1,0]
	v_min_f32_e64 v10, |v8|, s33
	v_bfi_b32 v8, s2, v10, v8
	v_min_f32_e64 v10, |v9|, s33
	v_bfi_b32 v9, s2, v10, v9
	v_min_f32_e64 v10, |v6|, s33
	v_bfi_b32 v10, s2, v10, v6
	v_min_f32_e64 v6, |v7|, s33
	v_bfi_b32 v7, s2, v6, v7
	v_mov_b32_e32 v6, v207
	v_cvt_pk_fp8_f32 v6, v8, v9
	v_mov_b32_dpp v94, v106 row_ror:8 row_mask:0xf bank_mask:0x3
	v_mov_b32_dpp v95, v102 row_ror:8 row_mask:0xf bank_mask:0x3
	v_mov_b32_dpp v78, v89 row_ror:8 row_mask:0xf bank_mask:0x3
	v_cvt_pk_fp8_f32 v6, v10, v7 op_sel:[0,0,1]
	v_min_f32_e64 v7, |v4|, s33
	v_bfi_b32 v4, s2, v7, v4
	v_min_f32_e64 v7, |v5|, s33
	v_bfi_b32 v5, s2, v7, v5
	v_min_f32_e64 v7, |v12|, s33
	v_bfi_b32 v8, s2, v7, v12
	v_min_f32_e64 v7, |v13|, s33
	v_bfi_b32 v9, s2, v7, v13
	v_mov_b32_e32 v7, v207
	v_cvt_pk_fp8_f32 v7, v4, v5
	v_mov_b32_e32 v4, v22
	v_mov_b32_e32 v5, v18
	v_mov_b32_dpp v79, v85 row_ror:8 row_mask:0xf bank_mask:0x3
	v_cvt_pk_fp8_f32 v7, v8, v9 op_sel:[0,0,1]
	v_add_co_u32_e32 v8, vcc, 0x2c000, v2
	v_mov_b32_dpp v4, v6 row_ror:8 row_mask:0xf bank_mask:0xc
	s_nop 0
	v_addc_co_u32_e32 v9, vcc, 0, v3, vcc
	v_add_co_u32_e32 v2, vcc, 0x2e000, v2
	v_mov_b32_dpp v6, v22 row_ror:8 row_mask:0xf bank_mask:0x3
	s_nop 0
	v_addc_co_u32_e32 v3, vcc, 0, v3, vcc
	v_mov_b32_dpp v5, v7 row_ror:8 row_mask:0xf bank_mask:0xc
	v_mov_b32_dpp v7, v18 row_ror:8 row_mask:0xf bank_mask:0x3
	s_mov_b64 s[0:1], -1
	s_andn2_b64 vcc, exec, s[52:53]
	v_readlane_b32 s52, v255, 55
	global_store_dwordx2 v[90:91], v[94:95], off nt
	global_store_dwordx2 v[74:75], v[78:79], off nt
	global_store_dwordx2 v[8:9], v[4:5], off nt
	global_store_dwordx2 v[2:3], v[6:7], off nt
	s_cbranch_vccnz .LBB0_1346
	s_andn2_b64 vcc, exec, s[38:39]
	s_cbranch_vccnz .LBB0_1345
	s_barrier
	s_branch .LBB0_1345
